# nt cache policy on the once-read f32 weight loads of all weight-copy loops and the adaLN GEMV; branch mid-epilogue gate loads hoisted
# speedup vs baseline: 1.0208x; 1.0193x over previous
.LBB0_13:
	v_add_co_u32_e32 v26, vcc, 0xffd00000, v8
	global_load_dwordx4 v[0:3], v[8:9], off nt
	s_nop 0
	v_addc_co_u32_e32 v27, vcc, -1, v9, vcc
	v_add_co_u32_e32 v28, vcc, 0xffd60000, v8
	s_add_i32 s14, s14, 16
	s_nop 0
	v_addc_co_u32_e32 v29, vcc, -1, v9, vcc
	v_add_co_u32_e32 v34, vcc, 0xffdc0000, v8
	global_load_dwordx4 v[18:21], v[26:27], off nt
	global_load_dwordx4 v[22:25], v[28:29], off nt
	v_addc_co_u32_e32 v35, vcc, -1, v9, vcc
	v_add_co_u32_e32 v36, vcc, 0xffe20000, v8
	s_cmpk_lt_u32 s14, 0xf0
	s_nop 0
	v_addc_co_u32_e32 v37, vcc, -1, v9, vcc
	v_add_co_u32_e32 v42, vcc, 0xffe80000, v8
	global_load_dwordx4 v[26:29], v[34:35], off nt
	global_load_dwordx4 v[30:33], v[36:37], off nt
	v_addc_co_u32_e32 v43, vcc, -1, v9, vcc
	v_add_co_u32_e32 v44, vcc, 0xffee0000, v8
	s_nop 1
	v_addc_co_u32_e32 v45, vcc, -1, v9, vcc
	v_add_co_u32_e32 v50, vcc, 0xfff40000, v8
	global_load_dwordx4 v[34:37], v[42:43], off nt
	global_load_dwordx4 v[38:41], v[44:45], off nt
	v_addc_co_u32_e32 v51, vcc, -1, v9, vcc
	v_add_co_u32_e32 v52, vcc, 0xfffa0000, v8
	s_nop 1
	v_addc_co_u32_e32 v53, vcc, -1, v9, vcc
	v_add_co_u32_e32 v58, vcc, 0x60000, v8
	global_load_dwordx4 v[42:45], v[50:51], off nt
	global_load_dwordx4 v[46:49], v[52:53], off nt
	v_addc_co_u32_e32 v59, vcc, 0, v9, vcc
	v_add_co_u32_e32 v60, vcc, 0xc0000, v8
	s_nop 1
	v_addc_co_u32_e32 v61, vcc, 0, v9, vcc
	v_add_co_u32_e32 v66, vcc, 0x120000, v8
	global_load_dwordx4 v[50:53], v[58:59], off nt
	global_load_dwordx4 v[54:57], v[60:61], off nt
	v_addc_co_u32_e32 v67, vcc, 0, v9, vcc
	v_add_co_u32_e32 v68, vcc, 0x180000, v8
	s_nop 1
	v_addc_co_u32_e32 v69, vcc, 0, v9, vcc
	v_add_co_u32_e32 v74, vcc, 0x1e0000, v8
	global_load_dwordx4 v[58:61], v[66:67], off nt
	global_load_dwordx4 v[62:65], v[68:69], off nt
	v_addc_co_u32_e32 v75, vcc, 0, v9, vcc
	v_add_co_u32_e32 v76, vcc, 0x240000, v8
	s_nop 1
	v_addc_co_u32_e32 v77, vcc, 0, v9, vcc
	v_add_co_u32_e32 v78, vcc, 0x2a0000, v8
	global_load_dwordx4 v[66:69], v[74:75], off nt
	global_load_dwordx4 v[70:73], v[76:77], off nt
	v_addc_co_u32_e32 v79, vcc, 0, v9, vcc
	global_load_dwordx4 v[74:77], v[78:79], off nt
	ds_read2_b32 v[78:79], v17 offset1:8
	ds_read2_b32 v[80:81], v17 offset0:16 offset1:24
	ds_read2_b32 v[82:83], v17 offset0:32 offset1:40
	ds_read2_b32 v[84:85], v17 offset0:48 offset1:56
	ds_read2_b32 v[86:87], v17 offset0:64 offset1:72
	ds_read2_b32 v[88:89], v17 offset0:80 offset1:88
	ds_read2_b32 v[90:91], v17 offset0:96 offset1:104
	ds_read2_b32 v[92:93], v17 offset0:112 offset1:120
	s_waitcnt lgkmcnt(7)
	v_mov_b32_e32 v94, v79
	s_waitcnt lgkmcnt(6)
	v_mov_b32_e32 v96, v81
	s_waitcnt lgkmcnt(5)
	v_mov_b32_e32 v98, v83
	s_waitcnt lgkmcnt(4)
	v_mov_b32_e32 v100, v85
	s_waitcnt lgkmcnt(3)
	v_mov_b32_e32 v102, v87
	s_waitcnt lgkmcnt(2)
	v_mov_b32_e32 v104, v89
	s_waitcnt lgkmcnt(1)
	v_mov_b32_e32 v106, v91
	s_waitcnt lgkmcnt(0)
	v_mov_b32_e32 v108, v93
	v_add_u32_e32 v17, 0x200, v17
	v_lshl_add_u64 v[8:9], v[8:9], 0, s[10:11]
	s_waitcnt vmcnt(14)
	v_pk_fma_f32 v[6:7], v[20:21], v[78:79], v[6:7] op_sel_hi:[1,0,1]
	v_pk_fma_f32 v[10:11], v[18:19], v[78:79], v[10:11] op_sel_hi:[1,0,1]
	s_waitcnt vmcnt(13)
	v_pk_fma_f32 v[6:7], v[24:25], v[94:95], v[6:7] op_sel_hi:[1,0,1]
	v_pk_fma_f32 v[10:11], v[22:23], v[94:95], v[10:11] op_sel_hi:[1,0,1]
	s_waitcnt vmcnt(12)
	v_pk_fma_f32 v[6:7], v[28:29], v[80:81], v[6:7] op_sel_hi:[1,0,1]
	v_pk_fma_f32 v[10:11], v[26:27], v[80:81], v[10:11] op_sel_hi:[1,0,1]
	s_waitcnt vmcnt(11)
	v_pk_fma_f32 v[6:7], v[32:33], v[96:97], v[6:7] op_sel_hi:[1,0,1]
	v_pk_fma_f32 v[10:11], v[30:31], v[96:97], v[10:11] op_sel_hi:[1,0,1]
	s_waitcnt vmcnt(10)
	v_pk_fma_f32 v[6:7], v[36:37], v[82:83], v[6:7] op_sel_hi:[1,0,1]
	v_pk_fma_f32 v[10:11], v[34:35], v[82:83], v[10:11] op_sel_hi:[1,0,1]
	s_waitcnt vmcnt(9)
	v_pk_fma_f32 v[6:7], v[40:41], v[98:99], v[6:7] op_sel_hi:[1,0,1]
	v_pk_fma_f32 v[10:11], v[38:39], v[98:99], v[10:11] op_sel_hi:[1,0,1]
	s_waitcnt vmcnt(8)
	v_pk_fma_f32 v[6:7], v[44:45], v[84:85], v[6:7] op_sel_hi:[1,0,1]
	v_pk_fma_f32 v[10:11], v[42:43], v[84:85], v[10:11] op_sel_hi:[1,0,1]
	s_waitcnt vmcnt(7)
	v_pk_fma_f32 v[6:7], v[48:49], v[100:101], v[6:7] op_sel_hi:[1,0,1]
	v_pk_fma_f32 v[10:11], v[46:47], v[100:101], v[10:11] op_sel_hi:[1,0,1]
	v_pk_fma_f32 v[2:3], v[2:3], v[86:87], v[6:7] op_sel_hi:[1,0,1]
	v_pk_fma_f32 v[0:1], v[0:1], v[86:87], v[10:11] op_sel_hi:[1,0,1]
	s_waitcnt vmcnt(6)
	v_pk_fma_f32 v[2:3], v[52:53], v[102:103], v[2:3] op_sel_hi:[1,0,1]
	v_pk_fma_f32 v[0:1], v[50:51], v[102:103], v[0:1] op_sel_hi:[1,0,1]
	s_waitcnt vmcnt(5)
	v_pk_fma_f32 v[2:3], v[56:57], v[88:89], v[2:3] op_sel_hi:[1,0,1]
	v_pk_fma_f32 v[0:1], v[54:55], v[88:89], v[0:1] op_sel_hi:[1,0,1]
	s_waitcnt vmcnt(4)
	v_pk_fma_f32 v[2:3], v[60:61], v[104:105], v[2:3] op_sel_hi:[1,0,1]
	v_pk_fma_f32 v[0:1], v[58:59], v[104:105], v[0:1] op_sel_hi:[1,0,1]
	s_waitcnt vmcnt(3)
	v_pk_fma_f32 v[2:3], v[64:65], v[90:91], v[2:3] op_sel_hi:[1,0,1]
	v_pk_fma_f32 v[0:1], v[62:63], v[90:91], v[0:1] op_sel_hi:[1,0,1]
	s_waitcnt vmcnt(2)
	v_pk_fma_f32 v[2:3], v[68:69], v[106:107], v[2:3] op_sel_hi:[1,0,1]
	v_pk_fma_f32 v[0:1], v[66:67], v[106:107], v[0:1] op_sel_hi:[1,0,1]
	s_waitcnt vmcnt(1)
	v_pk_fma_f32 v[2:3], v[72:73], v[92:93], v[2:3] op_sel_hi:[1,0,1]
	v_pk_fma_f32 v[0:1], v[70:71], v[92:93], v[0:1] op_sel_hi:[1,0,1]
	s_waitcnt vmcnt(0)
	v_pk_fma_f32 v[6:7], v[76:77], v[108:109], v[2:3] op_sel_hi:[1,0,1]
	v_pk_fma_f32 v[10:11], v[74:75], v[108:109], v[0:1] op_sel_hi:[1,0,1]
	s_cbranch_scc1 .LBB0_13
	v_mov_b32_e32 v0, v144
	v_mov_b32_e32 v1, v144
	v_mov_b32_e32 v8, v144
	v_lshlrev_b32_e32 v17, 2, v0
	v_lshlrev_b32_e32 v18, 2, v1
	v_xor_b32_e32 v0, 32, v17
	v_xor_b32_e32 v1, 32, v18
	ds_bpermute_b32 v0, v0, v10
	ds_bpermute_b32 v1, v1, v11
	v_mov_b32_e32 v9, v144
	v_xor_b32_e32 v2, 64, v17
	s_waitcnt lgkmcnt(0)
	v_pk_add_f32 v[0:1], v[10:11], v[0:1]
	v_lshlrev_b32_e32 v10, 2, v8
	v_lshlrev_b32_e32 v11, 2, v9
	v_xor_b32_e32 v3, 64, v18
	v_xor_b32_e32 v8, 32, v10
	v_xor_b32_e32 v9, 32, v11
	ds_bpermute_b32 v2, v2, v0
	ds_bpermute_b32 v3, v3, v1
	ds_bpermute_b32 v8, v8, v6
	ds_bpermute_b32 v9, v9, v7
	v_xor_b32_e32 v17, 0x80, v17
	s_waitcnt lgkmcnt(2)
	v_pk_add_f32 v[0:1], v[0:1], v[2:3]
	v_xor_b32_e32 v2, 64, v10
	v_xor_b32_e32 v3, 64, v11
	s_waitcnt lgkmcnt(0)
	v_pk_add_f32 v[6:7], v[6:7], v[8:9]
	ds_bpermute_b32 v8, v2, v6
	ds_bpermute_b32 v9, v3, v7
	v_xor_b32_e32 v3, 0x80, v18
	v_xor_b32_e32 v10, 0x80, v10
	ds_bpermute_b32 v2, v17, v0
	ds_bpermute_b32 v3, v3, v1
	s_waitcnt lgkmcnt(2)
	v_pk_add_f32 v[6:7], v[6:7], v[8:9]
	v_xor_b32_e32 v9, 0x80, v11
	ds_bpermute_b32 v8, v10, v6
	ds_bpermute_b32 v9, v9, v7
	s_and_saveexec_b64 s[14:15], s[4:5]
	s_cbranch_execz .LBB0_11
	s_load_dwordx2 s[16:17], s[8:9], 0x18
	s_load_dwordx2 s[20:21], s[8:9], 0xd8
	s_mul_i32 s18, s1, 0x3000
	s_ashr_i32 s19, s18, 31
	s_lshl_b64 s[18:19], s[18:19], 2
	s_waitcnt lgkmcnt(0)
	s_add_u32 s1, s16, s18
	s_addc_u32 s17, s17, s19
	s_add_u32 s16, s1, s12
	s_addc_u32 s17, s17, s13
	global_load_dwordx4 v[18:21], v16, s[16:17]
	s_add_u32 s1, s20, s18
	s_addc_u32 s16, s21, s19
	v_pk_add_f32 v[0:1], v[0:1], v[2:3]
	v_pk_add_f32 v[2:3], v[6:7], v[8:9]
	s_add_u32 s12, s1, s12
	s_addc_u32 s13, s16, s13
	s_waitcnt vmcnt(0)
	v_pk_add_f32 v[2:3], v[2:3], v[20:21]
	v_pk_add_f32 v[0:1], v[0:1], v[18:19]
	global_store_dwordx4 v16, v[0:3], s[12:13]
	s_branch .LBB0_11

.LBB0_21:
	s_add_i32 s4, s17, 0xffffe900
	s_mul_hi_u32 s10, s4, s16
	s_mul_i32 s11, s10, s1
	s_sub_i32 s11, s4, s11
	s_add_i32 s12, s10, 1
	s_sub_i32 s13, s11, s1
	s_cmp_ge_u32 s11, s1
	s_cselect_b32 s10, s12, s10
	s_cselect_b32 s11, s13, s11
	s_add_i32 s12, s10, 1
	s_cmp_ge_u32 s11, s1
	s_cselect_b32 s12, s12, s10
	s_mul_i32 s10, s12, s1
	s_sub_i32 s13, s4, s10
	s_add_i32 s13, s13, s0
	s_cmpk_gt_u32 s13, 0x3fff
	s_mov_b64 s[10:11], -1
	s_cbranch_scc0 .LBB0_23
	s_load_dwordx2 s[10:11], s[8:9], 0xc0
	s_load_dwordx2 s[76:77], s[8:9], 0x100
	s_add_i32 s4, s13, 0xffffc000
	s_lshr_b32 s4, s4, 9
	s_lshl_b32 s73, s12, 4
	s_add_i32 s4, s4, s73
	s_lshl_b64 s[74:75], s[4:5], 23
	s_waitcnt lgkmcnt(0)
	s_add_u32 s78, s10, s74
	s_addc_u32 s79, s11, s75
	s_lshl_b32 s10, s13, 2
	s_lshl_b32 s11, s13, 6
	s_and_b32 s10, s10, 0x7c0
	s_and_b32 s11, s11, 0x3c0
	s_lshl_b64 s[74:75], s[4:5], 22
	s_add_u32 s4, s76, s74
	s_addc_u32 s73, s77, s75
	s_lshl_b32 s74, s10, 2
	v_add_u32_e32 v48, s11, v4
	s_add_u32 s74, s78, s74
	s_addc_u32 s75, s79, 0
	v_ashrrev_i32_e32 v49, 31, v48
	v_lshl_add_u64 v[50:51], s[74:75], 0, v[0:1]
	v_lshlrev_b64 v[48:49], 13, v[48:49]
	v_lshl_add_u64 v[48:49], v[50:51], 0, v[48:49]
	v_add_co_u32_e32 v50, vcc, s18, v48
	s_lshl_b32 s11, s11, 1
	s_nop 0
	v_addc_co_u32_e32 v51, vcc, 0, v49, vcc
	v_add_co_u32_e32 v52, vcc, s19, v48
	s_add_u32 s74, s4, s11
	s_nop 0
	v_addc_co_u32_e32 v53, vcc, 0, v49, vcc
	v_add_co_u32_e32 v54, vcc, s20, v48
	s_addc_u32 s75, s73, 0
	s_nop 0
	v_addc_co_u32_e32 v55, vcc, 0, v49, vcc
	v_add_co_u32_e32 v58, vcc, s21, v48
	global_load_dwordx2 v[56:57], v[48:49], off nt
	s_nop 0
	global_load_dwordx2 v[50:51], v[50:51], off nt
	s_nop 0
	global_load_dwordx2 v[52:53], v[52:53], off nt
	s_nop 0
	global_load_dwordx2 v[54:55], v[54:55], off nt
	v_addc_co_u32_e32 v59, vcc, 0, v49, vcc
	v_add_co_u32_e32 v60, vcc, s22, v48
	v_mov_b32_e32 v3, v1
	s_nop 0
	v_addc_co_u32_e32 v61, vcc, 0, v49, vcc
	v_add_co_u32_e32 v62, vcc, s23, v48
	s_nop 1
	v_addc_co_u32_e32 v63, vcc, 0, v49, vcc
	v_add_co_u32_e32 v64, vcc, s24, v48
	s_nop 1
	v_addc_co_u32_e32 v65, vcc, 0, v49, vcc
	v_add_co_u32_e32 v66, vcc, s25, v48
	global_load_dwordx2 v[58:59], v[58:59], off nt
	s_nop 0
	global_load_dwordx2 v[60:61], v[60:61], off nt
	s_nop 0
	global_load_dwordx2 v[62:63], v[62:63], off nt
	s_nop 0
	global_load_dwordx2 v[64:65], v[64:65], off nt
	v_addc_co_u32_e32 v67, vcc, 0, v49, vcc
	v_add_co_u32_e32 v68, vcc, s26, v48
	s_nop 1
	v_addc_co_u32_e32 v69, vcc, 0, v49, vcc
	v_add_co_u32_e32 v70, vcc, s27, v48
	s_nop 1
	v_addc_co_u32_e32 v71, vcc, 0, v49, vcc
	v_add_co_u32_e32 v72, vcc, s28, v48
	s_nop 1
	v_addc_co_u32_e32 v73, vcc, 0, v49, vcc
	v_add_co_u32_e32 v74, vcc, s29, v48
	global_load_dwordx2 v[66:67], v[66:67], off nt
	s_nop 0
	global_load_dwordx2 v[68:69], v[68:69], off nt
	s_nop 0
	global_load_dwordx2 v[70:71], v[70:71], off nt
	s_nop 0
	global_load_dwordx2 v[72:73], v[72:73], off nt
	v_addc_co_u32_e32 v75, vcc, 0, v49, vcc
	v_add_co_u32_e32 v76, vcc, s30, v48
	s_nop 1
	v_addc_co_u32_e32 v77, vcc, 0, v49, vcc
	v_add_co_u32_e32 v78, vcc, s31, v48
	s_nop 1
	v_addc_co_u32_e32 v79, vcc, 0, v49, vcc
	v_add_co_u32_e32 v80, vcc, s34, v48
	s_nop 1
	v_addc_co_u32_e32 v81, vcc, 0, v49, vcc
	v_add_co_u32_e32 v82, vcc, s35, v48
	global_load_dwordx2 v[74:75], v[74:75], off nt
	s_nop 0
	global_load_dwordx2 v[76:77], v[76:77], off nt
	s_nop 0
	global_load_dwordx2 v[78:79], v[78:79], off nt
	s_nop 0
	global_load_dwordx2 v[80:81], v[80:81], off nt
	v_addc_co_u32_e32 v83, vcc, 0, v49, vcc
	v_add_co_u32_e32 v84, vcc, s38, v48
	s_nop 1
	v_addc_co_u32_e32 v85, vcc, 0, v49, vcc
	v_add_co_u32_e32 v86, vcc, s39, v48
	s_nop 1
	v_addc_co_u32_e32 v87, vcc, 0, v49, vcc
	v_add_co_u32_e32 v88, vcc, s40, v48
	s_nop 1
	v_addc_co_u32_e32 v89, vcc, 0, v49, vcc
	v_add_co_u32_e32 v90, vcc, s41, v48
	global_load_dwordx2 v[82:83], v[82:83], off nt
	s_nop 0
	global_load_dwordx2 v[84:85], v[84:85], off nt
	s_nop 0
	global_load_dwordx2 v[86:87], v[86:87], off nt
	s_nop 0
	global_load_dwordx2 v[88:89], v[88:89], off nt
	v_addc_co_u32_e32 v91, vcc, 0, v49, vcc
	v_add_co_u32_e32 v92, vcc, s42, v48
	s_nop 1
	v_addc_co_u32_e32 v93, vcc, 0, v49, vcc
	v_add_co_u32_e32 v94, vcc, s43, v48
	s_nop 1
	v_addc_co_u32_e32 v95, vcc, 0, v49, vcc
	v_add_co_u32_e32 v96, vcc, s44, v48
	s_nop 1
	v_addc_co_u32_e32 v97, vcc, 0, v49, vcc
	v_add_co_u32_e32 v98, vcc, s45, v48
	global_load_dwordx2 v[90:91], v[90:91], off nt
	s_nop 0
	global_load_dwordx2 v[92:93], v[92:93], off nt
	s_nop 0
	global_load_dwordx2 v[94:95], v[94:95], off nt
	s_nop 0
	global_load_dwordx2 v[96:97], v[96:97], off nt
	v_addc_co_u32_e32 v99, vcc, 0, v49, vcc
	v_add_co_u32_e32 v100, vcc, s46, v48
	s_nop 1
	v_addc_co_u32_e32 v101, vcc, 0, v49, vcc
	v_add_co_u32_e32 v102, vcc, s47, v48
	s_nop 1
	v_addc_co_u32_e32 v103, vcc, 0, v49, vcc
	v_add_co_u32_e32 v104, vcc, s48, v48
	s_nop 1
	v_addc_co_u32_e32 v105, vcc, 0, v49, vcc
	v_add_co_u32_e32 v106, vcc, s49, v48
	global_load_dwordx2 v[98:99], v[98:99], off nt
	s_nop 0
	global_load_dwordx2 v[100:101], v[100:101], off nt
	s_nop 0
	global_load_dwordx2 v[102:103], v[102:103], off nt
	s_nop 0
	global_load_dwordx2 v[104:105], v[104:105], off nt
	v_addc_co_u32_e32 v107, vcc, 0, v49, vcc
	v_add_co_u32_e32 v108, vcc, s50, v48
	s_nop 1
	v_addc_co_u32_e32 v109, vcc, 0, v49, vcc
	v_add_co_u32_e32 v110, vcc, s51, v48
	s_nop 1
	v_addc_co_u32_e32 v111, vcc, 0, v49, vcc
	v_add_co_u32_e32 v48, vcc, s52, v48
	s_nop 1
	v_addc_co_u32_e32 v49, vcc, 0, v49, vcc
	global_load_dwordx2 v[106:107], v[106:107], off nt
	s_nop 0
	global_load_dwordx2 v[108:109], v[108:109], off nt
	s_nop 0
	global_load_dwordx2 v[110:111], v[110:111], off nt
	s_nop 0
	global_load_dwordx2 v[48:49], v[48:49], off nt
	s_waitcnt vmcnt(31)
	ds_write2_b32 v5, v56, v57 offset1:1
	s_waitcnt vmcnt(30)
	ds_write2_b32 v5, v50, v51 offset0:130 offset1:131
	s_waitcnt vmcnt(29)
	ds_write2_b32 v16, v52, v53 offset1:1
	s_waitcnt vmcnt(28)
	ds_write2_b32 v17, v54, v55 offset1:1
	s_waitcnt vmcnt(27)
	ds_write2_b32 v18, v58, v59 offset1:1
	s_waitcnt vmcnt(26)
	ds_write2_b32 v19, v60, v61 offset1:1
	s_waitcnt vmcnt(25)
	ds_write2_b32 v20, v62, v63 offset1:1
	s_waitcnt vmcnt(24)
	ds_write2_b32 v21, v64, v65 offset1:1
	s_waitcnt vmcnt(23)
	ds_write2_b32 v22, v66, v67 offset1:1
	s_waitcnt vmcnt(22)
	ds_write2_b32 v23, v68, v69 offset1:1
	s_waitcnt vmcnt(21)
	ds_write2_b32 v24, v70, v71 offset1:1
	s_waitcnt vmcnt(20)
	ds_write2_b32 v25, v72, v73 offset1:1
	s_waitcnt vmcnt(19)
	ds_write2_b32 v26, v74, v75 offset1:1
	s_waitcnt vmcnt(18)
	ds_write2_b32 v27, v76, v77 offset1:1
	s_waitcnt vmcnt(17)
	ds_write2_b32 v28, v78, v79 offset1:1
	s_waitcnt vmcnt(16)
	ds_write2_b32 v29, v80, v81 offset1:1
	s_waitcnt vmcnt(15)
	ds_write2_b32 v30, v82, v83 offset1:1
	s_waitcnt vmcnt(14)
	ds_write2_b32 v31, v84, v85 offset1:1
	s_waitcnt vmcnt(13)
	ds_write2_b32 v32, v86, v87 offset1:1
	s_waitcnt vmcnt(12)
	ds_write2_b32 v33, v88, v89 offset1:1
	s_waitcnt vmcnt(11)
	ds_write2_b32 v34, v90, v91 offset1:1
	s_waitcnt vmcnt(10)
	ds_write2_b32 v35, v92, v93 offset1:1
	s_waitcnt vmcnt(9)
	ds_write2_b32 v36, v94, v95 offset1:1
	s_waitcnt vmcnt(8)
	ds_write2_b32 v37, v96, v97 offset1:1
	s_waitcnt vmcnt(7)
	ds_write2_b32 v38, v98, v99 offset1:1
	s_waitcnt vmcnt(6)
	ds_write2_b32 v39, v100, v101 offset1:1
	s_waitcnt vmcnt(5)
	ds_write2_b32 v40, v102, v103 offset1:1
	s_waitcnt vmcnt(4)
	ds_write2_b32 v41, v104, v105 offset1:1
	s_waitcnt vmcnt(3)
	ds_write2_b32 v42, v106, v107 offset1:1
	s_waitcnt vmcnt(2)
	ds_write2_b32 v43, v108, v109 offset1:1
	s_waitcnt vmcnt(1)
	ds_write2_b32 v44, v110, v111 offset1:1
	s_waitcnt vmcnt(0)
	ds_write2_b32 v45, v48, v49 offset1:1
	s_waitcnt lgkmcnt(0)
	ds_read2_b32 v[52:53], v6 offset0:65 offset1:73
	ds_read2_b32 v[54:55], v6 offset1:8
	ds_read2_b32 v[56:57], v6 offset0:130 offset1:138
	ds_read2_b32 v[58:59], v6 offset0:195 offset1:203
	ds_read2_b32 v[60:61], v46 offset0:4 offset1:12
	ds_read2_b32 v[62:63], v46 offset0:69 offset1:77
	ds_read2_b32 v[64:65], v46 offset0:134 offset1:142
	ds_read2_b32 v[66:67], v46 offset0:199 offset1:207
	v_add_u32_e32 v70, s10, v13
	v_ashrrev_i32_e32 v71, 31, v70
	v_lshl_add_u64 v[68:69], s[74:75], 0, v[2:3]
	v_lshlrev_b64 v[70:71], 11, v[70:71]
	s_waitcnt lgkmcnt(6)
	v_cvt_pk_bf16_f32 v48, v54, v52
	s_waitcnt lgkmcnt(4)
	v_cvt_pk_bf16_f32 v49, v56, v58
	s_waitcnt lgkmcnt(2)
	v_cvt_pk_bf16_f32 v50, v60, v62
	s_waitcnt lgkmcnt(0)
	v_cvt_pk_bf16_f32 v51, v64, v66
	v_lshl_add_u64 v[70:71], v[68:69], 0, v[70:71]
	v_add_u32_e32 v52, s10, v7
	global_store_dwordx4 v[70:71], v[48:51], off nt
	s_nop 1
	v_cvt_pk_bf16_f32 v48, v55, v53
	v_ashrrev_i32_e32 v53, 31, v52
	v_cvt_pk_bf16_f32 v49, v57, v59
	v_cvt_pk_bf16_f32 v50, v61, v63
	v_cvt_pk_bf16_f32 v51, v65, v67
	v_lshlrev_b64 v[52:53], 11, v[52:53]
	ds_read2_b32 v[54:55], v6 offset0:81 offset1:89
	ds_read2_b32 v[56:57], v6 offset0:16 offset1:24
	ds_read2_b32 v[58:59], v6 offset0:146 offset1:154
	ds_read2_b32 v[60:61], v6 offset0:211 offset1:219
	ds_read2_b32 v[62:63], v46 offset0:20 offset1:28
	ds_read2_b32 v[64:65], v46 offset0:85 offset1:93
	ds_read2_b32 v[66:67], v46 offset0:150 offset1:158
	ds_read2_b32 v[70:71], v46 offset0:215 offset1:223
	v_lshl_add_u64 v[52:53], v[68:69], 0, v[52:53]
	global_store_dwordx4 v[52:53], v[48:51], off nt
	v_add_u32_e32 v52, s10, v8
	v_ashrrev_i32_e32 v53, 31, v52
	v_lshlrev_b64 v[52:53], 11, v[52:53]
	s_waitcnt lgkmcnt(6)
	v_cvt_pk_bf16_f32 v48, v56, v54
	s_waitcnt lgkmcnt(4)
	v_cvt_pk_bf16_f32 v49, v58, v60
	s_waitcnt lgkmcnt(2)
	v_cvt_pk_bf16_f32 v50, v62, v64
	s_waitcnt lgkmcnt(0)
	v_cvt_pk_bf16_f32 v51, v66, v70
	v_lshl_add_u64 v[52:53], v[68:69], 0, v[52:53]
	global_store_dwordx4 v[52:53], v[48:51], off nt
	v_add_u32_e32 v52, s10, v9
	v_ashrrev_i32_e32 v53, 31, v52
	v_cvt_pk_bf16_f32 v48, v57, v55
	v_cvt_pk_bf16_f32 v49, v59, v61
	v_cvt_pk_bf16_f32 v50, v63, v65
	v_cvt_pk_bf16_f32 v51, v67, v71
	v_lshlrev_b64 v[52:53], 11, v[52:53]
	ds_read2_b32 v[54:55], v6 offset0:32 offset1:40
	ds_read2_b32 v[56:57], v6 offset0:97 offset1:105
	ds_read2_b32 v[58:59], v6 offset0:162 offset1:170
	ds_read2_b32 v[60:61], v6 offset0:227 offset1:235
	ds_read2_b32 v[62:63], v46 offset0:36 offset1:44
	ds_read2_b32 v[64:65], v46 offset0:101 offset1:109
	ds_read2_b32 v[66:67], v46 offset0:166 offset1:174
	ds_read2_b32 v[70:71], v46 offset0:231 offset1:239
	v_lshl_add_u64 v[52:53], v[68:69], 0, v[52:53]
	global_store_dwordx4 v[52:53], v[48:51], off nt
	v_add_u32_e32 v52, s10, v10
	v_ashrrev_i32_e32 v53, 31, v52
	v_lshlrev_b64 v[52:53], 11, v[52:53]
	s_waitcnt lgkmcnt(6)
	v_cvt_pk_bf16_f32 v48, v54, v56
	s_waitcnt lgkmcnt(4)
	v_cvt_pk_bf16_f32 v49, v58, v60
	s_waitcnt lgkmcnt(2)
	v_cvt_pk_bf16_f32 v50, v62, v64
	s_waitcnt lgkmcnt(0)
	v_cvt_pk_bf16_f32 v51, v66, v70
	v_lshl_add_u64 v[52:53], v[68:69], 0, v[52:53]
	global_store_dwordx4 v[52:53], v[48:51], off nt
	v_add_u32_e32 v52, s10, v11
	v_ashrrev_i32_e32 v53, 31, v52
	v_cvt_pk_bf16_f32 v48, v55, v57
	v_cvt_pk_bf16_f32 v49, v59, v61
	v_cvt_pk_bf16_f32 v50, v63, v65
	v_cvt_pk_bf16_f32 v51, v67, v71
	v_lshlrev_b64 v[52:53], 11, v[52:53]
	ds_read2_b32 v[54:55], v6 offset0:48 offset1:56
	ds_read2_b32 v[56:57], v6 offset0:113 offset1:121
	ds_read2_b32 v[58:59], v6 offset0:178 offset1:186
	ds_read2_b32 v[60:61], v6 offset0:243 offset1:251
	ds_read2_b32 v[62:63], v46 offset0:52 offset1:60
	ds_read2_b32 v[64:65], v46 offset0:117 offset1:125
	ds_read2_b32 v[66:67], v46 offset0:182 offset1:190
	ds_read2_b32 v[70:71], v46 offset0:247 offset1:255
	v_lshl_add_u64 v[52:53], v[68:69], 0, v[52:53]
	global_store_dwordx4 v[52:53], v[48:51], off nt
	v_add_u32_e32 v52, s10, v14
	v_ashrrev_i32_e32 v53, 31, v52
	v_lshlrev_b64 v[52:53], 11, v[52:53]
	s_waitcnt lgkmcnt(6)
	v_cvt_pk_bf16_f32 v48, v54, v56
	s_waitcnt lgkmcnt(4)
	v_cvt_pk_bf16_f32 v49, v58, v60
	s_waitcnt lgkmcnt(2)
	v_cvt_pk_bf16_f32 v50, v62, v64
	s_waitcnt lgkmcnt(0)
	v_cvt_pk_bf16_f32 v51, v66, v70
	v_lshl_add_u64 v[52:53], v[68:69], 0, v[52:53]
	global_store_dwordx4 v[52:53], v[48:51], off nt
	v_add_u32_e32 v52, s10, v15
	v_ashrrev_i32_e32 v53, 31, v52
	v_lshlrev_b64 v[52:53], 11, v[52:53]
	v_cvt_pk_bf16_f32 v48, v55, v57
	v_cvt_pk_bf16_f32 v49, v59, v61
	v_cvt_pk_bf16_f32 v50, v63, v65
	v_cvt_pk_bf16_f32 v51, v67, v71
	v_lshl_add_u64 v[52:53], v[68:69], 0, v[52:53]
	global_store_dwordx4 v[52:53], v[48:51], off nt
	s_waitcnt lgkmcnt(0)
	s_mov_b64 s[10:11], 0
.LBB0_23:
	s_andn2_b64 vcc, exec, s[10:11]
	s_cbranch_vccnz .LBB0_25
	s_cmpk_gt_u32 s13, 0x1fff
	s_cselect_b64 s[10:11], -1, 0
	s_add_i32 s4, s13, 0xe000
	s_and_b64 s[74:75], s[10:11], exec
	s_cselect_b32 s13, s4, s13
	s_sext_i32_i16 s4, s13
	s_bfe_u32 s4, s4, 0x90016
	s_add_i32 s73, s13, s4
	s_sext_i32_i16 s4, s73
	s_and_b32 s73, s73, 0xfe00
	s_sub_i32 s13, s13, s73
	s_sext_i32_i16 s73, s13
	s_bfe_u32 s73, s73, 0x5001a
	s_add_i32 s73, s13, s73
	s_sext_i32_i16 s74, s73
	s_and_b32 s73, s73, 0xffe0
	s_lshr_b32 s4, s4, 9
	s_ashr_i32 s76, s74, 5
	s_sub_i32 s13, s13, s73
	s_and_b64 s[10:11], s[10:11], exec
	s_cselect_b32 s10, s54, 0xb0
	s_cselect_b32 s77, 0x80, 0
	s_add_u32 s10, s8, s10
	s_addc_u32 s11, s9, 0
	s_load_dwordx2 s[10:11], s[10:11], 0x0
	s_sext_i32_i16 s73, s13
	s_lshl_b32 s74, s12, 4
	s_bfe_i64 s[12:13], s[4:5], 0x100000
	s_add_u32 s12, s12, s74
	s_load_dwordx2 s[74:75], s[8:9], 0xf8
	s_addc_u32 s13, s13, 0
	s_lshl_b64 s[12:13], s[12:13], 23
	s_waitcnt lgkmcnt(0)
	s_add_u32 s78, s10, s12
	s_addc_u32 s11, s11, s13
	s_add_u32 s12, s74, s12
	s_addc_u32 s13, s75, s13
	s_lshl_b32 s74, s76, 6
	s_lshl_b32 s10, s73, 6
	s_lshl_b32 s4, s76, 7
	s_and_b32 s73, s74, 64
	s_and_b32 s4, s4, 0xffffff00
	s_or_b32 s73, s73, s77
	s_ashr_i32 s75, s74, 31
	s_or_b32 s4, s73, s4
	s_lshl_b64 s[74:75], s[74:75], 2
	v_add_u32_e32 v48, s10, v4
	s_add_u32 s74, s78, s74
	s_addc_u32 s75, s11, s75
	v_ashrrev_i32_e32 v49, 31, v48
	v_lshl_add_u64 v[50:51], s[74:75], 0, v[0:1]
	v_lshlrev_b64 v[48:49], 12, v[48:49]
	v_lshl_add_u64 v[48:49], v[50:51], 0, v[48:49]
	v_add_co_u32_e32 v50, vcc, s55, v48
	s_ashr_i32 s11, s10, 31
	s_nop 0
	v_addc_co_u32_e32 v51, vcc, 0, v49, vcc
	v_add_co_u32_e32 v52, vcc, s18, v48
	s_lshl_b64 s[10:11], s[10:11], 1
	s_nop 0
	v_addc_co_u32_e32 v53, vcc, 0, v49, vcc
	v_add_co_u32_e32 v54, vcc, s15, v48
	s_add_u32 s10, s12, s10
	s_nop 0
	v_addc_co_u32_e32 v55, vcc, 0, v49, vcc
	v_add_co_u32_e32 v56, vcc, s19, v48
	s_addc_u32 s11, s13, s11
	s_nop 0
	v_addc_co_u32_e32 v57, vcc, 0, v49, vcc
	v_add_co_u32_e32 v58, vcc, s57, v48
	v_mov_b32_e32 v3, v1
	s_nop 0
	v_addc_co_u32_e32 v59, vcc, 0, v49, vcc
	v_add_co_u32_e32 v60, vcc, s20, v48
	s_nop 1
	v_addc_co_u32_e32 v61, vcc, 0, v49, vcc
	v_add_co_u32_e32 v62, vcc, s53, v48
	s_nop 1
	v_addc_co_u32_e32 v63, vcc, 0, v49, vcc
	v_add_co_u32_e32 v64, vcc, s21, v48
	s_nop 1
	v_addc_co_u32_e32 v65, vcc, 0, v49, vcc
	v_add_co_u32_e32 v66, vcc, s59, v48
	s_nop 1
	v_addc_co_u32_e32 v67, vcc, 0, v49, vcc
	v_add_co_u32_e32 v68, vcc, s22, v48
	s_nop 1
	v_addc_co_u32_e32 v69, vcc, 0, v49, vcc
	v_add_co_u32_e32 v70, vcc, s60, v48
	s_nop 1
	v_addc_co_u32_e32 v71, vcc, 0, v49, vcc
	v_add_co_u32_e32 v72, vcc, s23, v48
	s_nop 1
	v_addc_co_u32_e32 v73, vcc, 0, v49, vcc
	v_add_co_u32_e32 v74, vcc, s61, v48
	s_nop 1
	v_addc_co_u32_e32 v75, vcc, 0, v49, vcc
	v_add_co_u32_e32 v76, vcc, s24, v48
	s_nop 1
	v_addc_co_u32_e32 v77, vcc, 0, v49, vcc
	v_add_co_u32_e32 v78, vcc, s62, v48
	s_nop 1
	v_addc_co_u32_e32 v79, vcc, 0, v49, vcc
	v_add_co_u32_e32 v80, vcc, s25, v48
	s_nop 1
	v_addc_co_u32_e32 v81, vcc, 0, v49, vcc
	v_add_co_u32_e32 v82, vcc, s63, v48
	s_nop 1
	v_addc_co_u32_e32 v83, vcc, 0, v49, vcc
	v_add_co_u32_e32 v84, vcc, s26, v48
	s_nop 1
	v_addc_co_u32_e32 v85, vcc, 0, v49, vcc
	v_add_co_u32_e32 v86, vcc, s64, v48
	s_nop 1
	v_addc_co_u32_e32 v87, vcc, 0, v49, vcc
	v_add_co_u32_e32 v88, vcc, s27, v48
	s_nop 1
	v_addc_co_u32_e32 v89, vcc, 0, v49, vcc
	v_add_co_u32_e32 v90, vcc, s65, v48
	s_nop 1
	v_addc_co_u32_e32 v91, vcc, 0, v49, vcc
	v_add_co_u32_e32 v92, vcc, s28, v48
	s_nop 1
	v_addc_co_u32_e32 v93, vcc, 0, v49, vcc
	v_add_co_u32_e32 v94, vcc, s66, v48
	s_nop 1
	v_addc_co_u32_e32 v95, vcc, 0, v49, vcc
	v_add_co_u32_e32 v96, vcc, s29, v48
	s_nop 1
	v_addc_co_u32_e32 v97, vcc, 0, v49, vcc
	v_add_co_u32_e32 v98, vcc, s67, v48
	s_nop 1
	v_addc_co_u32_e32 v99, vcc, 0, v49, vcc
	v_add_co_u32_e32 v100, vcc, s30, v48
	s_nop 1
	v_addc_co_u32_e32 v101, vcc, 0, v49, vcc
	v_add_co_u32_e32 v102, vcc, s68, v48
	s_nop 1
	v_addc_co_u32_e32 v103, vcc, 0, v49, vcc
	v_add_co_u32_e32 v104, vcc, s31, v48
	s_nop 1
	v_addc_co_u32_e32 v105, vcc, 0, v49, vcc
	v_add_co_u32_e32 v106, vcc, s69, v48
	s_nop 1
	v_addc_co_u32_e32 v107, vcc, 0, v49, vcc
	v_add_co_u32_e32 v108, vcc, s34, v48
	s_nop 1
	v_addc_co_u32_e32 v109, vcc, 0, v49, vcc
	v_add_co_u32_e32 v110, vcc, s70, v48
	s_nop 1
	v_addc_co_u32_e32 v111, vcc, 0, v49, vcc
	global_load_dwordx2 v[48:49], v[48:49], off nt
	s_nop 0
	global_load_dwordx2 v[50:51], v[50:51], off nt
	s_nop 0
	global_load_dwordx2 v[52:53], v[52:53], off nt
	s_nop 0
	global_load_dwordx2 v[54:55], v[54:55], off nt
	s_nop 0
	global_load_dwordx2 v[56:57], v[56:57], off nt
	s_nop 0
	global_load_dwordx2 v[58:59], v[58:59], off nt
	s_nop 0
	global_load_dwordx2 v[60:61], v[60:61], off nt
	s_nop 0
	global_load_dwordx2 v[62:63], v[62:63], off nt
	s_nop 0
	global_load_dwordx2 v[64:65], v[64:65], off nt
	s_nop 0
	global_load_dwordx2 v[66:67], v[66:67], off nt
	s_nop 0
	global_load_dwordx2 v[68:69], v[68:69], off nt
	s_nop 0
	global_load_dwordx2 v[70:71], v[70:71], off nt
	s_nop 0
	global_load_dwordx2 v[72:73], v[72:73], off nt
	s_nop 0
	global_load_dwordx2 v[74:75], v[74:75], off nt
	s_nop 0
	global_load_dwordx2 v[76:77], v[76:77], off nt
	s_nop 0
	global_load_dwordx2 v[78:79], v[78:79], off nt
	s_nop 0
	global_load_dwordx2 v[80:81], v[80:81], off nt
	s_nop 0
	global_load_dwordx2 v[82:83], v[82:83], off nt
	s_nop 0
	global_load_dwordx2 v[84:85], v[84:85], off nt
	s_nop 0
	global_load_dwordx2 v[86:87], v[86:87], off nt
	s_nop 0
	global_load_dwordx2 v[88:89], v[88:89], off nt
	s_nop 0
	global_load_dwordx2 v[90:91], v[90:91], off nt
	s_nop 0
	global_load_dwordx2 v[92:93], v[92:93], off nt
	s_nop 0
	global_load_dwordx2 v[94:95], v[94:95], off nt
	s_nop 0
	global_load_dwordx2 v[96:97], v[96:97], off nt
	s_nop 0
	global_load_dwordx2 v[98:99], v[98:99], off nt
	s_nop 0
	global_load_dwordx2 v[100:101], v[100:101], off nt
	s_nop 0
	global_load_dwordx2 v[102:103], v[102:103], off nt
	s_nop 0
	global_load_dwordx2 v[104:105], v[104:105], off nt
	s_nop 0
	global_load_dwordx2 v[106:107], v[106:107], off nt
	s_nop 0
	global_load_dwordx2 v[108:109], v[108:109], off nt
	s_nop 0
	global_load_dwordx2 v[110:111], v[110:111], off nt
	s_waitcnt vmcnt(31)
	ds_write2_b32 v5, v48, v49 offset1:1
	s_waitcnt vmcnt(30)
	ds_write2_b32 v5, v50, v51 offset0:130 offset1:131
	s_waitcnt vmcnt(29)
	ds_write2_b32 v16, v52, v53 offset1:1
	s_waitcnt vmcnt(28)
	ds_write2_b32 v17, v54, v55 offset1:1
	s_waitcnt vmcnt(27)
	ds_write2_b32 v18, v56, v57 offset1:1
	s_waitcnt vmcnt(26)
	ds_write2_b32 v19, v58, v59 offset1:1
	s_waitcnt vmcnt(25)
	ds_write2_b32 v20, v60, v61 offset1:1
	s_waitcnt vmcnt(24)
	ds_write2_b32 v21, v62, v63 offset1:1
	s_waitcnt vmcnt(23)
	ds_write2_b32 v22, v64, v65 offset1:1
	s_waitcnt vmcnt(22)
	ds_write2_b32 v23, v66, v67 offset1:1
	s_waitcnt vmcnt(21)
	ds_write2_b32 v24, v68, v69 offset1:1
	s_waitcnt vmcnt(20)
	ds_write2_b32 v25, v70, v71 offset1:1
	s_waitcnt vmcnt(19)
	ds_write2_b32 v26, v72, v73 offset1:1
	s_waitcnt vmcnt(18)
	ds_write2_b32 v27, v74, v75 offset1:1
	s_waitcnt vmcnt(17)
	ds_write2_b32 v28, v76, v77 offset1:1
	s_waitcnt vmcnt(16)
	ds_write2_b32 v29, v78, v79 offset1:1
	s_waitcnt vmcnt(15)
	ds_write2_b32 v30, v80, v81 offset1:1
	s_waitcnt vmcnt(14)
	ds_write2_b32 v31, v82, v83 offset1:1
	s_waitcnt vmcnt(13)
	ds_write2_b32 v32, v84, v85 offset1:1
	s_waitcnt vmcnt(12)
	ds_write2_b32 v33, v86, v87 offset1:1
	s_waitcnt vmcnt(11)
	ds_write2_b32 v34, v88, v89 offset1:1
	s_waitcnt vmcnt(10)
	ds_write2_b32 v35, v90, v91 offset1:1
	s_waitcnt vmcnt(9)
	ds_write2_b32 v36, v92, v93 offset1:1
	s_waitcnt vmcnt(8)
	ds_write2_b32 v37, v94, v95 offset1:1
	s_waitcnt vmcnt(7)
	ds_write2_b32 v38, v96, v97 offset1:1
	s_waitcnt vmcnt(6)
	ds_write2_b32 v39, v98, v99 offset1:1
	s_waitcnt vmcnt(5)
	ds_write2_b32 v40, v100, v101 offset1:1
	s_waitcnt vmcnt(4)
	ds_write2_b32 v41, v102, v103 offset1:1
	s_waitcnt vmcnt(3)
	ds_write2_b32 v42, v104, v105 offset1:1
	s_waitcnt vmcnt(2)
	ds_write2_b32 v43, v106, v107 offset1:1
	s_waitcnt vmcnt(1)
	ds_write2_b32 v44, v108, v109 offset1:1
	s_waitcnt vmcnt(0)
	ds_write2_b32 v45, v110, v111 offset1:1
	s_waitcnt lgkmcnt(0)
	ds_read2_b32 v[52:53], v6 offset0:65 offset1:73
	ds_read2_b32 v[54:55], v6 offset1:8
	ds_read2_b32 v[56:57], v6 offset0:130 offset1:138
	ds_read2_b32 v[58:59], v6 offset0:195 offset1:203
	ds_read2_b32 v[60:61], v46 offset0:4 offset1:12
	ds_read2_b32 v[62:63], v46 offset0:69 offset1:77
	ds_read2_b32 v[64:65], v46 offset0:134 offset1:142
	ds_read2_b32 v[66:67], v46 offset0:199 offset1:207
	v_add_u32_e32 v68, s4, v13
	v_ashrrev_i32_e32 v69, 31, v68
	v_lshlrev_b64 v[68:69], 12, v[68:69]
	v_lshl_add_u64 v[70:71], s[10:11], 0, v[2:3]
	s_waitcnt lgkmcnt(6)
	v_cvt_pk_bf16_f32 v48, v54, v52
	s_waitcnt lgkmcnt(4)
	v_cvt_pk_bf16_f32 v49, v56, v58
	s_waitcnt lgkmcnt(2)
	v_cvt_pk_bf16_f32 v50, v60, v62
	s_waitcnt lgkmcnt(0)
	v_cvt_pk_bf16_f32 v51, v64, v66
	v_lshl_add_u64 v[68:69], v[70:71], 0, v[68:69]
	v_add_u32_e32 v52, s4, v7
	global_store_dwordx4 v[68:69], v[48:51], off nt
	s_nop 1
	v_cvt_pk_bf16_f32 v48, v55, v53
	v_ashrrev_i32_e32 v53, 31, v52
	v_cvt_pk_bf16_f32 v49, v57, v59
	v_cvt_pk_bf16_f32 v50, v61, v63
	v_cvt_pk_bf16_f32 v51, v65, v67
	v_lshlrev_b64 v[52:53], 12, v[52:53]
	ds_read2_b32 v[54:55], v6 offset0:81 offset1:89
	ds_read2_b32 v[56:57], v6 offset0:16 offset1:24
	ds_read2_b32 v[58:59], v6 offset0:146 offset1:154
	ds_read2_b32 v[60:61], v6 offset0:211 offset1:219
	ds_read2_b32 v[62:63], v46 offset0:20 offset1:28
	ds_read2_b32 v[64:65], v46 offset0:85 offset1:93
	ds_read2_b32 v[66:67], v46 offset0:150 offset1:158
	ds_read2_b32 v[68:69], v46 offset0:215 offset1:223
	v_lshl_add_u64 v[52:53], v[70:71], 0, v[52:53]
	global_store_dwordx4 v[52:53], v[48:51], off nt
	v_add_u32_e32 v52, s4, v8
	v_ashrrev_i32_e32 v53, 31, v52
	v_lshlrev_b64 v[52:53], 12, v[52:53]
	s_waitcnt lgkmcnt(6)
	v_cvt_pk_bf16_f32 v48, v56, v54
	s_waitcnt lgkmcnt(4)
	v_cvt_pk_bf16_f32 v49, v58, v60
	s_waitcnt lgkmcnt(2)
	v_cvt_pk_bf16_f32 v50, v62, v64
	s_waitcnt lgkmcnt(0)
	v_cvt_pk_bf16_f32 v51, v66, v68
	v_lshl_add_u64 v[52:53], v[70:71], 0, v[52:53]
	global_store_dwordx4 v[52:53], v[48:51], off nt
	v_add_u32_e32 v52, s4, v9
	v_ashrrev_i32_e32 v53, 31, v52
	v_cvt_pk_bf16_f32 v48, v57, v55
	v_cvt_pk_bf16_f32 v49, v59, v61
	v_cvt_pk_bf16_f32 v50, v63, v65
	v_cvt_pk_bf16_f32 v51, v67, v69
	v_lshlrev_b64 v[52:53], 12, v[52:53]
	ds_read2_b32 v[54:55], v6 offset0:32 offset1:40
	ds_read2_b32 v[56:57], v6 offset0:97 offset1:105
	ds_read2_b32 v[58:59], v6 offset0:162 offset1:170
	ds_read2_b32 v[60:61], v6 offset0:227 offset1:235
	ds_read2_b32 v[62:63], v46 offset0:36 offset1:44
	ds_read2_b32 v[64:65], v46 offset0:101 offset1:109
	ds_read2_b32 v[66:67], v46 offset0:166 offset1:174
	ds_read2_b32 v[68:69], v46 offset0:231 offset1:239
	v_lshl_add_u64 v[52:53], v[70:71], 0, v[52:53]
	global_store_dwordx4 v[52:53], v[48:51], off nt
	v_add_u32_e32 v52, s4, v10
	v_ashrrev_i32_e32 v53, 31, v52
	v_lshlrev_b64 v[52:53], 12, v[52:53]
	s_waitcnt lgkmcnt(6)
	v_cvt_pk_bf16_f32 v48, v54, v56
	s_waitcnt lgkmcnt(4)
	v_cvt_pk_bf16_f32 v49, v58, v60
	s_waitcnt lgkmcnt(2)
	v_cvt_pk_bf16_f32 v50, v62, v64
	s_waitcnt lgkmcnt(0)
	v_cvt_pk_bf16_f32 v51, v66, v68
	v_lshl_add_u64 v[52:53], v[70:71], 0, v[52:53]
	global_store_dwordx4 v[52:53], v[48:51], off nt
	v_add_u32_e32 v52, s4, v11
	v_ashrrev_i32_e32 v53, 31, v52
	v_cvt_pk_bf16_f32 v48, v55, v57
	v_cvt_pk_bf16_f32 v49, v59, v61
	v_cvt_pk_bf16_f32 v50, v63, v65
	v_cvt_pk_bf16_f32 v51, v67, v69
	v_lshlrev_b64 v[52:53], 12, v[52:53]
	ds_read2_b32 v[54:55], v6 offset0:48 offset1:56
	ds_read2_b32 v[56:57], v6 offset0:113 offset1:121
	ds_read2_b32 v[58:59], v6 offset0:178 offset1:186
	ds_read2_b32 v[60:61], v6 offset0:243 offset1:251
	ds_read2_b32 v[62:63], v46 offset0:52 offset1:60
	ds_read2_b32 v[64:65], v46 offset0:117 offset1:125
	ds_read2_b32 v[66:67], v46 offset0:182 offset1:190
	ds_read2_b32 v[68:69], v46 offset0:247 offset1:255
	v_lshl_add_u64 v[52:53], v[70:71], 0, v[52:53]
	global_store_dwordx4 v[52:53], v[48:51], off nt
	v_add_u32_e32 v52, s4, v14
	v_ashrrev_i32_e32 v53, 31, v52
	v_lshlrev_b64 v[52:53], 12, v[52:53]
	s_waitcnt lgkmcnt(6)
	v_cvt_pk_bf16_f32 v48, v54, v56
	s_waitcnt lgkmcnt(4)
	v_cvt_pk_bf16_f32 v49, v58, v60
	s_waitcnt lgkmcnt(2)
	v_cvt_pk_bf16_f32 v50, v62, v64
	s_waitcnt lgkmcnt(0)
	v_cvt_pk_bf16_f32 v51, v66, v68
	v_lshl_add_u64 v[52:53], v[70:71], 0, v[52:53]
	global_store_dwordx4 v[52:53], v[48:51], off nt
	v_add_u32_e32 v52, s4, v15
	v_ashrrev_i32_e32 v53, 31, v52
	v_lshlrev_b64 v[52:53], 12, v[52:53]
	v_cvt_pk_bf16_f32 v48, v55, v57
	v_cvt_pk_bf16_f32 v49, v59, v61
	v_cvt_pk_bf16_f32 v50, v63, v65
	v_cvt_pk_bf16_f32 v51, v67, v69
	v_lshl_add_u64 v[52:53], v[70:71], 0, v[52:53]
	global_store_dwordx4 v[52:53], v[48:51], off nt
	s_waitcnt lgkmcnt(0)

.LBB0_26:
	s_ashr_i32 s4, s17, 31
	s_lshr_b32 s4, s4, 27
	s_add_i32 s4, s17, s4
	s_and_b32 s10, s4, 0x3ffffe0
	s_lshl_b32 s4, s4, 1
	s_sub_i32 s10, s17, s10
	s_andn2_b32 s4, s4, 63
	s_cmpk_lt_i32 s17, 0xb00
	s_cselect_b32 s11, 4, 20
	s_cmpk_gt_i32 s17, 0x5ff
	s_cselect_b32 s11, s11, 0
	s_or_b32 s74, s11, s4
	s_lshl_b32 s12, s10, 6
	s_load_dwordx2 s[76:77], s[8:9], 0x28
	s_load_dwordx2 s[10:11], s[8:9], 0xe0
	s_ashr_i32 s75, s74, 31
	s_lshl_b64 s[74:75], s[74:75], 2
	v_add_u32_e32 v3, s12, v4
	s_waitcnt lgkmcnt(0)
	s_add_u32 s74, s76, s74
	s_addc_u32 s75, s77, s75
	v_lshl_add_u64 v[48:49], s[74:75], 0, v[0:1]
	v_add_u32_e32 v47, 2, v3
	v_mad_i64_i32 v[52:53], s[74:75], v47, s71, v[48:49]
	v_add_u32_e32 v47, 4, v3
	v_mad_i64_i32 v[54:55], s[74:75], v47, s71, v[48:49]
	v_add_u32_e32 v47, 6, v3
	v_mad_i64_i32 v[56:57], s[74:75], v47, s71, v[48:49]
	v_add_u32_e32 v47, 10, v3
	v_mad_i64_i32 v[60:61], s[74:75], v47, s71, v[48:49]
	v_add_u32_e32 v47, 12, v3
	v_mad_i64_i32 v[62:63], s[74:75], v47, s71, v[48:49]
	v_add_u32_e32 v47, 14, v3
	v_mad_i64_i32 v[64:65], s[74:75], v47, s71, v[48:49]
	v_add_u32_e32 v47, 16, v3
	v_mad_i64_i32 v[66:67], s[74:75], v47, s71, v[48:49]
	v_add_u32_e32 v47, 18, v3
	v_mad_i64_i32 v[68:69], s[74:75], v47, s71, v[48:49]
	v_add_u32_e32 v47, 20, v3
	v_mad_i64_i32 v[70:71], s[74:75], v47, s71, v[48:49]
	v_add_u32_e32 v47, 22, v3
	v_mad_i64_i32 v[72:73], s[74:75], v47, s71, v[48:49]
	v_add_u32_e32 v47, 24, v3
	v_mad_i64_i32 v[74:75], s[74:75], v47, s71, v[48:49]
	v_add_u32_e32 v47, 32, v3
	v_mad_i64_i32 v[82:83], s[74:75], v47, s71, v[48:49]
	v_add_u32_e32 v47, 36, v3
	v_mad_i64_i32 v[86:87], s[74:75], v47, s71, v[48:49]
	v_add_u32_e32 v47, 38, v3
	v_mad_i64_i32 v[88:89], s[74:75], v47, s71, v[48:49]
	v_add_u32_e32 v47, 40, v3
	v_mad_i64_i32 v[90:91], s[74:75], v47, s71, v[48:49]
	v_add_u32_e32 v47, 42, v3
	v_mad_i64_i32 v[92:93], s[74:75], v47, s71, v[48:49]
	v_add_u32_e32 v47, 44, v3
	v_mad_i64_i32 v[94:95], s[74:75], v47, s71, v[48:49]
	v_add_u32_e32 v47, 46, v3
	v_mad_i64_i32 v[96:97], s[74:75], v47, s71, v[48:49]
	v_add_u32_e32 v47, 48, v3
	v_mad_i64_i32 v[98:99], s[74:75], v47, s71, v[48:49]
	v_add_u32_e32 v47, 50, v3
	v_mad_i64_i32 v[100:101], s[74:75], v47, s71, v[48:49]
	v_add_u32_e32 v47, 52, v3
	v_mad_i64_i32 v[102:103], s[74:75], v47, s71, v[48:49]
	v_add_u32_e32 v47, 54, v3
	v_mad_i64_i32 v[104:105], s[74:75], v47, s71, v[48:49]
	v_add_u32_e32 v47, 56, v3
	v_mad_i64_i32 v[106:107], s[74:75], v47, s71, v[48:49]
	v_add_u32_e32 v47, 58, v3
	v_mad_i64_i32 v[50:51], s[74:75], v3, s71, v[48:49]
	v_add_u32_e32 v58, 8, v3
	v_add_u32_e32 v76, 26, v3
	v_add_u32_e32 v78, 28, v3
	v_add_u32_e32 v80, 30, v3
	v_add_u32_e32 v84, 34, v3
	v_mad_i64_i32 v[108:109], s[74:75], v47, s71, v[48:49]
	v_add_u32_e32 v47, 60, v3
	v_add_u32_e32 v3, 62, v3
	v_mad_i64_i32 v[58:59], s[74:75], v58, s71, v[48:49]
	v_mad_i64_i32 v[76:77], s[74:75], v76, s71, v[48:49]
	v_mad_i64_i32 v[78:79], s[74:75], v78, s71, v[48:49]
	v_mad_i64_i32 v[80:81], s[74:75], v80, s71, v[48:49]
	v_mad_i64_i32 v[84:85], s[74:75], v84, s71, v[48:49]
	v_mad_i64_i32 v[110:111], s[74:75], v47, s71, v[48:49]
	v_mad_i64_i32 v[48:49], s[74:75], v3, s71, v[48:49]
	global_load_dwordx2 v[50:51], v[50:51], off nt
	s_nop 0
	global_load_dwordx2 v[52:53], v[52:53], off nt
	s_nop 0
	global_load_dwordx2 v[54:55], v[54:55], off nt
	s_nop 0
	global_load_dwordx2 v[56:57], v[56:57], off nt
	s_nop 0
	global_load_dwordx2 v[58:59], v[58:59], off nt
	s_nop 0
	global_load_dwordx2 v[60:61], v[60:61], off nt
	s_nop 0
	global_load_dwordx2 v[62:63], v[62:63], off nt
	s_nop 0
	global_load_dwordx2 v[64:65], v[64:65], off nt
	s_nop 0
	global_load_dwordx2 v[66:67], v[66:67], off nt
	s_nop 0
	global_load_dwordx2 v[68:69], v[68:69], off nt
	s_nop 0
	global_load_dwordx2 v[70:71], v[70:71], off nt
	s_nop 0
	global_load_dwordx2 v[72:73], v[72:73], off nt
	s_nop 0
	global_load_dwordx2 v[74:75], v[74:75], off nt
	s_nop 0
	global_load_dwordx2 v[76:77], v[76:77], off nt
	s_nop 0
	global_load_dwordx2 v[78:79], v[78:79], off nt
	s_nop 0
	global_load_dwordx2 v[80:81], v[80:81], off nt
	s_nop 0
	global_load_dwordx2 v[82:83], v[82:83], off nt
	s_nop 0
	global_load_dwordx2 v[84:85], v[84:85], off nt
	s_nop 0
	global_load_dwordx2 v[86:87], v[86:87], off nt
	s_nop 0
	global_load_dwordx2 v[88:89], v[88:89], off nt
	s_nop 0
	global_load_dwordx2 v[90:91], v[90:91], off nt
	s_nop 0
	global_load_dwordx2 v[92:93], v[92:93], off nt
	s_nop 0
	global_load_dwordx2 v[94:95], v[94:95], off nt
	s_nop 0
	global_load_dwordx2 v[96:97], v[96:97], off nt
	s_nop 0
	global_load_dwordx2 v[98:99], v[98:99], off nt
	s_nop 0
	global_load_dwordx2 v[100:101], v[100:101], off nt
	s_nop 0
	global_load_dwordx2 v[102:103], v[102:103], off nt
	s_nop 0
	global_load_dwordx2 v[104:105], v[104:105], off nt
	s_nop 0
	global_load_dwordx2 v[106:107], v[106:107], off nt
	s_nop 0
	global_load_dwordx2 v[108:109], v[108:109], off nt
	s_nop 0
	global_load_dwordx2 v[110:111], v[110:111], off nt
	s_nop 0
	global_load_dwordx2 v[48:49], v[48:49], off nt
	s_waitcnt vmcnt(31)
	ds_write2_b32 v5, v50, v51 offset1:1
	s_waitcnt vmcnt(30)
	ds_write2_b32 v5, v52, v53 offset0:130 offset1:131
	s_waitcnt vmcnt(29)
	ds_write2_b32 v16, v54, v55 offset1:1
	s_waitcnt vmcnt(28)
	ds_write2_b32 v17, v56, v57 offset1:1
	s_waitcnt vmcnt(27)
	ds_write2_b32 v18, v58, v59 offset1:1
	s_waitcnt vmcnt(26)
	ds_write2_b32 v19, v60, v61 offset1:1
	s_waitcnt vmcnt(25)
	ds_write2_b32 v20, v62, v63 offset1:1
	s_waitcnt vmcnt(24)
	ds_write2_b32 v21, v64, v65 offset1:1
	s_waitcnt vmcnt(23)
	ds_write2_b32 v22, v66, v67 offset1:1
	s_waitcnt vmcnt(22)
	ds_write2_b32 v23, v68, v69 offset1:1
	s_waitcnt vmcnt(21)
	ds_write2_b32 v24, v70, v71 offset1:1
	s_waitcnt vmcnt(20)
	ds_write2_b32 v25, v72, v73 offset1:1
	s_waitcnt vmcnt(19)
	ds_write2_b32 v26, v74, v75 offset1:1
	s_waitcnt vmcnt(18)
	ds_write2_b32 v27, v76, v77 offset1:1
	s_waitcnt vmcnt(17)
	ds_write2_b32 v28, v78, v79 offset1:1
	s_waitcnt vmcnt(16)
	ds_write2_b32 v29, v80, v81 offset1:1
	s_waitcnt vmcnt(15)
	ds_write2_b32 v30, v82, v83 offset1:1
	s_waitcnt vmcnt(14)
	ds_write2_b32 v31, v84, v85 offset1:1
	s_waitcnt vmcnt(13)
	ds_write2_b32 v32, v86, v87 offset1:1
	s_waitcnt vmcnt(12)
	ds_write2_b32 v33, v88, v89 offset1:1
	s_waitcnt vmcnt(11)
	ds_write2_b32 v34, v90, v91 offset1:1
	s_waitcnt vmcnt(10)
	ds_write2_b32 v35, v92, v93 offset1:1
	s_waitcnt vmcnt(9)
	ds_write2_b32 v36, v94, v95 offset1:1
	s_waitcnt vmcnt(8)
	ds_write2_b32 v37, v96, v97 offset1:1
	s_waitcnt vmcnt(7)
	ds_write2_b32 v38, v98, v99 offset1:1
	s_waitcnt vmcnt(6)
	ds_write2_b32 v39, v100, v101 offset1:1
	s_waitcnt vmcnt(5)
	ds_write2_b32 v40, v102, v103 offset1:1
	s_waitcnt vmcnt(4)
	ds_write2_b32 v41, v104, v105 offset1:1
	s_waitcnt vmcnt(3)
	ds_write2_b32 v42, v106, v107 offset1:1
	s_waitcnt vmcnt(2)
	ds_write2_b32 v43, v108, v109 offset1:1
	s_waitcnt vmcnt(1)
	ds_write2_b32 v44, v110, v111 offset1:1
	s_waitcnt vmcnt(0)
	ds_write2_b32 v45, v48, v49 offset1:1
	s_waitcnt lgkmcnt(0)
	s_ashr_i32 s13, s12, 31
	ds_read2_b32 v[52:53], v6 offset0:65 offset1:73
	ds_read2_b32 v[54:55], v6 offset1:8
	ds_read2_b32 v[56:57], v6 offset0:130 offset1:138
	ds_read2_b32 v[58:59], v6 offset0:195 offset1:203
	ds_read2_b32 v[60:61], v46 offset0:4 offset1:12
	ds_read2_b32 v[62:63], v46 offset0:69 offset1:77
	ds_read2_b32 v[64:65], v46 offset0:134 offset1:142
	ds_read2_b32 v[66:67], v46 offset0:199 offset1:207
	s_lshl_b64 s[12:13], s[12:13], 1
	s_add_u32 s10, s10, s12
	v_add_u32_e32 v68, s4, v13
	s_addc_u32 s11, s11, s13
	v_mov_b32_e32 v3, v1
	v_ashrrev_i32_e32 v69, 31, v68
	v_lshlrev_b64 v[68:69], 12, v[68:69]
	v_lshl_add_u64 v[70:71], s[10:11], 0, v[2:3]
	s_waitcnt lgkmcnt(6)
	v_cvt_pk_bf16_f32 v48, v54, v52
	s_waitcnt lgkmcnt(4)
	v_cvt_pk_bf16_f32 v49, v56, v58
	s_waitcnt lgkmcnt(2)
	v_cvt_pk_bf16_f32 v50, v60, v62
	s_waitcnt lgkmcnt(0)
	v_cvt_pk_bf16_f32 v51, v64, v66
	v_lshl_add_u64 v[68:69], v[70:71], 0, v[68:69]
	v_add_u32_e32 v52, s4, v7
	global_store_dwordx4 v[68:69], v[48:51], off
	s_nop 1
	v_cvt_pk_bf16_f32 v48, v55, v53
	v_ashrrev_i32_e32 v53, 31, v52
	v_cvt_pk_bf16_f32 v49, v57, v59
	v_cvt_pk_bf16_f32 v50, v61, v63
	v_cvt_pk_bf16_f32 v51, v65, v67
	v_lshlrev_b64 v[52:53], 12, v[52:53]
	ds_read2_b32 v[54:55], v6 offset0:81 offset1:89
	ds_read2_b32 v[56:57], v6 offset0:16 offset1:24
	ds_read2_b32 v[58:59], v6 offset0:146 offset1:154
	ds_read2_b32 v[60:61], v6 offset0:211 offset1:219
	ds_read2_b32 v[62:63], v46 offset0:20 offset1:28
	ds_read2_b32 v[64:65], v46 offset0:85 offset1:93
	ds_read2_b32 v[66:67], v46 offset0:150 offset1:158
	ds_read2_b32 v[68:69], v46 offset0:215 offset1:223
	v_lshl_add_u64 v[52:53], v[70:71], 0, v[52:53]
	global_store_dwordx4 v[52:53], v[48:51], off
	v_add_u32_e32 v52, s4, v8
	v_ashrrev_i32_e32 v53, 31, v52
	v_lshlrev_b64 v[52:53], 12, v[52:53]
	s_waitcnt lgkmcnt(6)
	v_cvt_pk_bf16_f32 v48, v56, v54
	s_waitcnt lgkmcnt(4)
	v_cvt_pk_bf16_f32 v49, v58, v60
	s_waitcnt lgkmcnt(2)
	v_cvt_pk_bf16_f32 v50, v62, v64
	s_waitcnt lgkmcnt(0)
	v_cvt_pk_bf16_f32 v51, v66, v68
	v_lshl_add_u64 v[52:53], v[70:71], 0, v[52:53]
	global_store_dwordx4 v[52:53], v[48:51], off
	v_add_u32_e32 v52, s4, v9
	v_ashrrev_i32_e32 v53, 31, v52
	v_cvt_pk_bf16_f32 v48, v57, v55
	v_cvt_pk_bf16_f32 v49, v59, v61
	v_cvt_pk_bf16_f32 v50, v63, v65
	v_cvt_pk_bf16_f32 v51, v67, v69
	v_lshlrev_b64 v[52:53], 12, v[52:53]
	ds_read2_b32 v[54:55], v6 offset0:32 offset1:40
	ds_read2_b32 v[56:57], v6 offset0:97 offset1:105
	ds_read2_b32 v[58:59], v6 offset0:162 offset1:170
	ds_read2_b32 v[60:61], v6 offset0:227 offset1:235
	ds_read2_b32 v[62:63], v46 offset0:36 offset1:44
	ds_read2_b32 v[64:65], v46 offset0:101 offset1:109
	ds_read2_b32 v[66:67], v46 offset0:166 offset1:174
	ds_read2_b32 v[68:69], v46 offset0:231 offset1:239
	v_lshl_add_u64 v[52:53], v[70:71], 0, v[52:53]
	global_store_dwordx4 v[52:53], v[48:51], off
	v_add_u32_e32 v52, s4, v10
	v_ashrrev_i32_e32 v53, 31, v52
	v_lshlrev_b64 v[52:53], 12, v[52:53]
	s_waitcnt lgkmcnt(6)
	v_cvt_pk_bf16_f32 v48, v54, v56
	s_waitcnt lgkmcnt(4)
	v_cvt_pk_bf16_f32 v49, v58, v60
	s_waitcnt lgkmcnt(2)
	v_cvt_pk_bf16_f32 v50, v62, v64
	s_waitcnt lgkmcnt(0)
	v_cvt_pk_bf16_f32 v51, v66, v68
	v_lshl_add_u64 v[52:53], v[70:71], 0, v[52:53]
	global_store_dwordx4 v[52:53], v[48:51], off
	v_add_u32_e32 v52, s4, v11
	v_ashrrev_i32_e32 v53, 31, v52
	v_cvt_pk_bf16_f32 v48, v55, v57
	v_cvt_pk_bf16_f32 v49, v59, v61
	v_cvt_pk_bf16_f32 v50, v63, v65
	v_cvt_pk_bf16_f32 v51, v67, v69
	v_lshlrev_b64 v[52:53], 12, v[52:53]
	ds_read2_b32 v[54:55], v6 offset0:48 offset1:56
	ds_read2_b32 v[56:57], v6 offset0:113 offset1:121
	ds_read2_b32 v[58:59], v6 offset0:178 offset1:186
	ds_read2_b32 v[60:61], v6 offset0:243 offset1:251
	ds_read2_b32 v[62:63], v46 offset0:52 offset1:60
	ds_read2_b32 v[64:65], v46 offset0:117 offset1:125
	ds_read2_b32 v[66:67], v46 offset0:182 offset1:190
	ds_read2_b32 v[68:69], v46 offset0:247 offset1:255
	v_lshl_add_u64 v[52:53], v[70:71], 0, v[52:53]
	global_store_dwordx4 v[52:53], v[48:51], off
	v_add_u32_e32 v52, s4, v14
	v_ashrrev_i32_e32 v53, 31, v52
	v_lshlrev_b64 v[52:53], 12, v[52:53]
	s_waitcnt lgkmcnt(6)
	v_cvt_pk_bf16_f32 v48, v54, v56
	s_waitcnt lgkmcnt(4)
	v_cvt_pk_bf16_f32 v49, v58, v60
	s_waitcnt lgkmcnt(2)
	v_cvt_pk_bf16_f32 v50, v62, v64
	s_waitcnt lgkmcnt(0)
	v_cvt_pk_bf16_f32 v51, v66, v68
	v_lshl_add_u64 v[52:53], v[70:71], 0, v[52:53]
	global_store_dwordx4 v[52:53], v[48:51], off
	v_add_u32_e32 v52, s4, v15
	v_ashrrev_i32_e32 v53, 31, v52
	v_lshlrev_b64 v[52:53], 12, v[52:53]
	v_cvt_pk_bf16_f32 v48, v55, v57
	v_cvt_pk_bf16_f32 v49, v59, v61
	v_cvt_pk_bf16_f32 v50, v63, v65
	v_cvt_pk_bf16_f32 v51, v67, v69
	v_lshl_add_u64 v[52:53], v[70:71], 0, v[52:53]
	global_store_dwordx4 v[52:53], v[48:51], off
	s_waitcnt lgkmcnt(0)
	s_branch .LBB0_18

.LBB0_259:
	s_ashr_i32 s12, s0, 31
	s_lshr_b32 s12, s12, 23
	s_add_i32 s13, s0, s12
	s_ashr_i32 s12, s13, 9
	s_and_b32 s13, s13, 0xfe00
	s_sub_i32 s46, s0, s13
	s_ashr_i32 s13, s12, 31
	s_sext_i32_i16 s47, s46
	s_lshl_b64 s[14:15], s[12:13], 23
	s_bfe_u32 s12, s47, 0x5001a
	s_add_i32 s12, s46, s12
	s_sext_i32_i16 s13, s12
	s_and_b32 s12, s12, 0xffe0
	s_ashr_i32 s48, s13, 5
	s_sub_i32 s12, s46, s12
	s_waitcnt lgkmcnt(0)
	s_add_u32 s49, s4, s14
	s_addc_u32 s13, s5, s15
	s_add_u32 s47, s10, s14
	s_addc_u32 s46, s11, s15
	s_lshl_b32 s14, s48, 6
	s_lshl_b32 s15, s48, 7
	s_sext_i32_i16 s12, s12
	s_and_b32 s48, s15, 0xffffff00
	s_and_b32 s50, s14, 64
	s_ashr_i32 s15, s14, 31
	s_lshl_b32 s12, s12, 6
	s_or_b32 s48, s50, s48
	s_lshl_b64 s[14:15], s[14:15], 2
	v_add_u32_e32 v4, s12, v6
	s_add_u32 s14, s49, s14
	v_ashrrev_i32_e32 v5, 31, v4
	s_addc_u32 s15, s13, s15
	v_lshlrev_b64 v[4:5], 12, v[4:5]
	v_lshl_add_u64 v[58:59], s[14:15], 0, v[0:1]
	v_lshl_add_u64 v[4:5], v[58:59], 0, v[4:5]
	v_add_co_u32_e32 v58, vcc, s1, v4
	s_ashr_i32 s13, s12, 31
	s_nop 0
	v_addc_co_u32_e32 v59, vcc, 0, v5, vcc
	v_add_co_u32_e32 v60, vcc, s6, v4
	v_add_u32_e32 v42, s48, v7
	s_nop 0
	v_addc_co_u32_e32 v61, vcc, 0, v5, vcc
	v_add_co_u32_e32 v62, vcc, s7, v4
	s_lshl_b64 s[12:13], s[12:13], 1
	s_nop 0
	v_addc_co_u32_e32 v63, vcc, 0, v5, vcc
	v_add_co_u32_e32 v64, vcc, s8, v4
	v_add_u32_e32 v44, 8, v42
	s_nop 0
	v_addc_co_u32_e32 v65, vcc, 0, v5, vcc
	v_add_co_u32_e32 v66, vcc, s9, v4
	v_add_u32_e32 v46, 16, v42
	s_nop 0
	v_addc_co_u32_e32 v67, vcc, 0, v5, vcc
	v_add_co_u32_e32 v68, vcc, s16, v4
	v_add_u32_e32 v48, 24, v42
	s_nop 0
	v_addc_co_u32_e32 v69, vcc, 0, v5, vcc
	v_add_co_u32_e32 v70, vcc, s17, v4
	v_add_u32_e32 v50, 32, v42
	s_nop 0
	v_addc_co_u32_e32 v71, vcc, 0, v5, vcc
	v_add_co_u32_e32 v72, vcc, s18, v4
	v_add_u32_e32 v52, 40, v42
	s_nop 0
	v_addc_co_u32_e32 v73, vcc, 0, v5, vcc
	v_add_co_u32_e32 v74, vcc, s19, v4
	v_add_u32_e32 v54, 48, v42
	s_nop 0
	v_addc_co_u32_e32 v75, vcc, 0, v5, vcc
	v_add_co_u32_e32 v76, vcc, s20, v4
	v_add_u32_e32 v56, 56, v42
	s_nop 0
	v_addc_co_u32_e32 v77, vcc, 0, v5, vcc
	v_add_co_u32_e32 v78, vcc, s21, v4
	s_add_u32 s12, s47, s12
	s_nop 0
	v_addc_co_u32_e32 v79, vcc, 0, v5, vcc
	v_add_co_u32_e32 v80, vcc, s22, v4
	v_ashrrev_i32_e32 v43, 31, v42
	s_nop 0
	v_addc_co_u32_e32 v81, vcc, 0, v5, vcc
	v_add_co_u32_e32 v82, vcc, s23, v4
	v_ashrrev_i32_e32 v45, 31, v44
	s_nop 0
	v_addc_co_u32_e32 v83, vcc, 0, v5, vcc
	v_add_co_u32_e32 v84, vcc, s24, v4
	v_ashrrev_i32_e32 v47, 31, v46
	s_nop 0
	v_addc_co_u32_e32 v85, vcc, 0, v5, vcc
	v_add_co_u32_e32 v86, vcc, s25, v4
	v_ashrrev_i32_e32 v49, 31, v48
	s_nop 0
	v_addc_co_u32_e32 v87, vcc, 0, v5, vcc
	v_add_co_u32_e32 v88, vcc, s26, v4
	v_ashrrev_i32_e32 v51, 31, v50
	s_nop 0
	v_addc_co_u32_e32 v89, vcc, 0, v5, vcc
	v_add_co_u32_e32 v90, vcc, s27, v4
	v_ashrrev_i32_e32 v53, 31, v52
	s_nop 0
	v_addc_co_u32_e32 v91, vcc, 0, v5, vcc
	v_add_co_u32_e32 v92, vcc, s28, v4
	v_ashrrev_i32_e32 v55, 31, v54
	s_nop 0
	v_addc_co_u32_e32 v93, vcc, 0, v5, vcc
	v_add_co_u32_e32 v94, vcc, s29, v4
	v_ashrrev_i32_e32 v57, 31, v56
	s_nop 0
	v_addc_co_u32_e32 v95, vcc, 0, v5, vcc
	v_add_co_u32_e32 v96, vcc, s30, v4
	s_addc_u32 s13, s46, s13
	s_nop 0
	v_addc_co_u32_e32 v97, vcc, 0, v5, vcc
	v_add_co_u32_e32 v98, vcc, s31, v4
	v_lshlrev_b64 v[42:43], 12, v[42:43]
	s_nop 0
	v_addc_co_u32_e32 v99, vcc, 0, v5, vcc
	v_add_co_u32_e32 v100, vcc, s34, v4
	v_lshlrev_b64 v[44:45], 12, v[44:45]
	s_nop 0
	v_addc_co_u32_e32 v101, vcc, 0, v5, vcc
	v_add_co_u32_e32 v102, vcc, s35, v4
	v_lshlrev_b64 v[46:47], 12, v[46:47]
	s_nop 0
	v_addc_co_u32_e32 v103, vcc, 0, v5, vcc
	v_add_co_u32_e32 v104, vcc, s36, v4
	v_lshlrev_b64 v[48:49], 12, v[48:49]
	s_nop 0
	v_addc_co_u32_e32 v105, vcc, 0, v5, vcc
	v_add_co_u32_e32 v106, vcc, s37, v4
	v_lshlrev_b64 v[50:51], 12, v[50:51]
	s_nop 0
	v_addc_co_u32_e32 v107, vcc, 0, v5, vcc
	v_add_co_u32_e32 v108, vcc, s38, v4
	v_lshlrev_b64 v[52:53], 12, v[52:53]
	s_nop 0
	v_addc_co_u32_e32 v109, vcc, 0, v5, vcc
	v_add_co_u32_e32 v110, vcc, s39, v4
	v_lshlrev_b64 v[54:55], 12, v[54:55]
	s_nop 0
	v_addc_co_u32_e32 v111, vcc, 0, v5, vcc
	v_add_co_u32_e32 v112, vcc, s42, v4
	v_lshlrev_b64 v[56:57], 12, v[56:57]
	s_nop 0
	v_addc_co_u32_e32 v113, vcc, 0, v5, vcc
	v_add_co_u32_e32 v114, vcc, s43, v4
	v_lshl_add_u64 v[120:121], s[12:13], 0, v[2:3]
	s_nop 0
	v_addc_co_u32_e32 v115, vcc, 0, v5, vcc
	v_add_co_u32_e32 v116, vcc, s44, v4
	v_lshl_add_u64 v[122:123], v[120:121], 0, v[42:43]
	s_nop 0
	v_addc_co_u32_e32 v117, vcc, 0, v5, vcc
	v_add_co_u32_e32 v118, vcc, s45, v4
	v_lshl_add_u64 v[124:125], v[120:121], 0, v[44:45]
	s_nop 0
	v_addc_co_u32_e32 v119, vcc, 0, v5, vcc
	global_load_dwordx2 v[4:5], v[4:5], off nt
	s_nop 0
	global_load_dwordx2 v[58:59], v[58:59], off nt
	s_nop 0
	global_load_dwordx2 v[60:61], v[60:61], off nt
	s_nop 0
	global_load_dwordx2 v[62:63], v[62:63], off nt
	s_nop 0
	global_load_dwordx2 v[64:65], v[64:65], off nt
	s_nop 0
	global_load_dwordx2 v[66:67], v[66:67], off nt
	s_nop 0
	global_load_dwordx2 v[68:69], v[68:69], off nt
	s_nop 0
	global_load_dwordx2 v[70:71], v[70:71], off nt
	s_nop 0
	global_load_dwordx2 v[72:73], v[72:73], off nt
	s_nop 0
	global_load_dwordx2 v[74:75], v[74:75], off nt
	s_nop 0
	global_load_dwordx2 v[76:77], v[76:77], off nt
	s_nop 0
	global_load_dwordx2 v[78:79], v[78:79], off nt
	s_nop 0
	global_load_dwordx2 v[80:81], v[80:81], off nt
	s_nop 0
	global_load_dwordx2 v[82:83], v[82:83], off nt
	s_nop 0
	global_load_dwordx2 v[84:85], v[84:85], off nt
	s_nop 0
	global_load_dwordx2 v[86:87], v[86:87], off nt
	s_nop 0
	global_load_dwordx2 v[88:89], v[88:89], off nt
	s_nop 0
	global_load_dwordx2 v[90:91], v[90:91], off nt
	s_nop 0
	global_load_dwordx2 v[92:93], v[92:93], off nt
	s_nop 0
	global_load_dwordx2 v[94:95], v[94:95], off nt
	s_nop 0
	global_load_dwordx2 v[96:97], v[96:97], off nt
	s_nop 0
	global_load_dwordx2 v[98:99], v[98:99], off nt
	s_nop 0
	global_load_dwordx2 v[100:101], v[100:101], off nt
	s_nop 0
	global_load_dwordx2 v[102:103], v[102:103], off nt
	s_nop 0
	global_load_dwordx2 v[104:105], v[104:105], off nt
	s_nop 0
	global_load_dwordx2 v[106:107], v[106:107], off nt
	s_nop 0
	global_load_dwordx2 v[108:109], v[108:109], off nt
	s_nop 0
	global_load_dwordx2 v[110:111], v[110:111], off nt
	s_nop 0
	global_load_dwordx2 v[112:113], v[112:113], off nt
	s_nop 0
	global_load_dwordx2 v[114:115], v[114:115], off nt
	s_nop 0
	global_load_dwordx2 v[116:117], v[116:117], off nt
	s_nop 0
	global_load_dwordx2 v[118:119], v[118:119], off nt
	s_waitcnt vmcnt(0)
	ds_write2_b32 v9, v4, v5 offset1:1
	ds_write2_b32 v9, v58, v59 offset0:130 offset1:131
	ds_write2_b32 v10, v60, v61 offset1:1
	ds_write2_b32 v11, v62, v63 offset1:1
	ds_write2_b32 v12, v64, v65 offset1:1
	ds_write2_b32 v13, v66, v67 offset1:1
	ds_write2_b32 v14, v68, v69 offset1:1
	ds_write2_b32 v15, v70, v71 offset1:1
	ds_write2_b32 v16, v72, v73 offset1:1
	ds_write2_b32 v17, v74, v75 offset1:1
	ds_write2_b32 v18, v76, v77 offset1:1
	ds_write2_b32 v19, v78, v79 offset1:1
	ds_write2_b32 v20, v80, v81 offset1:1
	ds_write2_b32 v21, v82, v83 offset1:1
	ds_write2_b32 v22, v84, v85 offset1:1
	ds_write2_b32 v23, v86, v87 offset1:1
	ds_write2_b32 v24, v88, v89 offset1:1
	ds_write2_b32 v25, v90, v91 offset1:1
	ds_write2_b32 v26, v92, v93 offset1:1
	ds_write2_b32 v27, v94, v95 offset1:1
	ds_write2_b32 v28, v96, v97 offset1:1
	ds_write2_b32 v29, v98, v99 offset1:1
	ds_write2_b32 v30, v100, v101 offset1:1
	ds_write2_b32 v31, v102, v103 offset1:1
	ds_write2_b32 v32, v104, v105 offset1:1
	ds_write2_b32 v33, v106, v107 offset1:1
	ds_write2_b32 v34, v108, v109 offset1:1
	ds_write2_b32 v35, v110, v111 offset1:1
	ds_write2_b32 v36, v112, v113 offset1:1
	ds_write2_b32 v37, v114, v115 offset1:1
	ds_write2_b32 v38, v116, v117 offset1:1
	ds_write2_b32 v39, v118, v119 offset1:1
	s_waitcnt lgkmcnt(0)
	v_lshl_add_u64 v[126:127], v[120:121], 0, v[46:47]
	v_lshl_add_u64 v[128:129], v[120:121], 0, v[48:49]
	v_lshl_add_u64 v[130:131], v[120:121], 0, v[50:51]
	v_lshl_add_u64 v[132:133], v[120:121], 0, v[52:53]
	v_lshl_add_u64 v[134:135], v[120:121], 0, v[54:55]
	v_lshl_add_u64 v[120:121], v[120:121], 0, v[56:57]
	ds_read2_b32 v[4:5], v8 offset0:65 offset1:73
	ds_read2_b32 v[46:47], v8 offset1:8
	ds_read2_b32 v[48:49], v8 offset0:130 offset1:138
	ds_read2_b32 v[50:51], v8 offset0:195 offset1:203
	ds_read2_b32 v[52:53], v40 offset0:4 offset1:12
	ds_read2_b32 v[54:55], v40 offset0:69 offset1:77
	ds_read2_b32 v[56:57], v40 offset0:134 offset1:142
	ds_read2_b32 v[58:59], v40 offset0:199 offset1:207
	ds_read2_b32 v[60:61], v8 offset0:81 offset1:89
	ds_read2_b32 v[62:63], v8 offset0:16 offset1:24
	ds_read2_b32 v[64:65], v8 offset0:146 offset1:154
	ds_read2_b32 v[66:67], v8 offset0:211 offset1:219
	ds_read2_b32 v[68:69], v40 offset0:20 offset1:28
	ds_read2_b32 v[70:71], v40 offset0:85 offset1:93
	ds_read2_b32 v[72:73], v40 offset0:150 offset1:158
	ds_read2_b32 v[74:75], v40 offset0:215 offset1:223
	ds_read2_b32 v[76:77], v8 offset0:32 offset1:40
	ds_read2_b32 v[78:79], v8 offset0:97 offset1:105
	ds_read2_b32 v[80:81], v8 offset0:162 offset1:170
	ds_read2_b32 v[82:83], v8 offset0:227 offset1:235
	ds_read2_b32 v[84:85], v40 offset0:36 offset1:44
	ds_read2_b32 v[86:87], v40 offset0:101 offset1:109
	ds_read2_b32 v[88:89], v40 offset0:166 offset1:174
	ds_read2_b32 v[90:91], v40 offset0:231 offset1:239
	ds_read2_b32 v[92:93], v8 offset0:48 offset1:56
	ds_read2_b32 v[94:95], v8 offset0:113 offset1:121
	ds_read2_b32 v[96:97], v8 offset0:178 offset1:186
	ds_read2_b32 v[98:99], v8 offset0:243 offset1:251
	ds_read2_b32 v[100:101], v40 offset0:52 offset1:60
	ds_read2_b32 v[102:103], v40 offset0:117 offset1:125
	ds_read2_b32 v[104:105], v40 offset0:182 offset1:190
	ds_read2_b32 v[106:107], v40 offset0:247 offset1:255
	s_waitcnt lgkmcnt(14)
	v_cvt_pk_bf16_f32 v42, v46, v4
	v_cvt_pk_bf16_f32 v43, v48, v50
	v_cvt_pk_bf16_f32 v44, v52, v54
	v_cvt_pk_bf16_f32 v45, v56, v58
	v_cvt_pk_bf16_f32 v46, v47, v5
	v_cvt_pk_bf16_f32 v47, v49, v51
	v_cvt_pk_bf16_f32 v48, v53, v55
	v_cvt_pk_bf16_f32 v49, v57, v59
	v_cvt_pk_bf16_f32 v50, v62, v60
	v_cvt_pk_bf16_f32 v51, v64, v66
	v_cvt_pk_bf16_f32 v52, v68, v70
	v_cvt_pk_bf16_f32 v53, v72, v74
	v_cvt_pk_bf16_f32 v54, v63, v61
	v_cvt_pk_bf16_f32 v55, v65, v67
	v_cvt_pk_bf16_f32 v56, v69, v71
	v_cvt_pk_bf16_f32 v57, v73, v75
	v_cvt_pk_bf16_f32 v58, v76, v78
	s_waitcnt lgkmcnt(12)
	v_cvt_pk_bf16_f32 v59, v80, v82
	s_waitcnt lgkmcnt(10)
	v_cvt_pk_bf16_f32 v60, v84, v86
	s_waitcnt lgkmcnt(8)
	v_cvt_pk_bf16_f32 v61, v88, v90
	v_cvt_pk_bf16_f32 v62, v77, v79
	v_cvt_pk_bf16_f32 v63, v81, v83
	v_cvt_pk_bf16_f32 v64, v85, v87
	v_cvt_pk_bf16_f32 v65, v89, v91
	s_waitcnt lgkmcnt(6)
	v_cvt_pk_bf16_f32 v66, v92, v94
	s_waitcnt lgkmcnt(4)
	v_cvt_pk_bf16_f32 v67, v96, v98
	s_waitcnt lgkmcnt(2)
	v_cvt_pk_bf16_f32 v68, v100, v102
	s_waitcnt lgkmcnt(0)
	v_cvt_pk_bf16_f32 v69, v104, v106
	v_cvt_pk_bf16_f32 v70, v93, v95
	v_cvt_pk_bf16_f32 v71, v97, v99
	v_cvt_pk_bf16_f32 v72, v101, v103
	v_cvt_pk_bf16_f32 v73, v105, v107
	global_store_dwordx4 v[122:123], v[42:45], off nt
	global_store_dwordx4 v[124:125], v[46:49], off nt
	global_store_dwordx4 v[126:127], v[50:53], off nt
	global_store_dwordx4 v[128:129], v[54:57], off nt
	global_store_dwordx4 v[130:131], v[58:61], off nt
	global_store_dwordx4 v[132:133], v[62:65], off nt
	global_store_dwordx4 v[134:135], v[66:69], off nt
	global_store_dwordx4 v[120:121], v[70:73], off nt
	s_waitcnt lgkmcnt(0)
	s_add_i32 s12, s0, 0x100
	s_cmpk_lt_i32 s0, 0x700
	s_mov_b32 s0, s12
	s_cbranch_scc1 .LBB0_259

.LBB0_796:
	s_cmpk_gt_i32 s49, 0xff
	s_mov_b64 s[12:13], -1
	s_cbranch_scc0 .LBB0_806
	s_cmpk_gt_u32 s49, 0x1ff
	s_cbranch_scc0 .LBB0_803
	s_cmpk_gt_u32 s49, 0x3ff
	s_cbranch_scc0 .LBB0_800
	s_load_dwordx2 s[50:51], s[76:77], 0x90
	s_load_dwordx2 s[12:13], s[76:77], 0xf0
	s_and_b32 s10, s4, 0x7fffffc0
	s_addk_i32 s10, 0xf800
	s_and_b32 s14, s0, 0x7c0
	s_lshl_b64 s[52:53], s[10:11], 2
	v_add_u32_e32 v48, s14, v6
	s_waitcnt lgkmcnt(0)
	s_add_u32 s50, s50, s52
	s_addc_u32 s51, s51, s53
	v_ashrrev_i32_e32 v49, 31, v48
	v_lshl_add_u64 v[50:51], s[50:51], 0, v[0:1]
	v_lshlrev_b64 v[48:49], 13, v[48:49]
	v_lshl_add_u64 v[48:49], v[50:51], 0, v[48:49]
	v_add_co_u32_e32 v50, vcc, s16, v48
	s_lshl_b32 s14, s14, 1
	s_nop 0
	v_addc_co_u32_e32 v51, vcc, 0, v49, vcc
	v_add_co_u32_e32 v52, vcc, s17, v48
	s_add_u32 s12, s12, s14
	s_nop 0
	v_addc_co_u32_e32 v53, vcc, 0, v49, vcc
	v_add_co_u32_e32 v54, vcc, s18, v48
	s_addc_u32 s13, s13, 0
	s_nop 0
	v_addc_co_u32_e32 v55, vcc, 0, v49, vcc
	v_add_co_u32_e32 v58, vcc, s19, v48
	global_load_dwordx2 v[56:57], v[48:49], off nt
	s_nop 0
	global_load_dwordx2 v[50:51], v[50:51], off nt
	s_nop 0
	global_load_dwordx2 v[52:53], v[52:53], off nt
	s_nop 0
	global_load_dwordx2 v[54:55], v[54:55], off nt
	v_addc_co_u32_e32 v59, vcc, 0, v49, vcc
	v_add_co_u32_e32 v60, vcc, s20, v48
	v_mov_b32_e32 v5, v1
	s_nop 0
	v_addc_co_u32_e32 v61, vcc, 0, v49, vcc
	v_add_co_u32_e32 v62, vcc, s21, v48
	s_nop 1
	v_addc_co_u32_e32 v63, vcc, 0, v49, vcc
	v_add_co_u32_e32 v64, vcc, s22, v48
	s_nop 1
	v_addc_co_u32_e32 v65, vcc, 0, v49, vcc
	v_add_co_u32_e32 v66, vcc, s23, v48
	global_load_dwordx2 v[58:59], v[58:59], off nt
	s_nop 0
	global_load_dwordx2 v[60:61], v[60:61], off nt
	s_nop 0
	global_load_dwordx2 v[62:63], v[62:63], off nt
	s_nop 0
	global_load_dwordx2 v[64:65], v[64:65], off nt
	v_addc_co_u32_e32 v67, vcc, 0, v49, vcc
	v_add_co_u32_e32 v68, vcc, s24, v48
	s_nop 1
	v_addc_co_u32_e32 v69, vcc, 0, v49, vcc
	v_add_co_u32_e32 v70, vcc, s25, v48
	s_nop 1
	v_addc_co_u32_e32 v71, vcc, 0, v49, vcc
	v_add_co_u32_e32 v72, vcc, s26, v48
	s_nop 1
	v_addc_co_u32_e32 v73, vcc, 0, v49, vcc
	v_add_co_u32_e32 v74, vcc, s27, v48
	global_load_dwordx2 v[66:67], v[66:67], off nt
	s_nop 0
	global_load_dwordx2 v[68:69], v[68:69], off nt
	s_nop 0
	global_load_dwordx2 v[70:71], v[70:71], off nt
	s_nop 0
	global_load_dwordx2 v[72:73], v[72:73], off nt
	v_addc_co_u32_e32 v75, vcc, 0, v49, vcc
	v_add_co_u32_e32 v76, vcc, s28, v48
	s_nop 1
	v_addc_co_u32_e32 v77, vcc, 0, v49, vcc
	v_add_co_u32_e32 v78, vcc, s29, v48
	s_nop 1
	v_addc_co_u32_e32 v79, vcc, 0, v49, vcc
	v_add_co_u32_e32 v80, vcc, s30, v48
	s_nop 1
	v_addc_co_u32_e32 v81, vcc, 0, v49, vcc
	v_add_co_u32_e32 v82, vcc, s31, v48
	global_load_dwordx2 v[74:75], v[74:75], off nt
	s_nop 0
	global_load_dwordx2 v[76:77], v[76:77], off nt
	s_nop 0
	global_load_dwordx2 v[78:79], v[78:79], off nt
	s_nop 0
	global_load_dwordx2 v[80:81], v[80:81], off nt
	v_addc_co_u32_e32 v83, vcc, 0, v49, vcc
	v_add_co_u32_e32 v84, vcc, s34, v48
	s_nop 1
	v_addc_co_u32_e32 v85, vcc, 0, v49, vcc
	v_add_co_u32_e32 v86, vcc, s35, v48
	s_nop 1
	v_addc_co_u32_e32 v87, vcc, 0, v49, vcc
	v_add_co_u32_e32 v88, vcc, s36, v48
	s_nop 1
	v_addc_co_u32_e32 v89, vcc, 0, v49, vcc
	v_add_co_u32_e32 v90, vcc, s37, v48
	global_load_dwordx2 v[82:83], v[82:83], off nt
	s_nop 0
	global_load_dwordx2 v[84:85], v[84:85], off nt
	s_nop 0
	global_load_dwordx2 v[86:87], v[86:87], off nt
	s_nop 0
	global_load_dwordx2 v[88:89], v[88:89], off nt
	v_addc_co_u32_e32 v91, vcc, 0, v49, vcc
	v_add_co_u32_e32 v92, vcc, s38, v48
	s_nop 1
	v_addc_co_u32_e32 v93, vcc, 0, v49, vcc
	v_add_co_u32_e32 v94, vcc, s39, v48
	s_nop 1
	v_addc_co_u32_e32 v95, vcc, 0, v49, vcc
	v_add_co_u32_e32 v96, vcc, s40, v48
	s_nop 1
	v_addc_co_u32_e32 v97, vcc, 0, v49, vcc
	v_add_co_u32_e32 v98, vcc, s41, v48
	global_load_dwordx2 v[90:91], v[90:91], off nt
	s_nop 0
	global_load_dwordx2 v[92:93], v[92:93], off nt
	s_nop 0
	global_load_dwordx2 v[94:95], v[94:95], off nt
	s_nop 0
	global_load_dwordx2 v[96:97], v[96:97], off nt
	v_addc_co_u32_e32 v99, vcc, 0, v49, vcc
	v_add_co_u32_e32 v100, vcc, s42, v48
	s_nop 1
	v_addc_co_u32_e32 v101, vcc, 0, v49, vcc
	v_add_co_u32_e32 v102, vcc, s43, v48
	s_nop 1
	v_addc_co_u32_e32 v103, vcc, 0, v49, vcc
	v_add_co_u32_e32 v104, vcc, s44, v48
	s_nop 1
	v_addc_co_u32_e32 v105, vcc, 0, v49, vcc
	v_add_co_u32_e32 v106, vcc, s45, v48
	global_load_dwordx2 v[98:99], v[98:99], off nt
	s_nop 0
	global_load_dwordx2 v[100:101], v[100:101], off nt
	s_nop 0
	global_load_dwordx2 v[102:103], v[102:103], off nt
	s_nop 0
	global_load_dwordx2 v[104:105], v[104:105], off nt
	v_addc_co_u32_e32 v107, vcc, 0, v49, vcc
	v_add_co_u32_e32 v110, vcc, s46, v48
	s_nop 1
	v_addc_co_u32_e32 v111, vcc, 0, v49, vcc
	v_add_co_u32_e32 v112, vcc, s47, v48
	s_nop 1
	v_addc_co_u32_e32 v113, vcc, 0, v49, vcc
	v_add_co_u32_e32 v48, vcc, s48, v48
	s_nop 1
	v_addc_co_u32_e32 v49, vcc, 0, v49, vcc
	global_load_dwordx2 v[106:107], v[106:107], off nt
	s_nop 0
	global_load_dwordx2 v[110:111], v[110:111], off nt
	s_nop 0
	global_load_dwordx2 v[112:113], v[112:113], off nt
	s_nop 0
	global_load_dwordx2 v[48:49], v[48:49], off nt
	s_waitcnt vmcnt(0)
	ds_write2_b32 v7, v56, v57 offset1:1
	ds_write2_b32 v7, v50, v51 offset0:130 offset1:131
	ds_write2_b32 v17, v52, v53 offset1:1
	ds_write2_b32 v18, v54, v55 offset1:1
	ds_write2_b32 v19, v58, v59 offset1:1
	ds_write2_b32 v20, v60, v61 offset1:1
	ds_write2_b32 v21, v62, v63 offset1:1
	ds_write2_b32 v22, v64, v65 offset1:1
	ds_write2_b32 v23, v66, v67 offset1:1
	ds_write2_b32 v24, v68, v69 offset1:1
	ds_write2_b32 v25, v70, v71 offset1:1
	ds_write2_b32 v26, v72, v73 offset1:1
	ds_write2_b32 v27, v74, v75 offset1:1
	ds_write2_b32 v28, v76, v77 offset1:1
	ds_write2_b32 v29, v78, v79 offset1:1
	ds_write2_b32 v30, v80, v81 offset1:1
	ds_write2_b32 v31, v82, v83 offset1:1
	ds_write2_b32 v32, v84, v85 offset1:1
	ds_write2_b32 v33, v86, v87 offset1:1
	ds_write2_b32 v34, v88, v89 offset1:1
	ds_write2_b32 v35, v90, v91 offset1:1
	ds_write2_b32 v36, v92, v93 offset1:1
	ds_write2_b32 v37, v94, v95 offset1:1
	ds_write2_b32 v38, v96, v97 offset1:1
	ds_write2_b32 v39, v98, v99 offset1:1
	ds_write2_b32 v40, v100, v101 offset1:1
	ds_write2_b32 v41, v102, v103 offset1:1
	ds_write2_b32 v42, v104, v105 offset1:1
	ds_write2_b32 v43, v106, v107 offset1:1
	ds_write2_b32 v44, v110, v111 offset1:1
	ds_write2_b32 v45, v112, v113 offset1:1
	ds_write2_b32 v46, v48, v49 offset1:1
	s_waitcnt lgkmcnt(0)
	ds_read2_b32 v[52:53], v9 offset0:65 offset1:73
	ds_read2_b32 v[54:55], v9 offset1:8
	ds_read2_b32 v[56:57], v9 offset0:130 offset1:138
	ds_read2_b32 v[58:59], v9 offset0:195 offset1:203
	ds_read2_b32 v[60:61], v47 offset0:4 offset1:12
	ds_read2_b32 v[62:63], v47 offset0:69 offset1:77
	ds_read2_b32 v[64:65], v47 offset0:134 offset1:142
	ds_read2_b32 v[66:67], v47 offset0:199 offset1:207
	v_add_u32_e32 v70, s10, v8
	v_ashrrev_i32_e32 v71, 31, v70
	v_lshl_add_u64 v[68:69], s[12:13], 0, v[4:5]
	v_lshlrev_b64 v[70:71], 12, v[70:71]
	s_waitcnt lgkmcnt(6)
	v_cvt_pk_bf16_f32 v48, v54, v52
	s_waitcnt lgkmcnt(4)
	v_cvt_pk_bf16_f32 v49, v56, v58
	s_waitcnt lgkmcnt(2)
	v_cvt_pk_bf16_f32 v50, v60, v62
	s_waitcnt lgkmcnt(0)
	v_cvt_pk_bf16_f32 v51, v64, v66
	v_lshl_add_u64 v[70:71], v[68:69], 0, v[70:71]
	v_add_u32_e32 v52, s10, v10
	global_store_dwordx4 v[70:71], v[48:51], off
	s_mov_b64 s[12:13], 0
	s_nop 0
	v_cvt_pk_bf16_f32 v48, v55, v53
	v_ashrrev_i32_e32 v53, 31, v52
	v_cvt_pk_bf16_f32 v49, v57, v59
	v_cvt_pk_bf16_f32 v50, v61, v63
	v_cvt_pk_bf16_f32 v51, v65, v67
	v_lshlrev_b64 v[52:53], 12, v[52:53]
	ds_read2_b32 v[54:55], v9 offset0:81 offset1:89
	ds_read2_b32 v[56:57], v9 offset0:16 offset1:24
	ds_read2_b32 v[58:59], v9 offset0:146 offset1:154
	ds_read2_b32 v[60:61], v9 offset0:211 offset1:219
	ds_read2_b32 v[62:63], v47 offset0:20 offset1:28
	ds_read2_b32 v[64:65], v47 offset0:85 offset1:93
	ds_read2_b32 v[66:67], v47 offset0:150 offset1:158
	ds_read2_b32 v[70:71], v47 offset0:215 offset1:223
	v_lshl_add_u64 v[52:53], v[68:69], 0, v[52:53]
	global_store_dwordx4 v[52:53], v[48:51], off
	v_add_u32_e32 v52, s10, v11
	v_ashrrev_i32_e32 v53, 31, v52
	v_lshlrev_b64 v[52:53], 12, v[52:53]
	s_waitcnt lgkmcnt(6)
	v_cvt_pk_bf16_f32 v48, v56, v54
	s_waitcnt lgkmcnt(4)
	v_cvt_pk_bf16_f32 v49, v58, v60
	s_waitcnt lgkmcnt(2)
	v_cvt_pk_bf16_f32 v50, v62, v64
	s_waitcnt lgkmcnt(0)
	v_cvt_pk_bf16_f32 v51, v66, v70
	v_lshl_add_u64 v[52:53], v[68:69], 0, v[52:53]
	global_store_dwordx4 v[52:53], v[48:51], off
	v_add_u32_e32 v52, s10, v12
	v_ashrrev_i32_e32 v53, 31, v52
	v_cvt_pk_bf16_f32 v48, v57, v55
	v_cvt_pk_bf16_f32 v49, v59, v61
	v_cvt_pk_bf16_f32 v50, v63, v65
	v_cvt_pk_bf16_f32 v51, v67, v71
	v_lshlrev_b64 v[52:53], 12, v[52:53]
	ds_read2_b32 v[54:55], v9 offset0:32 offset1:40
	ds_read2_b32 v[56:57], v9 offset0:97 offset1:105
	ds_read2_b32 v[58:59], v9 offset0:162 offset1:170
	ds_read2_b32 v[60:61], v9 offset0:227 offset1:235
	ds_read2_b32 v[62:63], v47 offset0:36 offset1:44
	ds_read2_b32 v[64:65], v47 offset0:101 offset1:109
	ds_read2_b32 v[66:67], v47 offset0:166 offset1:174
	ds_read2_b32 v[70:71], v47 offset0:231 offset1:239
	v_lshl_add_u64 v[52:53], v[68:69], 0, v[52:53]
	global_store_dwordx4 v[52:53], v[48:51], off
	v_add_u32_e32 v52, s10, v13
	v_ashrrev_i32_e32 v53, 31, v52
	v_lshlrev_b64 v[52:53], 12, v[52:53]
	s_waitcnt lgkmcnt(6)
	v_cvt_pk_bf16_f32 v48, v54, v56
	s_waitcnt lgkmcnt(4)
	v_cvt_pk_bf16_f32 v49, v58, v60
	s_waitcnt lgkmcnt(2)
	v_cvt_pk_bf16_f32 v50, v62, v64
	s_waitcnt lgkmcnt(0)
	v_cvt_pk_bf16_f32 v51, v66, v70
	v_lshl_add_u64 v[52:53], v[68:69], 0, v[52:53]
	global_store_dwordx4 v[52:53], v[48:51], off
	v_add_u32_e32 v52, s10, v14
	v_ashrrev_i32_e32 v53, 31, v52
	v_cvt_pk_bf16_f32 v48, v55, v57
	v_cvt_pk_bf16_f32 v49, v59, v61
	v_cvt_pk_bf16_f32 v50, v63, v65
	v_cvt_pk_bf16_f32 v51, v67, v71
	v_lshlrev_b64 v[52:53], 12, v[52:53]
	ds_read2_b32 v[54:55], v9 offset0:48 offset1:56
	ds_read2_b32 v[56:57], v9 offset0:113 offset1:121
	ds_read2_b32 v[58:59], v9 offset0:178 offset1:186
	ds_read2_b32 v[60:61], v9 offset0:243 offset1:251
	ds_read2_b32 v[62:63], v47 offset0:52 offset1:60
	ds_read2_b32 v[64:65], v47 offset0:117 offset1:125
	ds_read2_b32 v[66:67], v47 offset0:182 offset1:190
	ds_read2_b32 v[70:71], v47 offset0:247 offset1:255
	v_lshl_add_u64 v[52:53], v[68:69], 0, v[52:53]
	global_store_dwordx4 v[52:53], v[48:51], off
	v_add_u32_e32 v52, s10, v15
	v_ashrrev_i32_e32 v53, 31, v52
	v_lshlrev_b64 v[52:53], 12, v[52:53]
	s_waitcnt lgkmcnt(6)
	v_cvt_pk_bf16_f32 v48, v54, v56
	s_waitcnt lgkmcnt(4)
	v_cvt_pk_bf16_f32 v49, v58, v60
	s_waitcnt lgkmcnt(2)
	v_cvt_pk_bf16_f32 v50, v62, v64
	s_waitcnt lgkmcnt(0)
	v_cvt_pk_bf16_f32 v51, v66, v70
	v_lshl_add_u64 v[52:53], v[68:69], 0, v[52:53]
	global_store_dwordx4 v[52:53], v[48:51], off
	v_add_u32_e32 v52, s10, v16
	v_ashrrev_i32_e32 v53, 31, v52
	v_lshlrev_b64 v[52:53], 12, v[52:53]
	v_cvt_pk_bf16_f32 v48, v55, v57
	v_cvt_pk_bf16_f32 v49, v59, v61
	v_cvt_pk_bf16_f32 v50, v63, v65
	v_cvt_pk_bf16_f32 v51, v67, v71
	v_lshl_add_u64 v[52:53], v[68:69], 0, v[52:53]
	global_store_dwordx4 v[52:53], v[48:51], off
	s_waitcnt lgkmcnt(0)
.LBB0_800:
	s_andn2_b64 vcc, exec, s[12:13]
	s_cbranch_vccnz .LBB0_802
	s_load_dwordx2 s[14:15], s[76:77], 0x88
	s_and_b32 s10, s6, 0xfc0
	s_addk_i32 s10, 0xf800
	s_and_b32 s12, s0, 0x3c0
	s_lshl_b64 s[50:51], s[10:11], 2
	v_add_u32_e32 v48, s12, v6
	s_waitcnt lgkmcnt(0)
	s_add_u32 s14, s14, s50
	s_addc_u32 s15, s15, s51
	v_ashrrev_i32_e32 v49, 31, v48
	v_lshl_add_u64 v[50:51], s[14:15], 0, v[0:1]
	v_lshlrev_b64 v[48:49], 13, v[48:49]
	v_lshl_add_u64 v[48:49], v[50:51], 0, v[48:49]
	v_add_co_u32_e32 v50, vcc, s16, v48
	s_lshl_b32 s12, s12, 1
	s_nop 0
	v_addc_co_u32_e32 v51, vcc, 0, v49, vcc
	v_add_co_u32_e32 v52, vcc, s17, v48
	s_mov_b32 s13, s11
	s_nop 0
	v_addc_co_u32_e32 v53, vcc, 0, v49, vcc
	v_add_co_u32_e32 v54, vcc, s18, v48
	s_nop 1
	v_addc_co_u32_e32 v55, vcc, 0, v49, vcc
	v_add_co_u32_e32 v58, vcc, s19, v48
	global_load_dwordx2 v[56:57], v[48:49], off nt
	s_nop 0
	global_load_dwordx2 v[50:51], v[50:51], off nt
	s_nop 0
	global_load_dwordx2 v[52:53], v[52:53], off nt
	s_nop 0
	global_load_dwordx2 v[54:55], v[54:55], off nt
	v_addc_co_u32_e32 v59, vcc, 0, v49, vcc
	v_add_co_u32_e32 v60, vcc, s20, v48
	s_nop 1
	v_addc_co_u32_e32 v61, vcc, 0, v49, vcc
	v_add_co_u32_e32 v62, vcc, s21, v48
	s_nop 1
	v_addc_co_u32_e32 v63, vcc, 0, v49, vcc
	v_add_co_u32_e32 v64, vcc, s22, v48
	s_nop 1
	v_addc_co_u32_e32 v65, vcc, 0, v49, vcc
	v_add_co_u32_e32 v66, vcc, s23, v48
	global_load_dwordx2 v[58:59], v[58:59], off nt
	s_nop 0
	global_load_dwordx2 v[60:61], v[60:61], off nt
	s_nop 0
	global_load_dwordx2 v[62:63], v[62:63], off nt
	s_nop 0
	global_load_dwordx2 v[64:65], v[64:65], off nt
	v_addc_co_u32_e32 v67, vcc, 0, v49, vcc
	v_add_co_u32_e32 v68, vcc, s24, v48
	s_nop 1
	v_addc_co_u32_e32 v69, vcc, 0, v49, vcc
	v_add_co_u32_e32 v70, vcc, s25, v48
	s_nop 1
	v_addc_co_u32_e32 v71, vcc, 0, v49, vcc
	v_add_co_u32_e32 v72, vcc, s26, v48
	s_nop 1
	v_addc_co_u32_e32 v73, vcc, 0, v49, vcc
	v_add_co_u32_e32 v74, vcc, s27, v48
	global_load_dwordx2 v[66:67], v[66:67], off nt
	s_nop 0
	global_load_dwordx2 v[68:69], v[68:69], off nt
	s_nop 0
	global_load_dwordx2 v[70:71], v[70:71], off nt
	s_nop 0
	global_load_dwordx2 v[72:73], v[72:73], off nt
	v_addc_co_u32_e32 v75, vcc, 0, v49, vcc
	v_add_co_u32_e32 v76, vcc, s28, v48
	s_nop 1
	v_addc_co_u32_e32 v77, vcc, 0, v49, vcc
	v_add_co_u32_e32 v78, vcc, s29, v48
	s_nop 1
	v_addc_co_u32_e32 v79, vcc, 0, v49, vcc
	v_add_co_u32_e32 v80, vcc, s30, v48
	s_nop 1
	v_addc_co_u32_e32 v81, vcc, 0, v49, vcc
	v_add_co_u32_e32 v82, vcc, s31, v48
	global_load_dwordx2 v[74:75], v[74:75], off nt
	s_nop 0
	global_load_dwordx2 v[76:77], v[76:77], off nt
	s_nop 0
	global_load_dwordx2 v[78:79], v[78:79], off nt
	s_nop 0
	global_load_dwordx2 v[80:81], v[80:81], off nt
	v_addc_co_u32_e32 v83, vcc, 0, v49, vcc
	v_add_co_u32_e32 v84, vcc, s34, v48
	s_nop 1
	v_addc_co_u32_e32 v85, vcc, 0, v49, vcc
	v_add_co_u32_e32 v86, vcc, s35, v48
	s_nop 1
	v_addc_co_u32_e32 v87, vcc, 0, v49, vcc
	v_add_co_u32_e32 v88, vcc, s36, v48
	s_nop 1
	v_addc_co_u32_e32 v89, vcc, 0, v49, vcc
	v_add_co_u32_e32 v90, vcc, s37, v48
	global_load_dwordx2 v[82:83], v[82:83], off nt
	s_nop 0
	global_load_dwordx2 v[84:85], v[84:85], off nt
	s_nop 0
	global_load_dwordx2 v[86:87], v[86:87], off nt
	s_nop 0
	global_load_dwordx2 v[88:89], v[88:89], off nt
	v_addc_co_u32_e32 v91, vcc, 0, v49, vcc
	v_add_co_u32_e32 v92, vcc, s38, v48
	s_nop 1
	v_addc_co_u32_e32 v93, vcc, 0, v49, vcc
	v_add_co_u32_e32 v94, vcc, s39, v48
	s_nop 1
	v_addc_co_u32_e32 v95, vcc, 0, v49, vcc
	v_add_co_u32_e32 v96, vcc, s40, v48
	s_nop 1
	v_addc_co_u32_e32 v97, vcc, 0, v49, vcc
	v_add_co_u32_e32 v98, vcc, s41, v48
	global_load_dwordx2 v[90:91], v[90:91], off nt
	s_nop 0
	global_load_dwordx2 v[92:93], v[92:93], off nt
	s_nop 0
	global_load_dwordx2 v[94:95], v[94:95], off nt
	s_nop 0
	global_load_dwordx2 v[96:97], v[96:97], off nt
	v_addc_co_u32_e32 v99, vcc, 0, v49, vcc
	v_add_co_u32_e32 v100, vcc, s42, v48
	s_nop 1
	v_addc_co_u32_e32 v101, vcc, 0, v49, vcc
	v_add_co_u32_e32 v102, vcc, s43, v48
	s_nop 1
	v_addc_co_u32_e32 v103, vcc, 0, v49, vcc
	v_add_co_u32_e32 v104, vcc, s44, v48
	s_nop 1
	v_addc_co_u32_e32 v105, vcc, 0, v49, vcc
	v_add_co_u32_e32 v106, vcc, s45, v48
	global_load_dwordx2 v[98:99], v[98:99], off nt
	s_nop 0
	global_load_dwordx2 v[100:101], v[100:101], off nt
	s_nop 0
	global_load_dwordx2 v[102:103], v[102:103], off nt
	s_nop 0
	global_load_dwordx2 v[104:105], v[104:105], off nt
	v_addc_co_u32_e32 v107, vcc, 0, v49, vcc
	v_add_co_u32_e32 v110, vcc, s46, v48
	s_nop 1
	v_addc_co_u32_e32 v111, vcc, 0, v49, vcc
	v_add_co_u32_e32 v112, vcc, s47, v48
	s_nop 1
	v_addc_co_u32_e32 v113, vcc, 0, v49, vcc
	v_add_co_u32_e32 v48, vcc, s48, v48
	s_nop 1
	v_addc_co_u32_e32 v49, vcc, 0, v49, vcc
	global_load_dwordx2 v[106:107], v[106:107], off nt
	s_nop 0
	global_load_dwordx2 v[110:111], v[110:111], off nt
	s_nop 0
	global_load_dwordx2 v[112:113], v[112:113], off nt
	s_nop 0
	global_load_dwordx2 v[48:49], v[48:49], off nt
	s_waitcnt vmcnt(0)
	ds_write2_b32 v7, v56, v57 offset1:1
	ds_write2_b32 v7, v50, v51 offset0:130 offset1:131
	ds_write2_b32 v17, v52, v53 offset1:1
	ds_write2_b32 v18, v54, v55 offset1:1
	ds_write2_b32 v19, v58, v59 offset1:1
	ds_write2_b32 v20, v60, v61 offset1:1
	ds_write2_b32 v21, v62, v63 offset1:1
	ds_write2_b32 v22, v64, v65 offset1:1
	ds_write2_b32 v23, v66, v67 offset1:1
	ds_write2_b32 v24, v68, v69 offset1:1
	ds_write2_b32 v25, v70, v71 offset1:1
	ds_write2_b32 v26, v72, v73 offset1:1
	ds_write2_b32 v27, v74, v75 offset1:1
	ds_write2_b32 v28, v76, v77 offset1:1
	ds_write2_b32 v29, v78, v79 offset1:1
	ds_write2_b32 v30, v80, v81 offset1:1
	ds_write2_b32 v31, v82, v83 offset1:1
	ds_write2_b32 v32, v84, v85 offset1:1
	ds_write2_b32 v33, v86, v87 offset1:1
	ds_write2_b32 v34, v88, v89 offset1:1
	ds_write2_b32 v35, v90, v91 offset1:1
	ds_write2_b32 v36, v92, v93 offset1:1
	ds_write2_b32 v37, v94, v95 offset1:1
	ds_write2_b32 v38, v96, v97 offset1:1
	ds_write2_b32 v39, v98, v99 offset1:1
	ds_write2_b32 v40, v100, v101 offset1:1
	ds_write2_b32 v41, v102, v103 offset1:1
	ds_write2_b32 v42, v104, v105 offset1:1
	ds_write2_b32 v43, v106, v107 offset1:1
	ds_write2_b32 v44, v110, v111 offset1:1
	ds_write2_b32 v45, v112, v113 offset1:1
	ds_write2_b32 v46, v48, v49 offset1:1
	s_waitcnt lgkmcnt(0)
	ds_read2_b32 v[52:53], v9 offset0:65 offset1:73
	ds_read2_b32 v[54:55], v9 offset1:8
	ds_read2_b32 v[56:57], v9 offset0:130 offset1:138
	ds_read2_b32 v[58:59], v9 offset0:195 offset1:203
	ds_read2_b32 v[60:61], v47 offset0:4 offset1:12
	ds_read2_b32 v[62:63], v47 offset0:69 offset1:77
	ds_read2_b32 v[64:65], v47 offset0:134 offset1:142
	ds_read2_b32 v[66:67], v47 offset0:199 offset1:207
	v_add_u32_e32 v70, s10, v8
	v_ashrrev_i32_e32 v71, 31, v70
	v_lshl_add_u64 v[68:69], v[2:3], 0, s[12:13]
	v_lshlrev_b64 v[70:71], 12, v[70:71]
	s_waitcnt lgkmcnt(6)
	v_cvt_pk_bf16_f32 v48, v54, v52
	s_waitcnt lgkmcnt(4)
	v_cvt_pk_bf16_f32 v49, v56, v58
	s_waitcnt lgkmcnt(2)
	v_cvt_pk_bf16_f32 v50, v60, v62
	s_waitcnt lgkmcnt(0)
	v_cvt_pk_bf16_f32 v51, v64, v66
	v_lshl_add_u64 v[70:71], v[68:69], 0, v[70:71]
	v_add_u32_e32 v52, s10, v10
	global_store_dwordx4 v[70:71], v[48:51], off offset:2048
	s_nop 1
	v_cvt_pk_bf16_f32 v48, v55, v53
	v_ashrrev_i32_e32 v53, 31, v52
	v_cvt_pk_bf16_f32 v49, v57, v59
	v_cvt_pk_bf16_f32 v50, v61, v63
	v_cvt_pk_bf16_f32 v51, v65, v67
	v_lshlrev_b64 v[52:53], 12, v[52:53]
	ds_read2_b32 v[54:55], v9 offset0:81 offset1:89
	ds_read2_b32 v[56:57], v9 offset0:16 offset1:24
	ds_read2_b32 v[58:59], v9 offset0:146 offset1:154
	ds_read2_b32 v[60:61], v9 offset0:211 offset1:219
	ds_read2_b32 v[62:63], v47 offset0:20 offset1:28
	ds_read2_b32 v[64:65], v47 offset0:85 offset1:93
	ds_read2_b32 v[66:67], v47 offset0:150 offset1:158
	ds_read2_b32 v[70:71], v47 offset0:215 offset1:223
	v_lshl_add_u64 v[52:53], v[68:69], 0, v[52:53]
	global_store_dwordx4 v[52:53], v[48:51], off offset:2048
	v_add_u32_e32 v52, s10, v11
	v_ashrrev_i32_e32 v53, 31, v52
	v_lshlrev_b64 v[52:53], 12, v[52:53]
	s_waitcnt lgkmcnt(6)
	v_cvt_pk_bf16_f32 v48, v56, v54
	s_waitcnt lgkmcnt(4)
	v_cvt_pk_bf16_f32 v49, v58, v60
	s_waitcnt lgkmcnt(2)
	v_cvt_pk_bf16_f32 v50, v62, v64
	s_waitcnt lgkmcnt(0)
	v_cvt_pk_bf16_f32 v51, v66, v70
	v_lshl_add_u64 v[52:53], v[68:69], 0, v[52:53]
	global_store_dwordx4 v[52:53], v[48:51], off offset:2048
	v_add_u32_e32 v52, s10, v12
	v_ashrrev_i32_e32 v53, 31, v52
	v_cvt_pk_bf16_f32 v48, v57, v55
	v_cvt_pk_bf16_f32 v49, v59, v61
	v_cvt_pk_bf16_f32 v50, v63, v65
	v_cvt_pk_bf16_f32 v51, v67, v71
	v_lshlrev_b64 v[52:53], 12, v[52:53]
	ds_read2_b32 v[54:55], v9 offset0:32 offset1:40
	ds_read2_b32 v[56:57], v9 offset0:97 offset1:105
	ds_read2_b32 v[58:59], v9 offset0:162 offset1:170
	ds_read2_b32 v[60:61], v9 offset0:227 offset1:235
	ds_read2_b32 v[62:63], v47 offset0:36 offset1:44
	ds_read2_b32 v[64:65], v47 offset0:101 offset1:109
	ds_read2_b32 v[66:67], v47 offset0:166 offset1:174
	ds_read2_b32 v[70:71], v47 offset0:231 offset1:239
	v_lshl_add_u64 v[52:53], v[68:69], 0, v[52:53]
	global_store_dwordx4 v[52:53], v[48:51], off offset:2048
	v_add_u32_e32 v52, s10, v13
	v_ashrrev_i32_e32 v53, 31, v52
	v_lshlrev_b64 v[52:53], 12, v[52:53]
	s_waitcnt lgkmcnt(6)
	v_cvt_pk_bf16_f32 v48, v54, v56
	s_waitcnt lgkmcnt(4)
	v_cvt_pk_bf16_f32 v49, v58, v60
	s_waitcnt lgkmcnt(2)
	v_cvt_pk_bf16_f32 v50, v62, v64
	s_waitcnt lgkmcnt(0)
	v_cvt_pk_bf16_f32 v51, v66, v70
	v_lshl_add_u64 v[52:53], v[68:69], 0, v[52:53]
	global_store_dwordx4 v[52:53], v[48:51], off offset:2048
	v_add_u32_e32 v52, s10, v14
	v_ashrrev_i32_e32 v53, 31, v52
	v_cvt_pk_bf16_f32 v48, v55, v57
	v_cvt_pk_bf16_f32 v49, v59, v61
	v_cvt_pk_bf16_f32 v50, v63, v65
	v_cvt_pk_bf16_f32 v51, v67, v71
	v_lshlrev_b64 v[52:53], 12, v[52:53]
	ds_read2_b32 v[54:55], v9 offset0:48 offset1:56
	ds_read2_b32 v[56:57], v9 offset0:113 offset1:121
	ds_read2_b32 v[58:59], v9 offset0:178 offset1:186
	ds_read2_b32 v[60:61], v9 offset0:243 offset1:251
	ds_read2_b32 v[62:63], v47 offset0:52 offset1:60
	ds_read2_b32 v[64:65], v47 offset0:117 offset1:125
	ds_read2_b32 v[66:67], v47 offset0:182 offset1:190
	ds_read2_b32 v[70:71], v47 offset0:247 offset1:255
	v_lshl_add_u64 v[52:53], v[68:69], 0, v[52:53]
	global_store_dwordx4 v[52:53], v[48:51], off offset:2048
	v_add_u32_e32 v52, s10, v15
	v_ashrrev_i32_e32 v53, 31, v52
	v_lshlrev_b64 v[52:53], 12, v[52:53]
	s_waitcnt lgkmcnt(6)
	v_cvt_pk_bf16_f32 v48, v54, v56
	s_waitcnt lgkmcnt(4)
	v_cvt_pk_bf16_f32 v49, v58, v60
	s_waitcnt lgkmcnt(2)
	v_cvt_pk_bf16_f32 v50, v62, v64
	s_waitcnt lgkmcnt(0)
	v_cvt_pk_bf16_f32 v51, v66, v70
	v_lshl_add_u64 v[52:53], v[68:69], 0, v[52:53]
	global_store_dwordx4 v[52:53], v[48:51], off offset:2048
	v_add_u32_e32 v52, s10, v16
	v_ashrrev_i32_e32 v53, 31, v52
	v_lshlrev_b64 v[52:53], 12, v[52:53]
	v_cvt_pk_bf16_f32 v48, v55, v57
	v_cvt_pk_bf16_f32 v49, v59, v61
	v_cvt_pk_bf16_f32 v50, v63, v65
	v_cvt_pk_bf16_f32 v51, v67, v71
	v_lshl_add_u64 v[52:53], v[68:69], 0, v[52:53]
	global_store_dwordx4 v[52:53], v[48:51], off offset:2048
	s_waitcnt lgkmcnt(0)

.LBB0_803:
	s_andn2_b64 vcc, exec, s[12:13]
	s_cbranch_vccnz .LBB0_805
	s_load_dwordx2 s[14:15], s[76:77], 0x80
	s_and_b32 s10, s8, 0xfc0
	s_addk_i32 s10, 0xf800
	s_and_b32 s12, s0, 0x1c0
	s_lshl_b64 s[50:51], s[10:11], 2
	v_add_u32_e32 v48, s12, v6
	s_waitcnt lgkmcnt(0)
	s_add_u32 s14, s14, s50
	s_addc_u32 s15, s15, s51
	v_ashrrev_i32_e32 v49, 31, v48
	v_lshl_add_u64 v[50:51], s[14:15], 0, v[0:1]
	v_lshlrev_b64 v[48:49], 13, v[48:49]
	v_lshl_add_u64 v[48:49], v[50:51], 0, v[48:49]
	v_add_co_u32_e32 v50, vcc, s16, v48
	s_lshl_b32 s12, s12, 1
	s_nop 0
	v_addc_co_u32_e32 v51, vcc, 0, v49, vcc
	v_add_co_u32_e32 v52, vcc, s17, v48
	s_mov_b32 s13, s11
	s_nop 0
	v_addc_co_u32_e32 v53, vcc, 0, v49, vcc
	v_add_co_u32_e32 v54, vcc, s18, v48
	s_nop 1
	v_addc_co_u32_e32 v55, vcc, 0, v49, vcc
	v_add_co_u32_e32 v58, vcc, s19, v48
	global_load_dwordx2 v[56:57], v[48:49], off nt
	s_nop 0
	global_load_dwordx2 v[50:51], v[50:51], off nt
	s_nop 0
	global_load_dwordx2 v[52:53], v[52:53], off nt
	s_nop 0
	global_load_dwordx2 v[54:55], v[54:55], off nt
	v_addc_co_u32_e32 v59, vcc, 0, v49, vcc
	v_add_co_u32_e32 v60, vcc, s20, v48
	s_nop 1
	v_addc_co_u32_e32 v61, vcc, 0, v49, vcc
	v_add_co_u32_e32 v62, vcc, s21, v48
	s_nop 1
	v_addc_co_u32_e32 v63, vcc, 0, v49, vcc
	v_add_co_u32_e32 v64, vcc, s22, v48
	s_nop 1
	v_addc_co_u32_e32 v65, vcc, 0, v49, vcc
	v_add_co_u32_e32 v66, vcc, s23, v48
	global_load_dwordx2 v[58:59], v[58:59], off nt
	s_nop 0
	global_load_dwordx2 v[60:61], v[60:61], off nt
	s_nop 0
	global_load_dwordx2 v[62:63], v[62:63], off nt
	s_nop 0
	global_load_dwordx2 v[64:65], v[64:65], off nt
	v_addc_co_u32_e32 v67, vcc, 0, v49, vcc
	v_add_co_u32_e32 v68, vcc, s24, v48
	s_nop 1
	v_addc_co_u32_e32 v69, vcc, 0, v49, vcc
	v_add_co_u32_e32 v70, vcc, s25, v48
	s_nop 1
	v_addc_co_u32_e32 v71, vcc, 0, v49, vcc
	v_add_co_u32_e32 v72, vcc, s26, v48
	s_nop 1
	v_addc_co_u32_e32 v73, vcc, 0, v49, vcc
	v_add_co_u32_e32 v74, vcc, s27, v48
	global_load_dwordx2 v[66:67], v[66:67], off nt
	s_nop 0
	global_load_dwordx2 v[68:69], v[68:69], off nt
	s_nop 0
	global_load_dwordx2 v[70:71], v[70:71], off nt
	s_nop 0
	global_load_dwordx2 v[72:73], v[72:73], off nt
	v_addc_co_u32_e32 v75, vcc, 0, v49, vcc
	v_add_co_u32_e32 v76, vcc, s28, v48
	s_nop 1
	v_addc_co_u32_e32 v77, vcc, 0, v49, vcc
	v_add_co_u32_e32 v78, vcc, s29, v48
	s_nop 1
	v_addc_co_u32_e32 v79, vcc, 0, v49, vcc
	v_add_co_u32_e32 v80, vcc, s30, v48
	s_nop 1
	v_addc_co_u32_e32 v81, vcc, 0, v49, vcc
	v_add_co_u32_e32 v82, vcc, s31, v48
	global_load_dwordx2 v[74:75], v[74:75], off nt
	s_nop 0
	global_load_dwordx2 v[76:77], v[76:77], off nt
	s_nop 0
	global_load_dwordx2 v[78:79], v[78:79], off nt
	s_nop 0
	global_load_dwordx2 v[80:81], v[80:81], off nt
	v_addc_co_u32_e32 v83, vcc, 0, v49, vcc
	v_add_co_u32_e32 v84, vcc, s34, v48
	s_nop 1
	v_addc_co_u32_e32 v85, vcc, 0, v49, vcc
	v_add_co_u32_e32 v86, vcc, s35, v48
	s_nop 1
	v_addc_co_u32_e32 v87, vcc, 0, v49, vcc
	v_add_co_u32_e32 v88, vcc, s36, v48
	s_nop 1
	v_addc_co_u32_e32 v89, vcc, 0, v49, vcc
	v_add_co_u32_e32 v90, vcc, s37, v48
	global_load_dwordx2 v[82:83], v[82:83], off nt
	s_nop 0
	global_load_dwordx2 v[84:85], v[84:85], off nt
	s_nop 0
	global_load_dwordx2 v[86:87], v[86:87], off nt
	s_nop 0
	global_load_dwordx2 v[88:89], v[88:89], off nt
	v_addc_co_u32_e32 v91, vcc, 0, v49, vcc
	v_add_co_u32_e32 v92, vcc, s38, v48
	s_nop 1
	v_addc_co_u32_e32 v93, vcc, 0, v49, vcc
	v_add_co_u32_e32 v94, vcc, s39, v48
	s_nop 1
	v_addc_co_u32_e32 v95, vcc, 0, v49, vcc
	v_add_co_u32_e32 v96, vcc, s40, v48
	s_nop 1
	v_addc_co_u32_e32 v97, vcc, 0, v49, vcc
	v_add_co_u32_e32 v98, vcc, s41, v48
	global_load_dwordx2 v[90:91], v[90:91], off nt
	s_nop 0
	global_load_dwordx2 v[92:93], v[92:93], off nt
	s_nop 0
	global_load_dwordx2 v[94:95], v[94:95], off nt
	s_nop 0
	global_load_dwordx2 v[96:97], v[96:97], off nt
	v_addc_co_u32_e32 v99, vcc, 0, v49, vcc
	v_add_co_u32_e32 v100, vcc, s42, v48
	s_nop 1
	v_addc_co_u32_e32 v101, vcc, 0, v49, vcc
	v_add_co_u32_e32 v102, vcc, s43, v48
	s_nop 1
	v_addc_co_u32_e32 v103, vcc, 0, v49, vcc
	v_add_co_u32_e32 v104, vcc, s44, v48
	s_nop 1
	v_addc_co_u32_e32 v105, vcc, 0, v49, vcc
	v_add_co_u32_e32 v106, vcc, s45, v48
	global_load_dwordx2 v[98:99], v[98:99], off nt
	s_nop 0
	global_load_dwordx2 v[100:101], v[100:101], off nt
	s_nop 0
	global_load_dwordx2 v[102:103], v[102:103], off nt
	s_nop 0
	global_load_dwordx2 v[104:105], v[104:105], off nt
	v_addc_co_u32_e32 v107, vcc, 0, v49, vcc
	v_add_co_u32_e32 v110, vcc, s46, v48
	s_nop 1
	v_addc_co_u32_e32 v111, vcc, 0, v49, vcc
	v_add_co_u32_e32 v112, vcc, s47, v48
	s_nop 1
	v_addc_co_u32_e32 v113, vcc, 0, v49, vcc
	v_add_co_u32_e32 v48, vcc, s48, v48
	s_nop 1
	v_addc_co_u32_e32 v49, vcc, 0, v49, vcc
	global_load_dwordx2 v[106:107], v[106:107], off nt
	s_nop 0
	global_load_dwordx2 v[110:111], v[110:111], off nt
	s_nop 0
	global_load_dwordx2 v[112:113], v[112:113], off nt
	s_nop 0
	global_load_dwordx2 v[48:49], v[48:49], off nt
	s_waitcnt vmcnt(0)
	ds_write2_b32 v7, v56, v57 offset1:1
	ds_write2_b32 v7, v50, v51 offset0:130 offset1:131
	ds_write2_b32 v17, v52, v53 offset1:1
	ds_write2_b32 v18, v54, v55 offset1:1
	ds_write2_b32 v19, v58, v59 offset1:1
	ds_write2_b32 v20, v60, v61 offset1:1
	ds_write2_b32 v21, v62, v63 offset1:1
	ds_write2_b32 v22, v64, v65 offset1:1
	ds_write2_b32 v23, v66, v67 offset1:1
	ds_write2_b32 v24, v68, v69 offset1:1
	ds_write2_b32 v25, v70, v71 offset1:1
	ds_write2_b32 v26, v72, v73 offset1:1
	ds_write2_b32 v27, v74, v75 offset1:1
	ds_write2_b32 v28, v76, v77 offset1:1
	ds_write2_b32 v29, v78, v79 offset1:1
	ds_write2_b32 v30, v80, v81 offset1:1
	ds_write2_b32 v31, v82, v83 offset1:1
	ds_write2_b32 v32, v84, v85 offset1:1
	ds_write2_b32 v33, v86, v87 offset1:1
	ds_write2_b32 v34, v88, v89 offset1:1
	ds_write2_b32 v35, v90, v91 offset1:1
	ds_write2_b32 v36, v92, v93 offset1:1
	ds_write2_b32 v37, v94, v95 offset1:1
	ds_write2_b32 v38, v96, v97 offset1:1
	ds_write2_b32 v39, v98, v99 offset1:1
	ds_write2_b32 v40, v100, v101 offset1:1
	ds_write2_b32 v41, v102, v103 offset1:1
	ds_write2_b32 v42, v104, v105 offset1:1
	ds_write2_b32 v43, v106, v107 offset1:1
	ds_write2_b32 v44, v110, v111 offset1:1
	ds_write2_b32 v45, v112, v113 offset1:1
	ds_write2_b32 v46, v48, v49 offset1:1
	s_waitcnt lgkmcnt(0)
	ds_read2_b32 v[52:53], v9 offset0:65 offset1:73
	ds_read2_b32 v[54:55], v9 offset1:8
	ds_read2_b32 v[56:57], v9 offset0:130 offset1:138
	ds_read2_b32 v[58:59], v9 offset0:195 offset1:203
	ds_read2_b32 v[60:61], v47 offset0:4 offset1:12
	ds_read2_b32 v[62:63], v47 offset0:69 offset1:77
	ds_read2_b32 v[64:65], v47 offset0:134 offset1:142
	ds_read2_b32 v[66:67], v47 offset0:199 offset1:207
	v_add_u32_e32 v70, s10, v8
	v_ashrrev_i32_e32 v71, 31, v70
	v_lshl_add_u64 v[68:69], v[2:3], 0, s[12:13]
	v_lshlrev_b64 v[70:71], 12, v[70:71]
	s_waitcnt lgkmcnt(6)
	v_cvt_pk_bf16_f32 v48, v54, v52
	s_waitcnt lgkmcnt(4)
	v_cvt_pk_bf16_f32 v49, v56, v58
	s_waitcnt lgkmcnt(2)
	v_cvt_pk_bf16_f32 v50, v60, v62
	s_waitcnt lgkmcnt(0)
	v_cvt_pk_bf16_f32 v51, v64, v66
	v_lshl_add_u64 v[70:71], v[68:69], 0, v[70:71]
	v_add_u32_e32 v52, s10, v10
	global_store_dwordx4 v[70:71], v[48:51], off offset:1024
	s_nop 1
	v_cvt_pk_bf16_f32 v48, v55, v53
	v_ashrrev_i32_e32 v53, 31, v52
	v_cvt_pk_bf16_f32 v49, v57, v59
	v_cvt_pk_bf16_f32 v50, v61, v63
	v_cvt_pk_bf16_f32 v51, v65, v67
	v_lshlrev_b64 v[52:53], 12, v[52:53]
	ds_read2_b32 v[54:55], v9 offset0:81 offset1:89
	ds_read2_b32 v[56:57], v9 offset0:16 offset1:24
	ds_read2_b32 v[58:59], v9 offset0:146 offset1:154
	ds_read2_b32 v[60:61], v9 offset0:211 offset1:219
	ds_read2_b32 v[62:63], v47 offset0:20 offset1:28
	ds_read2_b32 v[64:65], v47 offset0:85 offset1:93
	ds_read2_b32 v[66:67], v47 offset0:150 offset1:158
	ds_read2_b32 v[70:71], v47 offset0:215 offset1:223
	v_lshl_add_u64 v[52:53], v[68:69], 0, v[52:53]
	global_store_dwordx4 v[52:53], v[48:51], off offset:1024
	v_add_u32_e32 v52, s10, v11
	v_ashrrev_i32_e32 v53, 31, v52
	v_lshlrev_b64 v[52:53], 12, v[52:53]
	s_waitcnt lgkmcnt(6)
	v_cvt_pk_bf16_f32 v48, v56, v54
	s_waitcnt lgkmcnt(4)
	v_cvt_pk_bf16_f32 v49, v58, v60
	s_waitcnt lgkmcnt(2)
	v_cvt_pk_bf16_f32 v50, v62, v64
	s_waitcnt lgkmcnt(0)
	v_cvt_pk_bf16_f32 v51, v66, v70
	v_lshl_add_u64 v[52:53], v[68:69], 0, v[52:53]
	global_store_dwordx4 v[52:53], v[48:51], off offset:1024
	v_add_u32_e32 v52, s10, v12
	v_ashrrev_i32_e32 v53, 31, v52
	v_cvt_pk_bf16_f32 v48, v57, v55
	v_cvt_pk_bf16_f32 v49, v59, v61
	v_cvt_pk_bf16_f32 v50, v63, v65
	v_cvt_pk_bf16_f32 v51, v67, v71
	v_lshlrev_b64 v[52:53], 12, v[52:53]
	ds_read2_b32 v[54:55], v9 offset0:32 offset1:40
	ds_read2_b32 v[56:57], v9 offset0:97 offset1:105
	ds_read2_b32 v[58:59], v9 offset0:162 offset1:170
	ds_read2_b32 v[60:61], v9 offset0:227 offset1:235
	ds_read2_b32 v[62:63], v47 offset0:36 offset1:44
	ds_read2_b32 v[64:65], v47 offset0:101 offset1:109
	ds_read2_b32 v[66:67], v47 offset0:166 offset1:174
	ds_read2_b32 v[70:71], v47 offset0:231 offset1:239
	v_lshl_add_u64 v[52:53], v[68:69], 0, v[52:53]
	global_store_dwordx4 v[52:53], v[48:51], off offset:1024
	v_add_u32_e32 v52, s10, v13
	v_ashrrev_i32_e32 v53, 31, v52
	v_lshlrev_b64 v[52:53], 12, v[52:53]
	s_waitcnt lgkmcnt(6)
	v_cvt_pk_bf16_f32 v48, v54, v56
	s_waitcnt lgkmcnt(4)
	v_cvt_pk_bf16_f32 v49, v58, v60
	s_waitcnt lgkmcnt(2)
	v_cvt_pk_bf16_f32 v50, v62, v64
	s_waitcnt lgkmcnt(0)
	v_cvt_pk_bf16_f32 v51, v66, v70
	v_lshl_add_u64 v[52:53], v[68:69], 0, v[52:53]
	global_store_dwordx4 v[52:53], v[48:51], off offset:1024
	v_add_u32_e32 v52, s10, v14
	v_ashrrev_i32_e32 v53, 31, v52
	v_cvt_pk_bf16_f32 v48, v55, v57
	v_cvt_pk_bf16_f32 v49, v59, v61
	v_cvt_pk_bf16_f32 v50, v63, v65
	v_cvt_pk_bf16_f32 v51, v67, v71
	v_lshlrev_b64 v[52:53], 12, v[52:53]
	ds_read2_b32 v[54:55], v9 offset0:48 offset1:56
	ds_read2_b32 v[56:57], v9 offset0:113 offset1:121
	ds_read2_b32 v[58:59], v9 offset0:178 offset1:186
	ds_read2_b32 v[60:61], v9 offset0:243 offset1:251
	ds_read2_b32 v[62:63], v47 offset0:52 offset1:60
	ds_read2_b32 v[64:65], v47 offset0:117 offset1:125
	ds_read2_b32 v[66:67], v47 offset0:182 offset1:190
	ds_read2_b32 v[70:71], v47 offset0:247 offset1:255
	v_lshl_add_u64 v[52:53], v[68:69], 0, v[52:53]
	global_store_dwordx4 v[52:53], v[48:51], off offset:1024
	v_add_u32_e32 v52, s10, v15
	v_ashrrev_i32_e32 v53, 31, v52
	v_lshlrev_b64 v[52:53], 12, v[52:53]
	s_waitcnt lgkmcnt(6)
	v_cvt_pk_bf16_f32 v48, v54, v56
	s_waitcnt lgkmcnt(4)
	v_cvt_pk_bf16_f32 v49, v58, v60
	s_waitcnt lgkmcnt(2)
	v_cvt_pk_bf16_f32 v50, v62, v64
	s_waitcnt lgkmcnt(0)
	v_cvt_pk_bf16_f32 v51, v66, v70
	v_lshl_add_u64 v[52:53], v[68:69], 0, v[52:53]
	global_store_dwordx4 v[52:53], v[48:51], off offset:1024
	v_add_u32_e32 v52, s10, v16
	v_ashrrev_i32_e32 v53, 31, v52
	v_lshlrev_b64 v[52:53], 12, v[52:53]
	v_cvt_pk_bf16_f32 v48, v55, v57
	v_cvt_pk_bf16_f32 v49, v59, v61
	v_cvt_pk_bf16_f32 v50, v63, v65
	v_cvt_pk_bf16_f32 v51, v67, v71
	v_lshl_add_u64 v[52:53], v[68:69], 0, v[52:53]
	global_store_dwordx4 v[52:53], v[48:51], off offset:1024
	s_waitcnt lgkmcnt(0)

.LBB0_806:
	s_andn2_b64 vcc, exec, s[12:13]
	s_cbranch_vccnz .LBB0_795
	s_ashr_i32 s10, s49, 31
	s_lshr_b32 s10, s10, 29
	s_add_i32 s10, s49, s10
	s_ashr_i32 s10, s10, 3
	s_load_dwordx2 s[50:51], s[76:77], 0x78
	s_lshl_b32 s12, s10, 6
	s_lshl_b32 s10, s10, 9
	s_sub_i32 s14, s0, s10
	v_add_u32_e32 v48, s14, v6
	s_ashr_i32 s13, s12, 31
	s_lshl_b64 s[52:53], s[12:13], 2
	v_ashrrev_i32_e32 v49, 31, v48
	s_waitcnt lgkmcnt(0)
	s_add_u32 s50, s50, s52
	v_lshlrev_b64 v[52:53], 13, v[48:49]
	v_add_u32_e32 v54, 2, v48
	v_add_u32_e32 v56, 4, v48
	v_add_u32_e32 v58, 6, v48
	v_add_u32_e32 v60, 8, v48
	v_add_u32_e32 v62, 10, v48
	v_add_u32_e32 v64, 12, v48
	v_add_u32_e32 v66, 14, v48
	v_add_u32_e32 v68, 16, v48
	v_add_u32_e32 v70, 18, v48
	v_add_u32_e32 v72, 20, v48
	v_add_u32_e32 v74, 22, v48
	v_add_u32_e32 v76, 24, v48
	v_add_u32_e32 v78, 26, v48
	v_add_u32_e32 v80, 28, v48
	v_add_u32_e32 v82, 30, v48
	v_add_u32_e32 v84, 32, v48
	v_add_u32_e32 v86, 34, v48
	v_add_u32_e32 v88, 36, v48
	v_add_u32_e32 v90, 38, v48
	v_add_u32_e32 v92, 40, v48
	v_add_u32_e32 v94, 42, v48
	v_add_u32_e32 v96, 44, v48
	v_add_u32_e32 v98, 46, v48
	v_add_u32_e32 v100, 48, v48
	v_add_u32_e32 v102, 50, v48
	v_add_u32_e32 v104, 52, v48
	v_add_u32_e32 v106, 54, v48
	v_add_u32_e32 v110, 56, v48
	v_add_u32_e32 v112, 58, v48
	v_add_u32_e32 v114, 60, v48
	v_add_u32_e32 v48, 62, v48
	s_addc_u32 s51, s51, s53
	v_ashrrev_i32_e32 v55, 31, v54
	v_ashrrev_i32_e32 v57, 31, v56
	v_ashrrev_i32_e32 v59, 31, v58
	v_ashrrev_i32_e32 v61, 31, v60
	v_ashrrev_i32_e32 v63, 31, v62
	v_ashrrev_i32_e32 v65, 31, v64
	v_ashrrev_i32_e32 v67, 31, v66
	v_ashrrev_i32_e32 v69, 31, v68
	v_ashrrev_i32_e32 v71, 31, v70
	v_ashrrev_i32_e32 v73, 31, v72
	v_ashrrev_i32_e32 v75, 31, v74
	v_ashrrev_i32_e32 v77, 31, v76
	v_ashrrev_i32_e32 v79, 31, v78
	v_ashrrev_i32_e32 v81, 31, v80
	v_ashrrev_i32_e32 v83, 31, v82
	v_ashrrev_i32_e32 v85, 31, v84
	v_ashrrev_i32_e32 v87, 31, v86
	v_ashrrev_i32_e32 v89, 31, v88
	v_ashrrev_i32_e32 v91, 31, v90
	v_ashrrev_i32_e32 v93, 31, v92
	v_ashrrev_i32_e32 v95, 31, v94
	v_ashrrev_i32_e32 v97, 31, v96
	v_ashrrev_i32_e32 v99, 31, v98
	v_ashrrev_i32_e32 v101, 31, v100
	v_ashrrev_i32_e32 v103, 31, v102
	v_ashrrev_i32_e32 v105, 31, v104
	v_ashrrev_i32_e32 v107, 31, v106
	v_ashrrev_i32_e32 v111, 31, v110
	v_ashrrev_i32_e32 v113, 31, v112
	v_ashrrev_i32_e32 v49, 31, v48
	v_lshl_add_u64 v[50:51], s[50:51], 0, v[0:1]
	v_lshlrev_b64 v[54:55], 13, v[54:55]
	v_lshlrev_b64 v[56:57], 13, v[56:57]
	v_lshlrev_b64 v[58:59], 13, v[58:59]
	v_lshlrev_b64 v[60:61], 13, v[60:61]
	v_lshlrev_b64 v[62:63], 13, v[62:63]
	v_lshlrev_b64 v[64:65], 13, v[64:65]
	v_lshlrev_b64 v[66:67], 13, v[66:67]
	v_lshlrev_b64 v[68:69], 13, v[68:69]
	v_lshlrev_b64 v[70:71], 13, v[70:71]
	v_lshlrev_b64 v[72:73], 13, v[72:73]
	v_lshlrev_b64 v[74:75], 13, v[74:75]
	v_lshlrev_b64 v[76:77], 13, v[76:77]
	v_lshlrev_b64 v[78:79], 13, v[78:79]
	v_lshlrev_b64 v[80:81], 13, v[80:81]
	v_lshlrev_b64 v[82:83], 13, v[82:83]
	v_lshlrev_b64 v[84:85], 13, v[84:85]
	v_lshlrev_b64 v[86:87], 13, v[86:87]
	v_lshlrev_b64 v[88:89], 13, v[88:89]
	v_lshlrev_b64 v[90:91], 13, v[90:91]
	v_lshlrev_b64 v[92:93], 13, v[92:93]
	v_lshlrev_b64 v[94:95], 13, v[94:95]
	v_lshlrev_b64 v[96:97], 13, v[96:97]
	v_lshlrev_b64 v[98:99], 13, v[98:99]
	v_lshlrev_b64 v[100:101], 13, v[100:101]
	v_lshlrev_b64 v[102:103], 13, v[102:103]
	v_lshlrev_b64 v[104:105], 13, v[104:105]
	v_lshlrev_b64 v[106:107], 13, v[106:107]
	v_lshlrev_b64 v[110:111], 13, v[110:111]
	v_lshlrev_b64 v[112:113], 13, v[112:113]
	v_ashrrev_i32_e32 v115, 31, v114
	v_lshlrev_b64 v[48:49], 13, v[48:49]
	v_lshl_add_u64 v[52:53], v[50:51], 0, v[52:53]
	v_lshl_add_u64 v[54:55], v[50:51], 0, v[54:55]
	v_lshl_add_u64 v[56:57], v[50:51], 0, v[56:57]
	v_lshl_add_u64 v[58:59], v[50:51], 0, v[58:59]
	v_lshl_add_u64 v[60:61], v[50:51], 0, v[60:61]
	v_lshl_add_u64 v[62:63], v[50:51], 0, v[62:63]
	v_lshl_add_u64 v[64:65], v[50:51], 0, v[64:65]
	v_lshl_add_u64 v[66:67], v[50:51], 0, v[66:67]
	v_lshl_add_u64 v[68:69], v[50:51], 0, v[68:69]
	v_lshl_add_u64 v[70:71], v[50:51], 0, v[70:71]
	v_lshl_add_u64 v[72:73], v[50:51], 0, v[72:73]
	v_lshl_add_u64 v[74:75], v[50:51], 0, v[74:75]
	v_lshl_add_u64 v[76:77], v[50:51], 0, v[76:77]
	v_lshl_add_u64 v[78:79], v[50:51], 0, v[78:79]
	v_lshl_add_u64 v[80:81], v[50:51], 0, v[80:81]
	v_lshl_add_u64 v[82:83], v[50:51], 0, v[82:83]
	v_lshl_add_u64 v[84:85], v[50:51], 0, v[84:85]
	v_lshl_add_u64 v[86:87], v[50:51], 0, v[86:87]
	v_lshl_add_u64 v[88:89], v[50:51], 0, v[88:89]
	v_lshl_add_u64 v[90:91], v[50:51], 0, v[90:91]
	v_lshl_add_u64 v[92:93], v[50:51], 0, v[92:93]
	v_lshl_add_u64 v[94:95], v[50:51], 0, v[94:95]
	v_lshl_add_u64 v[96:97], v[50:51], 0, v[96:97]
	v_lshl_add_u64 v[98:99], v[50:51], 0, v[98:99]
	v_lshl_add_u64 v[100:101], v[50:51], 0, v[100:101]
	v_lshl_add_u64 v[102:103], v[50:51], 0, v[102:103]
	v_lshl_add_u64 v[104:105], v[50:51], 0, v[104:105]
	v_lshl_add_u64 v[106:107], v[50:51], 0, v[106:107]
	v_lshl_add_u64 v[110:111], v[50:51], 0, v[110:111]
	v_lshl_add_u64 v[112:113], v[50:51], 0, v[112:113]
	v_lshlrev_b64 v[114:115], 13, v[114:115]
	v_lshl_add_u64 v[48:49], v[50:51], 0, v[48:49]
	global_load_dwordx2 v[52:53], v[52:53], off nt
	s_nop 0
	global_load_dwordx2 v[54:55], v[54:55], off nt
	s_nop 0
	global_load_dwordx2 v[56:57], v[56:57], off nt
	s_nop 0
	global_load_dwordx2 v[58:59], v[58:59], off nt
	s_nop 0
	global_load_dwordx2 v[60:61], v[60:61], off nt
	s_nop 0
	global_load_dwordx2 v[62:63], v[62:63], off nt
	s_nop 0
	global_load_dwordx2 v[64:65], v[64:65], off nt
	s_nop 0
	global_load_dwordx2 v[66:67], v[66:67], off nt
	s_nop 0
	global_load_dwordx2 v[68:69], v[68:69], off nt
	s_nop 0
	global_load_dwordx2 v[70:71], v[70:71], off nt
	s_nop 0
	global_load_dwordx2 v[72:73], v[72:73], off nt
	s_nop 0
	global_load_dwordx2 v[74:75], v[74:75], off nt
	s_nop 0
	global_load_dwordx2 v[76:77], v[76:77], off nt
	s_nop 0
	global_load_dwordx2 v[78:79], v[78:79], off nt
	s_nop 0
	global_load_dwordx2 v[80:81], v[80:81], off nt
	s_nop 0
	global_load_dwordx2 v[82:83], v[82:83], off nt
	s_nop 0
	global_load_dwordx2 v[84:85], v[84:85], off nt
	s_nop 0
	global_load_dwordx2 v[86:87], v[86:87], off nt
	s_nop 0
	global_load_dwordx2 v[88:89], v[88:89], off nt
	s_nop 0
	global_load_dwordx2 v[90:91], v[90:91], off nt
	s_nop 0
	global_load_dwordx2 v[92:93], v[92:93], off nt
	s_nop 0
	global_load_dwordx2 v[94:95], v[94:95], off nt
	s_nop 0
	global_load_dwordx2 v[96:97], v[96:97], off nt
	s_nop 0
	global_load_dwordx2 v[98:99], v[98:99], off nt
	s_nop 0
	global_load_dwordx2 v[100:101], v[100:101], off nt
	s_nop 0
	global_load_dwordx2 v[102:103], v[102:103], off nt
	s_nop 0
	global_load_dwordx2 v[104:105], v[104:105], off nt
	s_nop 0
	global_load_dwordx2 v[106:107], v[106:107], off nt
	v_lshl_add_u64 v[114:115], v[50:51], 0, v[114:115]
	global_load_dwordx2 v[50:51], v[110:111], off nt
	s_nop 0
	global_load_dwordx2 v[110:111], v[112:113], off nt
	s_nop 0
	global_load_dwordx2 v[112:113], v[114:115], off nt
	s_nop 0
	global_load_dwordx2 v[48:49], v[48:49], off nt
	s_waitcnt vmcnt(0)
	ds_write2_b32 v7, v52, v53 offset1:1
	ds_write2_b32 v7, v54, v55 offset0:130 offset1:131
	ds_write2_b32 v17, v56, v57 offset1:1
	ds_write2_b32 v18, v58, v59 offset1:1
	ds_write2_b32 v19, v60, v61 offset1:1
	ds_write2_b32 v20, v62, v63 offset1:1
	ds_write2_b32 v21, v64, v65 offset1:1
	ds_write2_b32 v22, v66, v67 offset1:1
	ds_write2_b32 v23, v68, v69 offset1:1
	ds_write2_b32 v24, v70, v71 offset1:1
	ds_write2_b32 v25, v72, v73 offset1:1
	ds_write2_b32 v26, v74, v75 offset1:1
	ds_write2_b32 v27, v76, v77 offset1:1
	ds_write2_b32 v28, v78, v79 offset1:1
	ds_write2_b32 v29, v80, v81 offset1:1
	ds_write2_b32 v30, v82, v83 offset1:1
	ds_write2_b32 v31, v84, v85 offset1:1
	ds_write2_b32 v32, v86, v87 offset1:1
	ds_write2_b32 v33, v88, v89 offset1:1
	ds_write2_b32 v34, v90, v91 offset1:1
	ds_write2_b32 v35, v92, v93 offset1:1
	ds_write2_b32 v36, v94, v95 offset1:1
	ds_write2_b32 v37, v96, v97 offset1:1
	ds_write2_b32 v38, v98, v99 offset1:1
	ds_write2_b32 v39, v100, v101 offset1:1
	ds_write2_b32 v40, v102, v103 offset1:1
	ds_write2_b32 v41, v104, v105 offset1:1
	ds_write2_b32 v42, v106, v107 offset1:1
	ds_write2_b32 v43, v50, v51 offset1:1
	ds_write2_b32 v44, v110, v111 offset1:1
	ds_write2_b32 v45, v112, v113 offset1:1
	ds_write2_b32 v46, v48, v49 offset1:1
	s_waitcnt lgkmcnt(0)
	ds_read2_b32 v[52:53], v9 offset0:65 offset1:73
	ds_read2_b32 v[54:55], v9 offset1:8
	ds_read2_b32 v[56:57], v9 offset0:130 offset1:138
	ds_read2_b32 v[58:59], v9 offset0:195 offset1:203
	ds_read2_b32 v[60:61], v47 offset0:4 offset1:12
	ds_read2_b32 v[62:63], v47 offset0:69 offset1:77
	ds_read2_b32 v[64:65], v47 offset0:134 offset1:142
	ds_read2_b32 v[66:67], v47 offset0:199 offset1:207
	v_add_u32_e32 v70, s12, v8
	s_ashr_i32 s15, s14, 31
	v_ashrrev_i32_e32 v71, 31, v70
	v_lshl_add_u64 v[68:69], s[14:15], 1, v[2:3]
	v_lshlrev_b64 v[70:71], 12, v[70:71]
	s_waitcnt lgkmcnt(6)
	v_cvt_pk_bf16_f32 v48, v54, v52
	s_waitcnt lgkmcnt(4)
	v_cvt_pk_bf16_f32 v49, v56, v58
	s_waitcnt lgkmcnt(2)
	v_cvt_pk_bf16_f32 v50, v60, v62
	s_waitcnt lgkmcnt(0)
	v_cvt_pk_bf16_f32 v51, v64, v66
	v_lshl_add_u64 v[70:71], v[68:69], 0, v[70:71]
	v_add_u32_e32 v52, s12, v10
	global_store_dwordx4 v[70:71], v[48:51], off
	s_nop 1
	v_cvt_pk_bf16_f32 v48, v55, v53
	v_ashrrev_i32_e32 v53, 31, v52
	v_cvt_pk_bf16_f32 v49, v57, v59
	v_cvt_pk_bf16_f32 v50, v61, v63
	v_cvt_pk_bf16_f32 v51, v65, v67
	v_lshlrev_b64 v[52:53], 12, v[52:53]
	ds_read2_b32 v[54:55], v9 offset0:81 offset1:89
	ds_read2_b32 v[56:57], v9 offset0:16 offset1:24
	ds_read2_b32 v[58:59], v9 offset0:146 offset1:154
	ds_read2_b32 v[60:61], v9 offset0:211 offset1:219
	ds_read2_b32 v[62:63], v47 offset0:20 offset1:28
	ds_read2_b32 v[64:65], v47 offset0:85 offset1:93
	ds_read2_b32 v[66:67], v47 offset0:150 offset1:158
	ds_read2_b32 v[70:71], v47 offset0:215 offset1:223
	v_lshl_add_u64 v[52:53], v[68:69], 0, v[52:53]
	global_store_dwordx4 v[52:53], v[48:51], off
	v_add_u32_e32 v52, s12, v11
	v_ashrrev_i32_e32 v53, 31, v52
	v_lshlrev_b64 v[52:53], 12, v[52:53]
	s_waitcnt lgkmcnt(6)
	v_cvt_pk_bf16_f32 v48, v56, v54
	s_waitcnt lgkmcnt(4)
	v_cvt_pk_bf16_f32 v49, v58, v60
	s_waitcnt lgkmcnt(2)
	v_cvt_pk_bf16_f32 v50, v62, v64
	s_waitcnt lgkmcnt(0)
	v_cvt_pk_bf16_f32 v51, v66, v70
	v_lshl_add_u64 v[52:53], v[68:69], 0, v[52:53]
	global_store_dwordx4 v[52:53], v[48:51], off
	v_add_u32_e32 v52, s12, v12
	v_ashrrev_i32_e32 v53, 31, v52
	v_cvt_pk_bf16_f32 v48, v57, v55
	v_cvt_pk_bf16_f32 v49, v59, v61
	v_cvt_pk_bf16_f32 v50, v63, v65
	v_cvt_pk_bf16_f32 v51, v67, v71
	v_lshlrev_b64 v[52:53], 12, v[52:53]
	ds_read2_b32 v[54:55], v9 offset0:32 offset1:40
	ds_read2_b32 v[56:57], v9 offset0:97 offset1:105
	ds_read2_b32 v[58:59], v9 offset0:162 offset1:170
	ds_read2_b32 v[60:61], v9 offset0:227 offset1:235
	ds_read2_b32 v[62:63], v47 offset0:36 offset1:44
	ds_read2_b32 v[64:65], v47 offset0:101 offset1:109
	ds_read2_b32 v[66:67], v47 offset0:166 offset1:174
	ds_read2_b32 v[70:71], v47 offset0:231 offset1:239
	v_lshl_add_u64 v[52:53], v[68:69], 0, v[52:53]
	global_store_dwordx4 v[52:53], v[48:51], off
	v_add_u32_e32 v52, s12, v13
	v_ashrrev_i32_e32 v53, 31, v52
	v_lshlrev_b64 v[52:53], 12, v[52:53]
	s_waitcnt lgkmcnt(6)
	v_cvt_pk_bf16_f32 v48, v54, v56
	s_waitcnt lgkmcnt(4)
	v_cvt_pk_bf16_f32 v49, v58, v60
	s_waitcnt lgkmcnt(2)
	v_cvt_pk_bf16_f32 v50, v62, v64
	s_waitcnt lgkmcnt(0)
	v_cvt_pk_bf16_f32 v51, v66, v70
	v_lshl_add_u64 v[52:53], v[68:69], 0, v[52:53]
	global_store_dwordx4 v[52:53], v[48:51], off
	v_add_u32_e32 v52, s12, v14
	v_ashrrev_i32_e32 v53, 31, v52
	v_cvt_pk_bf16_f32 v48, v55, v57
	v_cvt_pk_bf16_f32 v49, v59, v61
	v_cvt_pk_bf16_f32 v50, v63, v65
	v_cvt_pk_bf16_f32 v51, v67, v71
	v_lshlrev_b64 v[52:53], 12, v[52:53]
	ds_read2_b32 v[54:55], v9 offset0:48 offset1:56
	ds_read2_b32 v[56:57], v9 offset0:113 offset1:121
	ds_read2_b32 v[58:59], v9 offset0:178 offset1:186
	ds_read2_b32 v[60:61], v9 offset0:243 offset1:251
	ds_read2_b32 v[62:63], v47 offset0:52 offset1:60
	ds_read2_b32 v[64:65], v47 offset0:117 offset1:125
	ds_read2_b32 v[66:67], v47 offset0:182 offset1:190
	ds_read2_b32 v[70:71], v47 offset0:247 offset1:255
	v_lshl_add_u64 v[52:53], v[68:69], 0, v[52:53]
	global_store_dwordx4 v[52:53], v[48:51], off
	v_add_u32_e32 v52, s12, v15
	v_ashrrev_i32_e32 v53, 31, v52
	v_lshlrev_b64 v[52:53], 12, v[52:53]
	s_waitcnt lgkmcnt(6)
	v_cvt_pk_bf16_f32 v48, v54, v56
	s_waitcnt lgkmcnt(4)
	v_cvt_pk_bf16_f32 v49, v58, v60
	s_waitcnt lgkmcnt(2)
	v_cvt_pk_bf16_f32 v50, v62, v64
	s_waitcnt lgkmcnt(0)
	v_cvt_pk_bf16_f32 v51, v66, v70
	v_lshl_add_u64 v[52:53], v[68:69], 0, v[52:53]
	global_store_dwordx4 v[52:53], v[48:51], off
	v_add_u32_e32 v52, s12, v16
	v_ashrrev_i32_e32 v53, 31, v52
	v_lshlrev_b64 v[52:53], 12, v[52:53]
	v_cvt_pk_bf16_f32 v48, v55, v57
	v_cvt_pk_bf16_f32 v49, v59, v61
	v_cvt_pk_bf16_f32 v50, v63, v65
	v_cvt_pk_bf16_f32 v51, v67, v71
	v_lshl_add_u64 v[52:53], v[68:69], 0, v[52:53]
	global_store_dwordx4 v[52:53], v[48:51], off
	s_waitcnt lgkmcnt(0)
	s_branch .LBB0_795

.LBB0_814:
	s_cmpk_gt_i32 s48, 0xff
	s_mov_b64 s[12:13], -1
	s_cbranch_scc0 .LBB0_824
	s_cmpk_gt_u32 s48, 0x1ff
	s_cbranch_scc0 .LBB0_821
	s_cmpk_gt_u32 s48, 0x3ff
	s_cbranch_scc0 .LBB0_818
	s_load_dwordx2 s[50:51], s[76:77], 0x90
	s_load_dwordx2 s[12:13], s[76:77], 0xf0
	s_and_b32 s10, s6, 0x7fffffc0
	s_addk_i32 s10, 0xf800
	s_and_b32 s14, s5, 0x7c0
	s_lshl_b64 s[52:53], s[10:11], 2
	v_add_u32_e32 v50, s14, v6
	s_waitcnt lgkmcnt(0)
	s_add_u32 s50, s50, s52
	s_addc_u32 s51, s51, s53
	v_ashrrev_i32_e32 v51, 31, v50
	v_lshl_add_u64 v[52:53], s[50:51], 0, v[0:1]
	v_lshlrev_b64 v[50:51], 13, v[50:51]
	v_lshl_add_u64 v[50:51], v[52:53], 0, v[50:51]
	v_add_co_u32_e32 v52, vcc, s9, v50
	s_lshl_b32 s14, s14, 1
	s_nop 0
	v_addc_co_u32_e32 v53, vcc, 0, v51, vcc
	v_add_co_u32_e32 v54, vcc, s16, v50
	s_add_u32 s12, s12, s14
	s_nop 0
	v_addc_co_u32_e32 v55, vcc, 0, v51, vcc
	v_add_co_u32_e32 v56, vcc, s17, v50
	s_addc_u32 s13, s13, 0
	s_nop 0
	v_addc_co_u32_e32 v57, vcc, 0, v51, vcc
	v_add_co_u32_e32 v60, vcc, s18, v50
	global_load_dwordx2 v[58:59], v[50:51], off nt
	s_nop 0
	global_load_dwordx2 v[52:53], v[52:53], off nt
	s_nop 0
	global_load_dwordx2 v[54:55], v[54:55], off nt
	s_nop 0
	global_load_dwordx2 v[56:57], v[56:57], off nt
	v_addc_co_u32_e32 v61, vcc, 0, v51, vcc
	v_add_co_u32_e32 v62, vcc, s19, v50
	v_mov_b32_e32 v5, v1
	s_nop 0
	v_addc_co_u32_e32 v63, vcc, 0, v51, vcc
	v_add_co_u32_e32 v64, vcc, s20, v50
	s_nop 1
	v_addc_co_u32_e32 v65, vcc, 0, v51, vcc
	v_add_co_u32_e32 v66, vcc, s21, v50
	s_nop 1
	v_addc_co_u32_e32 v67, vcc, 0, v51, vcc
	v_add_co_u32_e32 v68, vcc, s22, v50
	global_load_dwordx2 v[60:61], v[60:61], off nt
	s_nop 0
	global_load_dwordx2 v[62:63], v[62:63], off nt
	s_nop 0
	global_load_dwordx2 v[64:65], v[64:65], off nt
	s_nop 0
	global_load_dwordx2 v[66:67], v[66:67], off nt
	v_addc_co_u32_e32 v69, vcc, 0, v51, vcc
	v_add_co_u32_e32 v70, vcc, s23, v50
	s_nop 1
	v_addc_co_u32_e32 v71, vcc, 0, v51, vcc
	v_add_co_u32_e32 v72, vcc, s24, v50
	s_nop 1
	v_addc_co_u32_e32 v73, vcc, 0, v51, vcc
	v_add_co_u32_e32 v74, vcc, s25, v50
	s_nop 1
	v_addc_co_u32_e32 v75, vcc, 0, v51, vcc
	v_add_co_u32_e32 v76, vcc, s26, v50
	global_load_dwordx2 v[68:69], v[68:69], off nt
	s_nop 0
	global_load_dwordx2 v[70:71], v[70:71], off nt
	s_nop 0
	global_load_dwordx2 v[72:73], v[72:73], off nt
	s_nop 0
	global_load_dwordx2 v[74:75], v[74:75], off nt
	v_addc_co_u32_e32 v77, vcc, 0, v51, vcc
	v_add_co_u32_e32 v78, vcc, s27, v50
	s_nop 1
	v_addc_co_u32_e32 v79, vcc, 0, v51, vcc
	v_add_co_u32_e32 v80, vcc, s28, v50
	s_nop 1
	v_addc_co_u32_e32 v81, vcc, 0, v51, vcc
	v_add_co_u32_e32 v82, vcc, s29, v50
	s_nop 1
	v_addc_co_u32_e32 v83, vcc, 0, v51, vcc
	v_add_co_u32_e32 v84, vcc, s30, v50
	global_load_dwordx2 v[76:77], v[76:77], off nt
	s_nop 0
	global_load_dwordx2 v[78:79], v[78:79], off nt
	s_nop 0
	global_load_dwordx2 v[80:81], v[80:81], off nt
	s_nop 0
	global_load_dwordx2 v[82:83], v[82:83], off nt
	v_addc_co_u32_e32 v85, vcc, 0, v51, vcc
	v_add_co_u32_e32 v86, vcc, s31, v50
	s_nop 1
	v_addc_co_u32_e32 v87, vcc, 0, v51, vcc
	v_add_co_u32_e32 v88, vcc, s34, v50
	s_nop 1
	v_addc_co_u32_e32 v89, vcc, 0, v51, vcc
	v_add_co_u32_e32 v90, vcc, s35, v50
	s_nop 1
	v_addc_co_u32_e32 v91, vcc, 0, v51, vcc
	v_add_co_u32_e32 v92, vcc, s36, v50
	global_load_dwordx2 v[84:85], v[84:85], off nt
	s_nop 0
	global_load_dwordx2 v[86:87], v[86:87], off nt
	s_nop 0
	global_load_dwordx2 v[88:89], v[88:89], off nt
	s_nop 0
	global_load_dwordx2 v[90:91], v[90:91], off nt
	v_addc_co_u32_e32 v93, vcc, 0, v51, vcc
	v_add_co_u32_e32 v94, vcc, s37, v50
	s_nop 1
	v_addc_co_u32_e32 v95, vcc, 0, v51, vcc
	v_add_co_u32_e32 v96, vcc, s38, v50
	s_nop 1
	v_addc_co_u32_e32 v97, vcc, 0, v51, vcc
	v_add_co_u32_e32 v98, vcc, s39, v50
	s_nop 1
	v_addc_co_u32_e32 v99, vcc, 0, v51, vcc
	v_add_co_u32_e32 v100, vcc, s40, v50
	global_load_dwordx2 v[92:93], v[92:93], off nt
	s_nop 0
	global_load_dwordx2 v[94:95], v[94:95], off nt
	s_nop 0
	global_load_dwordx2 v[96:97], v[96:97], off nt
	s_nop 0
	global_load_dwordx2 v[98:99], v[98:99], off nt
	v_addc_co_u32_e32 v101, vcc, 0, v51, vcc
	v_add_co_u32_e32 v102, vcc, s41, v50
	s_nop 1
	v_addc_co_u32_e32 v103, vcc, 0, v51, vcc
	v_add_co_u32_e32 v104, vcc, s42, v50
	s_nop 1
	v_addc_co_u32_e32 v105, vcc, 0, v51, vcc
	v_add_co_u32_e32 v106, vcc, s43, v50
	s_nop 1
	v_addc_co_u32_e32 v107, vcc, 0, v51, vcc
	v_add_co_u32_e32 v108, vcc, s44, v50
	global_load_dwordx2 v[100:101], v[100:101], off nt
	s_nop 0
	global_load_dwordx2 v[102:103], v[102:103], off nt
	s_nop 0
	global_load_dwordx2 v[104:105], v[104:105], off nt
	s_nop 0
	global_load_dwordx2 v[106:107], v[106:107], off nt
	v_addc_co_u32_e32 v109, vcc, 0, v51, vcc
	v_add_co_u32_e32 v110, vcc, s45, v50
	s_nop 1
	v_addc_co_u32_e32 v111, vcc, 0, v51, vcc
	v_add_co_u32_e32 v112, vcc, s46, v50
	s_nop 1
	v_addc_co_u32_e32 v113, vcc, 0, v51, vcc
	v_add_co_u32_e32 v50, vcc, s47, v50
	s_nop 1
	v_addc_co_u32_e32 v51, vcc, 0, v51, vcc
	global_load_dwordx2 v[108:109], v[108:109], off nt
	s_nop 0
	global_load_dwordx2 v[110:111], v[110:111], off nt
	s_nop 0
	global_load_dwordx2 v[112:113], v[112:113], off nt
	s_nop 0
	global_load_dwordx2 v[50:51], v[50:51], off nt
	s_waitcnt vmcnt(0)
	ds_write2_b32 v10, v58, v59 offset1:1
	ds_write2_b32 v10, v52, v53 offset0:130 offset1:131
	ds_write2_b32 v19, v54, v55 offset1:1
	ds_write2_b32 v20, v56, v57 offset1:1
	ds_write2_b32 v21, v60, v61 offset1:1
	ds_write2_b32 v22, v62, v63 offset1:1
	ds_write2_b32 v23, v64, v65 offset1:1
	ds_write2_b32 v24, v66, v67 offset1:1
	ds_write2_b32 v25, v68, v69 offset1:1
	ds_write2_b32 v26, v70, v71 offset1:1
	ds_write2_b32 v27, v72, v73 offset1:1
	ds_write2_b32 v28, v74, v75 offset1:1
	ds_write2_b32 v29, v76, v77 offset1:1
	ds_write2_b32 v30, v78, v79 offset1:1
	ds_write2_b32 v31, v80, v81 offset1:1
	ds_write2_b32 v32, v82, v83 offset1:1
	ds_write2_b32 v33, v84, v85 offset1:1
	ds_write2_b32 v34, v86, v87 offset1:1
	ds_write2_b32 v35, v88, v89 offset1:1
	ds_write2_b32 v36, v90, v91 offset1:1
	ds_write2_b32 v37, v92, v93 offset1:1
	ds_write2_b32 v38, v94, v95 offset1:1
	ds_write2_b32 v39, v96, v97 offset1:1
	ds_write2_b32 v40, v98, v99 offset1:1
	ds_write2_b32 v41, v100, v101 offset1:1
	ds_write2_b32 v42, v102, v103 offset1:1
	ds_write2_b32 v43, v104, v105 offset1:1
	ds_write2_b32 v44, v106, v107 offset1:1
	ds_write2_b32 v45, v108, v109 offset1:1
	ds_write2_b32 v46, v110, v111 offset1:1
	ds_write2_b32 v47, v112, v113 offset1:1
	ds_write2_b32 v48, v50, v51 offset1:1
	s_waitcnt lgkmcnt(0)
	ds_read2_b32 v[54:55], v11 offset0:65 offset1:73
	ds_read2_b32 v[56:57], v11 offset1:8
	ds_read2_b32 v[58:59], v11 offset0:130 offset1:138
	ds_read2_b32 v[60:61], v11 offset0:195 offset1:203
	ds_read2_b32 v[62:63], v49 offset0:4 offset1:12
	ds_read2_b32 v[64:65], v49 offset0:69 offset1:77
	ds_read2_b32 v[66:67], v49 offset0:134 offset1:142
	ds_read2_b32 v[68:69], v49 offset0:199 offset1:207
	v_add_u32_e32 v72, s10, v7
	v_ashrrev_i32_e32 v73, 31, v72
	v_lshl_add_u64 v[70:71], s[12:13], 0, v[4:5]
	v_lshlrev_b64 v[72:73], 12, v[72:73]
	s_waitcnt lgkmcnt(6)
	v_cvt_pk_bf16_f32 v50, v56, v54
	s_waitcnt lgkmcnt(4)
	v_cvt_pk_bf16_f32 v51, v58, v60
	s_waitcnt lgkmcnt(2)
	v_cvt_pk_bf16_f32 v52, v62, v64
	s_waitcnt lgkmcnt(0)
	v_cvt_pk_bf16_f32 v53, v66, v68
	v_lshl_add_u64 v[72:73], v[70:71], 0, v[72:73]
	v_add_u32_e32 v54, s10, v12
	global_store_dwordx4 v[72:73], v[50:53], off
	s_mov_b64 s[12:13], 0
	s_nop 0
	v_cvt_pk_bf16_f32 v50, v57, v55
	v_ashrrev_i32_e32 v55, 31, v54
	v_cvt_pk_bf16_f32 v51, v59, v61
	v_cvt_pk_bf16_f32 v52, v63, v65
	v_cvt_pk_bf16_f32 v53, v67, v69
	v_lshlrev_b64 v[54:55], 12, v[54:55]
	ds_read2_b32 v[56:57], v11 offset0:81 offset1:89
	ds_read2_b32 v[58:59], v11 offset0:16 offset1:24
	ds_read2_b32 v[60:61], v11 offset0:146 offset1:154
	ds_read2_b32 v[62:63], v11 offset0:211 offset1:219
	ds_read2_b32 v[64:65], v49 offset0:20 offset1:28
	ds_read2_b32 v[66:67], v49 offset0:85 offset1:93
	ds_read2_b32 v[68:69], v49 offset0:150 offset1:158
	ds_read2_b32 v[72:73], v49 offset0:215 offset1:223
	v_lshl_add_u64 v[54:55], v[70:71], 0, v[54:55]
	global_store_dwordx4 v[54:55], v[50:53], off
	v_add_u32_e32 v54, s10, v13
	v_ashrrev_i32_e32 v55, 31, v54
	v_lshlrev_b64 v[54:55], 12, v[54:55]
	s_waitcnt lgkmcnt(6)
	v_cvt_pk_bf16_f32 v50, v58, v56
	s_waitcnt lgkmcnt(4)
	v_cvt_pk_bf16_f32 v51, v60, v62
	s_waitcnt lgkmcnt(2)
	v_cvt_pk_bf16_f32 v52, v64, v66
	s_waitcnt lgkmcnt(0)
	v_cvt_pk_bf16_f32 v53, v68, v72
	v_lshl_add_u64 v[54:55], v[70:71], 0, v[54:55]
	global_store_dwordx4 v[54:55], v[50:53], off
	v_add_u32_e32 v54, s10, v14
	v_ashrrev_i32_e32 v55, 31, v54
	v_cvt_pk_bf16_f32 v50, v59, v57
	v_cvt_pk_bf16_f32 v51, v61, v63
	v_cvt_pk_bf16_f32 v52, v65, v67
	v_cvt_pk_bf16_f32 v53, v69, v73
	v_lshlrev_b64 v[54:55], 12, v[54:55]
	ds_read2_b32 v[56:57], v11 offset0:32 offset1:40
	ds_read2_b32 v[58:59], v11 offset0:97 offset1:105
	ds_read2_b32 v[60:61], v11 offset0:162 offset1:170
	ds_read2_b32 v[62:63], v11 offset0:227 offset1:235
	ds_read2_b32 v[64:65], v49 offset0:36 offset1:44
	ds_read2_b32 v[66:67], v49 offset0:101 offset1:109
	ds_read2_b32 v[68:69], v49 offset0:166 offset1:174
	ds_read2_b32 v[72:73], v49 offset0:231 offset1:239
	v_lshl_add_u64 v[54:55], v[70:71], 0, v[54:55]
	global_store_dwordx4 v[54:55], v[50:53], off
	v_add_u32_e32 v54, s10, v15
	v_ashrrev_i32_e32 v55, 31, v54
	v_lshlrev_b64 v[54:55], 12, v[54:55]
	s_waitcnt lgkmcnt(6)
	v_cvt_pk_bf16_f32 v50, v56, v58
	s_waitcnt lgkmcnt(4)
	v_cvt_pk_bf16_f32 v51, v60, v62
	s_waitcnt lgkmcnt(2)
	v_cvt_pk_bf16_f32 v52, v64, v66
	s_waitcnt lgkmcnt(0)
	v_cvt_pk_bf16_f32 v53, v68, v72
	v_lshl_add_u64 v[54:55], v[70:71], 0, v[54:55]
	global_store_dwordx4 v[54:55], v[50:53], off
	v_add_u32_e32 v54, s10, v16
	v_ashrrev_i32_e32 v55, 31, v54
	v_cvt_pk_bf16_f32 v50, v57, v59
	v_cvt_pk_bf16_f32 v51, v61, v63
	v_cvt_pk_bf16_f32 v52, v65, v67
	v_cvt_pk_bf16_f32 v53, v69, v73
	v_lshlrev_b64 v[54:55], 12, v[54:55]
	ds_read2_b32 v[56:57], v11 offset0:48 offset1:56
	ds_read2_b32 v[58:59], v11 offset0:113 offset1:121
	ds_read2_b32 v[60:61], v11 offset0:178 offset1:186
	ds_read2_b32 v[62:63], v11 offset0:243 offset1:251
	ds_read2_b32 v[64:65], v49 offset0:52 offset1:60
	ds_read2_b32 v[66:67], v49 offset0:117 offset1:125
	ds_read2_b32 v[68:69], v49 offset0:182 offset1:190
	ds_read2_b32 v[72:73], v49 offset0:247 offset1:255
	v_lshl_add_u64 v[54:55], v[70:71], 0, v[54:55]
	global_store_dwordx4 v[54:55], v[50:53], off
	v_add_u32_e32 v54, s10, v17
	v_ashrrev_i32_e32 v55, 31, v54
	v_lshlrev_b64 v[54:55], 12, v[54:55]
	s_waitcnt lgkmcnt(6)
	v_cvt_pk_bf16_f32 v50, v56, v58
	s_waitcnt lgkmcnt(4)
	v_cvt_pk_bf16_f32 v51, v60, v62
	s_waitcnt lgkmcnt(2)
	v_cvt_pk_bf16_f32 v52, v64, v66
	s_waitcnt lgkmcnt(0)
	v_cvt_pk_bf16_f32 v53, v68, v72
	v_lshl_add_u64 v[54:55], v[70:71], 0, v[54:55]
	global_store_dwordx4 v[54:55], v[50:53], off
	v_add_u32_e32 v54, s10, v18
	v_ashrrev_i32_e32 v55, 31, v54
	v_lshlrev_b64 v[54:55], 12, v[54:55]
	v_cvt_pk_bf16_f32 v50, v57, v59
	v_cvt_pk_bf16_f32 v51, v61, v63
	v_cvt_pk_bf16_f32 v52, v65, v67
	v_cvt_pk_bf16_f32 v53, v69, v73
	v_lshl_add_u64 v[54:55], v[70:71], 0, v[54:55]
	global_store_dwordx4 v[54:55], v[50:53], off
	s_waitcnt lgkmcnt(0)
.LBB0_818:
	s_andn2_b64 vcc, exec, s[12:13]
	s_cbranch_vccnz .LBB0_820
	s_load_dwordx2 s[14:15], s[76:77], 0x88
	s_and_b32 s10, s7, 0xfc0
	s_addk_i32 s10, 0xf800
	s_and_b32 s12, s5, 0x3c0
	s_lshl_b64 s[50:51], s[10:11], 2
	v_add_u32_e32 v50, s12, v6
	s_waitcnt lgkmcnt(0)
	s_add_u32 s14, s14, s50
	s_addc_u32 s15, s15, s51
	v_ashrrev_i32_e32 v51, 31, v50
	v_lshl_add_u64 v[52:53], s[14:15], 0, v[0:1]
	v_lshlrev_b64 v[50:51], 13, v[50:51]
	v_lshl_add_u64 v[50:51], v[52:53], 0, v[50:51]
	v_add_co_u32_e32 v52, vcc, s9, v50
	s_lshl_b32 s12, s12, 1
	s_nop 0
	v_addc_co_u32_e32 v53, vcc, 0, v51, vcc
	v_add_co_u32_e32 v54, vcc, s16, v50
	s_mov_b32 s13, s11
	s_nop 0
	v_addc_co_u32_e32 v55, vcc, 0, v51, vcc
	v_add_co_u32_e32 v56, vcc, s17, v50
	s_nop 1
	v_addc_co_u32_e32 v57, vcc, 0, v51, vcc
	v_add_co_u32_e32 v60, vcc, s18, v50
	global_load_dwordx2 v[58:59], v[50:51], off nt
	s_nop 0
	global_load_dwordx2 v[52:53], v[52:53], off nt
	s_nop 0
	global_load_dwordx2 v[54:55], v[54:55], off nt
	s_nop 0
	global_load_dwordx2 v[56:57], v[56:57], off nt
	v_addc_co_u32_e32 v61, vcc, 0, v51, vcc
	v_add_co_u32_e32 v62, vcc, s19, v50
	s_nop 1
	v_addc_co_u32_e32 v63, vcc, 0, v51, vcc
	v_add_co_u32_e32 v64, vcc, s20, v50
	s_nop 1
	v_addc_co_u32_e32 v65, vcc, 0, v51, vcc
	v_add_co_u32_e32 v66, vcc, s21, v50
	s_nop 1
	v_addc_co_u32_e32 v67, vcc, 0, v51, vcc
	v_add_co_u32_e32 v68, vcc, s22, v50
	global_load_dwordx2 v[60:61], v[60:61], off nt
	s_nop 0
	global_load_dwordx2 v[62:63], v[62:63], off nt
	s_nop 0
	global_load_dwordx2 v[64:65], v[64:65], off nt
	s_nop 0
	global_load_dwordx2 v[66:67], v[66:67], off nt
	v_addc_co_u32_e32 v69, vcc, 0, v51, vcc
	v_add_co_u32_e32 v70, vcc, s23, v50
	s_nop 1
	v_addc_co_u32_e32 v71, vcc, 0, v51, vcc
	v_add_co_u32_e32 v72, vcc, s24, v50
	s_nop 1
	v_addc_co_u32_e32 v73, vcc, 0, v51, vcc
	v_add_co_u32_e32 v74, vcc, s25, v50
	s_nop 1
	v_addc_co_u32_e32 v75, vcc, 0, v51, vcc
	v_add_co_u32_e32 v76, vcc, s26, v50
	global_load_dwordx2 v[68:69], v[68:69], off nt
	s_nop 0
	global_load_dwordx2 v[70:71], v[70:71], off nt
	s_nop 0
	global_load_dwordx2 v[72:73], v[72:73], off nt
	s_nop 0
	global_load_dwordx2 v[74:75], v[74:75], off nt
	v_addc_co_u32_e32 v77, vcc, 0, v51, vcc
	v_add_co_u32_e32 v78, vcc, s27, v50
	s_nop 1
	v_addc_co_u32_e32 v79, vcc, 0, v51, vcc
	v_add_co_u32_e32 v80, vcc, s28, v50
	s_nop 1
	v_addc_co_u32_e32 v81, vcc, 0, v51, vcc
	v_add_co_u32_e32 v82, vcc, s29, v50
	s_nop 1
	v_addc_co_u32_e32 v83, vcc, 0, v51, vcc
	v_add_co_u32_e32 v84, vcc, s30, v50
	global_load_dwordx2 v[76:77], v[76:77], off nt
	s_nop 0
	global_load_dwordx2 v[78:79], v[78:79], off nt
	s_nop 0
	global_load_dwordx2 v[80:81], v[80:81], off nt
	s_nop 0
	global_load_dwordx2 v[82:83], v[82:83], off nt
	v_addc_co_u32_e32 v85, vcc, 0, v51, vcc
	v_add_co_u32_e32 v86, vcc, s31, v50
	s_nop 1
	v_addc_co_u32_e32 v87, vcc, 0, v51, vcc
	v_add_co_u32_e32 v88, vcc, s34, v50
	s_nop 1
	v_addc_co_u32_e32 v89, vcc, 0, v51, vcc
	v_add_co_u32_e32 v90, vcc, s35, v50
	s_nop 1
	v_addc_co_u32_e32 v91, vcc, 0, v51, vcc
	v_add_co_u32_e32 v92, vcc, s36, v50
	global_load_dwordx2 v[84:85], v[84:85], off nt
	s_nop 0
	global_load_dwordx2 v[86:87], v[86:87], off nt
	s_nop 0
	global_load_dwordx2 v[88:89], v[88:89], off nt
	s_nop 0
	global_load_dwordx2 v[90:91], v[90:91], off nt
	v_addc_co_u32_e32 v93, vcc, 0, v51, vcc
	v_add_co_u32_e32 v94, vcc, s37, v50
	s_nop 1
	v_addc_co_u32_e32 v95, vcc, 0, v51, vcc
	v_add_co_u32_e32 v96, vcc, s38, v50
	s_nop 1
	v_addc_co_u32_e32 v97, vcc, 0, v51, vcc
	v_add_co_u32_e32 v98, vcc, s39, v50
	s_nop 1
	v_addc_co_u32_e32 v99, vcc, 0, v51, vcc
	v_add_co_u32_e32 v100, vcc, s40, v50
	global_load_dwordx2 v[92:93], v[92:93], off nt
	s_nop 0
	global_load_dwordx2 v[94:95], v[94:95], off nt
	s_nop 0
	global_load_dwordx2 v[96:97], v[96:97], off nt
	s_nop 0
	global_load_dwordx2 v[98:99], v[98:99], off nt
	v_addc_co_u32_e32 v101, vcc, 0, v51, vcc
	v_add_co_u32_e32 v102, vcc, s41, v50
	s_nop 1
	v_addc_co_u32_e32 v103, vcc, 0, v51, vcc
	v_add_co_u32_e32 v104, vcc, s42, v50
	s_nop 1
	v_addc_co_u32_e32 v105, vcc, 0, v51, vcc
	v_add_co_u32_e32 v106, vcc, s43, v50
	s_nop 1
	v_addc_co_u32_e32 v107, vcc, 0, v51, vcc
	v_add_co_u32_e32 v108, vcc, s44, v50
	global_load_dwordx2 v[100:101], v[100:101], off nt
	s_nop 0
	global_load_dwordx2 v[102:103], v[102:103], off nt
	s_nop 0
	global_load_dwordx2 v[104:105], v[104:105], off nt
	s_nop 0
	global_load_dwordx2 v[106:107], v[106:107], off nt
	v_addc_co_u32_e32 v109, vcc, 0, v51, vcc
	v_add_co_u32_e32 v110, vcc, s45, v50
	s_nop 1
	v_addc_co_u32_e32 v111, vcc, 0, v51, vcc
	v_add_co_u32_e32 v112, vcc, s46, v50
	s_nop 1
	v_addc_co_u32_e32 v113, vcc, 0, v51, vcc
	v_add_co_u32_e32 v50, vcc, s47, v50
	s_nop 1
	v_addc_co_u32_e32 v51, vcc, 0, v51, vcc
	global_load_dwordx2 v[108:109], v[108:109], off nt
	s_nop 0
	global_load_dwordx2 v[110:111], v[110:111], off nt
	s_nop 0
	global_load_dwordx2 v[112:113], v[112:113], off nt
	s_nop 0
	global_load_dwordx2 v[50:51], v[50:51], off nt
	s_waitcnt vmcnt(0)
	ds_write2_b32 v10, v58, v59 offset1:1
	ds_write2_b32 v10, v52, v53 offset0:130 offset1:131
	ds_write2_b32 v19, v54, v55 offset1:1
	ds_write2_b32 v20, v56, v57 offset1:1
	ds_write2_b32 v21, v60, v61 offset1:1
	ds_write2_b32 v22, v62, v63 offset1:1
	ds_write2_b32 v23, v64, v65 offset1:1
	ds_write2_b32 v24, v66, v67 offset1:1
	ds_write2_b32 v25, v68, v69 offset1:1
	ds_write2_b32 v26, v70, v71 offset1:1
	ds_write2_b32 v27, v72, v73 offset1:1
	ds_write2_b32 v28, v74, v75 offset1:1
	ds_write2_b32 v29, v76, v77 offset1:1
	ds_write2_b32 v30, v78, v79 offset1:1
	ds_write2_b32 v31, v80, v81 offset1:1
	ds_write2_b32 v32, v82, v83 offset1:1
	ds_write2_b32 v33, v84, v85 offset1:1
	ds_write2_b32 v34, v86, v87 offset1:1
	ds_write2_b32 v35, v88, v89 offset1:1
	ds_write2_b32 v36, v90, v91 offset1:1
	ds_write2_b32 v37, v92, v93 offset1:1
	ds_write2_b32 v38, v94, v95 offset1:1
	ds_write2_b32 v39, v96, v97 offset1:1
	ds_write2_b32 v40, v98, v99 offset1:1
	ds_write2_b32 v41, v100, v101 offset1:1
	ds_write2_b32 v42, v102, v103 offset1:1
	ds_write2_b32 v43, v104, v105 offset1:1
	ds_write2_b32 v44, v106, v107 offset1:1
	ds_write2_b32 v45, v108, v109 offset1:1
	ds_write2_b32 v46, v110, v111 offset1:1
	ds_write2_b32 v47, v112, v113 offset1:1
	ds_write2_b32 v48, v50, v51 offset1:1
	s_waitcnt lgkmcnt(0)
	ds_read2_b32 v[54:55], v11 offset0:65 offset1:73
	ds_read2_b32 v[56:57], v11 offset1:8
	ds_read2_b32 v[58:59], v11 offset0:130 offset1:138
	ds_read2_b32 v[60:61], v11 offset0:195 offset1:203
	ds_read2_b32 v[62:63], v49 offset0:4 offset1:12
	ds_read2_b32 v[64:65], v49 offset0:69 offset1:77
	ds_read2_b32 v[66:67], v49 offset0:134 offset1:142
	ds_read2_b32 v[68:69], v49 offset0:199 offset1:207
	v_add_u32_e32 v72, s10, v7
	v_ashrrev_i32_e32 v73, 31, v72
	v_lshl_add_u64 v[70:71], v[2:3], 0, s[12:13]
	v_lshlrev_b64 v[72:73], 12, v[72:73]
	s_waitcnt lgkmcnt(6)
	v_cvt_pk_bf16_f32 v50, v56, v54
	s_waitcnt lgkmcnt(4)
	v_cvt_pk_bf16_f32 v51, v58, v60
	s_waitcnt lgkmcnt(2)
	v_cvt_pk_bf16_f32 v52, v62, v64
	s_waitcnt lgkmcnt(0)
	v_cvt_pk_bf16_f32 v53, v66, v68
	v_lshl_add_u64 v[72:73], v[70:71], 0, v[72:73]
	v_add_u32_e32 v54, s10, v12
	global_store_dwordx4 v[72:73], v[50:53], off offset:2048
	s_nop 1
	v_cvt_pk_bf16_f32 v50, v57, v55
	v_ashrrev_i32_e32 v55, 31, v54
	v_cvt_pk_bf16_f32 v51, v59, v61
	v_cvt_pk_bf16_f32 v52, v63, v65
	v_cvt_pk_bf16_f32 v53, v67, v69
	v_lshlrev_b64 v[54:55], 12, v[54:55]
	ds_read2_b32 v[56:57], v11 offset0:81 offset1:89
	ds_read2_b32 v[58:59], v11 offset0:16 offset1:24
	ds_read2_b32 v[60:61], v11 offset0:146 offset1:154
	ds_read2_b32 v[62:63], v11 offset0:211 offset1:219
	ds_read2_b32 v[64:65], v49 offset0:20 offset1:28
	ds_read2_b32 v[66:67], v49 offset0:85 offset1:93
	ds_read2_b32 v[68:69], v49 offset0:150 offset1:158
	ds_read2_b32 v[72:73], v49 offset0:215 offset1:223
	v_lshl_add_u64 v[54:55], v[70:71], 0, v[54:55]
	global_store_dwordx4 v[54:55], v[50:53], off offset:2048
	v_add_u32_e32 v54, s10, v13
	v_ashrrev_i32_e32 v55, 31, v54
	v_lshlrev_b64 v[54:55], 12, v[54:55]
	s_waitcnt lgkmcnt(6)
	v_cvt_pk_bf16_f32 v50, v58, v56
	s_waitcnt lgkmcnt(4)
	v_cvt_pk_bf16_f32 v51, v60, v62
	s_waitcnt lgkmcnt(2)
	v_cvt_pk_bf16_f32 v52, v64, v66
	s_waitcnt lgkmcnt(0)
	v_cvt_pk_bf16_f32 v53, v68, v72
	v_lshl_add_u64 v[54:55], v[70:71], 0, v[54:55]
	global_store_dwordx4 v[54:55], v[50:53], off offset:2048
	v_add_u32_e32 v54, s10, v14
	v_ashrrev_i32_e32 v55, 31, v54
	v_cvt_pk_bf16_f32 v50, v59, v57
	v_cvt_pk_bf16_f32 v51, v61, v63
	v_cvt_pk_bf16_f32 v52, v65, v67
	v_cvt_pk_bf16_f32 v53, v69, v73
	v_lshlrev_b64 v[54:55], 12, v[54:55]
	ds_read2_b32 v[56:57], v11 offset0:32 offset1:40
	ds_read2_b32 v[58:59], v11 offset0:97 offset1:105
	ds_read2_b32 v[60:61], v11 offset0:162 offset1:170
	ds_read2_b32 v[62:63], v11 offset0:227 offset1:235
	ds_read2_b32 v[64:65], v49 offset0:36 offset1:44
	ds_read2_b32 v[66:67], v49 offset0:101 offset1:109
	ds_read2_b32 v[68:69], v49 offset0:166 offset1:174
	ds_read2_b32 v[72:73], v49 offset0:231 offset1:239
	v_lshl_add_u64 v[54:55], v[70:71], 0, v[54:55]
	global_store_dwordx4 v[54:55], v[50:53], off offset:2048
	v_add_u32_e32 v54, s10, v15
	v_ashrrev_i32_e32 v55, 31, v54
	v_lshlrev_b64 v[54:55], 12, v[54:55]
	s_waitcnt lgkmcnt(6)
	v_cvt_pk_bf16_f32 v50, v56, v58
	s_waitcnt lgkmcnt(4)
	v_cvt_pk_bf16_f32 v51, v60, v62
	s_waitcnt lgkmcnt(2)
	v_cvt_pk_bf16_f32 v52, v64, v66
	s_waitcnt lgkmcnt(0)
	v_cvt_pk_bf16_f32 v53, v68, v72
	v_lshl_add_u64 v[54:55], v[70:71], 0, v[54:55]
	global_store_dwordx4 v[54:55], v[50:53], off offset:2048
	v_add_u32_e32 v54, s10, v16
	v_ashrrev_i32_e32 v55, 31, v54
	v_cvt_pk_bf16_f32 v50, v57, v59
	v_cvt_pk_bf16_f32 v51, v61, v63
	v_cvt_pk_bf16_f32 v52, v65, v67
	v_cvt_pk_bf16_f32 v53, v69, v73
	v_lshlrev_b64 v[54:55], 12, v[54:55]
	ds_read2_b32 v[56:57], v11 offset0:48 offset1:56
	ds_read2_b32 v[58:59], v11 offset0:113 offset1:121
	ds_read2_b32 v[60:61], v11 offset0:178 offset1:186
	ds_read2_b32 v[62:63], v11 offset0:243 offset1:251
	ds_read2_b32 v[64:65], v49 offset0:52 offset1:60
	ds_read2_b32 v[66:67], v49 offset0:117 offset1:125
	ds_read2_b32 v[68:69], v49 offset0:182 offset1:190
	ds_read2_b32 v[72:73], v49 offset0:247 offset1:255
	v_lshl_add_u64 v[54:55], v[70:71], 0, v[54:55]
	global_store_dwordx4 v[54:55], v[50:53], off offset:2048
	v_add_u32_e32 v54, s10, v17
	v_ashrrev_i32_e32 v55, 31, v54
	v_lshlrev_b64 v[54:55], 12, v[54:55]
	s_waitcnt lgkmcnt(6)
	v_cvt_pk_bf16_f32 v50, v56, v58
	s_waitcnt lgkmcnt(4)
	v_cvt_pk_bf16_f32 v51, v60, v62
	s_waitcnt lgkmcnt(2)
	v_cvt_pk_bf16_f32 v52, v64, v66
	s_waitcnt lgkmcnt(0)
	v_cvt_pk_bf16_f32 v53, v68, v72
	v_lshl_add_u64 v[54:55], v[70:71], 0, v[54:55]
	global_store_dwordx4 v[54:55], v[50:53], off offset:2048
	v_add_u32_e32 v54, s10, v18
	v_ashrrev_i32_e32 v55, 31, v54
	v_lshlrev_b64 v[54:55], 12, v[54:55]
	v_cvt_pk_bf16_f32 v50, v57, v59
	v_cvt_pk_bf16_f32 v51, v61, v63
	v_cvt_pk_bf16_f32 v52, v65, v67
	v_cvt_pk_bf16_f32 v53, v69, v73
	v_lshl_add_u64 v[54:55], v[70:71], 0, v[54:55]
	global_store_dwordx4 v[54:55], v[50:53], off offset:2048
	s_waitcnt lgkmcnt(0)

.LBB0_821:
	s_andn2_b64 vcc, exec, s[12:13]
	s_cbranch_vccnz .LBB0_823
	s_load_dwordx2 s[14:15], s[76:77], 0x80
	s_and_b32 s10, s8, 0xfc0
	s_addk_i32 s10, 0xf800
	s_and_b32 s12, s5, 0x1c0
	s_lshl_b64 s[50:51], s[10:11], 2
	v_add_u32_e32 v50, s12, v6
	s_waitcnt lgkmcnt(0)
	s_add_u32 s14, s14, s50
	s_addc_u32 s15, s15, s51
	v_ashrrev_i32_e32 v51, 31, v50
	v_lshl_add_u64 v[52:53], s[14:15], 0, v[0:1]
	v_lshlrev_b64 v[50:51], 13, v[50:51]
	v_lshl_add_u64 v[50:51], v[52:53], 0, v[50:51]
	v_add_co_u32_e32 v52, vcc, s9, v50
	s_lshl_b32 s12, s12, 1
	s_nop 0
	v_addc_co_u32_e32 v53, vcc, 0, v51, vcc
	v_add_co_u32_e32 v54, vcc, s16, v50
	s_mov_b32 s13, s11
	s_nop 0
	v_addc_co_u32_e32 v55, vcc, 0, v51, vcc
	v_add_co_u32_e32 v56, vcc, s17, v50
	s_nop 1
	v_addc_co_u32_e32 v57, vcc, 0, v51, vcc
	v_add_co_u32_e32 v60, vcc, s18, v50
	global_load_dwordx2 v[58:59], v[50:51], off nt
	s_nop 0
	global_load_dwordx2 v[52:53], v[52:53], off nt
	s_nop 0
	global_load_dwordx2 v[54:55], v[54:55], off nt
	s_nop 0
	global_load_dwordx2 v[56:57], v[56:57], off nt
	v_addc_co_u32_e32 v61, vcc, 0, v51, vcc
	v_add_co_u32_e32 v62, vcc, s19, v50
	s_nop 1
	v_addc_co_u32_e32 v63, vcc, 0, v51, vcc
	v_add_co_u32_e32 v64, vcc, s20, v50
	s_nop 1
	v_addc_co_u32_e32 v65, vcc, 0, v51, vcc
	v_add_co_u32_e32 v66, vcc, s21, v50
	s_nop 1
	v_addc_co_u32_e32 v67, vcc, 0, v51, vcc
	v_add_co_u32_e32 v68, vcc, s22, v50
	global_load_dwordx2 v[60:61], v[60:61], off nt
	s_nop 0
	global_load_dwordx2 v[62:63], v[62:63], off nt
	s_nop 0
	global_load_dwordx2 v[64:65], v[64:65], off nt
	s_nop 0
	global_load_dwordx2 v[66:67], v[66:67], off nt
	v_addc_co_u32_e32 v69, vcc, 0, v51, vcc
	v_add_co_u32_e32 v70, vcc, s23, v50
	s_nop 1
	v_addc_co_u32_e32 v71, vcc, 0, v51, vcc
	v_add_co_u32_e32 v72, vcc, s24, v50
	s_nop 1
	v_addc_co_u32_e32 v73, vcc, 0, v51, vcc
	v_add_co_u32_e32 v74, vcc, s25, v50
	s_nop 1
	v_addc_co_u32_e32 v75, vcc, 0, v51, vcc
	v_add_co_u32_e32 v76, vcc, s26, v50
	global_load_dwordx2 v[68:69], v[68:69], off nt
	s_nop 0
	global_load_dwordx2 v[70:71], v[70:71], off nt
	s_nop 0
	global_load_dwordx2 v[72:73], v[72:73], off nt
	s_nop 0
	global_load_dwordx2 v[74:75], v[74:75], off nt
	v_addc_co_u32_e32 v77, vcc, 0, v51, vcc
	v_add_co_u32_e32 v78, vcc, s27, v50
	s_nop 1
	v_addc_co_u32_e32 v79, vcc, 0, v51, vcc
	v_add_co_u32_e32 v80, vcc, s28, v50
	s_nop 1
	v_addc_co_u32_e32 v81, vcc, 0, v51, vcc
	v_add_co_u32_e32 v82, vcc, s29, v50
	s_nop 1
	v_addc_co_u32_e32 v83, vcc, 0, v51, vcc
	v_add_co_u32_e32 v84, vcc, s30, v50
	global_load_dwordx2 v[76:77], v[76:77], off nt
	s_nop 0
	global_load_dwordx2 v[78:79], v[78:79], off nt
	s_nop 0
	global_load_dwordx2 v[80:81], v[80:81], off nt
	s_nop 0
	global_load_dwordx2 v[82:83], v[82:83], off nt
	v_addc_co_u32_e32 v85, vcc, 0, v51, vcc
	v_add_co_u32_e32 v86, vcc, s31, v50
	s_nop 1
	v_addc_co_u32_e32 v87, vcc, 0, v51, vcc
	v_add_co_u32_e32 v88, vcc, s34, v50
	s_nop 1
	v_addc_co_u32_e32 v89, vcc, 0, v51, vcc
	v_add_co_u32_e32 v90, vcc, s35, v50
	s_nop 1
	v_addc_co_u32_e32 v91, vcc, 0, v51, vcc
	v_add_co_u32_e32 v92, vcc, s36, v50
	global_load_dwordx2 v[84:85], v[84:85], off nt
	s_nop 0
	global_load_dwordx2 v[86:87], v[86:87], off nt
	s_nop 0
	global_load_dwordx2 v[88:89], v[88:89], off nt
	s_nop 0
	global_load_dwordx2 v[90:91], v[90:91], off nt
	v_addc_co_u32_e32 v93, vcc, 0, v51, vcc
	v_add_co_u32_e32 v94, vcc, s37, v50
	s_nop 1
	v_addc_co_u32_e32 v95, vcc, 0, v51, vcc
	v_add_co_u32_e32 v96, vcc, s38, v50
	s_nop 1
	v_addc_co_u32_e32 v97, vcc, 0, v51, vcc
	v_add_co_u32_e32 v98, vcc, s39, v50
	s_nop 1
	v_addc_co_u32_e32 v99, vcc, 0, v51, vcc
	v_add_co_u32_e32 v100, vcc, s40, v50
	global_load_dwordx2 v[92:93], v[92:93], off nt
	s_nop 0
	global_load_dwordx2 v[94:95], v[94:95], off nt
	s_nop 0
	global_load_dwordx2 v[96:97], v[96:97], off nt
	s_nop 0
	global_load_dwordx2 v[98:99], v[98:99], off nt
	v_addc_co_u32_e32 v101, vcc, 0, v51, vcc
	v_add_co_u32_e32 v102, vcc, s41, v50
	s_nop 1
	v_addc_co_u32_e32 v103, vcc, 0, v51, vcc
	v_add_co_u32_e32 v104, vcc, s42, v50
	s_nop 1
	v_addc_co_u32_e32 v105, vcc, 0, v51, vcc
	v_add_co_u32_e32 v106, vcc, s43, v50
	s_nop 1
	v_addc_co_u32_e32 v107, vcc, 0, v51, vcc
	v_add_co_u32_e32 v108, vcc, s44, v50
	global_load_dwordx2 v[100:101], v[100:101], off nt
	s_nop 0
	global_load_dwordx2 v[102:103], v[102:103], off nt
	s_nop 0
	global_load_dwordx2 v[104:105], v[104:105], off nt
	s_nop 0
	global_load_dwordx2 v[106:107], v[106:107], off nt
	v_addc_co_u32_e32 v109, vcc, 0, v51, vcc
	v_add_co_u32_e32 v110, vcc, s45, v50
	s_nop 1
	v_addc_co_u32_e32 v111, vcc, 0, v51, vcc
	v_add_co_u32_e32 v112, vcc, s46, v50
	s_nop 1
	v_addc_co_u32_e32 v113, vcc, 0, v51, vcc
	v_add_co_u32_e32 v50, vcc, s47, v50
	s_nop 1
	v_addc_co_u32_e32 v51, vcc, 0, v51, vcc
	global_load_dwordx2 v[108:109], v[108:109], off nt
	s_nop 0
	global_load_dwordx2 v[110:111], v[110:111], off nt
	s_nop 0
	global_load_dwordx2 v[112:113], v[112:113], off nt
	s_nop 0
	global_load_dwordx2 v[50:51], v[50:51], off nt
	s_waitcnt vmcnt(0)
	ds_write2_b32 v10, v58, v59 offset1:1
	ds_write2_b32 v10, v52, v53 offset0:130 offset1:131
	ds_write2_b32 v19, v54, v55 offset1:1
	ds_write2_b32 v20, v56, v57 offset1:1
	ds_write2_b32 v21, v60, v61 offset1:1
	ds_write2_b32 v22, v62, v63 offset1:1
	ds_write2_b32 v23, v64, v65 offset1:1
	ds_write2_b32 v24, v66, v67 offset1:1
	ds_write2_b32 v25, v68, v69 offset1:1
	ds_write2_b32 v26, v70, v71 offset1:1
	ds_write2_b32 v27, v72, v73 offset1:1
	ds_write2_b32 v28, v74, v75 offset1:1
	ds_write2_b32 v29, v76, v77 offset1:1
	ds_write2_b32 v30, v78, v79 offset1:1
	ds_write2_b32 v31, v80, v81 offset1:1
	ds_write2_b32 v32, v82, v83 offset1:1
	ds_write2_b32 v33, v84, v85 offset1:1
	ds_write2_b32 v34, v86, v87 offset1:1
	ds_write2_b32 v35, v88, v89 offset1:1
	ds_write2_b32 v36, v90, v91 offset1:1
	ds_write2_b32 v37, v92, v93 offset1:1
	ds_write2_b32 v38, v94, v95 offset1:1
	ds_write2_b32 v39, v96, v97 offset1:1
	ds_write2_b32 v40, v98, v99 offset1:1
	ds_write2_b32 v41, v100, v101 offset1:1
	ds_write2_b32 v42, v102, v103 offset1:1
	ds_write2_b32 v43, v104, v105 offset1:1
	ds_write2_b32 v44, v106, v107 offset1:1
	ds_write2_b32 v45, v108, v109 offset1:1
	ds_write2_b32 v46, v110, v111 offset1:1
	ds_write2_b32 v47, v112, v113 offset1:1
	ds_write2_b32 v48, v50, v51 offset1:1
	s_waitcnt lgkmcnt(0)
	ds_read2_b32 v[54:55], v11 offset0:65 offset1:73
	ds_read2_b32 v[56:57], v11 offset1:8
	ds_read2_b32 v[58:59], v11 offset0:130 offset1:138
	ds_read2_b32 v[60:61], v11 offset0:195 offset1:203
	ds_read2_b32 v[62:63], v49 offset0:4 offset1:12
	ds_read2_b32 v[64:65], v49 offset0:69 offset1:77
	ds_read2_b32 v[66:67], v49 offset0:134 offset1:142
	ds_read2_b32 v[68:69], v49 offset0:199 offset1:207
	v_add_u32_e32 v72, s10, v7
	v_ashrrev_i32_e32 v73, 31, v72
	v_lshl_add_u64 v[70:71], v[2:3], 0, s[12:13]
	v_lshlrev_b64 v[72:73], 12, v[72:73]
	s_waitcnt lgkmcnt(6)
	v_cvt_pk_bf16_f32 v50, v56, v54
	s_waitcnt lgkmcnt(4)
	v_cvt_pk_bf16_f32 v51, v58, v60
	s_waitcnt lgkmcnt(2)
	v_cvt_pk_bf16_f32 v52, v62, v64
	s_waitcnt lgkmcnt(0)
	v_cvt_pk_bf16_f32 v53, v66, v68
	v_lshl_add_u64 v[72:73], v[70:71], 0, v[72:73]
	v_add_u32_e32 v54, s10, v12
	global_store_dwordx4 v[72:73], v[50:53], off offset:1024
	s_nop 1
	v_cvt_pk_bf16_f32 v50, v57, v55
	v_ashrrev_i32_e32 v55, 31, v54
	v_cvt_pk_bf16_f32 v51, v59, v61
	v_cvt_pk_bf16_f32 v52, v63, v65
	v_cvt_pk_bf16_f32 v53, v67, v69
	v_lshlrev_b64 v[54:55], 12, v[54:55]
	ds_read2_b32 v[56:57], v11 offset0:81 offset1:89
	ds_read2_b32 v[58:59], v11 offset0:16 offset1:24
	ds_read2_b32 v[60:61], v11 offset0:146 offset1:154
	ds_read2_b32 v[62:63], v11 offset0:211 offset1:219
	ds_read2_b32 v[64:65], v49 offset0:20 offset1:28
	ds_read2_b32 v[66:67], v49 offset0:85 offset1:93
	ds_read2_b32 v[68:69], v49 offset0:150 offset1:158
	ds_read2_b32 v[72:73], v49 offset0:215 offset1:223
	v_lshl_add_u64 v[54:55], v[70:71], 0, v[54:55]
	global_store_dwordx4 v[54:55], v[50:53], off offset:1024
	v_add_u32_e32 v54, s10, v13
	v_ashrrev_i32_e32 v55, 31, v54
	v_lshlrev_b64 v[54:55], 12, v[54:55]
	s_waitcnt lgkmcnt(6)
	v_cvt_pk_bf16_f32 v50, v58, v56
	s_waitcnt lgkmcnt(4)
	v_cvt_pk_bf16_f32 v51, v60, v62
	s_waitcnt lgkmcnt(2)
	v_cvt_pk_bf16_f32 v52, v64, v66
	s_waitcnt lgkmcnt(0)
	v_cvt_pk_bf16_f32 v53, v68, v72
	v_lshl_add_u64 v[54:55], v[70:71], 0, v[54:55]
	global_store_dwordx4 v[54:55], v[50:53], off offset:1024
	v_add_u32_e32 v54, s10, v14
	v_ashrrev_i32_e32 v55, 31, v54
	v_cvt_pk_bf16_f32 v50, v59, v57
	v_cvt_pk_bf16_f32 v51, v61, v63
	v_cvt_pk_bf16_f32 v52, v65, v67
	v_cvt_pk_bf16_f32 v53, v69, v73
	v_lshlrev_b64 v[54:55], 12, v[54:55]
	ds_read2_b32 v[56:57], v11 offset0:32 offset1:40
	ds_read2_b32 v[58:59], v11 offset0:97 offset1:105
	ds_read2_b32 v[60:61], v11 offset0:162 offset1:170
	ds_read2_b32 v[62:63], v11 offset0:227 offset1:235
	ds_read2_b32 v[64:65], v49 offset0:36 offset1:44
	ds_read2_b32 v[66:67], v49 offset0:101 offset1:109
	ds_read2_b32 v[68:69], v49 offset0:166 offset1:174
	ds_read2_b32 v[72:73], v49 offset0:231 offset1:239
	v_lshl_add_u64 v[54:55], v[70:71], 0, v[54:55]
	global_store_dwordx4 v[54:55], v[50:53], off offset:1024
	v_add_u32_e32 v54, s10, v15
	v_ashrrev_i32_e32 v55, 31, v54
	v_lshlrev_b64 v[54:55], 12, v[54:55]
	s_waitcnt lgkmcnt(6)
	v_cvt_pk_bf16_f32 v50, v56, v58
	s_waitcnt lgkmcnt(4)
	v_cvt_pk_bf16_f32 v51, v60, v62
	s_waitcnt lgkmcnt(2)
	v_cvt_pk_bf16_f32 v52, v64, v66
	s_waitcnt lgkmcnt(0)
	v_cvt_pk_bf16_f32 v53, v68, v72
	v_lshl_add_u64 v[54:55], v[70:71], 0, v[54:55]
	global_store_dwordx4 v[54:55], v[50:53], off offset:1024
	v_add_u32_e32 v54, s10, v16
	v_ashrrev_i32_e32 v55, 31, v54
	v_cvt_pk_bf16_f32 v50, v57, v59
	v_cvt_pk_bf16_f32 v51, v61, v63
	v_cvt_pk_bf16_f32 v52, v65, v67
	v_cvt_pk_bf16_f32 v53, v69, v73
	v_lshlrev_b64 v[54:55], 12, v[54:55]
	ds_read2_b32 v[56:57], v11 offset0:48 offset1:56
	ds_read2_b32 v[58:59], v11 offset0:113 offset1:121
	ds_read2_b32 v[60:61], v11 offset0:178 offset1:186
	ds_read2_b32 v[62:63], v11 offset0:243 offset1:251
	ds_read2_b32 v[64:65], v49 offset0:52 offset1:60
	ds_read2_b32 v[66:67], v49 offset0:117 offset1:125
	ds_read2_b32 v[68:69], v49 offset0:182 offset1:190
	ds_read2_b32 v[72:73], v49 offset0:247 offset1:255
	v_lshl_add_u64 v[54:55], v[70:71], 0, v[54:55]
	global_store_dwordx4 v[54:55], v[50:53], off offset:1024
	v_add_u32_e32 v54, s10, v17
	v_ashrrev_i32_e32 v55, 31, v54
	v_lshlrev_b64 v[54:55], 12, v[54:55]
	s_waitcnt lgkmcnt(6)
	v_cvt_pk_bf16_f32 v50, v56, v58
	s_waitcnt lgkmcnt(4)
	v_cvt_pk_bf16_f32 v51, v60, v62
	s_waitcnt lgkmcnt(2)
	v_cvt_pk_bf16_f32 v52, v64, v66
	s_waitcnt lgkmcnt(0)
	v_cvt_pk_bf16_f32 v53, v68, v72
	v_lshl_add_u64 v[54:55], v[70:71], 0, v[54:55]
	global_store_dwordx4 v[54:55], v[50:53], off offset:1024
	v_add_u32_e32 v54, s10, v18
	v_ashrrev_i32_e32 v55, 31, v54
	v_lshlrev_b64 v[54:55], 12, v[54:55]
	v_cvt_pk_bf16_f32 v50, v57, v59
	v_cvt_pk_bf16_f32 v51, v61, v63
	v_cvt_pk_bf16_f32 v52, v65, v67
	v_cvt_pk_bf16_f32 v53, v69, v73
	v_lshl_add_u64 v[54:55], v[70:71], 0, v[54:55]
	global_store_dwordx4 v[54:55], v[50:53], off offset:1024
	s_waitcnt lgkmcnt(0)

.LBB0_824:
	s_andn2_b64 vcc, exec, s[12:13]
	s_cbranch_vccnz .LBB0_813
	s_ashr_i32 s10, s48, 31
	s_lshr_b32 s10, s10, 29
	s_add_i32 s10, s48, s10
	s_ashr_i32 s10, s10, 3
	s_load_dwordx2 s[50:51], s[76:77], 0x78
	s_lshl_b32 s12, s10, 6
	s_lshl_b32 s10, s10, 9
	s_sub_i32 s14, s5, s10
	v_add_u32_e32 v50, s14, v6
	s_ashr_i32 s13, s12, 31
	s_lshl_b64 s[52:53], s[12:13], 2
	v_ashrrev_i32_e32 v51, 31, v50
	s_waitcnt lgkmcnt(0)
	s_add_u32 s50, s50, s52
	v_lshlrev_b64 v[54:55], 13, v[50:51]
	v_add_u32_e32 v56, 2, v50
	v_add_u32_e32 v58, 4, v50
	v_add_u32_e32 v60, 6, v50
	v_add_u32_e32 v62, 8, v50
	v_add_u32_e32 v64, 10, v50
	v_add_u32_e32 v66, 12, v50
	v_add_u32_e32 v68, 14, v50
	v_add_u32_e32 v70, 16, v50
	v_add_u32_e32 v72, 18, v50
	v_add_u32_e32 v74, 20, v50
	v_add_u32_e32 v76, 22, v50
	v_add_u32_e32 v78, 24, v50
	v_add_u32_e32 v80, 26, v50
	v_add_u32_e32 v82, 28, v50
	v_add_u32_e32 v84, 30, v50
	v_add_u32_e32 v86, 32, v50
	v_add_u32_e32 v88, 34, v50
	v_add_u32_e32 v90, 36, v50
	v_add_u32_e32 v92, 38, v50
	v_add_u32_e32 v94, 40, v50
	v_add_u32_e32 v96, 42, v50
	v_add_u32_e32 v98, 44, v50
	v_add_u32_e32 v100, 46, v50
	v_add_u32_e32 v102, 48, v50
	v_add_u32_e32 v104, 50, v50
	v_add_u32_e32 v106, 52, v50
	v_add_u32_e32 v108, 54, v50
	v_add_u32_e32 v110, 56, v50
	v_add_u32_e32 v112, 58, v50
	v_add_u32_e32 v114, 60, v50
	v_add_u32_e32 v50, 62, v50
	s_addc_u32 s51, s51, s53
	v_ashrrev_i32_e32 v57, 31, v56
	v_ashrrev_i32_e32 v59, 31, v58
	v_ashrrev_i32_e32 v61, 31, v60
	v_ashrrev_i32_e32 v63, 31, v62
	v_ashrrev_i32_e32 v65, 31, v64
	v_ashrrev_i32_e32 v67, 31, v66
	v_ashrrev_i32_e32 v69, 31, v68
	v_ashrrev_i32_e32 v71, 31, v70
	v_ashrrev_i32_e32 v73, 31, v72
	v_ashrrev_i32_e32 v75, 31, v74
	v_ashrrev_i32_e32 v77, 31, v76
	v_ashrrev_i32_e32 v79, 31, v78
	v_ashrrev_i32_e32 v81, 31, v80
	v_ashrrev_i32_e32 v83, 31, v82
	v_ashrrev_i32_e32 v85, 31, v84
	v_ashrrev_i32_e32 v87, 31, v86
	v_ashrrev_i32_e32 v89, 31, v88
	v_ashrrev_i32_e32 v91, 31, v90
	v_ashrrev_i32_e32 v93, 31, v92
	v_ashrrev_i32_e32 v95, 31, v94
	v_ashrrev_i32_e32 v97, 31, v96
	v_ashrrev_i32_e32 v99, 31, v98
	v_ashrrev_i32_e32 v101, 31, v100
	v_ashrrev_i32_e32 v103, 31, v102
	v_ashrrev_i32_e32 v105, 31, v104
	v_ashrrev_i32_e32 v107, 31, v106
	v_ashrrev_i32_e32 v109, 31, v108
	v_ashrrev_i32_e32 v111, 31, v110
	v_ashrrev_i32_e32 v113, 31, v112
	v_ashrrev_i32_e32 v51, 31, v50
	v_lshl_add_u64 v[52:53], s[50:51], 0, v[0:1]
	v_lshlrev_b64 v[56:57], 13, v[56:57]
	v_lshlrev_b64 v[58:59], 13, v[58:59]
	v_lshlrev_b64 v[60:61], 13, v[60:61]
	v_lshlrev_b64 v[62:63], 13, v[62:63]
	v_lshlrev_b64 v[64:65], 13, v[64:65]
	v_lshlrev_b64 v[66:67], 13, v[66:67]
	v_lshlrev_b64 v[68:69], 13, v[68:69]
	v_lshlrev_b64 v[70:71], 13, v[70:71]
	v_lshlrev_b64 v[72:73], 13, v[72:73]
	v_lshlrev_b64 v[74:75], 13, v[74:75]
	v_lshlrev_b64 v[76:77], 13, v[76:77]
	v_lshlrev_b64 v[78:79], 13, v[78:79]
	v_lshlrev_b64 v[80:81], 13, v[80:81]
	v_lshlrev_b64 v[82:83], 13, v[82:83]
	v_lshlrev_b64 v[84:85], 13, v[84:85]
	v_lshlrev_b64 v[86:87], 13, v[86:87]
	v_lshlrev_b64 v[88:89], 13, v[88:89]
	v_lshlrev_b64 v[90:91], 13, v[90:91]
	v_lshlrev_b64 v[92:93], 13, v[92:93]
	v_lshlrev_b64 v[94:95], 13, v[94:95]
	v_lshlrev_b64 v[96:97], 13, v[96:97]
	v_lshlrev_b64 v[98:99], 13, v[98:99]
	v_lshlrev_b64 v[100:101], 13, v[100:101]
	v_lshlrev_b64 v[102:103], 13, v[102:103]
	v_lshlrev_b64 v[104:105], 13, v[104:105]
	v_lshlrev_b64 v[106:107], 13, v[106:107]
	v_lshlrev_b64 v[108:109], 13, v[108:109]
	v_lshlrev_b64 v[110:111], 13, v[110:111]
	v_lshlrev_b64 v[112:113], 13, v[112:113]
	v_ashrrev_i32_e32 v115, 31, v114
	v_lshlrev_b64 v[50:51], 13, v[50:51]
	v_lshl_add_u64 v[54:55], v[52:53], 0, v[54:55]
	v_lshl_add_u64 v[56:57], v[52:53], 0, v[56:57]
	v_lshl_add_u64 v[58:59], v[52:53], 0, v[58:59]
	v_lshl_add_u64 v[60:61], v[52:53], 0, v[60:61]
	v_lshl_add_u64 v[62:63], v[52:53], 0, v[62:63]
	v_lshl_add_u64 v[64:65], v[52:53], 0, v[64:65]
	v_lshl_add_u64 v[66:67], v[52:53], 0, v[66:67]
	v_lshl_add_u64 v[68:69], v[52:53], 0, v[68:69]
	v_lshl_add_u64 v[70:71], v[52:53], 0, v[70:71]
	v_lshl_add_u64 v[72:73], v[52:53], 0, v[72:73]
	v_lshl_add_u64 v[74:75], v[52:53], 0, v[74:75]
	v_lshl_add_u64 v[76:77], v[52:53], 0, v[76:77]
	v_lshl_add_u64 v[78:79], v[52:53], 0, v[78:79]
	v_lshl_add_u64 v[80:81], v[52:53], 0, v[80:81]
	v_lshl_add_u64 v[82:83], v[52:53], 0, v[82:83]
	v_lshl_add_u64 v[84:85], v[52:53], 0, v[84:85]
	v_lshl_add_u64 v[86:87], v[52:53], 0, v[86:87]
	v_lshl_add_u64 v[88:89], v[52:53], 0, v[88:89]
	v_lshl_add_u64 v[90:91], v[52:53], 0, v[90:91]
	v_lshl_add_u64 v[92:93], v[52:53], 0, v[92:93]
	v_lshl_add_u64 v[94:95], v[52:53], 0, v[94:95]
	v_lshl_add_u64 v[96:97], v[52:53], 0, v[96:97]
	v_lshl_add_u64 v[98:99], v[52:53], 0, v[98:99]
	v_lshl_add_u64 v[100:101], v[52:53], 0, v[100:101]
	v_lshl_add_u64 v[102:103], v[52:53], 0, v[102:103]
	v_lshl_add_u64 v[104:105], v[52:53], 0, v[104:105]
	v_lshl_add_u64 v[106:107], v[52:53], 0, v[106:107]
	v_lshl_add_u64 v[108:109], v[52:53], 0, v[108:109]
	v_lshl_add_u64 v[110:111], v[52:53], 0, v[110:111]
	v_lshl_add_u64 v[112:113], v[52:53], 0, v[112:113]
	v_lshlrev_b64 v[114:115], 13, v[114:115]
	v_lshl_add_u64 v[50:51], v[52:53], 0, v[50:51]
	global_load_dwordx2 v[54:55], v[54:55], off nt
	s_nop 0
	global_load_dwordx2 v[56:57], v[56:57], off nt
	s_nop 0
	global_load_dwordx2 v[58:59], v[58:59], off nt
	s_nop 0
	global_load_dwordx2 v[60:61], v[60:61], off nt
	s_nop 0
	global_load_dwordx2 v[62:63], v[62:63], off nt
	s_nop 0
	global_load_dwordx2 v[64:65], v[64:65], off nt
	s_nop 0
	global_load_dwordx2 v[66:67], v[66:67], off nt
	s_nop 0
	global_load_dwordx2 v[68:69], v[68:69], off nt
	s_nop 0
	global_load_dwordx2 v[70:71], v[70:71], off nt
	s_nop 0
	global_load_dwordx2 v[72:73], v[72:73], off nt
	s_nop 0
	global_load_dwordx2 v[74:75], v[74:75], off nt
	s_nop 0
	global_load_dwordx2 v[76:77], v[76:77], off nt
	s_nop 0
	global_load_dwordx2 v[78:79], v[78:79], off nt
	s_nop 0
	global_load_dwordx2 v[80:81], v[80:81], off nt
	s_nop 0
	global_load_dwordx2 v[82:83], v[82:83], off nt
	s_nop 0
	global_load_dwordx2 v[84:85], v[84:85], off nt
	s_nop 0
	global_load_dwordx2 v[86:87], v[86:87], off nt
	s_nop 0
	global_load_dwordx2 v[88:89], v[88:89], off nt
	s_nop 0
	global_load_dwordx2 v[90:91], v[90:91], off nt
	s_nop 0
	global_load_dwordx2 v[92:93], v[92:93], off nt
	s_nop 0
	global_load_dwordx2 v[94:95], v[94:95], off nt
	s_nop 0
	global_load_dwordx2 v[96:97], v[96:97], off nt
	s_nop 0
	global_load_dwordx2 v[98:99], v[98:99], off nt
	s_nop 0
	global_load_dwordx2 v[100:101], v[100:101], off nt
	s_nop 0
	global_load_dwordx2 v[102:103], v[102:103], off nt
	s_nop 0
	global_load_dwordx2 v[104:105], v[104:105], off nt
	s_nop 0
	global_load_dwordx2 v[106:107], v[106:107], off nt
	s_nop 0
	global_load_dwordx2 v[108:109], v[108:109], off nt
	v_lshl_add_u64 v[114:115], v[52:53], 0, v[114:115]
	global_load_dwordx2 v[52:53], v[110:111], off nt
	s_nop 0
	global_load_dwordx2 v[110:111], v[112:113], off nt
	s_nop 0
	global_load_dwordx2 v[112:113], v[114:115], off nt
	s_nop 0
	global_load_dwordx2 v[50:51], v[50:51], off nt
	s_waitcnt vmcnt(0)
	ds_write2_b32 v10, v54, v55 offset1:1
	ds_write2_b32 v10, v56, v57 offset0:130 offset1:131
	ds_write2_b32 v19, v58, v59 offset1:1
	ds_write2_b32 v20, v60, v61 offset1:1
	ds_write2_b32 v21, v62, v63 offset1:1
	ds_write2_b32 v22, v64, v65 offset1:1
	ds_write2_b32 v23, v66, v67 offset1:1
	ds_write2_b32 v24, v68, v69 offset1:1
	ds_write2_b32 v25, v70, v71 offset1:1
	ds_write2_b32 v26, v72, v73 offset1:1
	ds_write2_b32 v27, v74, v75 offset1:1
	ds_write2_b32 v28, v76, v77 offset1:1
	ds_write2_b32 v29, v78, v79 offset1:1
	ds_write2_b32 v30, v80, v81 offset1:1
	ds_write2_b32 v31, v82, v83 offset1:1
	ds_write2_b32 v32, v84, v85 offset1:1
	ds_write2_b32 v33, v86, v87 offset1:1
	ds_write2_b32 v34, v88, v89 offset1:1
	ds_write2_b32 v35, v90, v91 offset1:1
	ds_write2_b32 v36, v92, v93 offset1:1
	ds_write2_b32 v37, v94, v95 offset1:1
	ds_write2_b32 v38, v96, v97 offset1:1
	ds_write2_b32 v39, v98, v99 offset1:1
	ds_write2_b32 v40, v100, v101 offset1:1
	ds_write2_b32 v41, v102, v103 offset1:1
	ds_write2_b32 v42, v104, v105 offset1:1
	ds_write2_b32 v43, v106, v107 offset1:1
	ds_write2_b32 v44, v108, v109 offset1:1
	ds_write2_b32 v45, v52, v53 offset1:1
	ds_write2_b32 v46, v110, v111 offset1:1
	ds_write2_b32 v47, v112, v113 offset1:1
	ds_write2_b32 v48, v50, v51 offset1:1
	s_waitcnt lgkmcnt(0)
	ds_read2_b32 v[54:55], v11 offset0:65 offset1:73
	ds_read2_b32 v[56:57], v11 offset1:8
	ds_read2_b32 v[58:59], v11 offset0:130 offset1:138
	ds_read2_b32 v[60:61], v11 offset0:195 offset1:203
	ds_read2_b32 v[62:63], v49 offset0:4 offset1:12
	ds_read2_b32 v[64:65], v49 offset0:69 offset1:77
	ds_read2_b32 v[66:67], v49 offset0:134 offset1:142
	ds_read2_b32 v[68:69], v49 offset0:199 offset1:207
	v_add_u32_e32 v72, s12, v7
	s_ashr_i32 s15, s14, 31
	v_ashrrev_i32_e32 v73, 31, v72
	v_lshl_add_u64 v[70:71], s[14:15], 1, v[2:3]
	v_lshlrev_b64 v[72:73], 12, v[72:73]
	s_waitcnt lgkmcnt(6)
	v_cvt_pk_bf16_f32 v50, v56, v54
	s_waitcnt lgkmcnt(4)
	v_cvt_pk_bf16_f32 v51, v58, v60
	s_waitcnt lgkmcnt(2)
	v_cvt_pk_bf16_f32 v52, v62, v64
	s_waitcnt lgkmcnt(0)
	v_cvt_pk_bf16_f32 v53, v66, v68
	v_lshl_add_u64 v[72:73], v[70:71], 0, v[72:73]
	v_add_u32_e32 v54, s12, v12
	global_store_dwordx4 v[72:73], v[50:53], off
	s_nop 1
	v_cvt_pk_bf16_f32 v50, v57, v55
	v_ashrrev_i32_e32 v55, 31, v54
	v_cvt_pk_bf16_f32 v51, v59, v61
	v_cvt_pk_bf16_f32 v52, v63, v65
	v_cvt_pk_bf16_f32 v53, v67, v69
	v_lshlrev_b64 v[54:55], 12, v[54:55]
	ds_read2_b32 v[56:57], v11 offset0:81 offset1:89
	ds_read2_b32 v[58:59], v11 offset0:16 offset1:24
	ds_read2_b32 v[60:61], v11 offset0:146 offset1:154
	ds_read2_b32 v[62:63], v11 offset0:211 offset1:219
	ds_read2_b32 v[64:65], v49 offset0:20 offset1:28
	ds_read2_b32 v[66:67], v49 offset0:85 offset1:93
	ds_read2_b32 v[68:69], v49 offset0:150 offset1:158
	ds_read2_b32 v[72:73], v49 offset0:215 offset1:223
	v_lshl_add_u64 v[54:55], v[70:71], 0, v[54:55]
	global_store_dwordx4 v[54:55], v[50:53], off
	v_add_u32_e32 v54, s12, v13
	v_ashrrev_i32_e32 v55, 31, v54
	v_lshlrev_b64 v[54:55], 12, v[54:55]
	s_waitcnt lgkmcnt(6)
	v_cvt_pk_bf16_f32 v50, v58, v56
	s_waitcnt lgkmcnt(4)
	v_cvt_pk_bf16_f32 v51, v60, v62
	s_waitcnt lgkmcnt(2)
	v_cvt_pk_bf16_f32 v52, v64, v66
	s_waitcnt lgkmcnt(0)
	v_cvt_pk_bf16_f32 v53, v68, v72
	v_lshl_add_u64 v[54:55], v[70:71], 0, v[54:55]
	global_store_dwordx4 v[54:55], v[50:53], off
	v_add_u32_e32 v54, s12, v14
	v_ashrrev_i32_e32 v55, 31, v54
	v_cvt_pk_bf16_f32 v50, v59, v57
	v_cvt_pk_bf16_f32 v51, v61, v63
	v_cvt_pk_bf16_f32 v52, v65, v67
	v_cvt_pk_bf16_f32 v53, v69, v73
	v_lshlrev_b64 v[54:55], 12, v[54:55]
	ds_read2_b32 v[56:57], v11 offset0:32 offset1:40
	ds_read2_b32 v[58:59], v11 offset0:97 offset1:105
	ds_read2_b32 v[60:61], v11 offset0:162 offset1:170
	ds_read2_b32 v[62:63], v11 offset0:227 offset1:235
	ds_read2_b32 v[64:65], v49 offset0:36 offset1:44
	ds_read2_b32 v[66:67], v49 offset0:101 offset1:109
	ds_read2_b32 v[68:69], v49 offset0:166 offset1:174
	ds_read2_b32 v[72:73], v49 offset0:231 offset1:239
	v_lshl_add_u64 v[54:55], v[70:71], 0, v[54:55]
	global_store_dwordx4 v[54:55], v[50:53], off
	v_add_u32_e32 v54, s12, v15
	v_ashrrev_i32_e32 v55, 31, v54
	v_lshlrev_b64 v[54:55], 12, v[54:55]
	s_waitcnt lgkmcnt(6)
	v_cvt_pk_bf16_f32 v50, v56, v58
	s_waitcnt lgkmcnt(4)
	v_cvt_pk_bf16_f32 v51, v60, v62
	s_waitcnt lgkmcnt(2)
	v_cvt_pk_bf16_f32 v52, v64, v66
	s_waitcnt lgkmcnt(0)
	v_cvt_pk_bf16_f32 v53, v68, v72
	v_lshl_add_u64 v[54:55], v[70:71], 0, v[54:55]
	global_store_dwordx4 v[54:55], v[50:53], off
	v_add_u32_e32 v54, s12, v16
	v_ashrrev_i32_e32 v55, 31, v54
	v_cvt_pk_bf16_f32 v50, v57, v59
	v_cvt_pk_bf16_f32 v51, v61, v63
	v_cvt_pk_bf16_f32 v52, v65, v67
	v_cvt_pk_bf16_f32 v53, v69, v73
	v_lshlrev_b64 v[54:55], 12, v[54:55]
	ds_read2_b32 v[56:57], v11 offset0:48 offset1:56
	ds_read2_b32 v[58:59], v11 offset0:113 offset1:121
	ds_read2_b32 v[60:61], v11 offset0:178 offset1:186
	ds_read2_b32 v[62:63], v11 offset0:243 offset1:251
	ds_read2_b32 v[64:65], v49 offset0:52 offset1:60
	ds_read2_b32 v[66:67], v49 offset0:117 offset1:125
	ds_read2_b32 v[68:69], v49 offset0:182 offset1:190
	ds_read2_b32 v[72:73], v49 offset0:247 offset1:255
	v_lshl_add_u64 v[54:55], v[70:71], 0, v[54:55]
	global_store_dwordx4 v[54:55], v[50:53], off
	v_add_u32_e32 v54, s12, v17
	v_ashrrev_i32_e32 v55, 31, v54
	v_lshlrev_b64 v[54:55], 12, v[54:55]
	s_waitcnt lgkmcnt(6)
	v_cvt_pk_bf16_f32 v50, v56, v58
	s_waitcnt lgkmcnt(4)
	v_cvt_pk_bf16_f32 v51, v60, v62
	s_waitcnt lgkmcnt(2)
	v_cvt_pk_bf16_f32 v52, v64, v66
	s_waitcnt lgkmcnt(0)
	v_cvt_pk_bf16_f32 v53, v68, v72
	v_lshl_add_u64 v[54:55], v[70:71], 0, v[54:55]
	global_store_dwordx4 v[54:55], v[50:53], off
	v_add_u32_e32 v54, s12, v18
	v_ashrrev_i32_e32 v55, 31, v54
	v_lshlrev_b64 v[54:55], 12, v[54:55]
	v_cvt_pk_bf16_f32 v50, v57, v59
	v_cvt_pk_bf16_f32 v51, v61, v63
	v_cvt_pk_bf16_f32 v52, v65, v67
	v_cvt_pk_bf16_f32 v53, v69, v73
	v_lshl_add_u64 v[54:55], v[70:71], 0, v[54:55]
	global_store_dwordx4 v[54:55], v[50:53], off
	s_waitcnt lgkmcnt(0)
	s_branch .LBB0_813

.LBB0_828:
	s_add_i32 s15, s0, 0xc00
	s_ashr_i32 s14, s15, 31
	s_lshr_b32 s14, s14, 23
	s_add_i32 s16, s15, s14
	s_ashr_i32 s14, s16, 9
	s_and_b32 s16, s16, 0xfe00
	s_sub_i32 s44, s15, s16
	s_ashr_i32 s15, s14, 31
	s_sext_i32_i16 s45, s44
	s_lshl_b64 s[16:17], s[14:15], 23
	s_bfe_u32 s14, s45, 0x5001a
	s_add_i32 s14, s44, s14
	s_sext_i32_i16 s15, s14
	s_and_b32 s14, s14, 0xffe0
	s_ashr_i32 s46, s15, 5
	s_sub_i32 s14, s44, s14
	s_waitcnt lgkmcnt(0)
	s_add_u32 s47, s10, s16
	s_addc_u32 s15, s11, s17
	s_add_u32 s45, s12, s16
	s_addc_u32 s44, s13, s17
	s_lshl_b32 s16, s46, 6
	s_lshl_b32 s17, s46, 7
	s_sext_i32_i16 s14, s14
	s_and_b32 s46, s17, 0xffffff00
	s_and_b32 s48, s16, 64
	s_ashr_i32 s17, s16, 31
	s_lshl_b32 s14, s14, 6
	s_or_b32 s46, s48, s46
	s_lshl_b64 s[16:17], s[16:17], 2
	v_add_u32_e32 v4, s14, v6
	s_add_u32 s16, s47, s16
	v_ashrrev_i32_e32 v5, 31, v4
	s_addc_u32 s17, s15, s17
	v_lshlrev_b64 v[4:5], 12, v[4:5]
	v_lshl_add_u64 v[58:59], s[16:17], 0, v[0:1]
	v_lshl_add_u64 v[4:5], v[58:59], 0, v[4:5]
	v_add_co_u32_e32 v58, vcc, s1, v4
	s_ashr_i32 s15, s14, 31
	s_nop 0
	v_addc_co_u32_e32 v59, vcc, 0, v5, vcc
	v_add_co_u32_e32 v60, vcc, s4, v4
	v_add_u32_e32 v42, s46, v7
	s_nop 0
	v_addc_co_u32_e32 v61, vcc, 0, v5, vcc
	v_add_co_u32_e32 v62, vcc, s5, v4
	s_lshl_b64 s[14:15], s[14:15], 1
	s_nop 0
	v_addc_co_u32_e32 v63, vcc, 0, v5, vcc
	v_add_co_u32_e32 v64, vcc, s6, v4
	v_add_u32_e32 v44, 8, v42
	s_nop 0
	v_addc_co_u32_e32 v65, vcc, 0, v5, vcc
	v_add_co_u32_e32 v66, vcc, s7, v4
	v_add_u32_e32 v46, 16, v42
	s_nop 0
	v_addc_co_u32_e32 v67, vcc, 0, v5, vcc
	v_add_co_u32_e32 v68, vcc, s8, v4
	v_add_u32_e32 v48, 24, v42
	s_nop 0
	v_addc_co_u32_e32 v69, vcc, 0, v5, vcc
	v_add_co_u32_e32 v70, vcc, s9, v4
	v_add_u32_e32 v50, 32, v42
	s_nop 0
	v_addc_co_u32_e32 v71, vcc, 0, v5, vcc
	v_add_co_u32_e32 v72, vcc, s18, v4
	v_add_u32_e32 v52, 40, v42
	s_nop 0
	v_addc_co_u32_e32 v73, vcc, 0, v5, vcc
	v_add_co_u32_e32 v74, vcc, s19, v4
	v_add_u32_e32 v54, 48, v42
	s_nop 0
	v_addc_co_u32_e32 v75, vcc, 0, v5, vcc
	v_add_co_u32_e32 v76, vcc, s20, v4
	v_add_u32_e32 v56, 56, v42
	s_nop 0
	v_addc_co_u32_e32 v77, vcc, 0, v5, vcc
	v_add_co_u32_e32 v78, vcc, s21, v4
	s_add_u32 s14, s45, s14
	s_nop 0
	v_addc_co_u32_e32 v79, vcc, 0, v5, vcc
	v_add_co_u32_e32 v80, vcc, s22, v4
	v_ashrrev_i32_e32 v43, 31, v42
	s_nop 0
	v_addc_co_u32_e32 v81, vcc, 0, v5, vcc
	v_add_co_u32_e32 v82, vcc, s23, v4
	v_ashrrev_i32_e32 v45, 31, v44
	s_nop 0
	v_addc_co_u32_e32 v83, vcc, 0, v5, vcc
	v_add_co_u32_e32 v84, vcc, s24, v4
	v_ashrrev_i32_e32 v47, 31, v46
	s_nop 0
	v_addc_co_u32_e32 v85, vcc, 0, v5, vcc
	v_add_co_u32_e32 v86, vcc, s25, v4
	v_ashrrev_i32_e32 v49, 31, v48
	s_nop 0
	v_addc_co_u32_e32 v87, vcc, 0, v5, vcc
	v_add_co_u32_e32 v88, vcc, s26, v4
	v_ashrrev_i32_e32 v51, 31, v50
	s_nop 0
	v_addc_co_u32_e32 v89, vcc, 0, v5, vcc
	v_add_co_u32_e32 v90, vcc, s27, v4
	v_ashrrev_i32_e32 v53, 31, v52
	s_nop 0
	v_addc_co_u32_e32 v91, vcc, 0, v5, vcc
	v_add_co_u32_e32 v92, vcc, s28, v4
	v_ashrrev_i32_e32 v55, 31, v54
	s_nop 0
	v_addc_co_u32_e32 v93, vcc, 0, v5, vcc
	v_add_co_u32_e32 v94, vcc, s29, v4
	v_ashrrev_i32_e32 v57, 31, v56
	s_nop 0
	v_addc_co_u32_e32 v95, vcc, 0, v5, vcc
	v_add_co_u32_e32 v96, vcc, s30, v4
	s_addc_u32 s15, s44, s15
	s_nop 0
	v_addc_co_u32_e32 v97, vcc, 0, v5, vcc
	v_add_co_u32_e32 v98, vcc, s31, v4
	v_lshlrev_b64 v[42:43], 12, v[42:43]
	s_nop 0
	v_addc_co_u32_e32 v99, vcc, 0, v5, vcc
	v_add_co_u32_e32 v100, vcc, s34, v4
	v_lshlrev_b64 v[44:45], 12, v[44:45]
	s_nop 0
	v_addc_co_u32_e32 v101, vcc, 0, v5, vcc
	v_add_co_u32_e32 v102, vcc, s35, v4
	v_lshlrev_b64 v[46:47], 12, v[46:47]
	s_nop 0
	v_addc_co_u32_e32 v103, vcc, 0, v5, vcc
	v_add_co_u32_e32 v104, vcc, s36, v4
	v_lshlrev_b64 v[48:49], 12, v[48:49]
	s_nop 0
	v_addc_co_u32_e32 v105, vcc, 0, v5, vcc
	v_add_co_u32_e32 v106, vcc, s37, v4
	v_lshlrev_b64 v[50:51], 12, v[50:51]
	s_nop 0
	v_addc_co_u32_e32 v107, vcc, 0, v5, vcc
	v_add_co_u32_e32 v108, vcc, s38, v4
	v_lshlrev_b64 v[52:53], 12, v[52:53]
	s_nop 0
	v_addc_co_u32_e32 v109, vcc, 0, v5, vcc
	v_add_co_u32_e32 v110, vcc, s39, v4
	v_lshlrev_b64 v[54:55], 12, v[54:55]
	s_nop 0
	v_addc_co_u32_e32 v111, vcc, 0, v5, vcc
	v_add_co_u32_e32 v112, vcc, s40, v4
	v_lshlrev_b64 v[56:57], 12, v[56:57]
	s_nop 0
	v_addc_co_u32_e32 v113, vcc, 0, v5, vcc
	v_add_co_u32_e32 v114, vcc, s41, v4
	v_lshl_add_u64 v[120:121], s[14:15], 0, v[2:3]
	s_nop 0
	v_addc_co_u32_e32 v115, vcc, 0, v5, vcc
	v_add_co_u32_e32 v116, vcc, s42, v4
	v_lshl_add_u64 v[122:123], v[120:121], 0, v[42:43]
	s_nop 0
	v_addc_co_u32_e32 v117, vcc, 0, v5, vcc
	v_add_co_u32_e32 v118, vcc, s43, v4
	v_lshl_add_u64 v[124:125], v[120:121], 0, v[44:45]
	s_nop 0
	v_addc_co_u32_e32 v119, vcc, 0, v5, vcc
	global_load_dwordx2 v[4:5], v[4:5], off nt
	s_nop 0
	global_load_dwordx2 v[58:59], v[58:59], off nt
	s_nop 0
	global_load_dwordx2 v[60:61], v[60:61], off nt
	s_nop 0
	global_load_dwordx2 v[62:63], v[62:63], off nt
	s_nop 0
	global_load_dwordx2 v[64:65], v[64:65], off nt
	s_nop 0
	global_load_dwordx2 v[66:67], v[66:67], off nt
	s_nop 0
	global_load_dwordx2 v[68:69], v[68:69], off nt
	s_nop 0
	global_load_dwordx2 v[70:71], v[70:71], off nt
	s_nop 0
	global_load_dwordx2 v[72:73], v[72:73], off nt
	s_nop 0
	global_load_dwordx2 v[74:75], v[74:75], off nt
	s_nop 0
	global_load_dwordx2 v[76:77], v[76:77], off nt
	s_nop 0
	global_load_dwordx2 v[78:79], v[78:79], off nt
	s_nop 0
	global_load_dwordx2 v[80:81], v[80:81], off nt
	s_nop 0
	global_load_dwordx2 v[82:83], v[82:83], off nt
	s_nop 0
	global_load_dwordx2 v[84:85], v[84:85], off nt
	s_nop 0
	global_load_dwordx2 v[86:87], v[86:87], off nt
	s_nop 0
	global_load_dwordx2 v[88:89], v[88:89], off nt
	s_nop 0
	global_load_dwordx2 v[90:91], v[90:91], off nt
	s_nop 0
	global_load_dwordx2 v[92:93], v[92:93], off nt
	s_nop 0
	global_load_dwordx2 v[94:95], v[94:95], off nt
	s_nop 0
	global_load_dwordx2 v[96:97], v[96:97], off nt
	s_nop 0
	global_load_dwordx2 v[98:99], v[98:99], off nt
	s_nop 0
	global_load_dwordx2 v[100:101], v[100:101], off nt
	s_nop 0
	global_load_dwordx2 v[102:103], v[102:103], off nt
	s_nop 0
	global_load_dwordx2 v[104:105], v[104:105], off nt
	s_nop 0
	global_load_dwordx2 v[106:107], v[106:107], off nt
	s_nop 0
	global_load_dwordx2 v[108:109], v[108:109], off nt
	s_nop 0
	global_load_dwordx2 v[110:111], v[110:111], off nt
	s_nop 0
	global_load_dwordx2 v[112:113], v[112:113], off nt
	s_nop 0
	global_load_dwordx2 v[114:115], v[114:115], off nt
	s_nop 0
	global_load_dwordx2 v[116:117], v[116:117], off nt
	s_nop 0
	global_load_dwordx2 v[118:119], v[118:119], off nt
	s_waitcnt vmcnt(0)
	ds_write2_b32 v9, v4, v5 offset1:1
	ds_write2_b32 v9, v58, v59 offset0:130 offset1:131
	ds_write2_b32 v10, v60, v61 offset1:1
	ds_write2_b32 v11, v62, v63 offset1:1
	ds_write2_b32 v12, v64, v65 offset1:1
	ds_write2_b32 v13, v66, v67 offset1:1
	ds_write2_b32 v14, v68, v69 offset1:1
	ds_write2_b32 v15, v70, v71 offset1:1
	ds_write2_b32 v16, v72, v73 offset1:1
	ds_write2_b32 v17, v74, v75 offset1:1
	ds_write2_b32 v18, v76, v77 offset1:1
	ds_write2_b32 v19, v78, v79 offset1:1
	ds_write2_b32 v20, v80, v81 offset1:1
	ds_write2_b32 v21, v82, v83 offset1:1
	ds_write2_b32 v22, v84, v85 offset1:1
	ds_write2_b32 v23, v86, v87 offset1:1
	ds_write2_b32 v24, v88, v89 offset1:1
	ds_write2_b32 v25, v90, v91 offset1:1
	ds_write2_b32 v26, v92, v93 offset1:1
	ds_write2_b32 v27, v94, v95 offset1:1
	ds_write2_b32 v28, v96, v97 offset1:1
	ds_write2_b32 v29, v98, v99 offset1:1
	ds_write2_b32 v30, v100, v101 offset1:1
	ds_write2_b32 v31, v102, v103 offset1:1
	ds_write2_b32 v32, v104, v105 offset1:1
	ds_write2_b32 v33, v106, v107 offset1:1
	ds_write2_b32 v34, v108, v109 offset1:1
	ds_write2_b32 v35, v110, v111 offset1:1
	ds_write2_b32 v36, v112, v113 offset1:1
	ds_write2_b32 v37, v114, v115 offset1:1
	ds_write2_b32 v38, v116, v117 offset1:1
	ds_write2_b32 v39, v118, v119 offset1:1
	s_waitcnt lgkmcnt(0)
	v_lshl_add_u64 v[126:127], v[120:121], 0, v[46:47]
	v_lshl_add_u64 v[128:129], v[120:121], 0, v[48:49]
	v_lshl_add_u64 v[130:131], v[120:121], 0, v[50:51]
	v_lshl_add_u64 v[132:133], v[120:121], 0, v[52:53]
	v_lshl_add_u64 v[134:135], v[120:121], 0, v[54:55]
	v_lshl_add_u64 v[120:121], v[120:121], 0, v[56:57]
	ds_read2_b32 v[4:5], v8 offset0:65 offset1:73
	ds_read2_b32 v[46:47], v8 offset1:8
	ds_read2_b32 v[48:49], v8 offset0:130 offset1:138
	ds_read2_b32 v[50:51], v8 offset0:195 offset1:203
	ds_read2_b32 v[52:53], v40 offset0:4 offset1:12
	ds_read2_b32 v[54:55], v40 offset0:69 offset1:77
	ds_read2_b32 v[56:57], v40 offset0:134 offset1:142
	ds_read2_b32 v[58:59], v40 offset0:199 offset1:207
	ds_read2_b32 v[60:61], v8 offset0:81 offset1:89
	ds_read2_b32 v[62:63], v8 offset0:16 offset1:24
	ds_read2_b32 v[64:65], v8 offset0:146 offset1:154
	ds_read2_b32 v[66:67], v8 offset0:211 offset1:219
	ds_read2_b32 v[68:69], v40 offset0:20 offset1:28
	ds_read2_b32 v[70:71], v40 offset0:85 offset1:93
	ds_read2_b32 v[72:73], v40 offset0:150 offset1:158
	ds_read2_b32 v[74:75], v40 offset0:215 offset1:223
	ds_read2_b32 v[76:77], v8 offset0:32 offset1:40
	ds_read2_b32 v[78:79], v8 offset0:97 offset1:105
	ds_read2_b32 v[80:81], v8 offset0:162 offset1:170
	ds_read2_b32 v[82:83], v8 offset0:227 offset1:235
	ds_read2_b32 v[84:85], v40 offset0:36 offset1:44
	ds_read2_b32 v[86:87], v40 offset0:101 offset1:109
	ds_read2_b32 v[88:89], v40 offset0:166 offset1:174
	ds_read2_b32 v[90:91], v40 offset0:231 offset1:239
	ds_read2_b32 v[92:93], v8 offset0:48 offset1:56
	ds_read2_b32 v[94:95], v8 offset0:113 offset1:121
	ds_read2_b32 v[96:97], v8 offset0:178 offset1:186
	ds_read2_b32 v[98:99], v8 offset0:243 offset1:251
	ds_read2_b32 v[100:101], v40 offset0:52 offset1:60
	ds_read2_b32 v[102:103], v40 offset0:117 offset1:125
	ds_read2_b32 v[104:105], v40 offset0:182 offset1:190
	ds_read2_b32 v[106:107], v40 offset0:247 offset1:255
	s_waitcnt lgkmcnt(14)
	v_cvt_pk_bf16_f32 v42, v46, v4
	v_cvt_pk_bf16_f32 v43, v48, v50
	v_cvt_pk_bf16_f32 v44, v52, v54
	v_cvt_pk_bf16_f32 v45, v56, v58
	v_cvt_pk_bf16_f32 v46, v47, v5
	v_cvt_pk_bf16_f32 v47, v49, v51
	v_cvt_pk_bf16_f32 v48, v53, v55
	v_cvt_pk_bf16_f32 v49, v57, v59
	v_cvt_pk_bf16_f32 v50, v62, v60
	v_cvt_pk_bf16_f32 v51, v64, v66
	v_cvt_pk_bf16_f32 v52, v68, v70
	v_cvt_pk_bf16_f32 v53, v72, v74
	v_cvt_pk_bf16_f32 v54, v63, v61
	v_cvt_pk_bf16_f32 v55, v65, v67
	v_cvt_pk_bf16_f32 v56, v69, v71
	v_cvt_pk_bf16_f32 v57, v73, v75
	v_cvt_pk_bf16_f32 v58, v76, v78
	s_waitcnt lgkmcnt(12)
	v_cvt_pk_bf16_f32 v59, v80, v82
	s_waitcnt lgkmcnt(10)
	v_cvt_pk_bf16_f32 v60, v84, v86
	s_waitcnt lgkmcnt(8)
	v_cvt_pk_bf16_f32 v61, v88, v90
	v_cvt_pk_bf16_f32 v62, v77, v79
	v_cvt_pk_bf16_f32 v63, v81, v83
	v_cvt_pk_bf16_f32 v64, v85, v87
	v_cvt_pk_bf16_f32 v65, v89, v91
	s_waitcnt lgkmcnt(6)
	v_cvt_pk_bf16_f32 v66, v92, v94
	s_waitcnt lgkmcnt(4)
	v_cvt_pk_bf16_f32 v67, v96, v98
	s_waitcnt lgkmcnt(2)
	v_cvt_pk_bf16_f32 v68, v100, v102
	s_waitcnt lgkmcnt(0)
	v_cvt_pk_bf16_f32 v69, v104, v106
	v_cvt_pk_bf16_f32 v70, v93, v95
	v_cvt_pk_bf16_f32 v71, v97, v99
	v_cvt_pk_bf16_f32 v72, v101, v103
	v_cvt_pk_bf16_f32 v73, v105, v107
	global_store_dwordx4 v[122:123], v[42:45], off nt
	global_store_dwordx4 v[124:125], v[46:49], off nt
	global_store_dwordx4 v[126:127], v[50:53], off nt
	global_store_dwordx4 v[128:129], v[54:57], off nt
	global_store_dwordx4 v[130:131], v[58:61], off nt
	global_store_dwordx4 v[132:133], v[62:65], off nt
	global_store_dwordx4 v[134:135], v[66:69], off nt
	global_store_dwordx4 v[120:121], v[70:73], off nt
	s_waitcnt lgkmcnt(0)
	s_addk_i32 s0, 0x400
	s_cmpk_gt_i32 s0, 0x7ff
	s_cbranch_scc0 .LBB0_828

.LBB0_895:
	s_ashr_i32 s35, s34, 31
	s_lshl_b64 s[34:35], s[34:35], 12
	s_add_u32 s34, s7, s34
	s_addc_u32 s35, s8, s35
	v_lshl_or_b32 v130, s52, 9, v154
	v_mad_u64_u32 v[146:147], s[36:37], v128, s46, v[130:131]
	global_load_dwordx4 v[140:143], v146, s[34:35]
	s_add_u32 s36, s34, 0x1000
	s_addc_u32 s37, s35, 0
	v_or_b32_e32 v129, 0x100, v146
	global_load_dwordx4 v[160:163], v129, s[36:37]
	global_load_dwordx4 v[164:167], v146, s[36:37]
	global_load_dwordx4 v[168:171], v146, s[34:35] offset:256
	v_add_u32_e32 v129, 0x5e000, v146
	global_load_dwordx4 v[172:175], v129, s[34:35]
	global_load_dwordx4 v[176:179], v129, s[36:37]
	v_add_u32_e32 v246, 0x5e100, v146
	global_load_dwordx4 v[180:183], v246, s[36:37]
	global_load_dwordx4 v[184:187], v129, s[34:35] offset:256
	v_add_u32_e32 v245, 0xbc000, v146
	global_load_dwordx4 v[188:191], v245, s[36:37]
	global_load_dwordx4 v[192:195], v245, s[34:35]
	v_add_u32_e32 v129, 0xbc100, v146
	global_load_dwordx4 v[196:199], v129, s[36:37]
	global_load_dwordx4 v[200:203], v245, s[34:35] offset:256
	s_waitcnt vmcnt(11)
	v_lshlrev_b32_e32 v138, 16, v140
	s_waitcnt vmcnt(10)
	v_lshlrev_b32_e32 v136, 16, v160
	s_waitcnt vmcnt(9)
	v_lshlrev_b32_e32 v129, 16, v165
	v_and_b32_e32 v246, 0xffff0000, v165
	v_lshlrev_b32_e32 v245, 16, v166
	v_and_b32_e32 v244, 0xffff0000, v166
	v_lshlrev_b32_e32 v243, 16, v167
	v_and_b32_e32 v242, 0xffff0000, v167
	v_max_f32_e32 v241, v129, v129
	v_max_f32_e32 v240, v246, v246
	v_and_b32_e32 v239, 0xffff0000, v160
	v_max_f32_e32 v129, v244, v244
	v_max_f32_e32 v246, v242, v242
	v_max_f32_e32 v238, 0x1e3ce508, v241
	v_max_f32_e32 v244, 0x1e3ce508, v240
	v_max_f32_e32 v237, v243, v243
	v_max_f32_e32 v236, v136, v136
	v_max_f32_e32 v242, v239, v239
	v_max_f32_e32 v243, 0x1e3ce508, v129
	v_max_f32_e32 v136, 0x1e3ce508, v246
	v_rcp_f32_e32 v240, v238
	v_rcp_f32_e32 v241, v244
	v_lshlrev_b32_e32 v129, 16, v164
	v_and_b32_e32 v246, 0xffff0000, v164
	v_lshlrev_b32_e32 v244, 16, v162
	v_and_b32_e32 v239, 0xffff0000, v162
	v_max_f32_e32 v238, 0x1e3ce508, v237
	v_max_f32_e32 v235, 0x1e3ce508, v236
	v_max_f32_e32 v234, 0x1e3ce508, v242
	v_lshlrev_b32_e32 v237, 16, v163
	v_max_f32_e32 v236, v246, v246
	v_max_f32_e32 v242, v244, v244
	v_max_f32_e32 v233, v239, v239
	v_rcp_f32_e32 v230, v238
	v_rcp_f32_e32 v228, v235
	v_rcp_f32_e32 v229, v234
	v_and_b32_e32 v139, 0xffff0000, v140
	v_lshlrev_b32_e32 v238, 16, v141
	v_and_b32_e32 v239, 0xffff0000, v141
	v_lshlrev_b32_e32 v246, 16, v161
	v_and_b32_e32 v244, 0xffff0000, v161
	v_max_f32_e32 v235, v129, v129
	v_max_f32_e32 v234, v237, v237
	v_max_f32_e32 v232, 0x1e3ce508, v236
	v_max_f32_e32 v129, 0x1e3ce508, v242
	v_max_f32_e32 v237, 0x1e3ce508, v233
	v_max_f32_e32 v236, v246, v246
	v_max_f32_e32 v242, v244, v244
	v_max_f32_e32 v233, 0x1e3ce508, v235
	v_max_f32_e32 v246, 0x1e3ce508, v234
	v_rcp_f32_e32 v227, v232
	v_rcp_f32_e32 v224, v129
	v_rcp_f32_e32 v225, v237
	v_pk_mul_f32 v[234:235], v[240:241], v[238:239]
	v_max_f32_e32 v244, 0x1e3ce508, v236
	v_max_f32_e32 v232, 0x1e3ce508, v242
	v_rcp_f32_e32 v226, v233
	v_pk_mul_f32 v[110:111], v[110:111], v[234:235]
	v_and_b32_e32 v129, 0xffff0000, v163
	s_waitcnt vmcnt(8)
	v_lshlrev_b32_e32 v240, 16, v168
	v_and_b32_e32 v241, 0xffff0000, v168
	v_max_f32_e32 v242, v245, v245
	v_rcp_f32_e32 v234, v244
	v_rcp_f32_e32 v235, v232
	v_max_f32_e32 v245, v129, v129
	v_pk_mul_f32 v[238:239], v[228:229], v[240:241]
	v_max_f32_e32 v244, 0x1e3ce508, v242
	v_max_f32_e32 v129, 0x1e3ce508, v245
	v_pk_mul_f32 v[76:77], v[76:77], v[238:239]
	v_lshlrev_b32_e32 v232, 16, v170
	v_and_b32_e32 v233, 0xffff0000, v170
	v_rcp_f32_e32 v228, v244
	v_rcp_f32_e32 v231, v136
	v_rcp_f32_e32 v240, v246
	v_rcp_f32_e32 v241, v129
	v_pk_mul_f32 v[244:245], v[224:225], v[232:233]
	s_waitcnt vmcnt(6)
	v_lshlrev_b32_e32 v246, 16, v176
	v_pk_mul_f32 v[72:73], v[72:73], v[244:245]
	v_lshlrev_b32_e32 v232, 16, v169
	v_and_b32_e32 v233, 0xffff0000, v169
	v_max_f32_e32 v242, v246, v246
	v_pk_mul_f32 v[224:225], v[226:227], v[138:139]
	v_pk_mul_f32 v[244:245], v[234:235], v[232:233]
	v_max_f32_e32 v246, 0x1e3ce508, v242
	v_lshlrev_b32_e32 v226, 16, v142
	v_and_b32_e32 v227, 0xffff0000, v142
	v_lshlrev_b32_e32 v138, 16, v143
	v_and_b32_e32 v139, 0xffff0000, v143
	v_pk_mul_f32 v[108:109], v[108:109], v[224:225]
	v_pk_mul_f32 v[78:79], v[78:79], v[244:245]
	v_lshlrev_b32_e32 v238, 16, v171
	v_and_b32_e32 v239, 0xffff0000, v171
	v_rcp_f32_e32 v244, v246
	v_and_b32_e32 v242, 0xffff0000, v176
	v_pk_mul_f32 v[236:237], v[230:231], v[138:139]
	v_pk_mul_f32 v[224:225], v[240:241], v[238:239]
	v_max_f32_e32 v246, v242, v242
	v_rcp_f32_e32 v229, v243
	v_pk_mul_f32 v[106:107], v[106:107], v[236:237]
	v_pk_mul_f32 v[74:75], v[74:75], v[224:225]
	v_max_f32_e32 v129, 0x1e3ce508, v246
	v_rcp_f32_e32 v245, v129
	v_lshlrev_b32_e32 v231, 16, v177
	v_max_f32_e32 v246, v231, v231
	v_max_f32_e32 v129, 0x1e3ce508, v246
	v_pk_mul_f32 v[224:225], v[228:229], v[226:227]
	v_rcp_f32_e32 v138, v129
	v_and_b32_e32 v246, 0xffff0000, v177
	v_max_f32_e32 v136, v246, v246
	v_max_f32_e32 v129, 0x1e3ce508, v136
	v_rcp_f32_e32 v139, v129
	v_lshlrev_b32_e32 v246, 16, v178
	v_max_f32_e32 v136, v246, v246
	v_max_f32_e32 v129, 0x1e3ce508, v136
	v_rcp_f32_e32 v226, v129
	v_pk_mul_f32 v[104:105], v[104:105], v[224:225]
	v_and_b32_e32 v246, 0xffff0000, v178
	v_max_f32_e32 v136, v246, v246
	v_max_f32_e32 v129, 0x1e3ce508, v136
	v_rcp_f32_e32 v227, v129
	v_lshlrev_b32_e32 v246, 16, v179
	v_max_f32_e32 v136, v246, v246
	v_max_f32_e32 v129, 0x1e3ce508, v136
	v_lshlrev_b32_e32 v224, 16, v172
	v_and_b32_e32 v225, 0xffff0000, v172
	v_rcp_f32_e32 v242, v129
	v_and_b32_e32 v246, 0xffff0000, v179
	v_pk_mul_f32 v[240:241], v[244:245], v[224:225]
	v_max_f32_e32 v136, v246, v246
	v_pk_mul_f32 v[100:101], v[100:101], v[240:241]
	v_lshlrev_b32_e32 v224, 16, v174
	v_and_b32_e32 v225, 0xffff0000, v174
	v_max_f32_e32 v129, 0x1e3ce508, v136
	v_pk_mul_f32 v[240:241], v[226:227], v[224:225]
	v_rcp_f32_e32 v243, v129
	v_pk_mul_f32 v[96:97], v[96:97], v[240:241]
	v_lshlrev_b32_e32 v244, 16, v173
	v_and_b32_e32 v245, 0xffff0000, v173
	v_pk_mul_f32 v[240:241], v[138:139], v[244:245]
	s_waitcnt vmcnt(5)
	v_lshlrev_b32_e32 v129, 16, v180
	v_pk_mul_f32 v[102:103], v[102:103], v[240:241]
	v_lshlrev_b32_e32 v244, 16, v175
	v_and_b32_e32 v245, 0xffff0000, v175
	v_max_f32_e32 v246, v129, v129
	v_pk_mul_f32 v[240:241], v[242:243], v[244:245]
	v_max_f32_e32 v139, 0x1e3ce508, v246
	v_pk_mul_f32 v[98:99], v[98:99], v[240:241]
	v_rcp_f32_e32 v244, v139
	v_lshlrev_b32_e32 v246, 16, v182
	v_max_f32_e32 v129, v246, v246
	v_max_f32_e32 v139, 0x1e3ce508, v129
	v_rcp_f32_e32 v242, v139
	v_and_b32_e32 v246, 0xffff0000, v180
	v_max_f32_e32 v129, v246, v246
	v_max_f32_e32 v241, 0x1e3ce508, v129
	v_and_b32_e32 v240, 0xffff0000, v182
	v_rcp_f32_e32 v245, v241
	v_lshlrev_b32_e32 v246, 16, v181
	v_and_b32_e32 v129, 0xffff0000, v181
	v_max_f32_e32 v241, v240, v240
	v_max_f32_e32 v139, v246, v246
	v_max_f32_e32 v138, v129, v129
	v_max_f32_e32 v240, 0x1e3ce508, v241
	v_max_f32_e32 v246, 0x1e3ce508, v139
	v_max_f32_e32 v129, 0x1e3ce508, v138
	v_rcp_f32_e32 v243, v240
	v_lshlrev_b32_e32 v241, 16, v183
	v_and_b32_e32 v139, 0xffff0000, v183
	v_rcp_f32_e32 v238, v246
	v_rcp_f32_e32 v239, v129
	v_max_f32_e32 v240, v241, v241
	v_max_f32_e32 v246, v139, v139
	v_max_f32_e32 v129, 0x1e3ce508, v240
	v_max_f32_e32 v241, 0x1e3ce508, v246
	v_rcp_f32_e32 v236, v129
	v_rcp_f32_e32 v237, v241
	s_waitcnt vmcnt(4)
	v_lshlrev_b32_e32 v138, 16, v184
	v_and_b32_e32 v139, 0xffff0000, v184
	v_lshlrev_b32_e32 v240, 16, v185
	v_and_b32_e32 v241, 0xffff0000, v185
	v_pk_mul_f32 v[234:235], v[238:239], v[240:241]
	v_pk_mul_f32 v[232:233], v[244:245], v[138:139]
	v_pk_mul_f32 v[70:71], v[70:71], v[234:235]
	v_lshlrev_b32_e32 v240, 16, v187
	v_and_b32_e32 v241, 0xffff0000, v187
	v_pk_mul_f32 v[238:239], v[236:237], v[240:241]
	v_pk_mul_f32 v[68:69], v[68:69], v[232:233]
	v_pk_mul_f32 v[66:67], v[66:67], v[238:239]
	v_lshlrev_b32_e32 v240, 16, v186
	v_and_b32_e32 v241, 0xffff0000, v186
	v_pk_mul_f32 v[244:245], v[242:243], v[240:241]
	s_waitcnt vmcnt(3)
	v_lshlrev_b32_e32 v246, 16, v188
	v_max_f32_e32 v129, v246, v246
	v_max_f32_e32 v139, 0x1e3ce508, v129
	v_pk_mul_f32 v[64:65], v[64:65], v[244:245]
	v_rcp_f32_e32 v242, v139
	v_and_b32_e32 v129, 0xffff0000, v188
	v_max_f32_e32 v241, v129, v129
	v_max_f32_e32 v240, 0x1e3ce508, v241
	v_rcp_f32_e32 v243, v240
	v_lshlrev_b32_e32 v129, 16, v189
	v_max_f32_e32 v241, v129, v129
	v_max_f32_e32 v240, 0x1e3ce508, v241
	v_rcp_f32_e32 v244, v240
	v_and_b32_e32 v246, 0xffff0000, v189
	v_max_f32_e32 v129, v246, v246
	v_max_f32_e32 v241, 0x1e3ce508, v129
	v_rcp_f32_e32 v245, v241
	v_lshlrev_b32_e32 v246, 16, v190
	v_max_f32_e32 v129, v246, v246
	v_max_f32_e32 v241, 0x1e3ce508, v129
	v_rcp_f32_e32 v138, v241
	v_add_u32_e32 v246, 0x11a000, v146
	global_load_dwordx4 v[140:143], v246, s[36:37]
	v_and_b32_e32 v136, 0xffff0000, v190
	v_max_f32_e32 v129, v136, v136
	v_max_f32_e32 v241, 0x1e3ce508, v129
	v_rcp_f32_e32 v139, v241
	v_lshlrev_b32_e32 v136, 16, v191
	v_max_f32_e32 v129, v136, v136
	v_max_f32_e32 v241, 0x1e3ce508, v129
	v_rcp_f32_e32 v238, v241
	v_and_b32_e32 v136, 0xffff0000, v191
	s_waitcnt vmcnt(3)
	v_lshlrev_b32_e32 v236, 16, v192
	v_and_b32_e32 v237, 0xffff0000, v192
	v_max_f32_e32 v129, v136, v136
	v_pk_mul_f32 v[240:241], v[242:243], v[236:237]
	v_max_f32_e32 v235, 0x1e3ce508, v129
	v_pk_mul_f32 v[92:93], v[92:93], v[240:241]
	v_lshlrev_b32_e32 v236, 16, v194
	v_and_b32_e32 v237, 0xffff0000, v194
	v_rcp_f32_e32 v239, v235
	v_pk_mul_f32 v[242:243], v[138:139], v[236:237]
	s_waitcnt vmcnt(2)
	v_lshlrev_b32_e32 v129, 16, v196
	v_pk_mul_f32 v[88:89], v[88:89], v[242:243]
	v_lshlrev_b32_e32 v236, 16, v193
	v_and_b32_e32 v237, 0xffff0000, v193
	v_pk_mul_f32 v[138:139], v[244:245], v[236:237]
	v_max_f32_e32 v136, v129, v129
	v_pk_mul_f32 v[94:95], v[94:95], v[138:139]
	v_lshlrev_b32_e32 v244, 16, v195
	v_and_b32_e32 v245, 0xffff0000, v195
	v_pk_mul_f32 v[236:237], v[238:239], v[244:245]
	global_load_dwordx4 v[160:163], v246, s[34:35]
	v_max_f32_e32 v129, 0x1e3ce508, v136
	v_pk_mul_f32 v[90:91], v[90:91], v[236:237]
	v_rcp_f32_e32 v244, v129
	v_and_b32_e32 v139, 0xffff0000, v196
	v_add_u32_e32 v138, 0x11a100, v146
	v_max_f32_e32 v136, v139, v139
	global_load_dwordx4 v[164:167], v138, s[36:37]
	v_max_f32_e32 v129, 0x1e3ce508, v136
	v_rcp_f32_e32 v245, v129
	v_lshlrev_b32_e32 v139, 16, v197
	v_max_f32_e32 v138, v139, v139
	v_max_f32_e32 v129, 0x1e3ce508, v138
	v_rcp_f32_e32 v242, v129
	v_and_b32_e32 v241, 0xffff0000, v197
	v_max_f32_e32 v240, v241, v241
	v_max_f32_e32 v129, 0x1e3ce508, v240
	v_rcp_f32_e32 v243, v129
	v_lshlrev_b32_e32 v241, 16, v198
	v_max_f32_e32 v240, v241, v241
	v_max_f32_e32 v129, 0x1e3ce508, v240
	v_rcp_f32_e32 v138, v129
	v_and_b32_e32 v136, 0xffff0000, v198
	v_max_f32_e32 v241, v136, v136
	v_max_f32_e32 v240, 0x1e3ce508, v241
	v_rcp_f32_e32 v139, v240
	v_lshlrev_b32_e32 v136, 16, v199
	v_max_f32_e32 v129, v136, v136
	v_max_f32_e32 v241, 0x1e3ce508, v129
	v_rcp_f32_e32 v238, v241
	v_and_b32_e32 v136, 0xffff0000, v199
	v_max_f32_e32 v129, v136, v136
	v_max_f32_e32 v241, 0x1e3ce508, v129
	v_rcp_f32_e32 v239, v241
	s_waitcnt vmcnt(3)
	v_lshlrev_b32_e32 v236, 16, v200
	v_and_b32_e32 v237, 0xffff0000, v200
	v_lshlrev_b32_e32 v240, 16, v201
	v_and_b32_e32 v241, 0xffff0000, v201
	v_pk_mul_f32 v[234:235], v[242:243], v[240:241]
	v_pk_mul_f32 v[232:233], v[244:245], v[236:237]
	v_pk_mul_f32 v[62:63], v[62:63], v[234:235]
	v_lshlrev_b32_e32 v242, 16, v203
	v_and_b32_e32 v243, 0xffff0000, v203
	v_pk_mul_f32 v[244:245], v[238:239], v[242:243]
	v_pk_mul_f32 v[60:61], v[60:61], v[232:233]
	v_lshlrev_b32_e32 v240, 16, v202
	v_and_b32_e32 v241, 0xffff0000, v202
	v_pk_mul_f32 v[58:59], v[58:59], v[244:245]
	global_load_dwordx4 v[168:171], v246, s[34:35] offset:256
	v_pk_mul_f32 v[242:243], v[138:139], v[240:241]
	s_waitcnt vmcnt(3)
	v_lshlrev_b32_e32 v129, 16, v140
	v_max_f32_e32 v246, v129, v129
	v_max_f32_e32 v245, 0x1e3ce508, v246
	v_pk_mul_f32 v[56:57], v[56:57], v[242:243]
	v_rcp_f32_e32 v138, v245
	v_and_b32_e32 v136, 0xffff0000, v140
	v_max_f32_e32 v129, v136, v136
	v_max_f32_e32 v246, 0x1e3ce508, v129
	v_rcp_f32_e32 v139, v246
	v_lshlrev_b32_e32 v136, 16, v141
	v_max_f32_e32 v129, v136, v136
	v_max_f32_e32 v246, 0x1e3ce508, v129
	v_rcp_f32_e32 v244, v246
	v_and_b32_e32 v136, 0xffff0000, v141
	v_max_f32_e32 v129, v136, v136
	v_max_f32_e32 v246, 0x1e3ce508, v129
	v_rcp_f32_e32 v245, v246
	v_lshlrev_b32_e32 v136, 16, v142
	v_max_f32_e32 v129, v136, v136
	v_max_f32_e32 v246, 0x1e3ce508, v129
	v_rcp_f32_e32 v242, v246
	v_and_b32_e32 v136, 0xffff0000, v142
	v_max_f32_e32 v129, v136, v136
	v_max_f32_e32 v246, 0x1e3ce508, v129
	v_rcp_f32_e32 v243, v246
	v_lshlrev_b32_e32 v136, 16, v143
	v_max_f32_e32 v129, v136, v136
	v_max_f32_e32 v246, 0x1e3ce508, v129
	v_rcp_f32_e32 v240, v246
	v_and_b32_e32 v136, 0xffff0000, v143
	s_waitcnt vmcnt(2)
	v_lshlrev_b32_e32 v238, 16, v160
	v_and_b32_e32 v239, 0xffff0000, v160
	v_max_f32_e32 v246, v136, v136
	v_pk_mul_f32 v[236:237], v[138:139], v[238:239]
	v_max_f32_e32 v129, 0x1e3ce508, v246
	v_pk_mul_f32 v[84:85], v[84:85], v[236:237]
	v_lshlrev_b32_e32 v138, 16, v162
	v_and_b32_e32 v139, 0xffff0000, v162
	v_rcp_f32_e32 v241, v129
	v_pk_mul_f32 v[238:239], v[242:243], v[138:139]
	s_waitcnt vmcnt(1)
	v_lshlrev_b32_e32 v246, 16, v164
	v_pk_mul_f32 v[80:81], v[80:81], v[238:239]
	v_lshlrev_b32_e32 v242, 16, v161
	v_and_b32_e32 v243, 0xffff0000, v161
	v_pk_mul_f32 v[138:139], v[244:245], v[242:243]
	v_max_f32_e32 v136, v246, v246
	v_pk_mul_f32 v[86:87], v[86:87], v[138:139]
	v_lshlrev_b32_e32 v242, 16, v163
	v_and_b32_e32 v243, 0xffff0000, v163
	v_pk_mul_f32 v[138:139], v[240:241], v[242:243]
	v_max_f32_e32 v129, 0x1e3ce508, v136
	v_pk_mul_f32 v[82:83], v[82:83], v[138:139]
	v_rcp_f32_e32 v244, v129
	v_and_b32_e32 v246, 0xffff0000, v164
	v_max_f32_e32 v139, v246, v246
	v_max_f32_e32 v129, 0x1e3ce508, v139
	v_rcp_f32_e32 v245, v129
	v_lshlrev_b32_e32 v246, 16, v165
	v_max_f32_e32 v139, v246, v246
	v_max_f32_e32 v129, 0x1e3ce508, v139
	v_rcp_f32_e32 v242, v129
	v_and_b32_e32 v246, 0xffff0000, v165
	v_max_f32_e32 v241, v246, v246
	v_max_f32_e32 v240, 0x1e3ce508, v241
	v_rcp_f32_e32 v243, v240
	v_lshlrev_b32_e32 v246, 16, v166
	v_max_f32_e32 v129, v246, v246
	v_max_f32_e32 v241, 0x1e3ce508, v129
	v_rcp_f32_e32 v138, v241
	v_and_b32_e32 v246, 0xffff0000, v166
	v_max_f32_e32 v136, v246, v246
	v_max_f32_e32 v129, 0x1e3ce508, v136
	v_rcp_f32_e32 v139, v129
	v_lshlrev_b32_e32 v246, 16, v167
	v_max_f32_e32 v136, v246, v246
	v_max_f32_e32 v129, 0x1e3ce508, v136
	v_rcp_f32_e32 v240, v129
	v_and_b32_e32 v246, 0xffff0000, v167
	v_max_f32_e32 v136, v246, v246
	v_max_f32_e32 v129, 0x1e3ce508, v136
	v_rcp_f32_e32 v241, v129
	s_waitcnt vmcnt(0)
	v_lshlrev_b32_e32 v238, 16, v168
	v_and_b32_e32 v239, 0xffff0000, v168
	v_lshlrev_b32_e32 v236, 16, v169
	v_and_b32_e32 v237, 0xffff0000, v169
	v_pk_mul_f32 v[234:235], v[244:245], v[238:239]
	v_pk_mul_f32 v[232:233], v[242:243], v[236:237]
	v_pk_mul_f32 v[52:53], v[52:53], v[234:235]
	v_lshlrev_b32_e32 v244, 16, v170
	v_and_b32_e32 v245, 0xffff0000, v170
	v_pk_mul_f32 v[54:55], v[54:55], v[232:233]
	v_lshlrev_b32_e32 v242, 16, v171
	v_and_b32_e32 v243, 0xffff0000, v171
	v_pk_mul_f32 v[238:239], v[138:139], v[244:245]
	v_pk_mul_f32 v[236:237], v[240:241], v[242:243]
	v_pk_mul_f32 v[48:49], v[48:49], v[238:239]
	v_pk_mul_f32 v[50:51], v[50:51], v[236:237]
	v_add_u32_e32 v129, 0x2f0000, v146
	v_add_u32_e32 v246, 0x2f0100, v146
	global_load_dwordx4 v[140:143], v129, s[36:37]
	global_load_dwordx4 v[160:163], v129, s[34:35]
	global_load_dwordx4 v[164:167], v246, s[36:37]
	v_add_u32_e32 v245, 0x34e100, v146
	v_add_u32_e32 v244, 0x34e000, v146
	global_load_dwordx4 v[168:171], v129, s[34:35] offset:256
	global_load_dwordx4 v[172:175], v244, s[34:35]
	global_load_dwordx4 v[176:179], v244, s[36:37]
	global_load_dwordx4 v[180:183], v245, s[36:37]
	s_waitcnt vmcnt(6)
	v_lshlrev_b32_e32 v129, 16, v140
	v_and_b32_e32 v246, 0xffff0000, v140
	v_lshlrev_b32_e32 v245, 16, v141
	v_and_b32_e32 v139, 0xffff0000, v141
	v_lshlrev_b32_e32 v138, 16, v142
	v_and_b32_e32 v136, 0xffff0000, v142
	v_lshlrev_b32_e32 v243, 16, v143
	v_and_b32_e32 v242, 0xffff0000, v143
	s_waitcnt vmcnt(5)
	v_lshlrev_b32_e32 v240, 16, v160
	v_and_b32_e32 v241, 0xffff0000, v160
	v_lshlrev_b32_e32 v238, 16, v162
	v_and_b32_e32 v239, 0xffff0000, v162
	v_lshlrev_b32_e32 v236, 16, v161
	v_and_b32_e32 v237, 0xffff0000, v161
	v_lshlrev_b32_e32 v234, 16, v163
	v_and_b32_e32 v235, 0xffff0000, v163
	s_waitcnt vmcnt(4)
	v_lshlrev_b32_e32 v233, 16, v164
	v_and_b32_e32 v232, 0xffff0000, v164
	v_max_f32_e32 v231, v129, v129
	v_max_f32_e32 v230, v246, v246
	v_max_f32_e32 v229, v233, v233
	v_max_f32_e32 v228, v232, v232
	v_max_f32_e32 v246, 0x1e3ce508, v231
	v_max_f32_e32 v129, 0x1e3ce508, v230
	v_lshlrev_b32_e32 v233, 16, v165
	v_and_b32_e32 v232, 0xffff0000, v165
	v_lshlrev_b32_e32 v231, 16, v166
	v_and_b32_e32 v230, 0xffff0000, v166
	v_max_f32_e32 v227, v139, v139
	v_max_f32_e32 v226, v138, v138
	v_max_f32_e32 v225, 0x1e3ce508, v229
	v_max_f32_e32 v224, 0x1e3ce508, v228
	v_rcp_f32_e32 v138, v246
	v_rcp_f32_e32 v139, v129
	v_max_f32_e32 v229, v232, v232
	v_max_f32_e32 v246, v230, v230
	v_max_f32_e32 v129, 0x1e3ce508, v227
	v_max_f32_e32 v232, 0x1e3ce508, v226
	v_max_f32_e32 v230, v245, v245
	v_max_f32_e32 v228, v242, v242
	v_max_f32_e32 v227, v231, v231
	v_max_f32_e32 v245, 0x1e3ce508, v229
	v_max_f32_e32 v242, 0x1e3ce508, v246
	v_rcp_f32_e32 v223, v129
	v_rcp_f32_e32 v220, v232
	v_rcp_f32_e32 v218, v225
	v_rcp_f32_e32 v219, v224
	v_max_f32_e32 v246, v233, v233
	v_max_f32_e32 v129, 0x1e3ce508, v230
	v_max_f32_e32 v232, 0x1e3ce508, v228
	v_max_f32_e32 v233, 0x1e3ce508, v227
	v_lshlrev_b32_e32 v217, 16, v167
	v_and_b32_e32 v216, 0xffff0000, v167
	v_max_f32_e32 v231, v136, v136
	v_max_f32_e32 v230, v243, v243
	v_max_f32_e32 v229, 0x1e3ce508, v246
	v_rcp_f32_e32 v222, v129
	v_rcp_f32_e32 v227, v232
	v_rcp_f32_e32 v224, v233
	v_rcp_f32_e32 v225, v242
	v_pk_mul_f32 v[214:215], v[138:139], v[240:241]
	v_max_f32_e32 v246, v216, v216
	v_max_f32_e32 v228, 0x1e3ce508, v231
	v_max_f32_e32 v129, 0x1e3ce508, v230
	v_pk_mul_f32 v[44:45], v[44:45], v[214:215]
	s_waitcnt vmcnt(3)
	v_lshlrev_b32_e32 v232, 16, v168
	v_and_b32_e32 v233, 0xffff0000, v168
	v_max_f32_e32 v216, v217, v217
	v_max_f32_e32 v231, 0x1e3ce508, v246
	v_rcp_f32_e32 v221, v228
	v_rcp_f32_e32 v226, v129
	v_rcp_f32_e32 v138, v229
	v_rcp_f32_e32 v139, v245
	v_pk_mul_f32 v[242:243], v[218:219], v[232:233]
	v_max_f32_e32 v136, 0x1e3ce508, v216
	v_pk_mul_f32 v[12:13], v[12:13], v[242:243]
	v_lshlrev_b32_e32 v232, 16, v170
	v_and_b32_e32 v233, 0xffff0000, v170
	v_rcp_f32_e32 v228, v136
	v_rcp_f32_e32 v229, v231
	v_pk_mul_f32 v[242:243], v[224:225], v[232:233]
	s_waitcnt vmcnt(1)
	v_lshlrev_b32_e32 v136, 16, v176
	v_pk_mul_f32 v[8:9], v[8:9], v[242:243]
	v_lshlrev_b32_e32 v232, 16, v169
	v_and_b32_e32 v233, 0xffff0000, v169
	v_max_f32_e32 v129, v136, v136
	v_pk_mul_f32 v[230:231], v[222:223], v[236:237]
	v_pk_mul_f32 v[224:225], v[138:139], v[232:233]
	v_max_f32_e32 v246, 0x1e3ce508, v129
	v_pk_mul_f32 v[46:47], v[46:47], v[230:231]
	v_pk_mul_f32 v[14:15], v[14:15], v[224:225]
	v_lshlrev_b32_e32 v236, 16, v171
	v_and_b32_e32 v237, 0xffff0000, v171
	v_rcp_f32_e32 v232, v246
	v_and_b32_e32 v129, 0xffff0000, v176
	v_pk_mul_f32 v[230:231], v[220:221], v[238:239]
	v_pk_mul_f32 v[224:225], v[228:229], v[236:237]
	v_max_f32_e32 v246, v129, v129
	v_pk_mul_f32 v[40:41], v[40:41], v[230:231]
	v_pk_mul_f32 v[10:11], v[10:11], v[224:225]
	global_load_dwordx4 v[140:143], v244, s[34:35] offset:256
	v_max_f32_e32 v129, 0x1e3ce508, v246
	v_rcp_f32_e32 v233, v129
	v_lshlrev_b32_e32 v225, 16, v177
	v_max_f32_e32 v224, v225, v225
	v_max_f32_e32 v129, 0x1e3ce508, v224
	v_rcp_f32_e32 v244, v129
	v_and_b32_e32 v246, 0xffff0000, v177
	v_max_f32_e32 v225, v246, v246
	v_max_f32_e32 v224, 0x1e3ce508, v225
	v_rcp_f32_e32 v245, v224
	v_lshlrev_b32_e32 v246, 16, v178
	v_max_f32_e32 v129, v246, v246
	v_max_f32_e32 v225, 0x1e3ce508, v129
	v_pk_mul_f32 v[138:139], v[226:227], v[234:235]
	v_rcp_f32_e32 v242, v225
	v_add_u32_e32 v246, 0x3ac000, v146
	v_pk_mul_f32 v[42:43], v[42:43], v[138:139]
	global_load_dwordx4 v[160:163], v246, s[36:37]
	v_and_b32_e32 v129, 0xffff0000, v178
	v_max_f32_e32 v241, v129, v129
	v_max_f32_e32 v240, 0x1e3ce508, v241
	v_rcp_f32_e32 v243, v240
	v_lshlrev_b32_e32 v234, 16, v172
	v_and_b32_e32 v235, 0xffff0000, v172
	v_pk_mul_f32 v[240:241], v[232:233], v[234:235]
	v_lshlrev_b32_e32 v129, 16, v179
	v_pk_mul_f32 v[36:37], v[36:37], v[240:241]
	v_lshlrev_b32_e32 v138, 16, v174
	v_and_b32_e32 v139, 0xffff0000, v174
	v_pk_mul_f32 v[240:241], v[242:243], v[138:139]
	v_max_f32_e32 v136, v129, v129
	v_pk_mul_f32 v[32:33], v[32:33], v[240:241]
	v_lshlrev_b32_e32 v138, 16, v173
	v_and_b32_e32 v139, 0xffff0000, v173
	v_pk_mul_f32 v[242:243], v[244:245], v[138:139]
	global_load_dwordx4 v[164:167], v246, s[34:35]
	v_max_f32_e32 v129, 0x1e3ce508, v136
	v_rcp_f32_e32 v244, v129
	v_and_b32_e32 v241, 0xffff0000, v179
	v_max_f32_e32 v240, v241, v241
	v_max_f32_e32 v129, 0x1e3ce508, v240
	v_rcp_f32_e32 v245, v129
	s_waitcnt vmcnt(3)
	v_lshlrev_b32_e32 v241, 16, v180
	v_pk_mul_f32 v[38:39], v[38:39], v[242:243]
	v_lshlrev_b32_e32 v138, 16, v175
	v_and_b32_e32 v139, 0xffff0000, v175
	v_max_f32_e32 v136, v241, v241
	v_pk_mul_f32 v[242:243], v[244:245], v[138:139]
	v_max_f32_e32 v129, 0x1e3ce508, v136
	v_pk_mul_f32 v[34:35], v[34:35], v[242:243]
	v_rcp_f32_e32 v244, v129
	v_lshlrev_b32_e32 v139, 16, v182
	v_max_f32_e32 v138, v139, v139
	v_max_f32_e32 v129, 0x1e3ce508, v138
	v_rcp_f32_e32 v242, v129
	v_add_u32_e32 v241, 0x3ac100, v146
	global_load_dwordx4 v[168:171], v241, s[36:37]
	v_and_b32_e32 v129, 0xffff0000, v180
	v_max_f32_e32 v240, v129, v129
	v_max_f32_e32 v241, 0x1e3ce508, v240
	v_and_b32_e32 v139, 0xffff0000, v182
	v_rcp_f32_e32 v245, v241
	v_lshlrev_b32_e32 v129, 16, v181
	v_and_b32_e32 v240, 0xffff0000, v181
	v_max_f32_e32 v241, v139, v139
	v_max_f32_e32 v138, v129, v129
	v_max_f32_e32 v136, v240, v240
	v_max_f32_e32 v139, 0x1e3ce508, v241
	v_max_f32_e32 v129, 0x1e3ce508, v138
	v_max_f32_e32 v240, 0x1e3ce508, v136
	v_rcp_f32_e32 v243, v139
	v_lshlrev_b32_e32 v241, 16, v183
	v_and_b32_e32 v138, 0xffff0000, v183
	v_rcp_f32_e32 v238, v129
	v_rcp_f32_e32 v239, v240
	v_max_f32_e32 v237, v241, v241
	v_max_f32_e32 v236, v138, v138
	v_max_f32_e32 v129, 0x1e3ce508, v237
	v_max_f32_e32 v241, 0x1e3ce508, v236
	v_rcp_f32_e32 v138, v129
	v_rcp_f32_e32 v139, v241
	s_waitcnt vmcnt(3)
	v_lshlrev_b32_e32 v236, 16, v140
	v_and_b32_e32 v237, 0xffff0000, v140
	v_lshlrev_b32_e32 v240, 16, v141
	v_and_b32_e32 v241, 0xffff0000, v141
	v_pk_mul_f32 v[234:235], v[238:239], v[240:241]
	v_pk_mul_f32 v[232:233], v[244:245], v[236:237]
	v_pk_mul_f32 v[6:7], v[6:7], v[234:235]
	v_lshlrev_b32_e32 v240, 16, v143
	v_and_b32_e32 v241, 0xffff0000, v143
	v_pk_mul_f32 v[244:245], v[138:139], v[240:241]
	v_pk_mul_f32 v[4:5], v[4:5], v[232:233]
	v_pk_mul_f32 v[2:3], v[2:3], v[244:245]
	v_lshlrev_b32_e32 v240, 16, v142
	v_and_b32_e32 v241, 0xffff0000, v142
	v_pk_mul_f32 v[244:245], v[242:243], v[240:241]
	s_waitcnt vmcnt(2)
	v_lshlrev_b32_e32 v129, 16, v160
	v_max_f32_e32 v139, v129, v129
	v_max_f32_e32 v138, 0x1e3ce508, v139
	v_pk_mul_f32 v[0:1], v[0:1], v[244:245]
	v_rcp_f32_e32 v242, v138
	v_and_b32_e32 v129, 0xffff0000, v160
	v_max_f32_e32 v245, v129, v129
	global_load_dwordx4 v[140:143], v246, s[34:35] offset:256
	v_max_f32_e32 v244, 0x1e3ce508, v245
	v_rcp_f32_e32 v243, v244
	v_lshlrev_b32_e32 v129, 16, v161
	v_max_f32_e32 v241, v129, v129
	v_max_f32_e32 v240, 0x1e3ce508, v241
	v_rcp_f32_e32 v244, v240
	v_and_b32_e32 v246, 0xffff0000, v161
	v_max_f32_e32 v129, v246, v246
	v_max_f32_e32 v241, 0x1e3ce508, v129
	v_rcp_f32_e32 v245, v241
	v_lshlrev_b32_e32 v246, 16, v162
	v_max_f32_e32 v129, v246, v246
	v_max_f32_e32 v241, 0x1e3ce508, v129
	v_rcp_f32_e32 v138, v241
	v_add_u32_e32 v246, 0x40a000, v146
	global_load_dwordx4 v[172:175], v246, s[36:37]
	v_and_b32_e32 v136, 0xffff0000, v162
	v_max_f32_e32 v129, v136, v136
	v_max_f32_e32 v241, 0x1e3ce508, v129
	v_rcp_f32_e32 v139, v241
	v_lshlrev_b32_e32 v136, 16, v163
	v_max_f32_e32 v129, v136, v136
	v_max_f32_e32 v241, 0x1e3ce508, v129
	v_rcp_f32_e32 v238, v241
	v_and_b32_e32 v136, 0xffff0000, v163
	s_waitcnt vmcnt(3)
	v_lshlrev_b32_e32 v236, 16, v164
	v_and_b32_e32 v237, 0xffff0000, v164
	v_max_f32_e32 v129, v136, v136
	v_pk_mul_f32 v[240:241], v[242:243], v[236:237]
	v_max_f32_e32 v235, 0x1e3ce508, v129
	v_pk_mul_f32 v[28:29], v[28:29], v[240:241]
	v_lshlrev_b32_e32 v236, 16, v166
	v_and_b32_e32 v237, 0xffff0000, v166
	v_rcp_f32_e32 v239, v235
	v_pk_mul_f32 v[242:243], v[138:139], v[236:237]
	v_add_u32_e32 v129, 0x40a100, v146
	v_pk_mul_f32 v[24:25], v[24:25], v[242:243]
	v_lshlrev_b32_e32 v236, 16, v165
	v_and_b32_e32 v237, 0xffff0000, v165
	v_pk_mul_f32 v[146:147], v[244:245], v[236:237]
	s_waitcnt vmcnt(2)
	v_lshlrev_b32_e32 v139, 16, v168
	v_pk_mul_f32 v[30:31], v[30:31], v[146:147]
	v_lshlrev_b32_e32 v244, 16, v167
	v_and_b32_e32 v245, 0xffff0000, v167
	v_pk_mul_f32 v[236:237], v[238:239], v[244:245]
	global_load_dwordx4 v[160:163], v246, s[34:35]
	global_load_dwordx4 v[164:167], v129, s[36:37]
	v_max_f32_e32 v245, v139, v139
	v_max_f32_e32 v244, 0x1e3ce508, v245
	v_pk_mul_f32 v[26:27], v[26:27], v[236:237]
	v_rcp_f32_e32 v146, v244
	v_and_b32_e32 v129, 0xffff0000, v168
	v_max_f32_e32 v245, v129, v129
	v_max_f32_e32 v244, 0x1e3ce508, v245
	v_rcp_f32_e32 v147, v244
	v_lshlrev_b32_e32 v129, 16, v169
	v_max_f32_e32 v245, v129, v129
	v_max_f32_e32 v244, 0x1e3ce508, v245
	v_rcp_f32_e32 v138, v244
	v_and_b32_e32 v136, 0xffff0000, v169
	v_max_f32_e32 v129, v136, v136
	v_max_f32_e32 v245, 0x1e3ce508, v129
	v_rcp_f32_e32 v139, v245
	v_lshlrev_b32_e32 v136, 16, v170
	v_max_f32_e32 v129, v136, v136
	v_max_f32_e32 v245, 0x1e3ce508, v129
	v_and_b32_e32 v244, 0xffff0000, v170
	v_lshlrev_b32_e32 v136, 16, v171
	v_and_b32_e32 v129, 0xffff0000, v171
	v_max_f32_e32 v243, v136, v136
	v_max_f32_e32 v242, v129, v129
	v_max_f32_e32 v241, 0x1e3ce508, v243
	v_max_f32_e32 v136, 0x1e3ce508, v242
	v_rcp_f32_e32 v238, v241
	v_rcp_f32_e32 v239, v136
	v_max_f32_e32 v129, v244, v244
	v_max_f32_e32 v237, 0x1e3ce508, v129
	v_rcp_f32_e32 v242, v245
	v_rcp_f32_e32 v243, v237
	s_waitcnt vmcnt(3)
	v_lshlrev_b32_e32 v240, 16, v140
	v_and_b32_e32 v241, 0xffff0000, v140
	v_lshlrev_b32_e32 v244, 16, v141
	v_and_b32_e32 v245, 0xffff0000, v141
	v_pk_mul_f32 v[236:237], v[138:139], v[244:245]
	v_pk_mul_f32 v[234:235], v[146:147], v[240:241]
	v_pk_mul_f32 v[114:115], v[114:115], v[236:237]
	v_lshlrev_b32_e32 v244, 16, v143
	v_and_b32_e32 v245, 0xffff0000, v143
	v_pk_mul_f32 v[240:241], v[238:239], v[244:245]
	v_pk_mul_f32 v[112:113], v[112:113], v[234:235]
	v_lshlrev_b32_e32 v146, 16, v142
	v_and_b32_e32 v147, 0xffff0000, v142
	v_pk_mul_f32 v[118:119], v[118:119], v[240:241]
	global_load_dwordx4 v[168:171], v246, s[34:35] offset:256
	v_pk_mul_f32 v[244:245], v[242:243], v[146:147]
	s_waitcnt vmcnt(2)
	v_lshlrev_b32_e32 v138, 16, v160
	v_pk_mul_f32 v[116:117], v[116:117], v[244:245]
	v_lshlrev_b32_e32 v136, 16, v172
	v_max_f32_e32 v129, v136, v136
	v_max_f32_e32 v147, 0x1e3ce508, v129
	v_rcp_f32_e32 v244, v147
	v_and_b32_e32 v246, 0xffff0000, v172
	v_max_f32_e32 v136, v246, v246
	v_max_f32_e32 v129, 0x1e3ce508, v136
	v_rcp_f32_e32 v245, v129
	v_lshlrev_b32_e32 v246, 16, v173
	v_max_f32_e32 v136, v246, v246
	v_max_f32_e32 v129, 0x1e3ce508, v136
	v_rcp_f32_e32 v146, v129
	v_and_b32_e32 v246, 0xffff0000, v173
	v_max_f32_e32 v136, v246, v246
	v_max_f32_e32 v129, 0x1e3ce508, v136
	v_rcp_f32_e32 v147, v129
	v_lshlrev_b32_e32 v246, 16, v174
	v_max_f32_e32 v136, v246, v246
	v_max_f32_e32 v129, 0x1e3ce508, v136
	v_rcp_f32_e32 v242, v129
	v_and_b32_e32 v246, 0xffff0000, v174
	v_max_f32_e32 v136, v246, v246
	v_max_f32_e32 v129, 0x1e3ce508, v136
	v_rcp_f32_e32 v243, v129
	v_lshlrev_b32_e32 v246, 16, v175
	v_max_f32_e32 v136, v246, v246
	v_max_f32_e32 v129, 0x1e3ce508, v136
	v_rcp_f32_e32 v240, v129
	v_and_b32_e32 v246, 0xffff0000, v175
	v_and_b32_e32 v139, 0xffff0000, v160
	v_max_f32_e32 v136, v246, v246
	v_pk_mul_f32 v[238:239], v[244:245], v[138:139]
	v_max_f32_e32 v129, 0x1e3ce508, v136
	v_pk_mul_f32 v[20:21], v[20:21], v[238:239]
	v_lshlrev_b32_e32 v244, 16, v162
	v_and_b32_e32 v245, 0xffff0000, v162
	v_rcp_f32_e32 v241, v129
	v_pk_mul_f32 v[138:139], v[242:243], v[244:245]
	s_waitcnt vmcnt(1)
	v_lshlrev_b32_e32 v136, 16, v164
	v_pk_mul_f32 v[16:17], v[16:17], v[138:139]
	v_lshlrev_b32_e32 v242, 16, v161
	v_and_b32_e32 v243, 0xffff0000, v161
	v_pk_mul_f32 v[138:139], v[146:147], v[242:243]
	v_max_f32_e32 v129, v136, v136
	v_pk_mul_f32 v[22:23], v[22:23], v[138:139]
	v_lshlrev_b32_e32 v242, 16, v163
	v_and_b32_e32 v243, 0xffff0000, v163
	v_pk_mul_f32 v[146:147], v[240:241], v[242:243]
	v_max_f32_e32 v246, 0x1e3ce508, v129
	v_pk_mul_f32 v[18:19], v[18:19], v[146:147]
	v_rcp_f32_e32 v244, v246
	v_and_b32_e32 v129, 0xffff0000, v164
	v_max_f32_e32 v147, v129, v129
	v_max_f32_e32 v246, 0x1e3ce508, v147
	v_rcp_f32_e32 v245, v246
	v_lshlrev_b32_e32 v129, 16, v165
	v_max_f32_e32 v147, v129, v129
	v_max_f32_e32 v246, 0x1e3ce508, v147
	v_rcp_f32_e32 v138, v246
	v_and_b32_e32 v136, 0xffff0000, v165
	v_max_f32_e32 v129, v136, v136
	v_max_f32_e32 v246, 0x1e3ce508, v129
	v_rcp_f32_e32 v139, v246
	v_lshlrev_b32_e32 v136, 16, v166
	v_max_f32_e32 v129, v136, v136
	v_max_f32_e32 v246, 0x1e3ce508, v129
	v_rcp_f32_e32 v146, v246
	v_and_b32_e32 v136, 0xffff0000, v166
	v_max_f32_e32 v129, v136, v136
	v_max_f32_e32 v246, 0x1e3ce508, v129
	v_rcp_f32_e32 v147, v246
	v_lshlrev_b32_e32 v136, 16, v167
	v_max_f32_e32 v129, v136, v136
	v_max_f32_e32 v246, 0x1e3ce508, v129
	v_rcp_f32_e32 v242, v246
	v_and_b32_e32 v136, 0xffff0000, v167
	v_max_f32_e32 v129, v136, v136
	v_max_f32_e32 v246, 0x1e3ce508, v129
	v_rcp_f32_e32 v243, v246
	s_waitcnt vmcnt(0)
	v_lshlrev_b32_e32 v240, 16, v168
	v_and_b32_e32 v241, 0xffff0000, v168
	v_lshlrev_b32_e32 v238, 16, v169
	v_and_b32_e32 v239, 0xffff0000, v169
	v_pk_mul_f32 v[236:237], v[244:245], v[240:241]
	v_pk_mul_f32 v[234:235], v[138:139], v[238:239]
	v_pk_mul_f32 v[120:121], v[120:121], v[236:237]
	v_lshlrev_b32_e32 v240, 16, v170
	v_and_b32_e32 v241, 0xffff0000, v170
	v_pk_mul_f32 v[122:123], v[122:123], v[234:235]
	v_lshlrev_b32_e32 v244, 16, v171
	v_and_b32_e32 v245, 0xffff0000, v171
	v_pk_mul_f32 v[138:139], v[146:147], v[240:241]
	v_pk_mul_f32 v[238:239], v[242:243], v[244:245]
	v_pk_mul_f32 v[124:125], v[124:125], v[138:139]
	v_pk_mul_f32 v[126:127], v[126:127], v[238:239]
	s_cmp_eq_u32 s51, 2
	s_mov_b64 s[34:35], -1
	s_cbranch_scc1 .LBB0_882

.LBB0_1513:
	s_and_b32 s9, s5, 0x7fffffc0
	s_cmpk_lt_u32 s0, 0xb00
	s_cselect_b32 s10, 4, 20
	s_cmpk_gt_u32 s0, 0x5ff
	s_cselect_b32 s10, s10, 0
	s_and_b32 s12, s1, 0x7c0
	s_or_b32 s10, s10, s9
	v_add_u32_e32 v39, s12, v4
	v_lshl_add_u64 v[56:57], s[10:11], 2, v[0:1]
	v_add_u32_e32 v60, 2, v39
	v_add_u32_e32 v62, 4, v39
	v_add_u32_e32 v64, 6, v39
	v_add_u32_e32 v66, 8, v39
	v_add_u32_e32 v68, 10, v39
	v_add_u32_e32 v70, 12, v39
	v_add_u32_e32 v72, 14, v39
	v_add_u32_e32 v74, 16, v39
	v_add_u32_e32 v76, 18, v39
	v_add_u32_e32 v78, 20, v39
	v_add_u32_e32 v80, 22, v39
	v_add_u32_e32 v82, 24, v39
	v_add_u32_e32 v84, 26, v39
	v_add_u32_e32 v86, 28, v39
	v_add_u32_e32 v88, 30, v39
	v_add_u32_e32 v90, 32, v39
	v_add_u32_e32 v92, 34, v39
	v_add_u32_e32 v94, 36, v39
	v_add_u32_e32 v96, 38, v39
	v_add_u32_e32 v98, 40, v39
	v_add_u32_e32 v100, 42, v39
	v_add_u32_e32 v102, 44, v39
	v_add_u32_e32 v104, 46, v39
	v_add_u32_e32 v106, 48, v39
	v_add_u32_e32 v108, 50, v39
	v_add_u32_e32 v110, 52, v39
	v_add_u32_e32 v112, 54, v39
	v_add_u32_e32 v114, 56, v39
	v_add_u32_e32 v116, 58, v39
	v_add_u32_e32 v118, 60, v39
	v_add_u32_e32 v120, 62, v39
	s_lshl_b32 s10, s12, 1
	v_mad_i64_i32 v[58:59], s[12:13], v39, s7, v[56:57]
	v_mad_i64_i32 v[60:61], s[12:13], v60, s7, v[56:57]
	v_mad_i64_i32 v[62:63], s[12:13], v62, s7, v[56:57]
	v_mad_i64_i32 v[64:65], s[12:13], v64, s7, v[56:57]
	v_mad_i64_i32 v[66:67], s[12:13], v66, s7, v[56:57]
	v_mad_i64_i32 v[68:69], s[12:13], v68, s7, v[56:57]
	v_mad_i64_i32 v[70:71], s[12:13], v70, s7, v[56:57]
	v_mad_i64_i32 v[72:73], s[12:13], v72, s7, v[56:57]
	v_mad_i64_i32 v[74:75], s[12:13], v74, s7, v[56:57]
	v_mad_i64_i32 v[76:77], s[12:13], v76, s7, v[56:57]
	v_mad_i64_i32 v[78:79], s[12:13], v78, s7, v[56:57]
	v_mad_i64_i32 v[80:81], s[12:13], v80, s7, v[56:57]
	v_mad_i64_i32 v[82:83], s[12:13], v82, s7, v[56:57]
	v_mad_i64_i32 v[84:85], s[12:13], v84, s7, v[56:57]
	v_mad_i64_i32 v[86:87], s[12:13], v86, s7, v[56:57]
	v_mad_i64_i32 v[88:89], s[12:13], v88, s7, v[56:57]
	v_mad_i64_i32 v[90:91], s[12:13], v90, s7, v[56:57]
	v_mad_i64_i32 v[92:93], s[12:13], v92, s7, v[56:57]
	v_mad_i64_i32 v[94:95], s[12:13], v94, s7, v[56:57]
	v_mad_i64_i32 v[96:97], s[12:13], v96, s7, v[56:57]
	v_mad_i64_i32 v[98:99], s[12:13], v98, s7, v[56:57]
	v_mad_i64_i32 v[100:101], s[12:13], v100, s7, v[56:57]
	v_mad_i64_i32 v[102:103], s[12:13], v102, s7, v[56:57]
	v_mad_i64_i32 v[104:105], s[12:13], v104, s7, v[56:57]
	v_mad_i64_i32 v[106:107], s[12:13], v106, s7, v[56:57]
	v_mad_i64_i32 v[108:109], s[12:13], v108, s7, v[56:57]
	v_mad_i64_i32 v[110:111], s[12:13], v110, s7, v[56:57]
	v_mad_i64_i32 v[112:113], s[12:13], v112, s7, v[56:57]
	v_mad_i64_i32 v[114:115], s[12:13], v114, s7, v[56:57]
	v_mad_i64_i32 v[116:117], s[12:13], v116, s7, v[56:57]
	v_mad_i64_i32 v[118:119], s[12:13], v118, s7, v[56:57]
	v_mad_i64_i32 v[56:57], s[12:13], v120, s7, v[56:57]
	global_load_dwordx2 v[58:59], v[58:59], off nt
	s_nop 0
	global_load_dwordx2 v[60:61], v[60:61], off nt
	s_nop 0
	global_load_dwordx2 v[62:63], v[62:63], off nt
	s_nop 0
	global_load_dwordx2 v[64:65], v[64:65], off nt
	s_nop 0
	global_load_dwordx2 v[66:67], v[66:67], off nt
	s_nop 0
	global_load_dwordx2 v[68:69], v[68:69], off nt
	s_nop 0
	global_load_dwordx2 v[70:71], v[70:71], off nt
	s_nop 0
	global_load_dwordx2 v[72:73], v[72:73], off nt
	s_nop 0
	global_load_dwordx2 v[74:75], v[74:75], off nt
	s_nop 0
	global_load_dwordx2 v[76:77], v[76:77], off nt
	s_nop 0
	global_load_dwordx2 v[78:79], v[78:79], off nt
	s_nop 0
	global_load_dwordx2 v[80:81], v[80:81], off nt
	s_nop 0
	global_load_dwordx2 v[82:83], v[82:83], off nt
	s_nop 0
	global_load_dwordx2 v[84:85], v[84:85], off nt
	s_nop 0
	global_load_dwordx2 v[86:87], v[86:87], off nt
	s_nop 0
	global_load_dwordx2 v[88:89], v[88:89], off nt
	s_nop 0
	global_load_dwordx2 v[90:91], v[90:91], off nt
	s_nop 0
	global_load_dwordx2 v[92:93], v[92:93], off nt
	s_nop 0
	global_load_dwordx2 v[94:95], v[94:95], off nt
	s_nop 0
	global_load_dwordx2 v[96:97], v[96:97], off nt
	s_nop 0
	global_load_dwordx2 v[98:99], v[98:99], off nt
	s_nop 0
	global_load_dwordx2 v[100:101], v[100:101], off nt
	s_nop 0
	global_load_dwordx2 v[102:103], v[102:103], off nt
	s_nop 0
	global_load_dwordx2 v[104:105], v[104:105], off nt
	s_nop 0
	global_load_dwordx2 v[106:107], v[106:107], off nt
	s_nop 0
	global_load_dwordx2 v[108:109], v[108:109], off nt
	s_nop 0
	global_load_dwordx2 v[110:111], v[110:111], off nt
	s_nop 0
	global_load_dwordx2 v[112:113], v[112:113], off nt
	s_nop 0
	global_load_dwordx2 v[114:115], v[114:115], off nt
	s_nop 0
	global_load_dwordx2 v[116:117], v[116:117], off nt
	s_nop 0
	global_load_dwordx2 v[118:119], v[118:119], off nt
	s_nop 0
	global_load_dwordx2 v[56:57], v[56:57], off nt
	v_add_u32_e32 v40, s9, v5
	v_add_u32_e32 v42, 8, v40
	v_add_u32_e32 v44, 16, v40
	v_add_u32_e32 v46, 24, v40
	v_add_u32_e32 v48, 32, v40
	v_add_u32_e32 v50, 40, v40
	v_add_u32_e32 v52, 48, v40
	v_add_u32_e32 v54, 56, v40
	v_ashrrev_i32_e32 v41, 31, v40
	v_ashrrev_i32_e32 v43, 31, v42
	v_ashrrev_i32_e32 v45, 31, v44
	v_ashrrev_i32_e32 v47, 31, v46
	v_ashrrev_i32_e32 v49, 31, v48
	v_ashrrev_i32_e32 v51, 31, v50
	v_ashrrev_i32_e32 v53, 31, v52
	v_ashrrev_i32_e32 v55, 31, v54
	s_waitcnt vmcnt(0)
	ds_write2_b32 v7, v58, v59 offset1:1
	ds_write2_b32 v7, v60, v61 offset0:130 offset1:131
	ds_write2_b32 v8, v62, v63 offset1:1
	ds_write2_b32 v9, v64, v65 offset1:1
	ds_write2_b32 v10, v66, v67 offset1:1
	ds_write2_b32 v11, v68, v69 offset1:1
	ds_write2_b32 v12, v70, v71 offset1:1
	ds_write2_b32 v13, v72, v73 offset1:1
	ds_write2_b32 v14, v74, v75 offset1:1
	ds_write2_b32 v15, v76, v77 offset1:1
	ds_write2_b32 v16, v78, v79 offset1:1
	ds_write2_b32 v17, v80, v81 offset1:1
	ds_write2_b32 v18, v82, v83 offset1:1
	ds_write2_b32 v19, v84, v85 offset1:1
	ds_write2_b32 v20, v86, v87 offset1:1
	ds_write2_b32 v21, v88, v89 offset1:1
	ds_write2_b32 v22, v90, v91 offset1:1
	ds_write2_b32 v23, v92, v93 offset1:1
	ds_write2_b32 v24, v94, v95 offset1:1
	ds_write2_b32 v25, v96, v97 offset1:1
	ds_write2_b32 v26, v98, v99 offset1:1
	ds_write2_b32 v27, v100, v101 offset1:1
	ds_write2_b32 v28, v102, v103 offset1:1
	ds_write2_b32 v29, v104, v105 offset1:1
	ds_write2_b32 v30, v106, v107 offset1:1
	ds_write2_b32 v31, v108, v109 offset1:1
	ds_write2_b32 v32, v110, v111 offset1:1
	ds_write2_b32 v33, v112, v113 offset1:1
	ds_write2_b32 v34, v114, v115 offset1:1
	ds_write2_b32 v35, v116, v117 offset1:1
	ds_write2_b32 v36, v118, v119 offset1:1
	ds_write2_b32 v37, v56, v57 offset1:1
	v_lshlrev_b64 v[40:41], 12, v[40:41]
	v_lshlrev_b64 v[42:43], 12, v[42:43]
	v_lshlrev_b64 v[44:45], 12, v[44:45]
	v_lshlrev_b64 v[46:47], 12, v[46:47]
	v_lshlrev_b64 v[48:49], 12, v[48:49]
	v_lshlrev_b64 v[50:51], 12, v[50:51]
	v_lshlrev_b64 v[52:53], 12, v[52:53]
	v_lshlrev_b64 v[54:55], 12, v[54:55]
	v_lshl_add_u64 v[120:121], v[2:3], 0, s[10:11]
	s_waitcnt lgkmcnt(0)
	v_lshl_add_u64 v[122:123], v[120:121], 0, v[40:41]
	v_lshl_add_u64 v[124:125], v[120:121], 0, v[42:43]
	v_lshl_add_u64 v[126:127], v[120:121], 0, v[44:45]
	v_lshl_add_u64 v[128:129], v[120:121], 0, v[46:47]
	v_lshl_add_u64 v[130:131], v[120:121], 0, v[48:49]
	v_lshl_add_u64 v[132:133], v[120:121], 0, v[50:51]
	v_lshl_add_u64 v[134:135], v[120:121], 0, v[52:53]
	v_lshl_add_u64 v[120:121], v[120:121], 0, v[54:55]
	ds_read2_b32 v[44:45], v6 offset0:65 offset1:73
	ds_read2_b32 v[46:47], v6 offset1:8
	ds_read2_b32 v[48:49], v6 offset0:130 offset1:138
	ds_read2_b32 v[50:51], v6 offset0:195 offset1:203
	ds_read2_b32 v[52:53], v38 offset0:4 offset1:12
	ds_read2_b32 v[54:55], v38 offset0:69 offset1:77
	ds_read2_b32 v[56:57], v38 offset0:134 offset1:142
	ds_read2_b32 v[58:59], v38 offset0:199 offset1:207
	ds_read2_b32 v[60:61], v6 offset0:81 offset1:89
	ds_read2_b32 v[62:63], v6 offset0:16 offset1:24
	ds_read2_b32 v[64:65], v6 offset0:146 offset1:154
	ds_read2_b32 v[66:67], v6 offset0:211 offset1:219
	ds_read2_b32 v[68:69], v38 offset0:20 offset1:28
	ds_read2_b32 v[70:71], v38 offset0:85 offset1:93
	ds_read2_b32 v[72:73], v38 offset0:150 offset1:158
	ds_read2_b32 v[74:75], v38 offset0:215 offset1:223
	ds_read2_b32 v[76:77], v6 offset0:32 offset1:40
	ds_read2_b32 v[78:79], v6 offset0:97 offset1:105
	ds_read2_b32 v[80:81], v6 offset0:162 offset1:170
	ds_read2_b32 v[82:83], v6 offset0:227 offset1:235
	ds_read2_b32 v[84:85], v38 offset0:36 offset1:44
	ds_read2_b32 v[86:87], v38 offset0:101 offset1:109
	ds_read2_b32 v[88:89], v38 offset0:166 offset1:174
	ds_read2_b32 v[90:91], v38 offset0:231 offset1:239
	ds_read2_b32 v[92:93], v6 offset0:48 offset1:56
	ds_read2_b32 v[94:95], v6 offset0:113 offset1:121
	ds_read2_b32 v[96:97], v6 offset0:178 offset1:186
	ds_read2_b32 v[98:99], v6 offset0:243 offset1:251
	ds_read2_b32 v[100:101], v38 offset0:52 offset1:60
	ds_read2_b32 v[102:103], v38 offset0:117 offset1:125
	ds_read2_b32 v[104:105], v38 offset0:182 offset1:190
	ds_read2_b32 v[106:107], v38 offset0:247 offset1:255
	s_waitcnt lgkmcnt(14)
	v_cvt_pk_bf16_f32 v40, v46, v44
	v_cvt_pk_bf16_f32 v41, v48, v50
	v_cvt_pk_bf16_f32 v42, v52, v54
	v_cvt_pk_bf16_f32 v43, v56, v58
	v_cvt_pk_bf16_f32 v44, v47, v45
	v_cvt_pk_bf16_f32 v45, v49, v51
	v_cvt_pk_bf16_f32 v46, v53, v55
	v_cvt_pk_bf16_f32 v47, v57, v59
	v_cvt_pk_bf16_f32 v48, v62, v60
	v_cvt_pk_bf16_f32 v49, v64, v66
	v_cvt_pk_bf16_f32 v50, v68, v70
	v_cvt_pk_bf16_f32 v51, v72, v74
	v_cvt_pk_bf16_f32 v52, v63, v61
	v_cvt_pk_bf16_f32 v53, v65, v67
	v_cvt_pk_bf16_f32 v54, v69, v71
	v_cvt_pk_bf16_f32 v55, v73, v75
	v_cvt_pk_bf16_f32 v56, v76, v78
	s_waitcnt lgkmcnt(12)
	v_cvt_pk_bf16_f32 v57, v80, v82
	s_waitcnt lgkmcnt(10)
	v_cvt_pk_bf16_f32 v58, v84, v86
	s_waitcnt lgkmcnt(8)
	v_cvt_pk_bf16_f32 v59, v88, v90
	v_cvt_pk_bf16_f32 v60, v77, v79
	v_cvt_pk_bf16_f32 v61, v81, v83
	v_cvt_pk_bf16_f32 v62, v85, v87
	v_cvt_pk_bf16_f32 v63, v89, v91
	s_waitcnt lgkmcnt(6)
	v_cvt_pk_bf16_f32 v64, v92, v94
	s_waitcnt lgkmcnt(4)
	v_cvt_pk_bf16_f32 v65, v96, v98
	s_waitcnt lgkmcnt(2)
	v_cvt_pk_bf16_f32 v66, v100, v102
	s_waitcnt lgkmcnt(0)
	v_cvt_pk_bf16_f32 v67, v104, v106
	v_cvt_pk_bf16_f32 v68, v93, v95
	v_cvt_pk_bf16_f32 v69, v97, v99
	v_cvt_pk_bf16_f32 v70, v101, v103
	v_cvt_pk_bf16_f32 v71, v105, v107
	global_store_dwordx4 v[122:123], v[40:43], off
	global_store_dwordx4 v[124:125], v[44:47], off
	global_store_dwordx4 v[126:127], v[48:51], off
	global_store_dwordx4 v[128:129], v[52:55], off
	global_store_dwordx4 v[130:131], v[56:59], off
	global_store_dwordx4 v[132:133], v[60:63], off
	global_store_dwordx4 v[134:135], v[64:67], off
	global_store_dwordx4 v[120:121], v[68:71], off
	s_waitcnt lgkmcnt(0)
	s_add_i32 s8, s8, s58
	s_sub_i32 s1, s1, s4
	s_sub_i32 s0, s0, s58
	s_sub_i32 s5, s5, s6
	s_cmpk_lt_i32 s8, 0x1700
	s_cbranch_scc1 .LBB0_1513

.LBB0_1650:
	s_ashr_i32 s10, s0, 31
	s_lshr_b32 s10, s10, 23
	s_add_i32 s11, s0, s10
	s_ashr_i32 s10, s11, 9
	s_and_b32 s11, s11, 0xfe00
	s_sub_i32 s12, s0, s11
	s_sext_i32_i16 s13, s12
	s_bfe_u32 s13, s13, 0x5001a
	s_add_i32 s13, s12, s13
	s_ashr_i32 s11, s10, 31
	s_sext_i32_i16 s44, s13
	s_and_b32 s13, s13, 0xffe0
	s_lshl_b64 s[10:11], s[10:11], 23
	s_ashr_i32 s46, s44, 5
	s_sub_i32 s12, s12, s13
	s_add_u32 s10, s10, 0x8000000
	s_sext_i32_i16 s13, s12
	s_addc_u32 s12, s11, 0
	s_waitcnt lgkmcnt(0)
	s_add_u32 s47, s6, s10
	s_addc_u32 s11, s7, s12
	s_add_u32 s45, s8, s10
	s_addc_u32 s44, s9, s12
	s_lshl_b32 s12, s46, 6
	s_lshl_b32 s10, s13, 6
	s_lshl_b32 s13, s46, 7
	s_and_b32 s46, s13, 0xffffff00
	s_and_b32 s48, s12, 64
	s_ashr_i32 s13, s12, 31
	s_or_b32 s46, s48, s46
	s_lshl_b64 s[12:13], s[12:13], 2
	v_add_u32_e32 v4, s10, v6
	s_add_u32 s12, s47, s12
	v_ashrrev_i32_e32 v5, 31, v4
	s_addc_u32 s13, s11, s13
	v_lshlrev_b64 v[4:5], 12, v[4:5]
	v_lshl_add_u64 v[58:59], s[12:13], 0, v[0:1]
	v_lshl_add_u64 v[4:5], v[58:59], 0, v[4:5]
	v_add_co_u32_e32 v58, vcc, s1, v4
	s_ashr_i32 s11, s10, 31
	s_nop 0
	v_addc_co_u32_e32 v59, vcc, 0, v5, vcc
	v_add_co_u32_e32 v60, vcc, s4, v4
	v_add_u32_e32 v42, s46, v7
	s_nop 0
	v_addc_co_u32_e32 v61, vcc, 0, v5, vcc
	v_add_co_u32_e32 v62, vcc, s5, v4
	s_lshl_b64 s[10:11], s[10:11], 1
	s_nop 0
	v_addc_co_u32_e32 v63, vcc, 0, v5, vcc
	v_add_co_u32_e32 v64, vcc, s14, v4
	v_add_u32_e32 v44, 8, v42
	s_nop 0
	v_addc_co_u32_e32 v65, vcc, 0, v5, vcc
	v_add_co_u32_e32 v66, vcc, s15, v4
	v_add_u32_e32 v46, 16, v42
	s_nop 0
	v_addc_co_u32_e32 v67, vcc, 0, v5, vcc
	v_add_co_u32_e32 v68, vcc, s16, v4
	v_add_u32_e32 v48, 24, v42
	s_nop 0
	v_addc_co_u32_e32 v69, vcc, 0, v5, vcc
	v_add_co_u32_e32 v70, vcc, s17, v4
	v_add_u32_e32 v50, 32, v42
	s_nop 0
	v_addc_co_u32_e32 v71, vcc, 0, v5, vcc
	v_add_co_u32_e32 v72, vcc, s18, v4
	v_add_u32_e32 v52, 40, v42
	s_nop 0
	v_addc_co_u32_e32 v73, vcc, 0, v5, vcc
	v_add_co_u32_e32 v74, vcc, s19, v4
	v_add_u32_e32 v54, 48, v42
	s_nop 0
	v_addc_co_u32_e32 v75, vcc, 0, v5, vcc
	v_add_co_u32_e32 v76, vcc, s20, v4
	v_add_u32_e32 v56, 56, v42
	s_nop 0
	v_addc_co_u32_e32 v77, vcc, 0, v5, vcc
	v_add_co_u32_e32 v78, vcc, s21, v4
	s_add_u32 s10, s45, s10
	s_nop 0
	v_addc_co_u32_e32 v79, vcc, 0, v5, vcc
	v_add_co_u32_e32 v80, vcc, s22, v4
	v_ashrrev_i32_e32 v43, 31, v42
	s_nop 0
	v_addc_co_u32_e32 v81, vcc, 0, v5, vcc
	v_add_co_u32_e32 v82, vcc, s23, v4
	v_ashrrev_i32_e32 v45, 31, v44
	s_nop 0
	v_addc_co_u32_e32 v83, vcc, 0, v5, vcc
	v_add_co_u32_e32 v84, vcc, s24, v4
	v_ashrrev_i32_e32 v47, 31, v46
	s_nop 0
	v_addc_co_u32_e32 v85, vcc, 0, v5, vcc
	v_add_co_u32_e32 v86, vcc, s25, v4
	v_ashrrev_i32_e32 v49, 31, v48
	s_nop 0
	v_addc_co_u32_e32 v87, vcc, 0, v5, vcc
	v_add_co_u32_e32 v88, vcc, s26, v4
	v_ashrrev_i32_e32 v51, 31, v50
	s_nop 0
	v_addc_co_u32_e32 v89, vcc, 0, v5, vcc
	v_add_co_u32_e32 v90, vcc, s27, v4
	v_ashrrev_i32_e32 v53, 31, v52
	s_nop 0
	v_addc_co_u32_e32 v91, vcc, 0, v5, vcc
	v_add_co_u32_e32 v92, vcc, s28, v4
	v_ashrrev_i32_e32 v55, 31, v54
	s_nop 0
	v_addc_co_u32_e32 v93, vcc, 0, v5, vcc
	v_add_co_u32_e32 v94, vcc, s29, v4
	v_ashrrev_i32_e32 v57, 31, v56
	s_nop 0
	v_addc_co_u32_e32 v95, vcc, 0, v5, vcc
	v_add_co_u32_e32 v96, vcc, s30, v4
	s_addc_u32 s11, s44, s11
	s_nop 0
	v_addc_co_u32_e32 v97, vcc, 0, v5, vcc
	v_add_co_u32_e32 v98, vcc, s31, v4
	v_lshlrev_b64 v[42:43], 12, v[42:43]
	s_nop 0
	v_addc_co_u32_e32 v99, vcc, 0, v5, vcc
	v_add_co_u32_e32 v100, vcc, s34, v4
	v_lshlrev_b64 v[44:45], 12, v[44:45]
	s_nop 0
	v_addc_co_u32_e32 v101, vcc, 0, v5, vcc
	v_add_co_u32_e32 v102, vcc, s35, v4
	v_lshlrev_b64 v[46:47], 12, v[46:47]
	s_nop 0
	v_addc_co_u32_e32 v103, vcc, 0, v5, vcc
	v_add_co_u32_e32 v104, vcc, s36, v4
	v_lshlrev_b64 v[48:49], 12, v[48:49]
	s_nop 0
	v_addc_co_u32_e32 v105, vcc, 0, v5, vcc
	v_add_co_u32_e32 v106, vcc, s37, v4
	v_lshlrev_b64 v[50:51], 12, v[50:51]
	s_nop 0
	v_addc_co_u32_e32 v107, vcc, 0, v5, vcc
	v_add_co_u32_e32 v108, vcc, s38, v4
	v_lshlrev_b64 v[52:53], 12, v[52:53]
	s_nop 0
	v_addc_co_u32_e32 v109, vcc, 0, v5, vcc
	v_add_co_u32_e32 v110, vcc, s39, v4
	v_lshlrev_b64 v[54:55], 12, v[54:55]
	s_nop 0
	v_addc_co_u32_e32 v111, vcc, 0, v5, vcc
	v_add_co_u32_e32 v112, vcc, s40, v4
	v_lshlrev_b64 v[56:57], 12, v[56:57]
	s_nop 0
	v_addc_co_u32_e32 v113, vcc, 0, v5, vcc
	v_add_co_u32_e32 v114, vcc, s41, v4
	v_lshl_add_u64 v[120:121], s[10:11], 0, v[2:3]
	s_nop 0
	v_addc_co_u32_e32 v115, vcc, 0, v5, vcc
	v_add_co_u32_e32 v116, vcc, s42, v4
	v_lshl_add_u64 v[122:123], v[120:121], 0, v[42:43]
	s_nop 0
	v_addc_co_u32_e32 v117, vcc, 0, v5, vcc
	v_add_co_u32_e32 v118, vcc, s43, v4
	v_lshl_add_u64 v[124:125], v[120:121], 0, v[44:45]
	s_nop 0
	v_addc_co_u32_e32 v119, vcc, 0, v5, vcc
	global_load_dwordx2 v[4:5], v[4:5], off nt
	s_nop 0
	global_load_dwordx2 v[58:59], v[58:59], off nt
	s_nop 0
	global_load_dwordx2 v[60:61], v[60:61], off nt
	s_nop 0
	global_load_dwordx2 v[62:63], v[62:63], off nt
	s_nop 0
	global_load_dwordx2 v[64:65], v[64:65], off nt
	s_nop 0
	global_load_dwordx2 v[66:67], v[66:67], off nt
	s_nop 0
	global_load_dwordx2 v[68:69], v[68:69], off nt
	s_nop 0
	global_load_dwordx2 v[70:71], v[70:71], off nt
	s_nop 0
	global_load_dwordx2 v[72:73], v[72:73], off nt
	s_nop 0
	global_load_dwordx2 v[74:75], v[74:75], off nt
	s_nop 0
	global_load_dwordx2 v[76:77], v[76:77], off nt
	s_nop 0
	global_load_dwordx2 v[78:79], v[78:79], off nt
	s_nop 0
	global_load_dwordx2 v[80:81], v[80:81], off nt
	s_nop 0
	global_load_dwordx2 v[82:83], v[82:83], off nt
	s_nop 0
	global_load_dwordx2 v[84:85], v[84:85], off nt
	s_nop 0
	global_load_dwordx2 v[86:87], v[86:87], off nt
	s_nop 0
	global_load_dwordx2 v[88:89], v[88:89], off nt
	s_nop 0
	global_load_dwordx2 v[90:91], v[90:91], off nt
	s_nop 0
	global_load_dwordx2 v[92:93], v[92:93], off nt
	s_nop 0
	global_load_dwordx2 v[94:95], v[94:95], off nt
	s_nop 0
	global_load_dwordx2 v[96:97], v[96:97], off nt
	s_nop 0
	global_load_dwordx2 v[98:99], v[98:99], off nt
	s_nop 0
	global_load_dwordx2 v[100:101], v[100:101], off nt
	s_nop 0
	global_load_dwordx2 v[102:103], v[102:103], off nt
	s_nop 0
	global_load_dwordx2 v[104:105], v[104:105], off nt
	s_nop 0
	global_load_dwordx2 v[106:107], v[106:107], off nt
	s_nop 0
	global_load_dwordx2 v[108:109], v[108:109], off nt
	s_nop 0
	global_load_dwordx2 v[110:111], v[110:111], off nt
	s_nop 0
	global_load_dwordx2 v[112:113], v[112:113], off nt
	s_nop 0
	global_load_dwordx2 v[114:115], v[114:115], off nt
	s_nop 0
	global_load_dwordx2 v[116:117], v[116:117], off nt
	s_nop 0
	global_load_dwordx2 v[118:119], v[118:119], off nt
	s_waitcnt vmcnt(0)
	ds_write2_b32 v9, v4, v5 offset1:1
	ds_write2_b32 v9, v58, v59 offset0:130 offset1:131
	ds_write2_b32 v10, v60, v61 offset1:1
	ds_write2_b32 v11, v62, v63 offset1:1
	ds_write2_b32 v12, v64, v65 offset1:1
	ds_write2_b32 v13, v66, v67 offset1:1
	ds_write2_b32 v14, v68, v69 offset1:1
	ds_write2_b32 v15, v70, v71 offset1:1
	ds_write2_b32 v16, v72, v73 offset1:1
	ds_write2_b32 v17, v74, v75 offset1:1
	ds_write2_b32 v18, v76, v77 offset1:1
	ds_write2_b32 v19, v78, v79 offset1:1
	ds_write2_b32 v20, v80, v81 offset1:1
	ds_write2_b32 v21, v82, v83 offset1:1
	ds_write2_b32 v22, v84, v85 offset1:1
	ds_write2_b32 v23, v86, v87 offset1:1
	ds_write2_b32 v24, v88, v89 offset1:1
	ds_write2_b32 v25, v90, v91 offset1:1
	ds_write2_b32 v26, v92, v93 offset1:1
	ds_write2_b32 v27, v94, v95 offset1:1
	ds_write2_b32 v28, v96, v97 offset1:1
	ds_write2_b32 v29, v98, v99 offset1:1
	ds_write2_b32 v30, v100, v101 offset1:1
	ds_write2_b32 v31, v102, v103 offset1:1
	ds_write2_b32 v32, v104, v105 offset1:1
	ds_write2_b32 v33, v106, v107 offset1:1
	ds_write2_b32 v34, v108, v109 offset1:1
	ds_write2_b32 v35, v110, v111 offset1:1
	ds_write2_b32 v36, v112, v113 offset1:1
	ds_write2_b32 v37, v114, v115 offset1:1
	ds_write2_b32 v38, v116, v117 offset1:1
	ds_write2_b32 v39, v118, v119 offset1:1
	s_waitcnt lgkmcnt(0)
	v_lshl_add_u64 v[126:127], v[120:121], 0, v[46:47]
	v_lshl_add_u64 v[128:129], v[120:121], 0, v[48:49]
	v_lshl_add_u64 v[130:131], v[120:121], 0, v[50:51]
	v_lshl_add_u64 v[132:133], v[120:121], 0, v[52:53]
	v_lshl_add_u64 v[134:135], v[120:121], 0, v[54:55]
	v_lshl_add_u64 v[120:121], v[120:121], 0, v[56:57]
	ds_read2_b32 v[4:5], v8 offset0:65 offset1:73
	ds_read2_b32 v[46:47], v8 offset1:8
	ds_read2_b32 v[48:49], v8 offset0:130 offset1:138
	ds_read2_b32 v[50:51], v8 offset0:195 offset1:203
	ds_read2_b32 v[52:53], v40 offset0:4 offset1:12
	ds_read2_b32 v[54:55], v40 offset0:69 offset1:77
	ds_read2_b32 v[56:57], v40 offset0:134 offset1:142
	ds_read2_b32 v[58:59], v40 offset0:199 offset1:207
	ds_read2_b32 v[60:61], v8 offset0:81 offset1:89
	ds_read2_b32 v[62:63], v8 offset0:16 offset1:24
	ds_read2_b32 v[64:65], v8 offset0:146 offset1:154
	ds_read2_b32 v[66:67], v8 offset0:211 offset1:219
	ds_read2_b32 v[68:69], v40 offset0:20 offset1:28
	ds_read2_b32 v[70:71], v40 offset0:85 offset1:93
	ds_read2_b32 v[72:73], v40 offset0:150 offset1:158
	ds_read2_b32 v[74:75], v40 offset0:215 offset1:223
	ds_read2_b32 v[76:77], v8 offset0:32 offset1:40
	ds_read2_b32 v[78:79], v8 offset0:97 offset1:105
	ds_read2_b32 v[80:81], v8 offset0:162 offset1:170
	ds_read2_b32 v[82:83], v8 offset0:227 offset1:235
	ds_read2_b32 v[84:85], v40 offset0:36 offset1:44
	ds_read2_b32 v[86:87], v40 offset0:101 offset1:109
	ds_read2_b32 v[88:89], v40 offset0:166 offset1:174
	ds_read2_b32 v[90:91], v40 offset0:231 offset1:239
	ds_read2_b32 v[92:93], v8 offset0:48 offset1:56
	ds_read2_b32 v[94:95], v8 offset0:113 offset1:121
	ds_read2_b32 v[96:97], v8 offset0:178 offset1:186
	ds_read2_b32 v[98:99], v8 offset0:243 offset1:251
	ds_read2_b32 v[100:101], v40 offset0:52 offset1:60
	ds_read2_b32 v[102:103], v40 offset0:117 offset1:125
	ds_read2_b32 v[104:105], v40 offset0:182 offset1:190
	ds_read2_b32 v[106:107], v40 offset0:247 offset1:255
	s_waitcnt lgkmcnt(14)
	v_cvt_pk_bf16_f32 v42, v46, v4
	v_cvt_pk_bf16_f32 v43, v48, v50
	v_cvt_pk_bf16_f32 v44, v52, v54
	v_cvt_pk_bf16_f32 v45, v56, v58
	v_cvt_pk_bf16_f32 v46, v47, v5
	v_cvt_pk_bf16_f32 v47, v49, v51
	v_cvt_pk_bf16_f32 v48, v53, v55
	v_cvt_pk_bf16_f32 v49, v57, v59
	v_cvt_pk_bf16_f32 v50, v62, v60
	v_cvt_pk_bf16_f32 v51, v64, v66
	v_cvt_pk_bf16_f32 v52, v68, v70
	v_cvt_pk_bf16_f32 v53, v72, v74
	v_cvt_pk_bf16_f32 v54, v63, v61
	v_cvt_pk_bf16_f32 v55, v65, v67
	v_cvt_pk_bf16_f32 v56, v69, v71
	v_cvt_pk_bf16_f32 v57, v73, v75
	v_cvt_pk_bf16_f32 v58, v76, v78
	s_waitcnt lgkmcnt(12)
	v_cvt_pk_bf16_f32 v59, v80, v82
	s_waitcnt lgkmcnt(10)
	v_cvt_pk_bf16_f32 v60, v84, v86
	s_waitcnt lgkmcnt(8)
	v_cvt_pk_bf16_f32 v61, v88, v90
	v_cvt_pk_bf16_f32 v62, v77, v79
	v_cvt_pk_bf16_f32 v63, v81, v83
	v_cvt_pk_bf16_f32 v64, v85, v87
	v_cvt_pk_bf16_f32 v65, v89, v91
	s_waitcnt lgkmcnt(6)
	v_cvt_pk_bf16_f32 v66, v92, v94
	s_waitcnt lgkmcnt(4)
	v_cvt_pk_bf16_f32 v67, v96, v98
	s_waitcnt lgkmcnt(2)
	v_cvt_pk_bf16_f32 v68, v100, v102
	s_waitcnt lgkmcnt(0)
	v_cvt_pk_bf16_f32 v69, v104, v106
	v_cvt_pk_bf16_f32 v70, v93, v95
	v_cvt_pk_bf16_f32 v71, v97, v99
	v_cvt_pk_bf16_f32 v72, v101, v103
	v_cvt_pk_bf16_f32 v73, v105, v107
	global_store_dwordx4 v[122:123], v[42:45], off nt
	global_store_dwordx4 v[124:125], v[46:49], off nt
	global_store_dwordx4 v[126:127], v[50:53], off nt
	global_store_dwordx4 v[128:129], v[54:57], off nt
	global_store_dwordx4 v[130:131], v[58:61], off nt
	global_store_dwordx4 v[132:133], v[62:65], off nt
	global_store_dwordx4 v[134:135], v[66:69], off nt
	global_store_dwordx4 v[120:121], v[70:73], off nt
	s_waitcnt lgkmcnt(0)
	s_add_i32 s10, s0, 0x100
	s_cmpk_lt_i32 s0, 0x700
	s_mov_b32 s0, s10
	s_cbranch_scc1 .LBB0_1650

.LBB0_2187:
	s_cmpk_gt_i32 s80, 0xff
	s_mov_b64 s[12:13], -1
	s_cbranch_scc0 .LBB0_2197
	s_cmpk_gt_u32 s80, 0x1ff
	s_cbranch_scc0 .LBB0_2194
	s_cmpk_gt_u32 s80, 0x3ff
	s_cbranch_scc0 .LBB0_2191
	s_load_dwordx2 s[12:13], s[52:53], 0x90
	s_and_b32 s8, s4, 0x7fffffc0
	s_addk_i32 s8, 0xf800
	s_and_b32 s14, s0, 0x7c0
	s_lshl_b64 s[82:83], s[8:9], 2
	v_add_u32_e32 v10, s14, v74
	s_waitcnt lgkmcnt(0)
	s_add_u32 s12, s12, s82
	s_addc_u32 s13, s13, s83
	v_ashrrev_i32_e32 v11, 31, v10
	v_lshl_add_u64 v[12:13], s[12:13], 0, v[0:1]
	v_lshlrev_b64 v[10:11], 13, v[10:11]
	v_lshl_add_u64 v[66:67], v[12:13], 0, v[10:11]
	s_mov_b32 s12, 0x1000000
	v_add_co_u32_e32 v10, vcc, s12, v66
	s_mov_b32 s12, 0x1004000
	s_nop 0
	v_addc_co_u32_e32 v11, vcc, 0, v67, vcc
	v_add_co_u32_e32 v12, vcc, s12, v66
	s_mov_b32 s12, 0x1008000
	s_nop 0
	v_addc_co_u32_e32 v13, vcc, 0, v67, vcc
	v_add_co_u32_e32 v14, vcc, s12, v66
	s_mov_b32 s12, 0x100c000
	s_nop 0
	v_addc_co_u32_e32 v15, vcc, 0, v67, vcc
	v_add_co_u32_e32 v16, vcc, s12, v66
	s_mov_b32 s12, 0x1010000
	s_nop 0
	v_addc_co_u32_e32 v17, vcc, 0, v67, vcc
	v_add_co_u32_e32 v18, vcc, s12, v66
	s_mov_b32 s12, 0x1014000
	s_nop 0
	v_addc_co_u32_e32 v19, vcc, 0, v67, vcc
	v_add_co_u32_e32 v20, vcc, s12, v66
	s_mov_b32 s12, 0x1018000
	s_nop 0
	v_addc_co_u32_e32 v21, vcc, 0, v67, vcc
	v_add_co_u32_e32 v22, vcc, s12, v66
	s_mov_b32 s12, 0x101c000
	s_nop 0
	v_addc_co_u32_e32 v23, vcc, 0, v67, vcc
	v_add_co_u32_e32 v24, vcc, s12, v66
	s_mov_b32 s12, 0x1020000
	s_nop 0
	v_addc_co_u32_e32 v25, vcc, 0, v67, vcc
	v_add_co_u32_e32 v26, vcc, s12, v66
	s_mov_b32 s12, 0x1024000
	s_nop 0
	v_addc_co_u32_e32 v27, vcc, 0, v67, vcc
	v_add_co_u32_e32 v28, vcc, s12, v66
	s_mov_b32 s12, 0x1028000
	s_nop 0
	v_addc_co_u32_e32 v29, vcc, 0, v67, vcc
	v_add_co_u32_e32 v30, vcc, s12, v66
	s_mov_b32 s12, 0x102c000
	s_nop 0
	v_addc_co_u32_e32 v31, vcc, 0, v67, vcc
	v_add_co_u32_e32 v32, vcc, s12, v66
	s_mov_b32 s12, 0x1030000
	s_nop 0
	v_addc_co_u32_e32 v33, vcc, 0, v67, vcc
	v_add_co_u32_e32 v34, vcc, s12, v66
	s_mov_b32 s12, 0x1034000
	s_nop 0
	v_addc_co_u32_e32 v35, vcc, 0, v67, vcc
	v_add_co_u32_e32 v36, vcc, s12, v66
	s_mov_b32 s12, 0x1038000
	s_nop 0
	v_addc_co_u32_e32 v37, vcc, 0, v67, vcc
	v_add_co_u32_e32 v38, vcc, s12, v66
	s_mov_b32 s12, 0x103c000
	s_nop 0
	v_addc_co_u32_e32 v39, vcc, 0, v67, vcc
	v_add_co_u32_e32 v40, vcc, s12, v66
	s_mov_b32 s12, 0x1040000
	s_nop 0
	v_addc_co_u32_e32 v41, vcc, 0, v67, vcc
	v_add_co_u32_e32 v42, vcc, s12, v66
	s_mov_b32 s12, 0x1044000
	s_nop 0
	v_addc_co_u32_e32 v43, vcc, 0, v67, vcc
	v_add_co_u32_e32 v44, vcc, s12, v66
	s_mov_b32 s12, 0x1048000
	s_nop 0
	v_addc_co_u32_e32 v45, vcc, 0, v67, vcc
	v_add_co_u32_e32 v46, vcc, s12, v66
	s_mov_b32 s12, 0x104c000
	s_nop 0
	v_addc_co_u32_e32 v47, vcc, 0, v67, vcc
	v_add_co_u32_e32 v48, vcc, s12, v66
	s_mov_b32 s12, 0x1050000
	s_nop 0
	v_addc_co_u32_e32 v49, vcc, 0, v67, vcc
	v_add_co_u32_e32 v50, vcc, s12, v66
	s_mov_b32 s12, 0x1054000
	s_nop 0
	v_addc_co_u32_e32 v51, vcc, 0, v67, vcc
	v_add_co_u32_e32 v52, vcc, s12, v66
	s_mov_b32 s12, 0x1058000
	s_nop 0
	v_addc_co_u32_e32 v53, vcc, 0, v67, vcc
	v_add_co_u32_e32 v54, vcc, s12, v66
	s_mov_b32 s12, 0x105c000
	s_nop 0
	v_addc_co_u32_e32 v55, vcc, 0, v67, vcc
	v_add_co_u32_e32 v56, vcc, s12, v66
	s_mov_b32 s12, 0x1060000
	s_nop 0
	v_addc_co_u32_e32 v57, vcc, 0, v67, vcc
	v_add_co_u32_e32 v58, vcc, s12, v66
	s_mov_b32 s12, 0x1064000
	s_nop 0
	v_addc_co_u32_e32 v59, vcc, 0, v67, vcc
	v_add_co_u32_e32 v60, vcc, s12, v66
	s_mov_b32 s12, 0x1068000
	s_nop 0
	v_addc_co_u32_e32 v61, vcc, 0, v67, vcc
	v_add_co_u32_e32 v62, vcc, s12, v66
	s_mov_b32 s12, 0x106c000
	s_nop 0
	v_addc_co_u32_e32 v63, vcc, 0, v67, vcc
	v_add_co_u32_e32 v64, vcc, s12, v66
	s_mov_b32 s12, 0x1070000
	s_nop 0
	v_addc_co_u32_e32 v65, vcc, 0, v67, vcc
	v_add_co_u32_e32 v68, vcc, s12, v66
	s_mov_b32 s12, 0x1074000
	s_nop 0
	v_addc_co_u32_e32 v69, vcc, 0, v67, vcc
	v_add_co_u32_e32 v70, vcc, s12, v66
	s_mov_b32 s12, 0x1078000
	s_nop 0
	v_addc_co_u32_e32 v71, vcc, 0, v67, vcc
	v_add_co_u32_e32 v72, vcc, s12, v66
	s_mov_b32 s12, 0x107c000
	s_nop 0
	v_addc_co_u32_e32 v73, vcc, 0, v67, vcc
	v_add_co_u32_e32 v118, vcc, s12, v66
	global_load_dwordx2 v[10:11], v[10:11], off nt
	s_nop 0
	global_load_dwordx2 v[12:13], v[12:13], off nt
	s_nop 0
	global_load_dwordx2 v[14:15], v[14:15], off nt
	s_nop 0
	global_load_dwordx2 v[16:17], v[16:17], off nt
	s_nop 0
	global_load_dwordx2 v[18:19], v[18:19], off nt
	s_nop 0
	global_load_dwordx2 v[20:21], v[20:21], off nt
	s_nop 0
	global_load_dwordx2 v[22:23], v[22:23], off nt
	s_nop 0
	global_load_dwordx2 v[24:25], v[24:25], off nt
	s_nop 0
	global_load_dwordx2 v[26:27], v[26:27], off nt
	s_nop 0
	global_load_dwordx2 v[28:29], v[28:29], off nt
	s_nop 0
	global_load_dwordx2 v[30:31], v[30:31], off nt
	s_nop 0
	global_load_dwordx2 v[32:33], v[32:33], off nt
	s_nop 0
	global_load_dwordx2 v[34:35], v[34:35], off nt
	s_nop 0
	global_load_dwordx2 v[36:37], v[36:37], off nt
	s_nop 0
	global_load_dwordx2 v[38:39], v[38:39], off nt
	s_nop 0
	global_load_dwordx2 v[40:41], v[40:41], off nt
	s_nop 0
	global_load_dwordx2 v[42:43], v[42:43], off nt
	s_nop 0
	global_load_dwordx2 v[44:45], v[44:45], off nt
	s_nop 0
	global_load_dwordx2 v[46:47], v[46:47], off nt
	s_nop 0
	global_load_dwordx2 v[48:49], v[48:49], off nt
	s_nop 0
	global_load_dwordx2 v[50:51], v[50:51], off nt
	s_nop 0
	global_load_dwordx2 v[52:53], v[52:53], off nt
	s_nop 0
	global_load_dwordx2 v[54:55], v[54:55], off nt
	s_nop 0
	global_load_dwordx2 v[56:57], v[56:57], off nt
	s_nop 0
	global_load_dwordx2 v[58:59], v[58:59], off nt
	s_nop 0
	global_load_dwordx2 v[60:61], v[60:61], off nt
	s_nop 0
	global_load_dwordx2 v[62:63], v[62:63], off nt
	s_nop 0
	global_load_dwordx2 v[64:65], v[64:65], off nt
	v_addc_co_u32_e32 v119, vcc, 0, v67, vcc
	global_load_dwordx2 v[66:67], v[68:69], off nt
	s_nop 0
	global_load_dwordx2 v[68:69], v[70:71], off nt
	s_nop 0
	global_load_dwordx2 v[70:71], v[72:73], off nt
	s_nop 0
	global_load_dwordx2 v[72:73], v[118:119], off nt
	s_load_dwordx2 s[12:13], s[52:53], 0xf0
	s_waitcnt vmcnt(0)
	ds_write2_b32 v75, v10, v11 offset1:1
	ds_write2_b32 v75, v12, v13 offset0:130 offset1:131
	ds_write2_b32 v85, v14, v15 offset1:1
	ds_write2_b32 v86, v16, v17 offset1:1
	ds_write2_b32 v87, v18, v19 offset1:1
	ds_write2_b32 v88, v20, v21 offset1:1
	ds_write2_b32 v89, v22, v23 offset1:1
	ds_write2_b32 v90, v24, v25 offset1:1
	ds_write2_b32 v91, v26, v27 offset1:1
	ds_write2_b32 v92, v28, v29 offset1:1
	ds_write2_b32 v93, v30, v31 offset1:1
	ds_write2_b32 v94, v32, v33 offset1:1
	ds_write2_b32 v95, v34, v35 offset1:1
	ds_write2_b32 v96, v36, v37 offset1:1
	ds_write2_b32 v97, v38, v39 offset1:1
	ds_write2_b32 v98, v40, v41 offset1:1
	ds_write2_b32 v99, v42, v43 offset1:1
	ds_write2_b32 v100, v44, v45 offset1:1
	ds_write2_b32 v101, v46, v47 offset1:1
	ds_write2_b32 v102, v48, v49 offset1:1
	ds_write2_b32 v103, v50, v51 offset1:1
	ds_write2_b32 v104, v52, v53 offset1:1
	ds_write2_b32 v105, v54, v55 offset1:1
	ds_write2_b32 v106, v56, v57 offset1:1
	ds_write2_b32 v107, v58, v59 offset1:1
	ds_write2_b32 v109, v60, v61 offset1:1
	ds_write2_b32 v110, v62, v63 offset1:1
	ds_write2_b32 v111, v64, v65 offset1:1
	ds_write2_b32 v112, v66, v67 offset1:1
	ds_write2_b32 v113, v68, v69 offset1:1
	ds_write2_b32 v114, v70, v71 offset1:1
	ds_write2_b32 v115, v72, v73 offset1:1
	s_waitcnt lgkmcnt(0)
	s_lshl_b32 s14, s14, 1
	ds_read2_b32 v[14:15], v77 offset0:65 offset1:73
	ds_read2_b32 v[16:17], v77 offset1:8
	ds_read2_b32 v[18:19], v77 offset0:130 offset1:138
	ds_read2_b32 v[20:21], v77 offset0:195 offset1:203
	ds_read2_b32 v[22:23], v116 offset0:4 offset1:12
	ds_read2_b32 v[24:25], v116 offset0:69 offset1:77
	ds_read2_b32 v[26:27], v116 offset0:134 offset1:142
	ds_read2_b32 v[28:29], v116 offset0:199 offset1:207
	s_waitcnt lgkmcnt(0)
	s_add_u32 s12, s12, s14
	s_addc_u32 s13, s13, 0
	v_mov_b32_e32 v9, v1
	v_add_u32_e32 v32, s8, v76
	v_lshl_add_u64 v[10:11], s[12:13], 0, v[8:9]
	v_ashrrev_i32_e32 v33, 31, v32
	v_lshl_add_u64 v[30:31], v[10:11], 0, s[6:7]
	v_lshlrev_b64 v[32:33], 12, v[32:33]
	v_cvt_pk_bf16_f32 v10, v16, v14
	v_cvt_pk_bf16_f32 v11, v18, v20
	v_cvt_pk_bf16_f32 v12, v22, v24
	v_cvt_pk_bf16_f32 v13, v26, v28
	v_lshl_add_u64 v[32:33], v[30:31], 0, v[32:33]
	v_add_u32_e32 v14, s8, v78
	global_store_dwordx4 v[32:33], v[10:13], off
	s_mov_b64 s[12:13], 0
	s_nop 0
	v_cvt_pk_bf16_f32 v10, v17, v15
	v_ashrrev_i32_e32 v15, 31, v14
	v_cvt_pk_bf16_f32 v11, v19, v21
	v_cvt_pk_bf16_f32 v12, v23, v25
	v_cvt_pk_bf16_f32 v13, v27, v29
	v_lshlrev_b64 v[14:15], 12, v[14:15]
	ds_read2_b32 v[16:17], v77 offset0:81 offset1:89
	ds_read2_b32 v[18:19], v77 offset0:16 offset1:24
	ds_read2_b32 v[20:21], v77 offset0:146 offset1:154
	ds_read2_b32 v[22:23], v77 offset0:211 offset1:219
	ds_read2_b32 v[24:25], v116 offset0:20 offset1:28
	ds_read2_b32 v[26:27], v116 offset0:85 offset1:93
	ds_read2_b32 v[28:29], v116 offset0:150 offset1:158
	ds_read2_b32 v[32:33], v116 offset0:215 offset1:223
	v_lshl_add_u64 v[14:15], v[30:31], 0, v[14:15]
	global_store_dwordx4 v[14:15], v[10:13], off
	v_add_u32_e32 v14, s8, v79
	v_ashrrev_i32_e32 v15, 31, v14
	v_lshlrev_b64 v[14:15], 12, v[14:15]
	s_waitcnt lgkmcnt(6)
	v_cvt_pk_bf16_f32 v10, v18, v16
	s_waitcnt lgkmcnt(4)
	v_cvt_pk_bf16_f32 v11, v20, v22
	s_waitcnt lgkmcnt(2)
	v_cvt_pk_bf16_f32 v12, v24, v26
	s_waitcnt lgkmcnt(0)
	v_cvt_pk_bf16_f32 v13, v28, v32
	v_lshl_add_u64 v[14:15], v[30:31], 0, v[14:15]
	global_store_dwordx4 v[14:15], v[10:13], off
	v_add_u32_e32 v14, s8, v80
	v_ashrrev_i32_e32 v15, 31, v14
	v_cvt_pk_bf16_f32 v10, v19, v17
	v_cvt_pk_bf16_f32 v11, v21, v23
	v_cvt_pk_bf16_f32 v12, v25, v27
	v_cvt_pk_bf16_f32 v13, v29, v33
	v_lshlrev_b64 v[14:15], 12, v[14:15]
	ds_read2_b32 v[16:17], v77 offset0:32 offset1:40
	ds_read2_b32 v[18:19], v77 offset0:97 offset1:105
	ds_read2_b32 v[20:21], v77 offset0:162 offset1:170
	ds_read2_b32 v[22:23], v77 offset0:227 offset1:235
	ds_read2_b32 v[24:25], v116 offset0:36 offset1:44
	ds_read2_b32 v[26:27], v116 offset0:101 offset1:109
	ds_read2_b32 v[28:29], v116 offset0:166 offset1:174
	ds_read2_b32 v[32:33], v116 offset0:231 offset1:239
	v_lshl_add_u64 v[14:15], v[30:31], 0, v[14:15]
	global_store_dwordx4 v[14:15], v[10:13], off
	v_add_u32_e32 v14, s8, v81
	v_ashrrev_i32_e32 v15, 31, v14
	v_lshlrev_b64 v[14:15], 12, v[14:15]
	s_waitcnt lgkmcnt(6)
	v_cvt_pk_bf16_f32 v10, v16, v18
	s_waitcnt lgkmcnt(4)
	v_cvt_pk_bf16_f32 v11, v20, v22
	s_waitcnt lgkmcnt(2)
	v_cvt_pk_bf16_f32 v12, v24, v26
	s_waitcnt lgkmcnt(0)
	v_cvt_pk_bf16_f32 v13, v28, v32
	v_lshl_add_u64 v[14:15], v[30:31], 0, v[14:15]
	global_store_dwordx4 v[14:15], v[10:13], off
	v_add_u32_e32 v14, s8, v82
	v_ashrrev_i32_e32 v15, 31, v14
	v_cvt_pk_bf16_f32 v10, v17, v19
	v_cvt_pk_bf16_f32 v11, v21, v23
	v_cvt_pk_bf16_f32 v12, v25, v27
	v_cvt_pk_bf16_f32 v13, v29, v33
	v_lshlrev_b64 v[14:15], 12, v[14:15]
	ds_read2_b32 v[16:17], v77 offset0:48 offset1:56
	ds_read2_b32 v[18:19], v77 offset0:113 offset1:121
	ds_read2_b32 v[20:21], v77 offset0:178 offset1:186
	ds_read2_b32 v[22:23], v77 offset0:243 offset1:251
	ds_read2_b32 v[24:25], v116 offset0:52 offset1:60
	ds_read2_b32 v[26:27], v116 offset0:117 offset1:125
	ds_read2_b32 v[28:29], v116 offset0:182 offset1:190
	ds_read2_b32 v[32:33], v116 offset0:247 offset1:255
	v_lshl_add_u64 v[14:15], v[30:31], 0, v[14:15]
	global_store_dwordx4 v[14:15], v[10:13], off
	v_add_u32_e32 v14, s8, v83
	v_ashrrev_i32_e32 v15, 31, v14
	v_lshlrev_b64 v[14:15], 12, v[14:15]
	s_waitcnt lgkmcnt(6)
	v_cvt_pk_bf16_f32 v10, v16, v18
	s_waitcnt lgkmcnt(4)
	v_cvt_pk_bf16_f32 v11, v20, v22
	s_waitcnt lgkmcnt(2)
	v_cvt_pk_bf16_f32 v12, v24, v26
	s_waitcnt lgkmcnt(0)
	v_cvt_pk_bf16_f32 v13, v28, v32
	v_lshl_add_u64 v[14:15], v[30:31], 0, v[14:15]
	global_store_dwordx4 v[14:15], v[10:13], off
	v_add_u32_e32 v14, s8, v84
	v_ashrrev_i32_e32 v15, 31, v14
	v_lshlrev_b64 v[14:15], 12, v[14:15]
	v_cvt_pk_bf16_f32 v10, v17, v19
	v_cvt_pk_bf16_f32 v11, v21, v23
	v_cvt_pk_bf16_f32 v12, v25, v27
	v_cvt_pk_bf16_f32 v13, v29, v33
	v_lshl_add_u64 v[14:15], v[30:31], 0, v[14:15]
	global_store_dwordx4 v[14:15], v[10:13], off
	s_waitcnt lgkmcnt(0)
.LBB0_2191:
	s_andn2_b64 vcc, exec, s[12:13]
	s_cbranch_vccnz .LBB0_2193
	s_load_dwordx2 s[14:15], s[52:53], 0x88
	s_and_b32 s8, s16, 0xfc0
	s_addk_i32 s8, 0xf800
	s_and_b32 s12, s0, 0x3c0
	s_lshl_b64 s[82:83], s[8:9], 2
	v_add_u32_e32 v10, s12, v74
	s_waitcnt lgkmcnt(0)
	s_add_u32 s14, s14, s82
	s_addc_u32 s15, s15, s83
	v_ashrrev_i32_e32 v11, 31, v10
	v_lshl_add_u64 v[12:13], s[14:15], 0, v[0:1]
	v_lshlrev_b64 v[10:11], 13, v[10:11]
	v_lshl_add_u64 v[10:11], v[12:13], 0, v[10:11]
	s_mov_b32 s13, 0x800000
	v_add_co_u32_e32 v12, vcc, s13, v10
	s_mov_b32 s13, 0x804000
	s_nop 0
	v_addc_co_u32_e32 v13, vcc, 0, v11, vcc
	v_add_co_u32_e32 v14, vcc, s13, v10
	s_mov_b32 s13, 0x808000
	s_nop 0
	v_addc_co_u32_e32 v15, vcc, 0, v11, vcc
	v_add_co_u32_e32 v16, vcc, s13, v10
	s_mov_b32 s13, 0x80c000
	s_nop 0
	v_addc_co_u32_e32 v17, vcc, 0, v11, vcc
	v_add_co_u32_e32 v18, vcc, s13, v10
	s_mov_b32 s13, 0x810000
	s_nop 0
	v_addc_co_u32_e32 v19, vcc, 0, v11, vcc
	v_add_co_u32_e32 v20, vcc, s13, v10
	s_mov_b32 s13, 0x814000
	s_nop 0
	v_addc_co_u32_e32 v21, vcc, 0, v11, vcc
	v_add_co_u32_e32 v22, vcc, s13, v10
	s_mov_b32 s13, 0x818000
	s_nop 0
	v_addc_co_u32_e32 v23, vcc, 0, v11, vcc
	v_add_co_u32_e32 v24, vcc, s13, v10
	s_mov_b32 s13, 0x81c000
	s_nop 0
	v_addc_co_u32_e32 v25, vcc, 0, v11, vcc
	v_add_co_u32_e32 v26, vcc, s13, v10
	s_mov_b32 s13, 0x820000
	s_nop 0
	v_addc_co_u32_e32 v27, vcc, 0, v11, vcc
	v_add_co_u32_e32 v28, vcc, s13, v10
	s_mov_b32 s13, 0x824000
	s_nop 0
	v_addc_co_u32_e32 v29, vcc, 0, v11, vcc
	v_add_co_u32_e32 v30, vcc, s13, v10
	s_mov_b32 s13, 0x828000
	s_nop 0
	v_addc_co_u32_e32 v31, vcc, 0, v11, vcc
	v_add_co_u32_e32 v32, vcc, s13, v10
	s_mov_b32 s13, 0x82c000
	s_nop 0
	v_addc_co_u32_e32 v33, vcc, 0, v11, vcc
	v_add_co_u32_e32 v34, vcc, s13, v10
	global_load_dwordx2 v[12:13], v[12:13], off nt
	s_nop 0
	global_load_dwordx2 v[14:15], v[14:15], off nt
	s_nop 0
	global_load_dwordx2 v[16:17], v[16:17], off nt
	s_nop 0
	global_load_dwordx2 v[18:19], v[18:19], off nt
	v_addc_co_u32_e32 v35, vcc, 0, v11, vcc
	v_add_co_u32_e32 v36, vcc, s20, v10
	global_load_dwordx2 v[20:21], v[20:21], off nt
	s_nop 0
	global_load_dwordx2 v[22:23], v[22:23], off nt
	s_nop 0
	global_load_dwordx2 v[24:25], v[24:25], off nt
	s_nop 0
	global_load_dwordx2 v[26:27], v[26:27], off nt
	v_addc_co_u32_e32 v37, vcc, 0, v11, vcc
	v_add_co_u32_e32 v38, vcc, s21, v10
	global_load_dwordx2 v[28:29], v[28:29], off nt
	s_nop 0
	global_load_dwordx2 v[30:31], v[30:31], off nt
	s_nop 0
	global_load_dwordx2 v[32:33], v[32:33], off nt
	s_nop 0
	global_load_dwordx2 v[34:35], v[34:35], off nt
	v_addc_co_u32_e32 v39, vcc, 0, v11, vcc
	v_add_co_u32_e32 v40, vcc, s22, v10
	s_lshl_b32 s12, s12, 1
	s_nop 0
	v_addc_co_u32_e32 v41, vcc, 0, v11, vcc
	v_add_co_u32_e32 v42, vcc, s23, v10
	s_mov_b32 s13, s9
	s_nop 0
	v_addc_co_u32_e32 v43, vcc, 0, v11, vcc
	v_add_co_u32_e32 v44, vcc, s24, v10
	global_load_dwordx2 v[36:37], v[36:37], off nt
	s_nop 0
	global_load_dwordx2 v[38:39], v[38:39], off nt
	s_nop 0
	global_load_dwordx2 v[40:41], v[40:41], off nt
	s_nop 0
	global_load_dwordx2 v[42:43], v[42:43], off nt
	v_addc_co_u32_e32 v45, vcc, 0, v11, vcc
	v_add_co_u32_e32 v46, vcc, s25, v10
	s_nop 1
	v_addc_co_u32_e32 v47, vcc, 0, v11, vcc
	v_add_co_u32_e32 v48, vcc, s26, v10
	s_nop 1
	v_addc_co_u32_e32 v49, vcc, 0, v11, vcc
	v_add_co_u32_e32 v50, vcc, s27, v10
	s_nop 1
	v_addc_co_u32_e32 v51, vcc, 0, v11, vcc
	v_add_co_u32_e32 v52, vcc, s28, v10
	global_load_dwordx2 v[44:45], v[44:45], off nt
	s_nop 0
	global_load_dwordx2 v[46:47], v[46:47], off nt
	s_nop 0
	global_load_dwordx2 v[48:49], v[48:49], off nt
	s_nop 0
	global_load_dwordx2 v[50:51], v[50:51], off nt
	v_addc_co_u32_e32 v53, vcc, 0, v11, vcc
	v_add_co_u32_e32 v54, vcc, s29, v10
	s_nop 1
	v_addc_co_u32_e32 v55, vcc, 0, v11, vcc
	v_add_co_u32_e32 v56, vcc, s30, v10
	s_nop 1
	v_addc_co_u32_e32 v57, vcc, 0, v11, vcc
	v_add_co_u32_e32 v58, vcc, s31, v10
	s_nop 1
	v_addc_co_u32_e32 v59, vcc, 0, v11, vcc
	v_add_co_u32_e32 v60, vcc, s34, v10
	global_load_dwordx2 v[52:53], v[52:53], off nt
	s_nop 0
	global_load_dwordx2 v[54:55], v[54:55], off nt
	s_nop 0
	global_load_dwordx2 v[56:57], v[56:57], off nt
	s_nop 0
	global_load_dwordx2 v[58:59], v[58:59], off nt
	v_addc_co_u32_e32 v61, vcc, 0, v11, vcc
	v_add_co_u32_e32 v62, vcc, s35, v10
	s_nop 1
	v_addc_co_u32_e32 v63, vcc, 0, v11, vcc
	v_add_co_u32_e32 v64, vcc, s36, v10
	s_nop 1
	v_addc_co_u32_e32 v65, vcc, 0, v11, vcc
	v_add_co_u32_e32 v66, vcc, s37, v10
	s_nop 1
	v_addc_co_u32_e32 v67, vcc, 0, v11, vcc
	v_add_co_u32_e32 v68, vcc, s38, v10
	global_load_dwordx2 v[60:61], v[60:61], off nt
	s_nop 0
	global_load_dwordx2 v[62:63], v[62:63], off nt
	s_nop 0
	global_load_dwordx2 v[64:65], v[64:65], off nt
	s_nop 0
	global_load_dwordx2 v[66:67], v[66:67], off nt
	v_addc_co_u32_e32 v69, vcc, 0, v11, vcc
	v_add_co_u32_e32 v70, vcc, s39, v10
	s_nop 1
	v_addc_co_u32_e32 v71, vcc, 0, v11, vcc
	v_add_co_u32_e32 v72, vcc, s40, v10
	s_nop 1
	v_addc_co_u32_e32 v73, vcc, 0, v11, vcc
	v_add_co_u32_e32 v10, vcc, s41, v10
	s_nop 1
	v_addc_co_u32_e32 v11, vcc, 0, v11, vcc
	global_load_dwordx2 v[68:69], v[68:69], off nt
	s_nop 0
	global_load_dwordx2 v[70:71], v[70:71], off nt
	s_nop 0
	global_load_dwordx2 v[72:73], v[72:73], off nt
	s_nop 0
	global_load_dwordx2 v[10:11], v[10:11], off nt
	s_waitcnt vmcnt(0)
	ds_write2_b32 v75, v12, v13 offset1:1
	ds_write2_b32 v75, v14, v15 offset0:130 offset1:131
	ds_write2_b32 v85, v16, v17 offset1:1
	ds_write2_b32 v86, v18, v19 offset1:1
	ds_write2_b32 v87, v20, v21 offset1:1
	ds_write2_b32 v88, v22, v23 offset1:1
	ds_write2_b32 v89, v24, v25 offset1:1
	ds_write2_b32 v90, v26, v27 offset1:1
	ds_write2_b32 v91, v28, v29 offset1:1
	ds_write2_b32 v92, v30, v31 offset1:1
	ds_write2_b32 v93, v32, v33 offset1:1
	ds_write2_b32 v94, v34, v35 offset1:1
	ds_write2_b32 v95, v36, v37 offset1:1
	ds_write2_b32 v96, v38, v39 offset1:1
	ds_write2_b32 v97, v40, v41 offset1:1
	ds_write2_b32 v98, v42, v43 offset1:1
	ds_write2_b32 v99, v44, v45 offset1:1
	ds_write2_b32 v100, v46, v47 offset1:1
	ds_write2_b32 v101, v48, v49 offset1:1
	ds_write2_b32 v102, v50, v51 offset1:1
	ds_write2_b32 v103, v52, v53 offset1:1
	ds_write2_b32 v104, v54, v55 offset1:1
	ds_write2_b32 v105, v56, v57 offset1:1
	ds_write2_b32 v106, v58, v59 offset1:1
	ds_write2_b32 v107, v60, v61 offset1:1
	ds_write2_b32 v109, v62, v63 offset1:1
	ds_write2_b32 v110, v64, v65 offset1:1
	ds_write2_b32 v111, v66, v67 offset1:1
	ds_write2_b32 v112, v68, v69 offset1:1
	ds_write2_b32 v113, v70, v71 offset1:1
	ds_write2_b32 v114, v72, v73 offset1:1
	ds_write2_b32 v115, v10, v11 offset1:1
	s_waitcnt lgkmcnt(0)
	ds_read2_b32 v[14:15], v77 offset0:65 offset1:73
	ds_read2_b32 v[16:17], v77 offset1:8
	ds_read2_b32 v[18:19], v77 offset0:130 offset1:138
	ds_read2_b32 v[20:21], v77 offset0:195 offset1:203
	ds_read2_b32 v[22:23], v116 offset0:4 offset1:12
	ds_read2_b32 v[24:25], v116 offset0:69 offset1:77
	ds_read2_b32 v[26:27], v116 offset0:134 offset1:142
	ds_read2_b32 v[28:29], v116 offset0:199 offset1:207
	v_add_u32_e32 v32, s8, v76
	v_ashrrev_i32_e32 v33, 31, v32
	v_lshl_add_u64 v[30:31], v[2:3], 0, s[12:13]
	v_lshlrev_b64 v[32:33], 12, v[32:33]
	s_waitcnt lgkmcnt(6)
	v_cvt_pk_bf16_f32 v10, v16, v14
	s_waitcnt lgkmcnt(4)
	v_cvt_pk_bf16_f32 v11, v18, v20
	s_waitcnt lgkmcnt(2)
	v_cvt_pk_bf16_f32 v12, v22, v24
	s_waitcnt lgkmcnt(0)
	v_cvt_pk_bf16_f32 v13, v26, v28
	v_lshl_add_u64 v[32:33], v[30:31], 0, v[32:33]
	v_add_u32_e32 v14, s8, v78
	global_store_dwordx4 v[32:33], v[10:13], off
	s_nop 1
	v_cvt_pk_bf16_f32 v10, v17, v15
	v_ashrrev_i32_e32 v15, 31, v14
	v_cvt_pk_bf16_f32 v11, v19, v21
	v_cvt_pk_bf16_f32 v12, v23, v25
	v_cvt_pk_bf16_f32 v13, v27, v29
	v_lshlrev_b64 v[14:15], 12, v[14:15]
	ds_read2_b32 v[16:17], v77 offset0:81 offset1:89
	ds_read2_b32 v[18:19], v77 offset0:16 offset1:24
	ds_read2_b32 v[20:21], v77 offset0:146 offset1:154
	ds_read2_b32 v[22:23], v77 offset0:211 offset1:219
	ds_read2_b32 v[24:25], v116 offset0:20 offset1:28
	ds_read2_b32 v[26:27], v116 offset0:85 offset1:93
	ds_read2_b32 v[28:29], v116 offset0:150 offset1:158
	ds_read2_b32 v[32:33], v116 offset0:215 offset1:223
	v_lshl_add_u64 v[14:15], v[30:31], 0, v[14:15]
	global_store_dwordx4 v[14:15], v[10:13], off
	v_add_u32_e32 v14, s8, v79
	v_ashrrev_i32_e32 v15, 31, v14
	v_lshlrev_b64 v[14:15], 12, v[14:15]
	s_waitcnt lgkmcnt(6)
	v_cvt_pk_bf16_f32 v10, v18, v16
	s_waitcnt lgkmcnt(4)
	v_cvt_pk_bf16_f32 v11, v20, v22
	s_waitcnt lgkmcnt(2)
	v_cvt_pk_bf16_f32 v12, v24, v26
	s_waitcnt lgkmcnt(0)
	v_cvt_pk_bf16_f32 v13, v28, v32
	v_lshl_add_u64 v[14:15], v[30:31], 0, v[14:15]
	global_store_dwordx4 v[14:15], v[10:13], off
	v_add_u32_e32 v14, s8, v80
	v_ashrrev_i32_e32 v15, 31, v14
	v_cvt_pk_bf16_f32 v10, v19, v17
	v_cvt_pk_bf16_f32 v11, v21, v23
	v_cvt_pk_bf16_f32 v12, v25, v27
	v_cvt_pk_bf16_f32 v13, v29, v33
	v_lshlrev_b64 v[14:15], 12, v[14:15]
	ds_read2_b32 v[16:17], v77 offset0:32 offset1:40
	ds_read2_b32 v[18:19], v77 offset0:97 offset1:105
	ds_read2_b32 v[20:21], v77 offset0:162 offset1:170
	ds_read2_b32 v[22:23], v77 offset0:227 offset1:235
	ds_read2_b32 v[24:25], v116 offset0:36 offset1:44
	ds_read2_b32 v[26:27], v116 offset0:101 offset1:109
	ds_read2_b32 v[28:29], v116 offset0:166 offset1:174
	ds_read2_b32 v[32:33], v116 offset0:231 offset1:239
	v_lshl_add_u64 v[14:15], v[30:31], 0, v[14:15]
	global_store_dwordx4 v[14:15], v[10:13], off
	v_add_u32_e32 v14, s8, v81
	v_ashrrev_i32_e32 v15, 31, v14
	v_lshlrev_b64 v[14:15], 12, v[14:15]
	s_waitcnt lgkmcnt(6)
	v_cvt_pk_bf16_f32 v10, v16, v18
	s_waitcnt lgkmcnt(4)
	v_cvt_pk_bf16_f32 v11, v20, v22
	s_waitcnt lgkmcnt(2)
	v_cvt_pk_bf16_f32 v12, v24, v26
	s_waitcnt lgkmcnt(0)
	v_cvt_pk_bf16_f32 v13, v28, v32
	v_lshl_add_u64 v[14:15], v[30:31], 0, v[14:15]
	global_store_dwordx4 v[14:15], v[10:13], off
	v_add_u32_e32 v14, s8, v82
	v_ashrrev_i32_e32 v15, 31, v14
	v_cvt_pk_bf16_f32 v10, v17, v19
	v_cvt_pk_bf16_f32 v11, v21, v23
	v_cvt_pk_bf16_f32 v12, v25, v27
	v_cvt_pk_bf16_f32 v13, v29, v33
	v_lshlrev_b64 v[14:15], 12, v[14:15]
	ds_read2_b32 v[16:17], v77 offset0:48 offset1:56
	ds_read2_b32 v[18:19], v77 offset0:113 offset1:121
	ds_read2_b32 v[20:21], v77 offset0:178 offset1:186
	ds_read2_b32 v[22:23], v77 offset0:243 offset1:251
	ds_read2_b32 v[24:25], v116 offset0:52 offset1:60
	ds_read2_b32 v[26:27], v116 offset0:117 offset1:125
	ds_read2_b32 v[28:29], v116 offset0:182 offset1:190
	ds_read2_b32 v[32:33], v116 offset0:247 offset1:255
	v_lshl_add_u64 v[14:15], v[30:31], 0, v[14:15]
	global_store_dwordx4 v[14:15], v[10:13], off
	v_add_u32_e32 v14, s8, v83
	v_ashrrev_i32_e32 v15, 31, v14
	v_lshlrev_b64 v[14:15], 12, v[14:15]
	s_waitcnt lgkmcnt(6)
	v_cvt_pk_bf16_f32 v10, v16, v18
	s_waitcnt lgkmcnt(4)
	v_cvt_pk_bf16_f32 v11, v20, v22
	s_waitcnt lgkmcnt(2)
	v_cvt_pk_bf16_f32 v12, v24, v26
	s_waitcnt lgkmcnt(0)
	v_cvt_pk_bf16_f32 v13, v28, v32
	v_lshl_add_u64 v[14:15], v[30:31], 0, v[14:15]
	global_store_dwordx4 v[14:15], v[10:13], off
	v_add_u32_e32 v14, s8, v84
	v_ashrrev_i32_e32 v15, 31, v14
	v_lshlrev_b64 v[14:15], 12, v[14:15]
	v_cvt_pk_bf16_f32 v10, v17, v19
	v_cvt_pk_bf16_f32 v11, v21, v23
	v_cvt_pk_bf16_f32 v12, v25, v27
	v_cvt_pk_bf16_f32 v13, v29, v33
	v_lshl_add_u64 v[14:15], v[30:31], 0, v[14:15]
	global_store_dwordx4 v[14:15], v[10:13], off
	s_waitcnt lgkmcnt(0)

.LBB0_2194:
	s_andn2_b64 vcc, exec, s[12:13]
	s_cbranch_vccnz .LBB0_2196
	s_load_dwordx2 s[14:15], s[52:53], 0x80
	s_and_b32 s8, s18, 0xfc0
	s_addk_i32 s8, 0xf800
	s_and_b32 s12, s0, 0x1c0
	s_lshl_b64 s[82:83], s[8:9], 2
	v_add_u32_e32 v10, s12, v74
	s_waitcnt lgkmcnt(0)
	s_add_u32 s14, s14, s82
	s_addc_u32 s15, s15, s83
	v_ashrrev_i32_e32 v11, 31, v10
	v_lshl_add_u64 v[12:13], s[14:15], 0, v[0:1]
	v_lshlrev_b64 v[10:11], 13, v[10:11]
	v_lshl_add_u64 v[10:11], v[12:13], 0, v[10:11]
	v_add_co_u32_e32 v12, vcc, s42, v10
	s_lshl_b32 s12, s12, 1
	s_nop 0
	v_addc_co_u32_e32 v13, vcc, 0, v11, vcc
	v_add_co_u32_e32 v14, vcc, s43, v10
	s_mov_b32 s13, s9
	s_nop 0
	v_addc_co_u32_e32 v15, vcc, 0, v11, vcc
	v_add_co_u32_e32 v16, vcc, s44, v10
	s_nop 1
	v_addc_co_u32_e32 v17, vcc, 0, v11, vcc
	v_add_co_u32_e32 v18, vcc, s45, v10
	s_nop 1
	v_addc_co_u32_e32 v19, vcc, 0, v11, vcc
	v_add_co_u32_e32 v20, vcc, s46, v10
	global_load_dwordx2 v[12:13], v[12:13], off nt
	s_nop 0
	global_load_dwordx2 v[14:15], v[14:15], off nt
	s_nop 0
	global_load_dwordx2 v[16:17], v[16:17], off nt
	s_nop 0
	global_load_dwordx2 v[18:19], v[18:19], off nt
	v_addc_co_u32_e32 v21, vcc, 0, v11, vcc
	v_add_co_u32_e32 v22, vcc, s47, v10
	s_nop 1
	v_addc_co_u32_e32 v23, vcc, 0, v11, vcc
	v_add_co_u32_e32 v24, vcc, s48, v10
	s_nop 1
	v_addc_co_u32_e32 v25, vcc, 0, v11, vcc
	v_add_co_u32_e32 v26, vcc, s49, v10
	s_nop 1
	v_addc_co_u32_e32 v27, vcc, 0, v11, vcc
	v_add_co_u32_e32 v28, vcc, s51, v10
	global_load_dwordx2 v[20:21], v[20:21], off nt
	s_nop 0
	global_load_dwordx2 v[22:23], v[22:23], off nt
	s_nop 0
	global_load_dwordx2 v[24:25], v[24:25], off nt
	s_nop 0
	global_load_dwordx2 v[26:27], v[26:27], off nt
	v_addc_co_u32_e32 v29, vcc, 0, v11, vcc
	v_add_co_u32_e32 v30, vcc, s55, v10
	s_nop 1
	v_addc_co_u32_e32 v31, vcc, 0, v11, vcc
	v_add_co_u32_e32 v32, vcc, s57, v10
	s_nop 1
	v_addc_co_u32_e32 v33, vcc, 0, v11, vcc
	v_add_co_u32_e32 v34, vcc, s59, v10
	s_nop 1
	v_addc_co_u32_e32 v35, vcc, 0, v11, vcc
	v_add_co_u32_e32 v36, vcc, s60, v10
	global_load_dwordx2 v[28:29], v[28:29], off nt
	s_nop 0
	global_load_dwordx2 v[30:31], v[30:31], off nt
	s_nop 0
	global_load_dwordx2 v[32:33], v[32:33], off nt
	s_nop 0
	global_load_dwordx2 v[34:35], v[34:35], off nt
	v_addc_co_u32_e32 v37, vcc, 0, v11, vcc
	v_add_co_u32_e32 v38, vcc, s61, v10
	s_nop 1
	v_addc_co_u32_e32 v39, vcc, 0, v11, vcc
	v_add_co_u32_e32 v40, vcc, s62, v10
	s_nop 1
	v_addc_co_u32_e32 v41, vcc, 0, v11, vcc
	v_add_co_u32_e32 v42, vcc, s63, v10
	s_nop 1
	v_addc_co_u32_e32 v43, vcc, 0, v11, vcc
	v_add_co_u32_e32 v44, vcc, s64, v10
	global_load_dwordx2 v[36:37], v[36:37], off nt
	s_nop 0
	global_load_dwordx2 v[38:39], v[38:39], off nt
	s_nop 0
	global_load_dwordx2 v[40:41], v[40:41], off nt
	s_nop 0
	global_load_dwordx2 v[42:43], v[42:43], off nt
	v_addc_co_u32_e32 v45, vcc, 0, v11, vcc
	v_add_co_u32_e32 v46, vcc, s65, v10
	s_nop 1
	v_addc_co_u32_e32 v47, vcc, 0, v11, vcc
	v_add_co_u32_e32 v48, vcc, s66, v10
	s_nop 1
	v_addc_co_u32_e32 v49, vcc, 0, v11, vcc
	v_add_co_u32_e32 v50, vcc, s67, v10
	s_nop 1
	v_addc_co_u32_e32 v51, vcc, 0, v11, vcc
	v_add_co_u32_e32 v52, vcc, s68, v10
	global_load_dwordx2 v[44:45], v[44:45], off nt
	s_nop 0
	global_load_dwordx2 v[46:47], v[46:47], off nt
	s_nop 0
	global_load_dwordx2 v[48:49], v[48:49], off nt
	s_nop 0
	global_load_dwordx2 v[50:51], v[50:51], off nt
	v_addc_co_u32_e32 v53, vcc, 0, v11, vcc
	v_add_co_u32_e32 v54, vcc, s69, v10
	s_nop 1
	v_addc_co_u32_e32 v55, vcc, 0, v11, vcc
	v_add_co_u32_e32 v56, vcc, s70, v10
	s_nop 1
	v_addc_co_u32_e32 v57, vcc, 0, v11, vcc
	v_add_co_u32_e32 v58, vcc, s71, v10
	s_nop 1
	v_addc_co_u32_e32 v59, vcc, 0, v11, vcc
	v_add_co_u32_e32 v60, vcc, s72, v10
	global_load_dwordx2 v[52:53], v[52:53], off nt
	s_nop 0
	global_load_dwordx2 v[54:55], v[54:55], off nt
	s_nop 0
	global_load_dwordx2 v[56:57], v[56:57], off nt
	s_nop 0
	global_load_dwordx2 v[58:59], v[58:59], off nt
	v_addc_co_u32_e32 v61, vcc, 0, v11, vcc
	v_add_co_u32_e32 v62, vcc, s73, v10
	s_nop 1
	v_addc_co_u32_e32 v63, vcc, 0, v11, vcc
	v_add_co_u32_e32 v64, vcc, s74, v10
	s_nop 1
	v_addc_co_u32_e32 v65, vcc, 0, v11, vcc
	v_add_co_u32_e32 v66, vcc, s75, v10
	s_nop 1
	v_addc_co_u32_e32 v67, vcc, 0, v11, vcc
	v_add_co_u32_e32 v68, vcc, s76, v10
	global_load_dwordx2 v[60:61], v[60:61], off nt
	s_nop 0
	global_load_dwordx2 v[62:63], v[62:63], off nt
	s_nop 0
	global_load_dwordx2 v[64:65], v[64:65], off nt
	s_nop 0
	global_load_dwordx2 v[66:67], v[66:67], off nt
	v_addc_co_u32_e32 v69, vcc, 0, v11, vcc
	v_add_co_u32_e32 v70, vcc, s77, v10
	s_nop 1
	v_addc_co_u32_e32 v71, vcc, 0, v11, vcc
	v_add_co_u32_e32 v72, vcc, s78, v10
	s_nop 1
	v_addc_co_u32_e32 v73, vcc, 0, v11, vcc
	v_add_co_u32_e32 v10, vcc, s79, v10
	s_nop 1
	v_addc_co_u32_e32 v11, vcc, 0, v11, vcc
	global_load_dwordx2 v[68:69], v[68:69], off nt
	s_nop 0
	global_load_dwordx2 v[70:71], v[70:71], off nt
	s_nop 0
	global_load_dwordx2 v[72:73], v[72:73], off nt
	s_nop 0
	global_load_dwordx2 v[10:11], v[10:11], off nt
	s_waitcnt vmcnt(0)
	ds_write2_b32 v75, v12, v13 offset1:1
	ds_write2_b32 v75, v14, v15 offset0:130 offset1:131
	ds_write2_b32 v85, v16, v17 offset1:1
	ds_write2_b32 v86, v18, v19 offset1:1
	ds_write2_b32 v87, v20, v21 offset1:1
	ds_write2_b32 v88, v22, v23 offset1:1
	ds_write2_b32 v89, v24, v25 offset1:1
	ds_write2_b32 v90, v26, v27 offset1:1
	ds_write2_b32 v91, v28, v29 offset1:1
	ds_write2_b32 v92, v30, v31 offset1:1
	ds_write2_b32 v93, v32, v33 offset1:1
	ds_write2_b32 v94, v34, v35 offset1:1
	ds_write2_b32 v95, v36, v37 offset1:1
	ds_write2_b32 v96, v38, v39 offset1:1
	ds_write2_b32 v97, v40, v41 offset1:1
	ds_write2_b32 v98, v42, v43 offset1:1
	ds_write2_b32 v99, v44, v45 offset1:1
	ds_write2_b32 v100, v46, v47 offset1:1
	ds_write2_b32 v101, v48, v49 offset1:1
	ds_write2_b32 v102, v50, v51 offset1:1
	ds_write2_b32 v103, v52, v53 offset1:1
	ds_write2_b32 v104, v54, v55 offset1:1
	ds_write2_b32 v105, v56, v57 offset1:1
	ds_write2_b32 v106, v58, v59 offset1:1
	ds_write2_b32 v107, v60, v61 offset1:1
	ds_write2_b32 v109, v62, v63 offset1:1
	ds_write2_b32 v110, v64, v65 offset1:1
	ds_write2_b32 v111, v66, v67 offset1:1
	ds_write2_b32 v112, v68, v69 offset1:1
	ds_write2_b32 v113, v70, v71 offset1:1
	ds_write2_b32 v114, v72, v73 offset1:1
	ds_write2_b32 v115, v10, v11 offset1:1
	s_waitcnt lgkmcnt(0)
	ds_read2_b32 v[14:15], v77 offset0:65 offset1:73
	ds_read2_b32 v[16:17], v77 offset1:8
	ds_read2_b32 v[18:19], v77 offset0:130 offset1:138
	ds_read2_b32 v[20:21], v77 offset0:195 offset1:203
	ds_read2_b32 v[22:23], v116 offset0:4 offset1:12
	ds_read2_b32 v[24:25], v116 offset0:69 offset1:77
	ds_read2_b32 v[26:27], v116 offset0:134 offset1:142
	ds_read2_b32 v[28:29], v116 offset0:199 offset1:207
	v_add_u32_e32 v32, s8, v76
	v_ashrrev_i32_e32 v33, 31, v32
	v_lshl_add_u64 v[30:31], v[4:5], 0, s[12:13]
	v_lshlrev_b64 v[32:33], 12, v[32:33]
	s_waitcnt lgkmcnt(6)
	v_cvt_pk_bf16_f32 v10, v16, v14
	s_waitcnt lgkmcnt(4)
	v_cvt_pk_bf16_f32 v11, v18, v20
	s_waitcnt lgkmcnt(2)
	v_cvt_pk_bf16_f32 v12, v22, v24
	s_waitcnt lgkmcnt(0)
	v_cvt_pk_bf16_f32 v13, v26, v28
	v_lshl_add_u64 v[32:33], v[30:31], 0, v[32:33]
	v_add_u32_e32 v14, s8, v78
	global_store_dwordx4 v[32:33], v[10:13], off
	s_nop 1
	v_cvt_pk_bf16_f32 v10, v17, v15
	v_ashrrev_i32_e32 v15, 31, v14
	v_cvt_pk_bf16_f32 v11, v19, v21
	v_cvt_pk_bf16_f32 v12, v23, v25
	v_cvt_pk_bf16_f32 v13, v27, v29
	v_lshlrev_b64 v[14:15], 12, v[14:15]
	ds_read2_b32 v[16:17], v77 offset0:81 offset1:89
	ds_read2_b32 v[18:19], v77 offset0:16 offset1:24
	ds_read2_b32 v[20:21], v77 offset0:146 offset1:154
	ds_read2_b32 v[22:23], v77 offset0:211 offset1:219
	ds_read2_b32 v[24:25], v116 offset0:20 offset1:28
	ds_read2_b32 v[26:27], v116 offset0:85 offset1:93
	ds_read2_b32 v[28:29], v116 offset0:150 offset1:158
	ds_read2_b32 v[32:33], v116 offset0:215 offset1:223
	v_lshl_add_u64 v[14:15], v[30:31], 0, v[14:15]
	global_store_dwordx4 v[14:15], v[10:13], off
	v_add_u32_e32 v14, s8, v79
	v_ashrrev_i32_e32 v15, 31, v14
	v_lshlrev_b64 v[14:15], 12, v[14:15]
	s_waitcnt lgkmcnt(6)
	v_cvt_pk_bf16_f32 v10, v18, v16
	s_waitcnt lgkmcnt(4)
	v_cvt_pk_bf16_f32 v11, v20, v22
	s_waitcnt lgkmcnt(2)
	v_cvt_pk_bf16_f32 v12, v24, v26
	s_waitcnt lgkmcnt(0)
	v_cvt_pk_bf16_f32 v13, v28, v32
	v_lshl_add_u64 v[14:15], v[30:31], 0, v[14:15]
	global_store_dwordx4 v[14:15], v[10:13], off
	v_add_u32_e32 v14, s8, v80
	v_ashrrev_i32_e32 v15, 31, v14
	v_cvt_pk_bf16_f32 v10, v19, v17
	v_cvt_pk_bf16_f32 v11, v21, v23
	v_cvt_pk_bf16_f32 v12, v25, v27
	v_cvt_pk_bf16_f32 v13, v29, v33
	v_lshlrev_b64 v[14:15], 12, v[14:15]
	ds_read2_b32 v[16:17], v77 offset0:32 offset1:40
	ds_read2_b32 v[18:19], v77 offset0:97 offset1:105
	ds_read2_b32 v[20:21], v77 offset0:162 offset1:170
	ds_read2_b32 v[22:23], v77 offset0:227 offset1:235
	ds_read2_b32 v[24:25], v116 offset0:36 offset1:44
	ds_read2_b32 v[26:27], v116 offset0:101 offset1:109
	ds_read2_b32 v[28:29], v116 offset0:166 offset1:174
	ds_read2_b32 v[32:33], v116 offset0:231 offset1:239
	v_lshl_add_u64 v[14:15], v[30:31], 0, v[14:15]
	global_store_dwordx4 v[14:15], v[10:13], off
	v_add_u32_e32 v14, s8, v81
	v_ashrrev_i32_e32 v15, 31, v14
	v_lshlrev_b64 v[14:15], 12, v[14:15]
	s_waitcnt lgkmcnt(6)
	v_cvt_pk_bf16_f32 v10, v16, v18
	s_waitcnt lgkmcnt(4)
	v_cvt_pk_bf16_f32 v11, v20, v22
	s_waitcnt lgkmcnt(2)
	v_cvt_pk_bf16_f32 v12, v24, v26
	s_waitcnt lgkmcnt(0)
	v_cvt_pk_bf16_f32 v13, v28, v32
	v_lshl_add_u64 v[14:15], v[30:31], 0, v[14:15]
	global_store_dwordx4 v[14:15], v[10:13], off
	v_add_u32_e32 v14, s8, v82
	v_ashrrev_i32_e32 v15, 31, v14
	v_cvt_pk_bf16_f32 v10, v17, v19
	v_cvt_pk_bf16_f32 v11, v21, v23
	v_cvt_pk_bf16_f32 v12, v25, v27
	v_cvt_pk_bf16_f32 v13, v29, v33
	v_lshlrev_b64 v[14:15], 12, v[14:15]
	ds_read2_b32 v[16:17], v77 offset0:48 offset1:56
	ds_read2_b32 v[18:19], v77 offset0:113 offset1:121
	ds_read2_b32 v[20:21], v77 offset0:178 offset1:186
	ds_read2_b32 v[22:23], v77 offset0:243 offset1:251
	ds_read2_b32 v[24:25], v116 offset0:52 offset1:60
	ds_read2_b32 v[26:27], v116 offset0:117 offset1:125
	ds_read2_b32 v[28:29], v116 offset0:182 offset1:190
	ds_read2_b32 v[32:33], v116 offset0:247 offset1:255
	v_lshl_add_u64 v[14:15], v[30:31], 0, v[14:15]
	global_store_dwordx4 v[14:15], v[10:13], off
	v_add_u32_e32 v14, s8, v83
	v_ashrrev_i32_e32 v15, 31, v14
	v_lshlrev_b64 v[14:15], 12, v[14:15]
	s_waitcnt lgkmcnt(6)
	v_cvt_pk_bf16_f32 v10, v16, v18
	s_waitcnt lgkmcnt(4)
	v_cvt_pk_bf16_f32 v11, v20, v22
	s_waitcnt lgkmcnt(2)
	v_cvt_pk_bf16_f32 v12, v24, v26
	s_waitcnt lgkmcnt(0)
	v_cvt_pk_bf16_f32 v13, v28, v32
	v_lshl_add_u64 v[14:15], v[30:31], 0, v[14:15]
	global_store_dwordx4 v[14:15], v[10:13], off
	v_add_u32_e32 v14, s8, v84
	v_ashrrev_i32_e32 v15, 31, v14
	v_lshlrev_b64 v[14:15], 12, v[14:15]
	v_cvt_pk_bf16_f32 v10, v17, v19
	v_cvt_pk_bf16_f32 v11, v21, v23
	v_cvt_pk_bf16_f32 v12, v25, v27
	v_cvt_pk_bf16_f32 v13, v29, v33
	v_lshl_add_u64 v[14:15], v[30:31], 0, v[14:15]
	global_store_dwordx4 v[14:15], v[10:13], off
	s_waitcnt lgkmcnt(0)

.LBB0_2197:
	s_andn2_b64 vcc, exec, s[12:13]
	s_cbranch_vccnz .LBB0_2186
	s_ashr_i32 s8, s80, 31
	s_lshr_b32 s8, s8, 29
	s_add_i32 s8, s80, s8
	s_load_dwordx2 s[82:83], s[52:53], 0x78
	s_ashr_i32 s8, s8, 3
	s_lshl_b32 s12, s8, 6
	s_lshl_b32 s8, s8, 9
	s_sub_i32 s14, s0, s8
	s_ashr_i32 s13, s12, 31
	v_add_u32_e32 v10, s14, v74
	s_lshl_b64 s[84:85], s[12:13], 2
	s_waitcnt lgkmcnt(0)
	s_add_u32 s82, s82, s84
	v_ashrrev_i32_e32 v11, 31, v10
	s_addc_u32 s83, s83, s85
	v_lshlrev_b64 v[14:15], 13, v[10:11]
	v_add_u32_e32 v16, 2, v10
	v_add_u32_e32 v18, 4, v10
	v_add_u32_e32 v20, 6, v10
	v_add_u32_e32 v22, 8, v10
	v_add_u32_e32 v24, 10, v10
	v_add_u32_e32 v26, 12, v10
	v_add_u32_e32 v28, 14, v10
	v_add_u32_e32 v30, 16, v10
	v_add_u32_e32 v32, 18, v10
	v_add_u32_e32 v34, 20, v10
	v_add_u32_e32 v36, 22, v10
	v_add_u32_e32 v38, 24, v10
	v_add_u32_e32 v40, 26, v10
	v_add_u32_e32 v42, 28, v10
	v_add_u32_e32 v44, 30, v10
	v_add_u32_e32 v46, 32, v10
	v_add_u32_e32 v48, 34, v10
	v_add_u32_e32 v50, 36, v10
	v_add_u32_e32 v52, 38, v10
	v_add_u32_e32 v54, 40, v10
	v_add_u32_e32 v56, 42, v10
	v_add_u32_e32 v58, 44, v10
	v_add_u32_e32 v60, 46, v10
	v_add_u32_e32 v62, 48, v10
	v_add_u32_e32 v64, 50, v10
	v_add_u32_e32 v66, 52, v10
	v_add_u32_e32 v68, 54, v10
	v_add_u32_e32 v70, 56, v10
	v_add_u32_e32 v72, 58, v10
	v_add_u32_e32 v118, 60, v10
	v_add_u32_e32 v10, 62, v10
	v_lshl_add_u64 v[12:13], s[82:83], 0, v[0:1]
	v_ashrrev_i32_e32 v17, 31, v16
	v_ashrrev_i32_e32 v19, 31, v18
	v_ashrrev_i32_e32 v21, 31, v20
	v_ashrrev_i32_e32 v23, 31, v22
	v_ashrrev_i32_e32 v25, 31, v24
	v_ashrrev_i32_e32 v27, 31, v26
	v_ashrrev_i32_e32 v29, 31, v28
	v_ashrrev_i32_e32 v31, 31, v30
	v_ashrrev_i32_e32 v33, 31, v32
	v_ashrrev_i32_e32 v35, 31, v34
	v_ashrrev_i32_e32 v37, 31, v36
	v_ashrrev_i32_e32 v39, 31, v38
	v_ashrrev_i32_e32 v41, 31, v40
	v_ashrrev_i32_e32 v43, 31, v42
	v_ashrrev_i32_e32 v45, 31, v44
	v_ashrrev_i32_e32 v47, 31, v46
	v_ashrrev_i32_e32 v49, 31, v48
	v_ashrrev_i32_e32 v51, 31, v50
	v_ashrrev_i32_e32 v53, 31, v52
	v_ashrrev_i32_e32 v55, 31, v54
	v_ashrrev_i32_e32 v57, 31, v56
	v_ashrrev_i32_e32 v59, 31, v58
	v_ashrrev_i32_e32 v61, 31, v60
	v_ashrrev_i32_e32 v63, 31, v62
	v_ashrrev_i32_e32 v65, 31, v64
	v_ashrrev_i32_e32 v67, 31, v66
	v_ashrrev_i32_e32 v69, 31, v68
	v_ashrrev_i32_e32 v71, 31, v70
	v_ashrrev_i32_e32 v73, 31, v72
	v_ashrrev_i32_e32 v11, 31, v10
	v_lshl_add_u64 v[12:13], v[12:13], 0, s[10:11]
	v_lshlrev_b64 v[16:17], 13, v[16:17]
	v_lshlrev_b64 v[18:19], 13, v[18:19]
	v_lshlrev_b64 v[20:21], 13, v[20:21]
	v_lshlrev_b64 v[22:23], 13, v[22:23]
	v_lshlrev_b64 v[24:25], 13, v[24:25]
	v_lshlrev_b64 v[26:27], 13, v[26:27]
	v_lshlrev_b64 v[28:29], 13, v[28:29]
	v_lshlrev_b64 v[30:31], 13, v[30:31]
	v_lshlrev_b64 v[32:33], 13, v[32:33]
	v_lshlrev_b64 v[34:35], 13, v[34:35]
	v_lshlrev_b64 v[36:37], 13, v[36:37]
	v_lshlrev_b64 v[38:39], 13, v[38:39]
	v_lshlrev_b64 v[40:41], 13, v[40:41]
	v_lshlrev_b64 v[42:43], 13, v[42:43]
	v_lshlrev_b64 v[44:45], 13, v[44:45]
	v_lshlrev_b64 v[46:47], 13, v[46:47]
	v_lshlrev_b64 v[48:49], 13, v[48:49]
	v_lshlrev_b64 v[50:51], 13, v[50:51]
	v_lshlrev_b64 v[52:53], 13, v[52:53]
	v_lshlrev_b64 v[54:55], 13, v[54:55]
	v_lshlrev_b64 v[56:57], 13, v[56:57]
	v_lshlrev_b64 v[58:59], 13, v[58:59]
	v_lshlrev_b64 v[60:61], 13, v[60:61]
	v_lshlrev_b64 v[62:63], 13, v[62:63]
	v_lshlrev_b64 v[64:65], 13, v[64:65]
	v_lshlrev_b64 v[66:67], 13, v[66:67]
	v_lshlrev_b64 v[68:69], 13, v[68:69]
	v_lshlrev_b64 v[70:71], 13, v[70:71]
	v_lshlrev_b64 v[72:73], 13, v[72:73]
	v_ashrrev_i32_e32 v119, 31, v118
	v_lshlrev_b64 v[10:11], 13, v[10:11]
	v_lshl_add_u64 v[14:15], v[12:13], 0, v[14:15]
	v_lshl_add_u64 v[16:17], v[12:13], 0, v[16:17]
	v_lshl_add_u64 v[18:19], v[12:13], 0, v[18:19]
	v_lshl_add_u64 v[20:21], v[12:13], 0, v[20:21]
	v_lshl_add_u64 v[22:23], v[12:13], 0, v[22:23]
	v_lshl_add_u64 v[24:25], v[12:13], 0, v[24:25]
	v_lshl_add_u64 v[26:27], v[12:13], 0, v[26:27]
	v_lshl_add_u64 v[28:29], v[12:13], 0, v[28:29]
	v_lshl_add_u64 v[30:31], v[12:13], 0, v[30:31]
	v_lshl_add_u64 v[32:33], v[12:13], 0, v[32:33]
	v_lshl_add_u64 v[34:35], v[12:13], 0, v[34:35]
	v_lshl_add_u64 v[36:37], v[12:13], 0, v[36:37]
	v_lshl_add_u64 v[38:39], v[12:13], 0, v[38:39]
	v_lshl_add_u64 v[40:41], v[12:13], 0, v[40:41]
	v_lshl_add_u64 v[42:43], v[12:13], 0, v[42:43]
	v_lshl_add_u64 v[44:45], v[12:13], 0, v[44:45]
	v_lshl_add_u64 v[46:47], v[12:13], 0, v[46:47]
	v_lshl_add_u64 v[48:49], v[12:13], 0, v[48:49]
	v_lshl_add_u64 v[50:51], v[12:13], 0, v[50:51]
	v_lshl_add_u64 v[52:53], v[12:13], 0, v[52:53]
	v_lshl_add_u64 v[54:55], v[12:13], 0, v[54:55]
	v_lshl_add_u64 v[56:57], v[12:13], 0, v[56:57]
	v_lshl_add_u64 v[58:59], v[12:13], 0, v[58:59]
	v_lshl_add_u64 v[60:61], v[12:13], 0, v[60:61]
	v_lshl_add_u64 v[62:63], v[12:13], 0, v[62:63]
	v_lshl_add_u64 v[64:65], v[12:13], 0, v[64:65]
	v_lshl_add_u64 v[66:67], v[12:13], 0, v[66:67]
	v_lshl_add_u64 v[68:69], v[12:13], 0, v[68:69]
	v_lshl_add_u64 v[70:71], v[12:13], 0, v[70:71]
	v_lshl_add_u64 v[72:73], v[12:13], 0, v[72:73]
	v_lshlrev_b64 v[118:119], 13, v[118:119]
	v_lshl_add_u64 v[10:11], v[12:13], 0, v[10:11]
	global_load_dwordx2 v[14:15], v[14:15], off nt
	s_nop 0
	global_load_dwordx2 v[16:17], v[16:17], off nt
	s_nop 0
	global_load_dwordx2 v[18:19], v[18:19], off nt
	s_nop 0
	global_load_dwordx2 v[20:21], v[20:21], off nt
	s_nop 0
	global_load_dwordx2 v[22:23], v[22:23], off nt
	s_nop 0
	global_load_dwordx2 v[24:25], v[24:25], off nt
	s_nop 0
	global_load_dwordx2 v[26:27], v[26:27], off nt
	s_nop 0
	global_load_dwordx2 v[28:29], v[28:29], off nt
	s_nop 0
	global_load_dwordx2 v[30:31], v[30:31], off nt
	s_nop 0
	global_load_dwordx2 v[32:33], v[32:33], off nt
	s_nop 0
	global_load_dwordx2 v[34:35], v[34:35], off nt
	s_nop 0
	global_load_dwordx2 v[36:37], v[36:37], off nt
	s_nop 0
	global_load_dwordx2 v[38:39], v[38:39], off nt
	s_nop 0
	global_load_dwordx2 v[40:41], v[40:41], off nt
	s_nop 0
	global_load_dwordx2 v[42:43], v[42:43], off nt
	s_nop 0
	global_load_dwordx2 v[44:45], v[44:45], off nt
	s_nop 0
	global_load_dwordx2 v[46:47], v[46:47], off nt
	s_nop 0
	global_load_dwordx2 v[48:49], v[48:49], off nt
	s_nop 0
	global_load_dwordx2 v[50:51], v[50:51], off nt
	s_nop 0
	global_load_dwordx2 v[52:53], v[52:53], off nt
	s_nop 0
	global_load_dwordx2 v[54:55], v[54:55], off nt
	s_nop 0
	global_load_dwordx2 v[56:57], v[56:57], off nt
	s_nop 0
	global_load_dwordx2 v[58:59], v[58:59], off nt
	s_nop 0
	global_load_dwordx2 v[60:61], v[60:61], off nt
	s_nop 0
	global_load_dwordx2 v[62:63], v[62:63], off nt
	s_nop 0
	global_load_dwordx2 v[64:65], v[64:65], off nt
	s_nop 0
	global_load_dwordx2 v[66:67], v[66:67], off nt
	s_nop 0
	global_load_dwordx2 v[68:69], v[68:69], off nt
	v_lshl_add_u64 v[118:119], v[12:13], 0, v[118:119]
	global_load_dwordx2 v[12:13], v[70:71], off nt
	s_nop 0
	global_load_dwordx2 v[70:71], v[72:73], off nt
	s_nop 0
	global_load_dwordx2 v[72:73], v[118:119], off nt
	s_nop 0
	global_load_dwordx2 v[10:11], v[10:11], off nt
	s_waitcnt vmcnt(0)
	ds_write2_b32 v75, v14, v15 offset1:1
	ds_write2_b32 v75, v16, v17 offset0:130 offset1:131
	ds_write2_b32 v85, v18, v19 offset1:1
	ds_write2_b32 v86, v20, v21 offset1:1
	ds_write2_b32 v87, v22, v23 offset1:1
	ds_write2_b32 v88, v24, v25 offset1:1
	ds_write2_b32 v89, v26, v27 offset1:1
	ds_write2_b32 v90, v28, v29 offset1:1
	ds_write2_b32 v91, v30, v31 offset1:1
	ds_write2_b32 v92, v32, v33 offset1:1
	ds_write2_b32 v93, v34, v35 offset1:1
	ds_write2_b32 v94, v36, v37 offset1:1
	ds_write2_b32 v95, v38, v39 offset1:1
	ds_write2_b32 v96, v40, v41 offset1:1
	ds_write2_b32 v97, v42, v43 offset1:1
	ds_write2_b32 v98, v44, v45 offset1:1
	ds_write2_b32 v99, v46, v47 offset1:1
	ds_write2_b32 v100, v48, v49 offset1:1
	ds_write2_b32 v101, v50, v51 offset1:1
	ds_write2_b32 v102, v52, v53 offset1:1
	ds_write2_b32 v103, v54, v55 offset1:1
	ds_write2_b32 v104, v56, v57 offset1:1
	ds_write2_b32 v105, v58, v59 offset1:1
	ds_write2_b32 v106, v60, v61 offset1:1
	ds_write2_b32 v107, v62, v63 offset1:1
	ds_write2_b32 v109, v64, v65 offset1:1
	ds_write2_b32 v110, v66, v67 offset1:1
	ds_write2_b32 v111, v68, v69 offset1:1
	ds_write2_b32 v112, v12, v13 offset1:1
	ds_write2_b32 v113, v70, v71 offset1:1
	ds_write2_b32 v114, v72, v73 offset1:1
	ds_write2_b32 v115, v10, v11 offset1:1
	s_waitcnt lgkmcnt(0)
	ds_read2_b32 v[14:15], v77 offset0:65 offset1:73
	ds_read2_b32 v[16:17], v77 offset1:8
	ds_read2_b32 v[18:19], v77 offset0:130 offset1:138
	ds_read2_b32 v[20:21], v77 offset0:195 offset1:203
	ds_read2_b32 v[22:23], v116 offset0:4 offset1:12
	ds_read2_b32 v[24:25], v116 offset0:69 offset1:77
	ds_read2_b32 v[26:27], v116 offset0:134 offset1:142
	ds_read2_b32 v[28:29], v116 offset0:199 offset1:207
	v_add_u32_e32 v32, s12, v76
	s_ashr_i32 s15, s14, 31
	v_ashrrev_i32_e32 v33, 31, v32
	v_lshl_add_u64 v[30:31], s[14:15], 1, v[6:7]
	v_lshlrev_b64 v[32:33], 12, v[32:33]
	s_waitcnt lgkmcnt(6)
	v_cvt_pk_bf16_f32 v10, v16, v14
	s_waitcnt lgkmcnt(4)
	v_cvt_pk_bf16_f32 v11, v18, v20
	s_waitcnt lgkmcnt(2)
	v_cvt_pk_bf16_f32 v12, v22, v24
	s_waitcnt lgkmcnt(0)
	v_cvt_pk_bf16_f32 v13, v26, v28
	v_lshl_add_u64 v[32:33], v[30:31], 0, v[32:33]
	v_add_u32_e32 v14, s12, v78
	global_store_dwordx4 v[32:33], v[10:13], off
	s_nop 1
	v_cvt_pk_bf16_f32 v10, v17, v15
	v_ashrrev_i32_e32 v15, 31, v14
	v_cvt_pk_bf16_f32 v11, v19, v21
	v_cvt_pk_bf16_f32 v12, v23, v25
	v_cvt_pk_bf16_f32 v13, v27, v29
	v_lshlrev_b64 v[14:15], 12, v[14:15]
	ds_read2_b32 v[16:17], v77 offset0:81 offset1:89
	ds_read2_b32 v[18:19], v77 offset0:16 offset1:24
	ds_read2_b32 v[20:21], v77 offset0:146 offset1:154
	ds_read2_b32 v[22:23], v77 offset0:211 offset1:219
	ds_read2_b32 v[24:25], v116 offset0:20 offset1:28
	ds_read2_b32 v[26:27], v116 offset0:85 offset1:93
	ds_read2_b32 v[28:29], v116 offset0:150 offset1:158
	ds_read2_b32 v[32:33], v116 offset0:215 offset1:223
	v_lshl_add_u64 v[14:15], v[30:31], 0, v[14:15]
	global_store_dwordx4 v[14:15], v[10:13], off
	v_add_u32_e32 v14, s12, v79
	v_ashrrev_i32_e32 v15, 31, v14
	v_lshlrev_b64 v[14:15], 12, v[14:15]
	s_waitcnt lgkmcnt(6)
	v_cvt_pk_bf16_f32 v10, v18, v16
	s_waitcnt lgkmcnt(4)
	v_cvt_pk_bf16_f32 v11, v20, v22
	s_waitcnt lgkmcnt(2)
	v_cvt_pk_bf16_f32 v12, v24, v26
	s_waitcnt lgkmcnt(0)
	v_cvt_pk_bf16_f32 v13, v28, v32
	v_lshl_add_u64 v[14:15], v[30:31], 0, v[14:15]
	global_store_dwordx4 v[14:15], v[10:13], off
	v_add_u32_e32 v14, s12, v80
	v_ashrrev_i32_e32 v15, 31, v14
	v_cvt_pk_bf16_f32 v10, v19, v17
	v_cvt_pk_bf16_f32 v11, v21, v23
	v_cvt_pk_bf16_f32 v12, v25, v27
	v_cvt_pk_bf16_f32 v13, v29, v33
	v_lshlrev_b64 v[14:15], 12, v[14:15]
	ds_read2_b32 v[16:17], v77 offset0:32 offset1:40
	ds_read2_b32 v[18:19], v77 offset0:97 offset1:105
	ds_read2_b32 v[20:21], v77 offset0:162 offset1:170
	ds_read2_b32 v[22:23], v77 offset0:227 offset1:235
	ds_read2_b32 v[24:25], v116 offset0:36 offset1:44
	ds_read2_b32 v[26:27], v116 offset0:101 offset1:109
	ds_read2_b32 v[28:29], v116 offset0:166 offset1:174
	ds_read2_b32 v[32:33], v116 offset0:231 offset1:239
	v_lshl_add_u64 v[14:15], v[30:31], 0, v[14:15]
	global_store_dwordx4 v[14:15], v[10:13], off
	v_add_u32_e32 v14, s12, v81
	v_ashrrev_i32_e32 v15, 31, v14
	v_lshlrev_b64 v[14:15], 12, v[14:15]
	s_waitcnt lgkmcnt(6)
	v_cvt_pk_bf16_f32 v10, v16, v18
	s_waitcnt lgkmcnt(4)
	v_cvt_pk_bf16_f32 v11, v20, v22
	s_waitcnt lgkmcnt(2)
	v_cvt_pk_bf16_f32 v12, v24, v26
	s_waitcnt lgkmcnt(0)
	v_cvt_pk_bf16_f32 v13, v28, v32
	v_lshl_add_u64 v[14:15], v[30:31], 0, v[14:15]
	global_store_dwordx4 v[14:15], v[10:13], off
	v_add_u32_e32 v14, s12, v82
	v_ashrrev_i32_e32 v15, 31, v14
	v_cvt_pk_bf16_f32 v10, v17, v19
	v_cvt_pk_bf16_f32 v11, v21, v23
	v_cvt_pk_bf16_f32 v12, v25, v27
	v_cvt_pk_bf16_f32 v13, v29, v33
	v_lshlrev_b64 v[14:15], 12, v[14:15]
	ds_read2_b32 v[16:17], v77 offset0:48 offset1:56
	ds_read2_b32 v[18:19], v77 offset0:113 offset1:121
	ds_read2_b32 v[20:21], v77 offset0:178 offset1:186
	ds_read2_b32 v[22:23], v77 offset0:243 offset1:251
	ds_read2_b32 v[24:25], v116 offset0:52 offset1:60
	ds_read2_b32 v[26:27], v116 offset0:117 offset1:125
	ds_read2_b32 v[28:29], v116 offset0:182 offset1:190
	ds_read2_b32 v[32:33], v116 offset0:247 offset1:255
	v_lshl_add_u64 v[14:15], v[30:31], 0, v[14:15]
	global_store_dwordx4 v[14:15], v[10:13], off
	v_add_u32_e32 v14, s12, v83
	v_ashrrev_i32_e32 v15, 31, v14
	v_lshlrev_b64 v[14:15], 12, v[14:15]
	s_waitcnt lgkmcnt(6)
	v_cvt_pk_bf16_f32 v10, v16, v18
	s_waitcnt lgkmcnt(4)
	v_cvt_pk_bf16_f32 v11, v20, v22
	s_waitcnt lgkmcnt(2)
	v_cvt_pk_bf16_f32 v12, v24, v26
	s_waitcnt lgkmcnt(0)
	v_cvt_pk_bf16_f32 v13, v28, v32
	v_lshl_add_u64 v[14:15], v[30:31], 0, v[14:15]
	global_store_dwordx4 v[14:15], v[10:13], off
	v_add_u32_e32 v14, s12, v84
	v_ashrrev_i32_e32 v15, 31, v14
	v_lshlrev_b64 v[14:15], 12, v[14:15]
	v_cvt_pk_bf16_f32 v10, v17, v19
	v_cvt_pk_bf16_f32 v11, v21, v23
	v_cvt_pk_bf16_f32 v12, v25, v27
	v_cvt_pk_bf16_f32 v13, v29, v33
	v_lshl_add_u64 v[14:15], v[30:31], 0, v[14:15]
	global_store_dwordx4 v[14:15], v[10:13], off
	s_waitcnt lgkmcnt(0)
	s_branch .LBB0_2186

.LBB0_2205:
	s_cmpk_gt_i32 s81, 0xff
	s_mov_b64 s[12:13], -1
	s_cbranch_scc0 .LBB0_2215
	s_cmpk_gt_u32 s81, 0x1ff
	s_cbranch_scc0 .LBB0_2212
	s_cmpk_gt_u32 s81, 0x3ff
	s_cbranch_scc0 .LBB0_2209
	s_load_dwordx2 s[12:13], s[52:53], 0x90
	s_and_b32 s8, s16, 0x7fffffc0
	s_addk_i32 s8, 0xf800
	s_and_b32 s14, s5, 0x7c0
	s_lshl_b64 s[82:83], s[8:9], 2
	v_add_u32_e32 v10, s14, v74
	s_waitcnt lgkmcnt(0)
	s_add_u32 s12, s12, s82
	s_addc_u32 s13, s13, s83
	v_ashrrev_i32_e32 v11, 31, v10
	v_lshl_add_u64 v[12:13], s[12:13], 0, v[0:1]
	v_lshlrev_b64 v[10:11], 13, v[10:11]
	v_lshl_add_u64 v[66:67], v[12:13], 0, v[10:11]
	s_mov_b32 s12, 0x1000000
	v_add_co_u32_e32 v10, vcc, s12, v66
	s_mov_b32 s12, 0x1004000
	s_nop 0
	v_addc_co_u32_e32 v11, vcc, 0, v67, vcc
	v_add_co_u32_e32 v12, vcc, s12, v66
	s_mov_b32 s12, 0x1008000
	s_nop 0
	v_addc_co_u32_e32 v13, vcc, 0, v67, vcc
	v_add_co_u32_e32 v14, vcc, s12, v66
	s_mov_b32 s12, 0x100c000
	s_nop 0
	v_addc_co_u32_e32 v15, vcc, 0, v67, vcc
	v_add_co_u32_e32 v16, vcc, s12, v66
	s_mov_b32 s12, 0x1010000
	s_nop 0
	v_addc_co_u32_e32 v17, vcc, 0, v67, vcc
	v_add_co_u32_e32 v18, vcc, s12, v66
	s_mov_b32 s12, 0x1014000
	s_nop 0
	v_addc_co_u32_e32 v19, vcc, 0, v67, vcc
	v_add_co_u32_e32 v20, vcc, s12, v66
	s_mov_b32 s12, 0x1018000
	s_nop 0
	v_addc_co_u32_e32 v21, vcc, 0, v67, vcc
	v_add_co_u32_e32 v22, vcc, s12, v66
	s_mov_b32 s12, 0x101c000
	s_nop 0
	v_addc_co_u32_e32 v23, vcc, 0, v67, vcc
	v_add_co_u32_e32 v24, vcc, s12, v66
	s_mov_b32 s12, 0x1020000
	s_nop 0
	v_addc_co_u32_e32 v25, vcc, 0, v67, vcc
	v_add_co_u32_e32 v26, vcc, s12, v66
	s_mov_b32 s12, 0x1024000
	s_nop 0
	v_addc_co_u32_e32 v27, vcc, 0, v67, vcc
	v_add_co_u32_e32 v28, vcc, s12, v66
	s_mov_b32 s12, 0x1028000
	s_nop 0
	v_addc_co_u32_e32 v29, vcc, 0, v67, vcc
	v_add_co_u32_e32 v30, vcc, s12, v66
	s_mov_b32 s12, 0x102c000
	s_nop 0
	v_addc_co_u32_e32 v31, vcc, 0, v67, vcc
	v_add_co_u32_e32 v32, vcc, s12, v66
	s_mov_b32 s12, 0x1030000
	s_nop 0
	v_addc_co_u32_e32 v33, vcc, 0, v67, vcc
	v_add_co_u32_e32 v34, vcc, s12, v66
	s_mov_b32 s12, 0x1034000
	s_nop 0
	v_addc_co_u32_e32 v35, vcc, 0, v67, vcc
	v_add_co_u32_e32 v36, vcc, s12, v66
	s_mov_b32 s12, 0x1038000
	s_nop 0
	v_addc_co_u32_e32 v37, vcc, 0, v67, vcc
	v_add_co_u32_e32 v38, vcc, s12, v66
	s_mov_b32 s12, 0x103c000
	s_nop 0
	v_addc_co_u32_e32 v39, vcc, 0, v67, vcc
	v_add_co_u32_e32 v40, vcc, s12, v66
	s_mov_b32 s12, 0x1040000
	s_nop 0
	v_addc_co_u32_e32 v41, vcc, 0, v67, vcc
	v_add_co_u32_e32 v42, vcc, s12, v66
	s_mov_b32 s12, 0x1044000
	s_nop 0
	v_addc_co_u32_e32 v43, vcc, 0, v67, vcc
	v_add_co_u32_e32 v44, vcc, s12, v66
	s_mov_b32 s12, 0x1048000
	s_nop 0
	v_addc_co_u32_e32 v45, vcc, 0, v67, vcc
	v_add_co_u32_e32 v46, vcc, s12, v66
	s_mov_b32 s12, 0x104c000
	s_nop 0
	v_addc_co_u32_e32 v47, vcc, 0, v67, vcc
	v_add_co_u32_e32 v48, vcc, s12, v66
	s_mov_b32 s12, 0x1050000
	s_nop 0
	v_addc_co_u32_e32 v49, vcc, 0, v67, vcc
	v_add_co_u32_e32 v50, vcc, s12, v66
	s_mov_b32 s12, 0x1054000
	s_nop 0
	v_addc_co_u32_e32 v51, vcc, 0, v67, vcc
	v_add_co_u32_e32 v52, vcc, s12, v66
	s_mov_b32 s12, 0x1058000
	s_nop 0
	v_addc_co_u32_e32 v53, vcc, 0, v67, vcc
	v_add_co_u32_e32 v54, vcc, s12, v66
	s_mov_b32 s12, 0x105c000
	s_nop 0
	v_addc_co_u32_e32 v55, vcc, 0, v67, vcc
	v_add_co_u32_e32 v56, vcc, s12, v66
	s_mov_b32 s12, 0x1060000
	s_nop 0
	v_addc_co_u32_e32 v57, vcc, 0, v67, vcc
	v_add_co_u32_e32 v58, vcc, s12, v66
	s_mov_b32 s12, 0x1064000
	s_nop 0
	v_addc_co_u32_e32 v59, vcc, 0, v67, vcc
	v_add_co_u32_e32 v60, vcc, s12, v66
	s_mov_b32 s12, 0x1068000
	s_nop 0
	v_addc_co_u32_e32 v61, vcc, 0, v67, vcc
	v_add_co_u32_e32 v62, vcc, s12, v66
	s_mov_b32 s12, 0x106c000
	s_nop 0
	v_addc_co_u32_e32 v63, vcc, 0, v67, vcc
	v_add_co_u32_e32 v64, vcc, s12, v66
	s_mov_b32 s12, 0x1070000
	s_nop 0
	v_addc_co_u32_e32 v65, vcc, 0, v67, vcc
	v_add_co_u32_e32 v68, vcc, s12, v66
	s_mov_b32 s12, 0x1074000
	s_nop 0
	v_addc_co_u32_e32 v69, vcc, 0, v67, vcc
	v_add_co_u32_e32 v70, vcc, s12, v66
	s_mov_b32 s12, 0x1078000
	s_nop 0
	v_addc_co_u32_e32 v71, vcc, 0, v67, vcc
	v_add_co_u32_e32 v72, vcc, s12, v66
	s_mov_b32 s12, 0x107c000
	s_nop 0
	v_addc_co_u32_e32 v73, vcc, 0, v67, vcc
	v_add_co_u32_e32 v118, vcc, s12, v66
	global_load_dwordx2 v[10:11], v[10:11], off nt
	s_nop 0
	global_load_dwordx2 v[12:13], v[12:13], off nt
	s_nop 0
	global_load_dwordx2 v[14:15], v[14:15], off nt
	s_nop 0
	global_load_dwordx2 v[16:17], v[16:17], off nt
	s_nop 0
	global_load_dwordx2 v[18:19], v[18:19], off nt
	s_nop 0
	global_load_dwordx2 v[20:21], v[20:21], off nt
	s_nop 0
	global_load_dwordx2 v[22:23], v[22:23], off nt
	s_nop 0
	global_load_dwordx2 v[24:25], v[24:25], off nt
	s_nop 0
	global_load_dwordx2 v[26:27], v[26:27], off nt
	s_nop 0
	global_load_dwordx2 v[28:29], v[28:29], off nt
	s_nop 0
	global_load_dwordx2 v[30:31], v[30:31], off nt
	s_nop 0
	global_load_dwordx2 v[32:33], v[32:33], off nt
	s_nop 0
	global_load_dwordx2 v[34:35], v[34:35], off nt
	s_nop 0
	global_load_dwordx2 v[36:37], v[36:37], off nt
	s_nop 0
	global_load_dwordx2 v[38:39], v[38:39], off nt
	s_nop 0
	global_load_dwordx2 v[40:41], v[40:41], off nt
	s_nop 0
	global_load_dwordx2 v[42:43], v[42:43], off nt
	s_nop 0
	global_load_dwordx2 v[44:45], v[44:45], off nt
	s_nop 0
	global_load_dwordx2 v[46:47], v[46:47], off nt
	s_nop 0
	global_load_dwordx2 v[48:49], v[48:49], off nt
	s_nop 0
	global_load_dwordx2 v[50:51], v[50:51], off nt
	s_nop 0
	global_load_dwordx2 v[52:53], v[52:53], off nt
	s_nop 0
	global_load_dwordx2 v[54:55], v[54:55], off nt
	s_nop 0
	global_load_dwordx2 v[56:57], v[56:57], off nt
	s_nop 0
	global_load_dwordx2 v[58:59], v[58:59], off nt
	s_nop 0
	global_load_dwordx2 v[60:61], v[60:61], off nt
	s_nop 0
	global_load_dwordx2 v[62:63], v[62:63], off nt
	s_nop 0
	global_load_dwordx2 v[64:65], v[64:65], off nt
	v_addc_co_u32_e32 v119, vcc, 0, v67, vcc
	global_load_dwordx2 v[66:67], v[68:69], off nt
	s_nop 0
	global_load_dwordx2 v[68:69], v[70:71], off nt
	s_nop 0
	global_load_dwordx2 v[70:71], v[72:73], off nt
	s_nop 0
	global_load_dwordx2 v[72:73], v[118:119], off nt
	s_load_dwordx2 s[12:13], s[52:53], 0xf0
	s_waitcnt vmcnt(0)
	ds_write2_b32 v78, v10, v11 offset1:1
	ds_write2_b32 v78, v12, v13 offset0:130 offset1:131
	ds_write2_b32 v87, v14, v15 offset1:1
	ds_write2_b32 v88, v16, v17 offset1:1
	ds_write2_b32 v89, v18, v19 offset1:1
	ds_write2_b32 v90, v20, v21 offset1:1
	ds_write2_b32 v91, v22, v23 offset1:1
	ds_write2_b32 v92, v24, v25 offset1:1
	ds_write2_b32 v93, v26, v27 offset1:1
	ds_write2_b32 v94, v28, v29 offset1:1
	ds_write2_b32 v95, v30, v31 offset1:1
	ds_write2_b32 v96, v32, v33 offset1:1
	ds_write2_b32 v97, v34, v35 offset1:1
	ds_write2_b32 v98, v36, v37 offset1:1
	ds_write2_b32 v99, v38, v39 offset1:1
	ds_write2_b32 v100, v40, v41 offset1:1
	ds_write2_b32 v101, v42, v43 offset1:1
	ds_write2_b32 v102, v44, v45 offset1:1
	ds_write2_b32 v103, v46, v47 offset1:1
	ds_write2_b32 v104, v48, v49 offset1:1
	ds_write2_b32 v105, v50, v51 offset1:1
	ds_write2_b32 v106, v52, v53 offset1:1
	ds_write2_b32 v107, v54, v55 offset1:1
	ds_write2_b32 v108, v56, v57 offset1:1
	ds_write2_b32 v109, v58, v59 offset1:1
	ds_write2_b32 v110, v60, v61 offset1:1
	ds_write2_b32 v111, v62, v63 offset1:1
	ds_write2_b32 v112, v64, v65 offset1:1
	ds_write2_b32 v113, v66, v67 offset1:1
	ds_write2_b32 v114, v68, v69 offset1:1
	ds_write2_b32 v115, v70, v71 offset1:1
	ds_write2_b32 v116, v72, v73 offset1:1
	s_waitcnt lgkmcnt(0)
	s_lshl_b32 s14, s14, 1
	ds_read2_b32 v[14:15], v79 offset0:65 offset1:73
	ds_read2_b32 v[16:17], v79 offset1:8
	ds_read2_b32 v[18:19], v79 offset0:130 offset1:138
	ds_read2_b32 v[20:21], v79 offset0:195 offset1:203
	ds_read2_b32 v[22:23], v117 offset0:4 offset1:12
	ds_read2_b32 v[24:25], v117 offset0:69 offset1:77
	ds_read2_b32 v[26:27], v117 offset0:134 offset1:142
	ds_read2_b32 v[28:29], v117 offset0:199 offset1:207
	s_waitcnt lgkmcnt(0)
	s_add_u32 s12, s12, s14
	s_addc_u32 s13, s13, 0
	v_mov_b32_e32 v9, v1
	v_add_u32_e32 v32, s8, v75
	v_lshl_add_u64 v[10:11], s[12:13], 0, v[8:9]
	v_ashrrev_i32_e32 v33, 31, v32
	v_lshl_add_u64 v[30:31], v[10:11], 0, s[6:7]
	v_lshlrev_b64 v[32:33], 12, v[32:33]
	v_cvt_pk_bf16_f32 v10, v16, v14
	v_cvt_pk_bf16_f32 v11, v18, v20
	v_cvt_pk_bf16_f32 v12, v22, v24
	v_cvt_pk_bf16_f32 v13, v26, v28
	v_lshl_add_u64 v[32:33], v[30:31], 0, v[32:33]
	v_add_u32_e32 v14, s8, v80
	global_store_dwordx4 v[32:33], v[10:13], off
	s_mov_b64 s[12:13], 0
	s_nop 0
	v_cvt_pk_bf16_f32 v10, v17, v15
	v_ashrrev_i32_e32 v15, 31, v14
	v_cvt_pk_bf16_f32 v11, v19, v21
	v_cvt_pk_bf16_f32 v12, v23, v25
	v_cvt_pk_bf16_f32 v13, v27, v29
	v_lshlrev_b64 v[14:15], 12, v[14:15]
	ds_read2_b32 v[16:17], v79 offset0:81 offset1:89
	ds_read2_b32 v[18:19], v79 offset0:16 offset1:24
	ds_read2_b32 v[20:21], v79 offset0:146 offset1:154
	ds_read2_b32 v[22:23], v79 offset0:211 offset1:219
	ds_read2_b32 v[24:25], v117 offset0:20 offset1:28
	ds_read2_b32 v[26:27], v117 offset0:85 offset1:93
	ds_read2_b32 v[28:29], v117 offset0:150 offset1:158
	ds_read2_b32 v[32:33], v117 offset0:215 offset1:223
	v_lshl_add_u64 v[14:15], v[30:31], 0, v[14:15]
	global_store_dwordx4 v[14:15], v[10:13], off
	v_add_u32_e32 v14, s8, v81
	v_ashrrev_i32_e32 v15, 31, v14
	v_lshlrev_b64 v[14:15], 12, v[14:15]
	s_waitcnt lgkmcnt(6)
	v_cvt_pk_bf16_f32 v10, v18, v16
	s_waitcnt lgkmcnt(4)
	v_cvt_pk_bf16_f32 v11, v20, v22
	s_waitcnt lgkmcnt(2)
	v_cvt_pk_bf16_f32 v12, v24, v26
	s_waitcnt lgkmcnt(0)
	v_cvt_pk_bf16_f32 v13, v28, v32
	v_lshl_add_u64 v[14:15], v[30:31], 0, v[14:15]
	global_store_dwordx4 v[14:15], v[10:13], off
	v_add_u32_e32 v14, s8, v82
	v_ashrrev_i32_e32 v15, 31, v14
	v_cvt_pk_bf16_f32 v10, v19, v17
	v_cvt_pk_bf16_f32 v11, v21, v23
	v_cvt_pk_bf16_f32 v12, v25, v27
	v_cvt_pk_bf16_f32 v13, v29, v33
	v_lshlrev_b64 v[14:15], 12, v[14:15]
	ds_read2_b32 v[16:17], v79 offset0:32 offset1:40
	ds_read2_b32 v[18:19], v79 offset0:97 offset1:105
	ds_read2_b32 v[20:21], v79 offset0:162 offset1:170
	ds_read2_b32 v[22:23], v79 offset0:227 offset1:235
	ds_read2_b32 v[24:25], v117 offset0:36 offset1:44
	ds_read2_b32 v[26:27], v117 offset0:101 offset1:109
	ds_read2_b32 v[28:29], v117 offset0:166 offset1:174
	ds_read2_b32 v[32:33], v117 offset0:231 offset1:239
	v_lshl_add_u64 v[14:15], v[30:31], 0, v[14:15]
	global_store_dwordx4 v[14:15], v[10:13], off
	v_add_u32_e32 v14, s8, v83
	v_ashrrev_i32_e32 v15, 31, v14
	v_lshlrev_b64 v[14:15], 12, v[14:15]
	s_waitcnt lgkmcnt(6)
	v_cvt_pk_bf16_f32 v10, v16, v18
	s_waitcnt lgkmcnt(4)
	v_cvt_pk_bf16_f32 v11, v20, v22
	s_waitcnt lgkmcnt(2)
	v_cvt_pk_bf16_f32 v12, v24, v26
	s_waitcnt lgkmcnt(0)
	v_cvt_pk_bf16_f32 v13, v28, v32
	v_lshl_add_u64 v[14:15], v[30:31], 0, v[14:15]
	global_store_dwordx4 v[14:15], v[10:13], off
	v_add_u32_e32 v14, s8, v84
	v_ashrrev_i32_e32 v15, 31, v14
	v_cvt_pk_bf16_f32 v10, v17, v19
	v_cvt_pk_bf16_f32 v11, v21, v23
	v_cvt_pk_bf16_f32 v12, v25, v27
	v_cvt_pk_bf16_f32 v13, v29, v33
	v_lshlrev_b64 v[14:15], 12, v[14:15]
	ds_read2_b32 v[16:17], v79 offset0:48 offset1:56
	ds_read2_b32 v[18:19], v79 offset0:113 offset1:121
	ds_read2_b32 v[20:21], v79 offset0:178 offset1:186
	ds_read2_b32 v[22:23], v79 offset0:243 offset1:251
	ds_read2_b32 v[24:25], v117 offset0:52 offset1:60
	ds_read2_b32 v[26:27], v117 offset0:117 offset1:125
	ds_read2_b32 v[28:29], v117 offset0:182 offset1:190
	ds_read2_b32 v[32:33], v117 offset0:247 offset1:255
	v_lshl_add_u64 v[14:15], v[30:31], 0, v[14:15]
	global_store_dwordx4 v[14:15], v[10:13], off
	v_add_u32_e32 v14, s8, v85
	v_ashrrev_i32_e32 v15, 31, v14
	v_lshlrev_b64 v[14:15], 12, v[14:15]
	s_waitcnt lgkmcnt(6)
	v_cvt_pk_bf16_f32 v10, v16, v18
	s_waitcnt lgkmcnt(4)
	v_cvt_pk_bf16_f32 v11, v20, v22
	s_waitcnt lgkmcnt(2)
	v_cvt_pk_bf16_f32 v12, v24, v26
	s_waitcnt lgkmcnt(0)
	v_cvt_pk_bf16_f32 v13, v28, v32
	v_lshl_add_u64 v[14:15], v[30:31], 0, v[14:15]
	global_store_dwordx4 v[14:15], v[10:13], off
	v_add_u32_e32 v14, s8, v86
	v_ashrrev_i32_e32 v15, 31, v14
	v_lshlrev_b64 v[14:15], 12, v[14:15]
	v_cvt_pk_bf16_f32 v10, v17, v19
	v_cvt_pk_bf16_f32 v11, v21, v23
	v_cvt_pk_bf16_f32 v12, v25, v27
	v_cvt_pk_bf16_f32 v13, v29, v33
	v_lshl_add_u64 v[14:15], v[30:31], 0, v[14:15]
	global_store_dwordx4 v[14:15], v[10:13], off
	s_waitcnt lgkmcnt(0)
.LBB0_2209:
	s_andn2_b64 vcc, exec, s[12:13]
	s_cbranch_vccnz .LBB0_2211
	s_load_dwordx2 s[14:15], s[52:53], 0x88
	s_and_b32 s8, s17, 0xfc0
	s_addk_i32 s8, 0xf800
	s_and_b32 s12, s5, 0x3c0
	s_lshl_b64 s[82:83], s[8:9], 2
	v_add_u32_e32 v10, s12, v74
	s_waitcnt lgkmcnt(0)
	s_add_u32 s14, s14, s82
	s_addc_u32 s15, s15, s83
	v_ashrrev_i32_e32 v11, 31, v10
	v_lshl_add_u64 v[12:13], s[14:15], 0, v[0:1]
	v_lshlrev_b64 v[10:11], 13, v[10:11]
	v_lshl_add_u64 v[10:11], v[12:13], 0, v[10:11]
	s_mov_b32 s13, 0x800000
	v_add_co_u32_e32 v12, vcc, s13, v10
	s_mov_b32 s13, 0x804000
	s_nop 0
	v_addc_co_u32_e32 v13, vcc, 0, v11, vcc
	v_add_co_u32_e32 v14, vcc, s13, v10
	s_mov_b32 s13, 0x808000
	s_nop 0
	v_addc_co_u32_e32 v15, vcc, 0, v11, vcc
	v_add_co_u32_e32 v16, vcc, s13, v10
	s_mov_b32 s13, 0x80c000
	s_nop 0
	v_addc_co_u32_e32 v17, vcc, 0, v11, vcc
	v_add_co_u32_e32 v18, vcc, s13, v10
	s_mov_b32 s13, 0x810000
	s_nop 0
	v_addc_co_u32_e32 v19, vcc, 0, v11, vcc
	v_add_co_u32_e32 v20, vcc, s13, v10
	s_mov_b32 s13, 0x814000
	s_nop 0
	v_addc_co_u32_e32 v21, vcc, 0, v11, vcc
	v_add_co_u32_e32 v22, vcc, s13, v10
	s_mov_b32 s13, 0x818000
	s_nop 0
	v_addc_co_u32_e32 v23, vcc, 0, v11, vcc
	v_add_co_u32_e32 v24, vcc, s13, v10
	s_mov_b32 s13, 0x81c000
	s_nop 0
	v_addc_co_u32_e32 v25, vcc, 0, v11, vcc
	v_add_co_u32_e32 v26, vcc, s13, v10
	s_mov_b32 s13, 0x820000
	s_nop 0
	v_addc_co_u32_e32 v27, vcc, 0, v11, vcc
	v_add_co_u32_e32 v28, vcc, s13, v10
	s_mov_b32 s13, 0x824000
	s_nop 0
	v_addc_co_u32_e32 v29, vcc, 0, v11, vcc
	v_add_co_u32_e32 v30, vcc, s13, v10
	global_load_dwordx2 v[12:13], v[12:13], off nt
	s_nop 0
	global_load_dwordx2 v[14:15], v[14:15], off nt
	s_nop 0
	global_load_dwordx2 v[16:17], v[16:17], off nt
	s_nop 0
	global_load_dwordx2 v[18:19], v[18:19], off nt
	v_addc_co_u32_e32 v31, vcc, 0, v11, vcc
	v_add_co_u32_e32 v32, vcc, s19, v10
	global_load_dwordx2 v[20:21], v[20:21], off nt
	s_nop 0
	global_load_dwordx2 v[22:23], v[22:23], off nt
	s_nop 0
	global_load_dwordx2 v[24:25], v[24:25], off nt
	s_nop 0
	global_load_dwordx2 v[26:27], v[26:27], off nt
	v_addc_co_u32_e32 v33, vcc, 0, v11, vcc
	v_add_co_u32_e32 v34, vcc, s20, v10
	s_lshl_b32 s12, s12, 1
	s_nop 0
	v_addc_co_u32_e32 v35, vcc, 0, v11, vcc
	v_add_co_u32_e32 v36, vcc, s21, v10
	global_load_dwordx2 v[28:29], v[28:29], off nt
	s_nop 0
	global_load_dwordx2 v[30:31], v[30:31], off nt
	s_nop 0
	global_load_dwordx2 v[32:33], v[32:33], off nt
	s_nop 0
	global_load_dwordx2 v[34:35], v[34:35], off nt
	v_addc_co_u32_e32 v37, vcc, 0, v11, vcc
	v_add_co_u32_e32 v38, vcc, s22, v10
	s_mov_b32 s13, s9
	s_nop 0
	v_addc_co_u32_e32 v39, vcc, 0, v11, vcc
	v_add_co_u32_e32 v40, vcc, s23, v10
	s_nop 1
	v_addc_co_u32_e32 v41, vcc, 0, v11, vcc
	v_add_co_u32_e32 v42, vcc, s24, v10
	s_nop 1
	v_addc_co_u32_e32 v43, vcc, 0, v11, vcc
	v_add_co_u32_e32 v44, vcc, s25, v10
	global_load_dwordx2 v[36:37], v[36:37], off nt
	s_nop 0
	global_load_dwordx2 v[38:39], v[38:39], off nt
	s_nop 0
	global_load_dwordx2 v[40:41], v[40:41], off nt
	s_nop 0
	global_load_dwordx2 v[42:43], v[42:43], off nt
	v_addc_co_u32_e32 v45, vcc, 0, v11, vcc
	v_add_co_u32_e32 v46, vcc, s26, v10
	s_nop 1
	v_addc_co_u32_e32 v47, vcc, 0, v11, vcc
	v_add_co_u32_e32 v48, vcc, s27, v10
	s_nop 1
	v_addc_co_u32_e32 v49, vcc, 0, v11, vcc
	v_add_co_u32_e32 v50, vcc, s28, v10
	s_nop 1
	v_addc_co_u32_e32 v51, vcc, 0, v11, vcc
	v_add_co_u32_e32 v52, vcc, s29, v10
	global_load_dwordx2 v[44:45], v[44:45], off nt
	s_nop 0
	global_load_dwordx2 v[46:47], v[46:47], off nt
	s_nop 0
	global_load_dwordx2 v[48:49], v[48:49], off nt
	s_nop 0
	global_load_dwordx2 v[50:51], v[50:51], off nt
	v_addc_co_u32_e32 v53, vcc, 0, v11, vcc
	v_add_co_u32_e32 v54, vcc, s30, v10
	s_nop 1
	v_addc_co_u32_e32 v55, vcc, 0, v11, vcc
	v_add_co_u32_e32 v56, vcc, s31, v10
	s_nop 1
	v_addc_co_u32_e32 v57, vcc, 0, v11, vcc
	v_add_co_u32_e32 v58, vcc, s34, v10
	s_nop 1
	v_addc_co_u32_e32 v59, vcc, 0, v11, vcc
	v_add_co_u32_e32 v60, vcc, s35, v10
	global_load_dwordx2 v[52:53], v[52:53], off nt
	s_nop 0
	global_load_dwordx2 v[54:55], v[54:55], off nt
	s_nop 0
	global_load_dwordx2 v[56:57], v[56:57], off nt
	s_nop 0
	global_load_dwordx2 v[58:59], v[58:59], off nt
	v_addc_co_u32_e32 v61, vcc, 0, v11, vcc
	v_add_co_u32_e32 v62, vcc, s36, v10
	s_nop 1
	v_addc_co_u32_e32 v63, vcc, 0, v11, vcc
	v_add_co_u32_e32 v64, vcc, s37, v10
	s_nop 1
	v_addc_co_u32_e32 v65, vcc, 0, v11, vcc
	v_add_co_u32_e32 v66, vcc, s38, v10
	s_nop 1
	v_addc_co_u32_e32 v67, vcc, 0, v11, vcc
	v_add_co_u32_e32 v68, vcc, s39, v10
	global_load_dwordx2 v[60:61], v[60:61], off nt
	s_nop 0
	global_load_dwordx2 v[62:63], v[62:63], off nt
	s_nop 0
	global_load_dwordx2 v[64:65], v[64:65], off nt
	s_nop 0
	global_load_dwordx2 v[66:67], v[66:67], off nt
	v_addc_co_u32_e32 v69, vcc, 0, v11, vcc
	v_add_co_u32_e32 v70, vcc, s40, v10
	s_nop 1
	v_addc_co_u32_e32 v71, vcc, 0, v11, vcc
	v_add_co_u32_e32 v72, vcc, s41, v10
	s_nop 1
	v_addc_co_u32_e32 v73, vcc, 0, v11, vcc
	v_add_co_u32_e32 v10, vcc, s42, v10
	s_nop 1
	v_addc_co_u32_e32 v11, vcc, 0, v11, vcc
	global_load_dwordx2 v[68:69], v[68:69], off nt
	s_nop 0
	global_load_dwordx2 v[70:71], v[70:71], off nt
	s_nop 0
	global_load_dwordx2 v[72:73], v[72:73], off nt
	s_nop 0
	global_load_dwordx2 v[10:11], v[10:11], off nt
	s_waitcnt vmcnt(0)
	ds_write2_b32 v78, v12, v13 offset1:1
	ds_write2_b32 v78, v14, v15 offset0:130 offset1:131
	ds_write2_b32 v87, v16, v17 offset1:1
	ds_write2_b32 v88, v18, v19 offset1:1
	ds_write2_b32 v89, v20, v21 offset1:1
	ds_write2_b32 v90, v22, v23 offset1:1
	ds_write2_b32 v91, v24, v25 offset1:1
	ds_write2_b32 v92, v26, v27 offset1:1
	ds_write2_b32 v93, v28, v29 offset1:1
	ds_write2_b32 v94, v30, v31 offset1:1
	ds_write2_b32 v95, v32, v33 offset1:1
	ds_write2_b32 v96, v34, v35 offset1:1
	ds_write2_b32 v97, v36, v37 offset1:1
	ds_write2_b32 v98, v38, v39 offset1:1
	ds_write2_b32 v99, v40, v41 offset1:1
	ds_write2_b32 v100, v42, v43 offset1:1
	ds_write2_b32 v101, v44, v45 offset1:1
	ds_write2_b32 v102, v46, v47 offset1:1
	ds_write2_b32 v103, v48, v49 offset1:1
	ds_write2_b32 v104, v50, v51 offset1:1
	ds_write2_b32 v105, v52, v53 offset1:1
	ds_write2_b32 v106, v54, v55 offset1:1
	ds_write2_b32 v107, v56, v57 offset1:1
	ds_write2_b32 v108, v58, v59 offset1:1
	ds_write2_b32 v109, v60, v61 offset1:1
	ds_write2_b32 v110, v62, v63 offset1:1
	ds_write2_b32 v111, v64, v65 offset1:1
	ds_write2_b32 v112, v66, v67 offset1:1
	ds_write2_b32 v113, v68, v69 offset1:1
	ds_write2_b32 v114, v70, v71 offset1:1
	ds_write2_b32 v115, v72, v73 offset1:1
	ds_write2_b32 v116, v10, v11 offset1:1
	s_waitcnt lgkmcnt(0)
	ds_read2_b32 v[14:15], v79 offset0:65 offset1:73
	ds_read2_b32 v[16:17], v79 offset1:8
	ds_read2_b32 v[18:19], v79 offset0:130 offset1:138
	ds_read2_b32 v[20:21], v79 offset0:195 offset1:203
	ds_read2_b32 v[22:23], v117 offset0:4 offset1:12
	ds_read2_b32 v[24:25], v117 offset0:69 offset1:77
	ds_read2_b32 v[26:27], v117 offset0:134 offset1:142
	ds_read2_b32 v[28:29], v117 offset0:199 offset1:207
	v_add_u32_e32 v32, s8, v75
	v_ashrrev_i32_e32 v33, 31, v32
	v_lshl_add_u64 v[30:31], v[2:3], 0, s[12:13]
	v_lshlrev_b64 v[32:33], 12, v[32:33]
	s_waitcnt lgkmcnt(6)
	v_cvt_pk_bf16_f32 v10, v16, v14
	s_waitcnt lgkmcnt(4)
	v_cvt_pk_bf16_f32 v11, v18, v20
	s_waitcnt lgkmcnt(2)
	v_cvt_pk_bf16_f32 v12, v22, v24
	s_waitcnt lgkmcnt(0)
	v_cvt_pk_bf16_f32 v13, v26, v28
	v_lshl_add_u64 v[32:33], v[30:31], 0, v[32:33]
	v_add_u32_e32 v14, s8, v80
	global_store_dwordx4 v[32:33], v[10:13], off
	s_nop 1
	v_cvt_pk_bf16_f32 v10, v17, v15
	v_ashrrev_i32_e32 v15, 31, v14
	v_cvt_pk_bf16_f32 v11, v19, v21
	v_cvt_pk_bf16_f32 v12, v23, v25
	v_cvt_pk_bf16_f32 v13, v27, v29
	v_lshlrev_b64 v[14:15], 12, v[14:15]
	ds_read2_b32 v[16:17], v79 offset0:81 offset1:89
	ds_read2_b32 v[18:19], v79 offset0:16 offset1:24
	ds_read2_b32 v[20:21], v79 offset0:146 offset1:154
	ds_read2_b32 v[22:23], v79 offset0:211 offset1:219
	ds_read2_b32 v[24:25], v117 offset0:20 offset1:28
	ds_read2_b32 v[26:27], v117 offset0:85 offset1:93
	ds_read2_b32 v[28:29], v117 offset0:150 offset1:158
	ds_read2_b32 v[32:33], v117 offset0:215 offset1:223
	v_lshl_add_u64 v[14:15], v[30:31], 0, v[14:15]
	global_store_dwordx4 v[14:15], v[10:13], off
	v_add_u32_e32 v14, s8, v81
	v_ashrrev_i32_e32 v15, 31, v14
	v_lshlrev_b64 v[14:15], 12, v[14:15]
	s_waitcnt lgkmcnt(6)
	v_cvt_pk_bf16_f32 v10, v18, v16
	s_waitcnt lgkmcnt(4)
	v_cvt_pk_bf16_f32 v11, v20, v22
	s_waitcnt lgkmcnt(2)
	v_cvt_pk_bf16_f32 v12, v24, v26
	s_waitcnt lgkmcnt(0)
	v_cvt_pk_bf16_f32 v13, v28, v32
	v_lshl_add_u64 v[14:15], v[30:31], 0, v[14:15]
	global_store_dwordx4 v[14:15], v[10:13], off
	v_add_u32_e32 v14, s8, v82
	v_ashrrev_i32_e32 v15, 31, v14
	v_cvt_pk_bf16_f32 v10, v19, v17
	v_cvt_pk_bf16_f32 v11, v21, v23
	v_cvt_pk_bf16_f32 v12, v25, v27
	v_cvt_pk_bf16_f32 v13, v29, v33
	v_lshlrev_b64 v[14:15], 12, v[14:15]
	ds_read2_b32 v[16:17], v79 offset0:32 offset1:40
	ds_read2_b32 v[18:19], v79 offset0:97 offset1:105
	ds_read2_b32 v[20:21], v79 offset0:162 offset1:170
	ds_read2_b32 v[22:23], v79 offset0:227 offset1:235
	ds_read2_b32 v[24:25], v117 offset0:36 offset1:44
	ds_read2_b32 v[26:27], v117 offset0:101 offset1:109
	ds_read2_b32 v[28:29], v117 offset0:166 offset1:174
	ds_read2_b32 v[32:33], v117 offset0:231 offset1:239
	v_lshl_add_u64 v[14:15], v[30:31], 0, v[14:15]
	global_store_dwordx4 v[14:15], v[10:13], off
	v_add_u32_e32 v14, s8, v83
	v_ashrrev_i32_e32 v15, 31, v14
	v_lshlrev_b64 v[14:15], 12, v[14:15]
	s_waitcnt lgkmcnt(6)
	v_cvt_pk_bf16_f32 v10, v16, v18
	s_waitcnt lgkmcnt(4)
	v_cvt_pk_bf16_f32 v11, v20, v22
	s_waitcnt lgkmcnt(2)
	v_cvt_pk_bf16_f32 v12, v24, v26
	s_waitcnt lgkmcnt(0)
	v_cvt_pk_bf16_f32 v13, v28, v32
	v_lshl_add_u64 v[14:15], v[30:31], 0, v[14:15]
	global_store_dwordx4 v[14:15], v[10:13], off
	v_add_u32_e32 v14, s8, v84
	v_ashrrev_i32_e32 v15, 31, v14
	v_cvt_pk_bf16_f32 v10, v17, v19
	v_cvt_pk_bf16_f32 v11, v21, v23
	v_cvt_pk_bf16_f32 v12, v25, v27
	v_cvt_pk_bf16_f32 v13, v29, v33
	v_lshlrev_b64 v[14:15], 12, v[14:15]
	ds_read2_b32 v[16:17], v79 offset0:48 offset1:56
	ds_read2_b32 v[18:19], v79 offset0:113 offset1:121
	ds_read2_b32 v[20:21], v79 offset0:178 offset1:186
	ds_read2_b32 v[22:23], v79 offset0:243 offset1:251
	ds_read2_b32 v[24:25], v117 offset0:52 offset1:60
	ds_read2_b32 v[26:27], v117 offset0:117 offset1:125
	ds_read2_b32 v[28:29], v117 offset0:182 offset1:190
	ds_read2_b32 v[32:33], v117 offset0:247 offset1:255
	v_lshl_add_u64 v[14:15], v[30:31], 0, v[14:15]
	global_store_dwordx4 v[14:15], v[10:13], off
	v_add_u32_e32 v14, s8, v85
	v_ashrrev_i32_e32 v15, 31, v14
	v_lshlrev_b64 v[14:15], 12, v[14:15]
	s_waitcnt lgkmcnt(6)
	v_cvt_pk_bf16_f32 v10, v16, v18
	s_waitcnt lgkmcnt(4)
	v_cvt_pk_bf16_f32 v11, v20, v22
	s_waitcnt lgkmcnt(2)
	v_cvt_pk_bf16_f32 v12, v24, v26
	s_waitcnt lgkmcnt(0)
	v_cvt_pk_bf16_f32 v13, v28, v32
	v_lshl_add_u64 v[14:15], v[30:31], 0, v[14:15]
	global_store_dwordx4 v[14:15], v[10:13], off
	v_add_u32_e32 v14, s8, v86
	v_ashrrev_i32_e32 v15, 31, v14
	v_lshlrev_b64 v[14:15], 12, v[14:15]
	v_cvt_pk_bf16_f32 v10, v17, v19
	v_cvt_pk_bf16_f32 v11, v21, v23
	v_cvt_pk_bf16_f32 v12, v25, v27
	v_cvt_pk_bf16_f32 v13, v29, v33
	v_lshl_add_u64 v[14:15], v[30:31], 0, v[14:15]
	global_store_dwordx4 v[14:15], v[10:13], off
	s_waitcnt lgkmcnt(0)

.LBB0_2212:
	s_andn2_b64 vcc, exec, s[12:13]
	s_cbranch_vccnz .LBB0_2214
	s_load_dwordx2 s[14:15], s[52:53], 0x80
	s_and_b32 s8, s18, 0xfc0
	s_addk_i32 s8, 0xf800
	s_and_b32 s12, s5, 0x1c0
	s_lshl_b64 s[82:83], s[8:9], 2
	v_add_u32_e32 v10, s12, v74
	s_waitcnt lgkmcnt(0)
	s_add_u32 s14, s14, s82
	s_addc_u32 s15, s15, s83
	v_ashrrev_i32_e32 v11, 31, v10
	v_lshl_add_u64 v[12:13], s[14:15], 0, v[0:1]
	v_lshlrev_b64 v[10:11], 13, v[10:11]
	v_lshl_add_u64 v[10:11], v[12:13], 0, v[10:11]
	v_add_co_u32_e32 v12, vcc, s43, v10
	s_lshl_b32 s12, s12, 1
	s_nop 0
	v_addc_co_u32_e32 v13, vcc, 0, v11, vcc
	v_add_co_u32_e32 v14, vcc, s44, v10
	s_mov_b32 s13, s9
	s_nop 0
	v_addc_co_u32_e32 v15, vcc, 0, v11, vcc
	v_add_co_u32_e32 v16, vcc, s45, v10
	s_nop 1
	v_addc_co_u32_e32 v17, vcc, 0, v11, vcc
	v_add_co_u32_e32 v18, vcc, s46, v10
	s_nop 1
	v_addc_co_u32_e32 v19, vcc, 0, v11, vcc
	v_add_co_u32_e32 v20, vcc, s47, v10
	global_load_dwordx2 v[12:13], v[12:13], off nt
	s_nop 0
	global_load_dwordx2 v[14:15], v[14:15], off nt
	s_nop 0
	global_load_dwordx2 v[16:17], v[16:17], off nt
	s_nop 0
	global_load_dwordx2 v[18:19], v[18:19], off nt
	v_addc_co_u32_e32 v21, vcc, 0, v11, vcc
	v_add_co_u32_e32 v22, vcc, s48, v10
	s_nop 1
	v_addc_co_u32_e32 v23, vcc, 0, v11, vcc
	v_add_co_u32_e32 v24, vcc, s49, v10
	s_nop 1
	v_addc_co_u32_e32 v25, vcc, 0, v11, vcc
	v_add_co_u32_e32 v26, vcc, s51, v10
	s_nop 1
	v_addc_co_u32_e32 v27, vcc, 0, v11, vcc
	v_add_co_u32_e32 v28, vcc, s55, v10
	global_load_dwordx2 v[20:21], v[20:21], off nt
	s_nop 0
	global_load_dwordx2 v[22:23], v[22:23], off nt
	s_nop 0
	global_load_dwordx2 v[24:25], v[24:25], off nt
	s_nop 0
	global_load_dwordx2 v[26:27], v[26:27], off nt
	v_addc_co_u32_e32 v29, vcc, 0, v11, vcc
	v_add_co_u32_e32 v30, vcc, s57, v10
	s_nop 1
	v_addc_co_u32_e32 v31, vcc, 0, v11, vcc
	v_add_co_u32_e32 v32, vcc, s59, v10
	s_nop 1
	v_addc_co_u32_e32 v33, vcc, 0, v11, vcc
	v_add_co_u32_e32 v34, vcc, s60, v10
	s_nop 1
	v_addc_co_u32_e32 v35, vcc, 0, v11, vcc
	v_add_co_u32_e32 v36, vcc, s61, v10
	global_load_dwordx2 v[28:29], v[28:29], off nt
	s_nop 0
	global_load_dwordx2 v[30:31], v[30:31], off nt
	s_nop 0
	global_load_dwordx2 v[32:33], v[32:33], off nt
	s_nop 0
	global_load_dwordx2 v[34:35], v[34:35], off nt
	v_addc_co_u32_e32 v37, vcc, 0, v11, vcc
	v_add_co_u32_e32 v38, vcc, s62, v10
	s_nop 1
	v_addc_co_u32_e32 v39, vcc, 0, v11, vcc
	v_add_co_u32_e32 v40, vcc, s63, v10
	s_nop 1
	v_addc_co_u32_e32 v41, vcc, 0, v11, vcc
	v_add_co_u32_e32 v42, vcc, s64, v10
	s_nop 1
	v_addc_co_u32_e32 v43, vcc, 0, v11, vcc
	v_add_co_u32_e32 v44, vcc, s65, v10
	global_load_dwordx2 v[36:37], v[36:37], off nt
	s_nop 0
	global_load_dwordx2 v[38:39], v[38:39], off nt
	s_nop 0
	global_load_dwordx2 v[40:41], v[40:41], off nt
	s_nop 0
	global_load_dwordx2 v[42:43], v[42:43], off nt
	v_addc_co_u32_e32 v45, vcc, 0, v11, vcc
	v_add_co_u32_e32 v46, vcc, s66, v10
	s_nop 1
	v_addc_co_u32_e32 v47, vcc, 0, v11, vcc
	v_add_co_u32_e32 v48, vcc, s67, v10
	s_nop 1
	v_addc_co_u32_e32 v49, vcc, 0, v11, vcc
	v_add_co_u32_e32 v50, vcc, s68, v10
	s_nop 1
	v_addc_co_u32_e32 v51, vcc, 0, v11, vcc
	v_add_co_u32_e32 v52, vcc, s69, v10
	global_load_dwordx2 v[44:45], v[44:45], off nt
	s_nop 0
	global_load_dwordx2 v[46:47], v[46:47], off nt
	s_nop 0
	global_load_dwordx2 v[48:49], v[48:49], off nt
	s_nop 0
	global_load_dwordx2 v[50:51], v[50:51], off nt
	v_addc_co_u32_e32 v53, vcc, 0, v11, vcc
	v_add_co_u32_e32 v54, vcc, s70, v10
	s_nop 1
	v_addc_co_u32_e32 v55, vcc, 0, v11, vcc
	v_add_co_u32_e32 v56, vcc, s71, v10
	s_nop 1
	v_addc_co_u32_e32 v57, vcc, 0, v11, vcc
	v_add_co_u32_e32 v58, vcc, s72, v10
	s_nop 1
	v_addc_co_u32_e32 v59, vcc, 0, v11, vcc
	v_add_co_u32_e32 v60, vcc, s73, v10
	global_load_dwordx2 v[52:53], v[52:53], off nt
	s_nop 0
	global_load_dwordx2 v[54:55], v[54:55], off nt
	s_nop 0
	global_load_dwordx2 v[56:57], v[56:57], off nt
	s_nop 0
	global_load_dwordx2 v[58:59], v[58:59], off nt
	v_addc_co_u32_e32 v61, vcc, 0, v11, vcc
	v_add_co_u32_e32 v62, vcc, s74, v10
	s_nop 1
	v_addc_co_u32_e32 v63, vcc, 0, v11, vcc
	v_add_co_u32_e32 v64, vcc, s75, v10
	s_nop 1
	v_addc_co_u32_e32 v65, vcc, 0, v11, vcc
	v_add_co_u32_e32 v66, vcc, s76, v10
	s_nop 1
	v_addc_co_u32_e32 v67, vcc, 0, v11, vcc
	v_add_co_u32_e32 v68, vcc, s77, v10
	global_load_dwordx2 v[60:61], v[60:61], off nt
	s_nop 0
	global_load_dwordx2 v[62:63], v[62:63], off nt
	s_nop 0
	global_load_dwordx2 v[64:65], v[64:65], off nt
	s_nop 0
	global_load_dwordx2 v[66:67], v[66:67], off nt
	v_addc_co_u32_e32 v69, vcc, 0, v11, vcc
	v_add_co_u32_e32 v70, vcc, s78, v10
	s_nop 1
	v_addc_co_u32_e32 v71, vcc, 0, v11, vcc
	v_add_co_u32_e32 v72, vcc, s79, v10
	s_nop 1
	v_addc_co_u32_e32 v73, vcc, 0, v11, vcc
	v_add_co_u32_e32 v10, vcc, s80, v10
	s_nop 1
	v_addc_co_u32_e32 v11, vcc, 0, v11, vcc
	global_load_dwordx2 v[68:69], v[68:69], off nt
	s_nop 0
	global_load_dwordx2 v[70:71], v[70:71], off nt
	s_nop 0
	global_load_dwordx2 v[72:73], v[72:73], off nt
	s_nop 0
	global_load_dwordx2 v[10:11], v[10:11], off nt
	s_waitcnt vmcnt(0)
	ds_write2_b32 v78, v12, v13 offset1:1
	ds_write2_b32 v78, v14, v15 offset0:130 offset1:131
	ds_write2_b32 v87, v16, v17 offset1:1
	ds_write2_b32 v88, v18, v19 offset1:1
	ds_write2_b32 v89, v20, v21 offset1:1
	ds_write2_b32 v90, v22, v23 offset1:1
	ds_write2_b32 v91, v24, v25 offset1:1
	ds_write2_b32 v92, v26, v27 offset1:1
	ds_write2_b32 v93, v28, v29 offset1:1
	ds_write2_b32 v94, v30, v31 offset1:1
	ds_write2_b32 v95, v32, v33 offset1:1
	ds_write2_b32 v96, v34, v35 offset1:1
	ds_write2_b32 v97, v36, v37 offset1:1
	ds_write2_b32 v98, v38, v39 offset1:1
	ds_write2_b32 v99, v40, v41 offset1:1
	ds_write2_b32 v100, v42, v43 offset1:1
	ds_write2_b32 v101, v44, v45 offset1:1
	ds_write2_b32 v102, v46, v47 offset1:1
	ds_write2_b32 v103, v48, v49 offset1:1
	ds_write2_b32 v104, v50, v51 offset1:1
	ds_write2_b32 v105, v52, v53 offset1:1
	ds_write2_b32 v106, v54, v55 offset1:1
	ds_write2_b32 v107, v56, v57 offset1:1
	ds_write2_b32 v108, v58, v59 offset1:1
	ds_write2_b32 v109, v60, v61 offset1:1
	ds_write2_b32 v110, v62, v63 offset1:1
	ds_write2_b32 v111, v64, v65 offset1:1
	ds_write2_b32 v112, v66, v67 offset1:1
	ds_write2_b32 v113, v68, v69 offset1:1
	ds_write2_b32 v114, v70, v71 offset1:1
	ds_write2_b32 v115, v72, v73 offset1:1
	ds_write2_b32 v116, v10, v11 offset1:1
	s_waitcnt lgkmcnt(0)
	ds_read2_b32 v[14:15], v79 offset0:65 offset1:73
	ds_read2_b32 v[16:17], v79 offset1:8
	ds_read2_b32 v[18:19], v79 offset0:130 offset1:138
	ds_read2_b32 v[20:21], v79 offset0:195 offset1:203
	ds_read2_b32 v[22:23], v117 offset0:4 offset1:12
	ds_read2_b32 v[24:25], v117 offset0:69 offset1:77
	ds_read2_b32 v[26:27], v117 offset0:134 offset1:142
	ds_read2_b32 v[28:29], v117 offset0:199 offset1:207
	v_add_u32_e32 v32, s8, v75
	v_ashrrev_i32_e32 v33, 31, v32
	v_lshl_add_u64 v[30:31], v[4:5], 0, s[12:13]
	v_lshlrev_b64 v[32:33], 12, v[32:33]
	s_waitcnt lgkmcnt(6)
	v_cvt_pk_bf16_f32 v10, v16, v14
	s_waitcnt lgkmcnt(4)
	v_cvt_pk_bf16_f32 v11, v18, v20
	s_waitcnt lgkmcnt(2)
	v_cvt_pk_bf16_f32 v12, v22, v24
	s_waitcnt lgkmcnt(0)
	v_cvt_pk_bf16_f32 v13, v26, v28
	v_lshl_add_u64 v[32:33], v[30:31], 0, v[32:33]
	v_add_u32_e32 v14, s8, v80
	global_store_dwordx4 v[32:33], v[10:13], off
	s_nop 1
	v_cvt_pk_bf16_f32 v10, v17, v15
	v_ashrrev_i32_e32 v15, 31, v14
	v_cvt_pk_bf16_f32 v11, v19, v21
	v_cvt_pk_bf16_f32 v12, v23, v25
	v_cvt_pk_bf16_f32 v13, v27, v29
	v_lshlrev_b64 v[14:15], 12, v[14:15]
	ds_read2_b32 v[16:17], v79 offset0:81 offset1:89
	ds_read2_b32 v[18:19], v79 offset0:16 offset1:24
	ds_read2_b32 v[20:21], v79 offset0:146 offset1:154
	ds_read2_b32 v[22:23], v79 offset0:211 offset1:219
	ds_read2_b32 v[24:25], v117 offset0:20 offset1:28
	ds_read2_b32 v[26:27], v117 offset0:85 offset1:93
	ds_read2_b32 v[28:29], v117 offset0:150 offset1:158
	ds_read2_b32 v[32:33], v117 offset0:215 offset1:223
	v_lshl_add_u64 v[14:15], v[30:31], 0, v[14:15]
	global_store_dwordx4 v[14:15], v[10:13], off
	v_add_u32_e32 v14, s8, v81
	v_ashrrev_i32_e32 v15, 31, v14
	v_lshlrev_b64 v[14:15], 12, v[14:15]
	s_waitcnt lgkmcnt(6)
	v_cvt_pk_bf16_f32 v10, v18, v16
	s_waitcnt lgkmcnt(4)
	v_cvt_pk_bf16_f32 v11, v20, v22
	s_waitcnt lgkmcnt(2)
	v_cvt_pk_bf16_f32 v12, v24, v26
	s_waitcnt lgkmcnt(0)
	v_cvt_pk_bf16_f32 v13, v28, v32
	v_lshl_add_u64 v[14:15], v[30:31], 0, v[14:15]
	global_store_dwordx4 v[14:15], v[10:13], off
	v_add_u32_e32 v14, s8, v82
	v_ashrrev_i32_e32 v15, 31, v14
	v_cvt_pk_bf16_f32 v10, v19, v17
	v_cvt_pk_bf16_f32 v11, v21, v23
	v_cvt_pk_bf16_f32 v12, v25, v27
	v_cvt_pk_bf16_f32 v13, v29, v33
	v_lshlrev_b64 v[14:15], 12, v[14:15]
	ds_read2_b32 v[16:17], v79 offset0:32 offset1:40
	ds_read2_b32 v[18:19], v79 offset0:97 offset1:105
	ds_read2_b32 v[20:21], v79 offset0:162 offset1:170
	ds_read2_b32 v[22:23], v79 offset0:227 offset1:235
	ds_read2_b32 v[24:25], v117 offset0:36 offset1:44
	ds_read2_b32 v[26:27], v117 offset0:101 offset1:109
	ds_read2_b32 v[28:29], v117 offset0:166 offset1:174
	ds_read2_b32 v[32:33], v117 offset0:231 offset1:239
	v_lshl_add_u64 v[14:15], v[30:31], 0, v[14:15]
	global_store_dwordx4 v[14:15], v[10:13], off
	v_add_u32_e32 v14, s8, v83
	v_ashrrev_i32_e32 v15, 31, v14
	v_lshlrev_b64 v[14:15], 12, v[14:15]
	s_waitcnt lgkmcnt(6)
	v_cvt_pk_bf16_f32 v10, v16, v18
	s_waitcnt lgkmcnt(4)
	v_cvt_pk_bf16_f32 v11, v20, v22
	s_waitcnt lgkmcnt(2)
	v_cvt_pk_bf16_f32 v12, v24, v26
	s_waitcnt lgkmcnt(0)
	v_cvt_pk_bf16_f32 v13, v28, v32
	v_lshl_add_u64 v[14:15], v[30:31], 0, v[14:15]
	global_store_dwordx4 v[14:15], v[10:13], off
	v_add_u32_e32 v14, s8, v84
	v_ashrrev_i32_e32 v15, 31, v14
	v_cvt_pk_bf16_f32 v10, v17, v19
	v_cvt_pk_bf16_f32 v11, v21, v23
	v_cvt_pk_bf16_f32 v12, v25, v27
	v_cvt_pk_bf16_f32 v13, v29, v33
	v_lshlrev_b64 v[14:15], 12, v[14:15]
	ds_read2_b32 v[16:17], v79 offset0:48 offset1:56
	ds_read2_b32 v[18:19], v79 offset0:113 offset1:121
	ds_read2_b32 v[20:21], v79 offset0:178 offset1:186
	ds_read2_b32 v[22:23], v79 offset0:243 offset1:251
	ds_read2_b32 v[24:25], v117 offset0:52 offset1:60
	ds_read2_b32 v[26:27], v117 offset0:117 offset1:125
	ds_read2_b32 v[28:29], v117 offset0:182 offset1:190
	ds_read2_b32 v[32:33], v117 offset0:247 offset1:255
	v_lshl_add_u64 v[14:15], v[30:31], 0, v[14:15]
	global_store_dwordx4 v[14:15], v[10:13], off
	v_add_u32_e32 v14, s8, v85
	v_ashrrev_i32_e32 v15, 31, v14
	v_lshlrev_b64 v[14:15], 12, v[14:15]
	s_waitcnt lgkmcnt(6)
	v_cvt_pk_bf16_f32 v10, v16, v18
	s_waitcnt lgkmcnt(4)
	v_cvt_pk_bf16_f32 v11, v20, v22
	s_waitcnt lgkmcnt(2)
	v_cvt_pk_bf16_f32 v12, v24, v26
	s_waitcnt lgkmcnt(0)
	v_cvt_pk_bf16_f32 v13, v28, v32
	v_lshl_add_u64 v[14:15], v[30:31], 0, v[14:15]
	global_store_dwordx4 v[14:15], v[10:13], off
	v_add_u32_e32 v14, s8, v86
	v_ashrrev_i32_e32 v15, 31, v14
	v_lshlrev_b64 v[14:15], 12, v[14:15]
	v_cvt_pk_bf16_f32 v10, v17, v19
	v_cvt_pk_bf16_f32 v11, v21, v23
	v_cvt_pk_bf16_f32 v12, v25, v27
	v_cvt_pk_bf16_f32 v13, v29, v33
	v_lshl_add_u64 v[14:15], v[30:31], 0, v[14:15]
	global_store_dwordx4 v[14:15], v[10:13], off
	s_waitcnt lgkmcnt(0)

.LBB0_2215:
	s_andn2_b64 vcc, exec, s[12:13]
	s_cbranch_vccnz .LBB0_2204
	s_ashr_i32 s8, s81, 31
	s_lshr_b32 s8, s8, 29
	s_add_i32 s8, s81, s8
	s_load_dwordx2 s[82:83], s[52:53], 0x78
	s_ashr_i32 s8, s8, 3
	s_lshl_b32 s12, s8, 6
	s_lshl_b32 s8, s8, 9
	s_sub_i32 s14, s5, s8
	s_ashr_i32 s13, s12, 31
	v_add_u32_e32 v10, s14, v74
	s_lshl_b64 s[84:85], s[12:13], 2
	s_waitcnt lgkmcnt(0)
	s_add_u32 s82, s82, s84
	v_ashrrev_i32_e32 v11, 31, v10
	s_addc_u32 s83, s83, s85
	v_lshlrev_b64 v[14:15], 13, v[10:11]
	v_add_u32_e32 v16, 2, v10
	v_add_u32_e32 v18, 4, v10
	v_add_u32_e32 v20, 6, v10
	v_add_u32_e32 v22, 8, v10
	v_add_u32_e32 v24, 10, v10
	v_add_u32_e32 v26, 12, v10
	v_add_u32_e32 v28, 14, v10
	v_add_u32_e32 v30, 16, v10
	v_add_u32_e32 v32, 18, v10
	v_add_u32_e32 v34, 20, v10
	v_add_u32_e32 v36, 22, v10
	v_add_u32_e32 v38, 24, v10
	v_add_u32_e32 v40, 26, v10
	v_add_u32_e32 v42, 28, v10
	v_add_u32_e32 v44, 30, v10
	v_add_u32_e32 v46, 32, v10
	v_add_u32_e32 v48, 34, v10
	v_add_u32_e32 v50, 36, v10
	v_add_u32_e32 v52, 38, v10
	v_add_u32_e32 v54, 40, v10
	v_add_u32_e32 v56, 42, v10
	v_add_u32_e32 v58, 44, v10
	v_add_u32_e32 v60, 46, v10
	v_add_u32_e32 v62, 48, v10
	v_add_u32_e32 v64, 50, v10
	v_add_u32_e32 v66, 52, v10
	v_add_u32_e32 v68, 54, v10
	v_add_u32_e32 v70, 56, v10
	v_add_u32_e32 v72, 58, v10
	v_add_u32_e32 v118, 60, v10
	v_add_u32_e32 v10, 62, v10
	v_lshl_add_u64 v[12:13], s[82:83], 0, v[0:1]
	v_ashrrev_i32_e32 v17, 31, v16
	v_ashrrev_i32_e32 v19, 31, v18
	v_ashrrev_i32_e32 v21, 31, v20
	v_ashrrev_i32_e32 v23, 31, v22
	v_ashrrev_i32_e32 v25, 31, v24
	v_ashrrev_i32_e32 v27, 31, v26
	v_ashrrev_i32_e32 v29, 31, v28
	v_ashrrev_i32_e32 v31, 31, v30
	v_ashrrev_i32_e32 v33, 31, v32
	v_ashrrev_i32_e32 v35, 31, v34
	v_ashrrev_i32_e32 v37, 31, v36
	v_ashrrev_i32_e32 v39, 31, v38
	v_ashrrev_i32_e32 v41, 31, v40
	v_ashrrev_i32_e32 v43, 31, v42
	v_ashrrev_i32_e32 v45, 31, v44
	v_ashrrev_i32_e32 v47, 31, v46
	v_ashrrev_i32_e32 v49, 31, v48
	v_ashrrev_i32_e32 v51, 31, v50
	v_ashrrev_i32_e32 v53, 31, v52
	v_ashrrev_i32_e32 v55, 31, v54
	v_ashrrev_i32_e32 v57, 31, v56
	v_ashrrev_i32_e32 v59, 31, v58
	v_ashrrev_i32_e32 v61, 31, v60
	v_ashrrev_i32_e32 v63, 31, v62
	v_ashrrev_i32_e32 v65, 31, v64
	v_ashrrev_i32_e32 v67, 31, v66
	v_ashrrev_i32_e32 v69, 31, v68
	v_ashrrev_i32_e32 v71, 31, v70
	v_ashrrev_i32_e32 v73, 31, v72
	v_ashrrev_i32_e32 v11, 31, v10
	v_lshl_add_u64 v[12:13], v[12:13], 0, s[10:11]
	v_lshlrev_b64 v[16:17], 13, v[16:17]
	v_lshlrev_b64 v[18:19], 13, v[18:19]
	v_lshlrev_b64 v[20:21], 13, v[20:21]
	v_lshlrev_b64 v[22:23], 13, v[22:23]
	v_lshlrev_b64 v[24:25], 13, v[24:25]
	v_lshlrev_b64 v[26:27], 13, v[26:27]
	v_lshlrev_b64 v[28:29], 13, v[28:29]
	v_lshlrev_b64 v[30:31], 13, v[30:31]
	v_lshlrev_b64 v[32:33], 13, v[32:33]
	v_lshlrev_b64 v[34:35], 13, v[34:35]
	v_lshlrev_b64 v[36:37], 13, v[36:37]
	v_lshlrev_b64 v[38:39], 13, v[38:39]
	v_lshlrev_b64 v[40:41], 13, v[40:41]
	v_lshlrev_b64 v[42:43], 13, v[42:43]
	v_lshlrev_b64 v[44:45], 13, v[44:45]
	v_lshlrev_b64 v[46:47], 13, v[46:47]
	v_lshlrev_b64 v[48:49], 13, v[48:49]
	v_lshlrev_b64 v[50:51], 13, v[50:51]
	v_lshlrev_b64 v[52:53], 13, v[52:53]
	v_lshlrev_b64 v[54:55], 13, v[54:55]
	v_lshlrev_b64 v[56:57], 13, v[56:57]
	v_lshlrev_b64 v[58:59], 13, v[58:59]
	v_lshlrev_b64 v[60:61], 13, v[60:61]
	v_lshlrev_b64 v[62:63], 13, v[62:63]
	v_lshlrev_b64 v[64:65], 13, v[64:65]
	v_lshlrev_b64 v[66:67], 13, v[66:67]
	v_lshlrev_b64 v[68:69], 13, v[68:69]
	v_lshlrev_b64 v[70:71], 13, v[70:71]
	v_lshlrev_b64 v[72:73], 13, v[72:73]
	v_ashrrev_i32_e32 v119, 31, v118
	v_lshlrev_b64 v[10:11], 13, v[10:11]
	v_lshl_add_u64 v[14:15], v[12:13], 0, v[14:15]
	v_lshl_add_u64 v[16:17], v[12:13], 0, v[16:17]
	v_lshl_add_u64 v[18:19], v[12:13], 0, v[18:19]
	v_lshl_add_u64 v[20:21], v[12:13], 0, v[20:21]
	v_lshl_add_u64 v[22:23], v[12:13], 0, v[22:23]
	v_lshl_add_u64 v[24:25], v[12:13], 0, v[24:25]
	v_lshl_add_u64 v[26:27], v[12:13], 0, v[26:27]
	v_lshl_add_u64 v[28:29], v[12:13], 0, v[28:29]
	v_lshl_add_u64 v[30:31], v[12:13], 0, v[30:31]
	v_lshl_add_u64 v[32:33], v[12:13], 0, v[32:33]
	v_lshl_add_u64 v[34:35], v[12:13], 0, v[34:35]
	v_lshl_add_u64 v[36:37], v[12:13], 0, v[36:37]
	v_lshl_add_u64 v[38:39], v[12:13], 0, v[38:39]
	v_lshl_add_u64 v[40:41], v[12:13], 0, v[40:41]
	v_lshl_add_u64 v[42:43], v[12:13], 0, v[42:43]
	v_lshl_add_u64 v[44:45], v[12:13], 0, v[44:45]
	v_lshl_add_u64 v[46:47], v[12:13], 0, v[46:47]
	v_lshl_add_u64 v[48:49], v[12:13], 0, v[48:49]
	v_lshl_add_u64 v[50:51], v[12:13], 0, v[50:51]
	v_lshl_add_u64 v[52:53], v[12:13], 0, v[52:53]
	v_lshl_add_u64 v[54:55], v[12:13], 0, v[54:55]
	v_lshl_add_u64 v[56:57], v[12:13], 0, v[56:57]
	v_lshl_add_u64 v[58:59], v[12:13], 0, v[58:59]
	v_lshl_add_u64 v[60:61], v[12:13], 0, v[60:61]
	v_lshl_add_u64 v[62:63], v[12:13], 0, v[62:63]
	v_lshl_add_u64 v[64:65], v[12:13], 0, v[64:65]
	v_lshl_add_u64 v[66:67], v[12:13], 0, v[66:67]
	v_lshl_add_u64 v[68:69], v[12:13], 0, v[68:69]
	v_lshl_add_u64 v[70:71], v[12:13], 0, v[70:71]
	v_lshl_add_u64 v[72:73], v[12:13], 0, v[72:73]
	v_lshlrev_b64 v[118:119], 13, v[118:119]
	v_lshl_add_u64 v[10:11], v[12:13], 0, v[10:11]
	global_load_dwordx2 v[14:15], v[14:15], off nt
	s_nop 0
	global_load_dwordx2 v[16:17], v[16:17], off nt
	s_nop 0
	global_load_dwordx2 v[18:19], v[18:19], off nt
	s_nop 0
	global_load_dwordx2 v[20:21], v[20:21], off nt
	s_nop 0
	global_load_dwordx2 v[22:23], v[22:23], off nt
	s_nop 0
	global_load_dwordx2 v[24:25], v[24:25], off nt
	s_nop 0
	global_load_dwordx2 v[26:27], v[26:27], off nt
	s_nop 0
	global_load_dwordx2 v[28:29], v[28:29], off nt
	s_nop 0
	global_load_dwordx2 v[30:31], v[30:31], off nt
	s_nop 0
	global_load_dwordx2 v[32:33], v[32:33], off nt
	s_nop 0
	global_load_dwordx2 v[34:35], v[34:35], off nt
	s_nop 0
	global_load_dwordx2 v[36:37], v[36:37], off nt
	s_nop 0
	global_load_dwordx2 v[38:39], v[38:39], off nt
	s_nop 0
	global_load_dwordx2 v[40:41], v[40:41], off nt
	s_nop 0
	global_load_dwordx2 v[42:43], v[42:43], off nt
	s_nop 0
	global_load_dwordx2 v[44:45], v[44:45], off nt
	s_nop 0
	global_load_dwordx2 v[46:47], v[46:47], off nt
	s_nop 0
	global_load_dwordx2 v[48:49], v[48:49], off nt
	s_nop 0
	global_load_dwordx2 v[50:51], v[50:51], off nt
	s_nop 0
	global_load_dwordx2 v[52:53], v[52:53], off nt
	s_nop 0
	global_load_dwordx2 v[54:55], v[54:55], off nt
	s_nop 0
	global_load_dwordx2 v[56:57], v[56:57], off nt
	s_nop 0
	global_load_dwordx2 v[58:59], v[58:59], off nt
	s_nop 0
	global_load_dwordx2 v[60:61], v[60:61], off nt
	s_nop 0
	global_load_dwordx2 v[62:63], v[62:63], off nt
	s_nop 0
	global_load_dwordx2 v[64:65], v[64:65], off nt
	s_nop 0
	global_load_dwordx2 v[66:67], v[66:67], off nt
	s_nop 0
	global_load_dwordx2 v[68:69], v[68:69], off nt
	v_lshl_add_u64 v[118:119], v[12:13], 0, v[118:119]
	global_load_dwordx2 v[12:13], v[70:71], off nt
	s_nop 0
	global_load_dwordx2 v[70:71], v[72:73], off nt
	s_nop 0
	global_load_dwordx2 v[72:73], v[118:119], off nt
	s_nop 0
	global_load_dwordx2 v[10:11], v[10:11], off nt
	s_waitcnt vmcnt(0)
	ds_write2_b32 v78, v14, v15 offset1:1
	ds_write2_b32 v78, v16, v17 offset0:130 offset1:131
	ds_write2_b32 v87, v18, v19 offset1:1
	ds_write2_b32 v88, v20, v21 offset1:1
	ds_write2_b32 v89, v22, v23 offset1:1
	ds_write2_b32 v90, v24, v25 offset1:1
	ds_write2_b32 v91, v26, v27 offset1:1
	ds_write2_b32 v92, v28, v29 offset1:1
	ds_write2_b32 v93, v30, v31 offset1:1
	ds_write2_b32 v94, v32, v33 offset1:1
	ds_write2_b32 v95, v34, v35 offset1:1
	ds_write2_b32 v96, v36, v37 offset1:1
	ds_write2_b32 v97, v38, v39 offset1:1
	ds_write2_b32 v98, v40, v41 offset1:1
	ds_write2_b32 v99, v42, v43 offset1:1
	ds_write2_b32 v100, v44, v45 offset1:1
	ds_write2_b32 v101, v46, v47 offset1:1
	ds_write2_b32 v102, v48, v49 offset1:1
	ds_write2_b32 v103, v50, v51 offset1:1
	ds_write2_b32 v104, v52, v53 offset1:1
	ds_write2_b32 v105, v54, v55 offset1:1
	ds_write2_b32 v106, v56, v57 offset1:1
	ds_write2_b32 v107, v58, v59 offset1:1
	ds_write2_b32 v108, v60, v61 offset1:1
	ds_write2_b32 v109, v62, v63 offset1:1
	ds_write2_b32 v110, v64, v65 offset1:1
	ds_write2_b32 v111, v66, v67 offset1:1
	ds_write2_b32 v112, v68, v69 offset1:1
	ds_write2_b32 v113, v12, v13 offset1:1
	ds_write2_b32 v114, v70, v71 offset1:1
	ds_write2_b32 v115, v72, v73 offset1:1
	ds_write2_b32 v116, v10, v11 offset1:1
	s_waitcnt lgkmcnt(0)
	ds_read2_b32 v[14:15], v79 offset0:65 offset1:73
	ds_read2_b32 v[16:17], v79 offset1:8
	ds_read2_b32 v[18:19], v79 offset0:130 offset1:138
	ds_read2_b32 v[20:21], v79 offset0:195 offset1:203
	ds_read2_b32 v[22:23], v117 offset0:4 offset1:12
	ds_read2_b32 v[24:25], v117 offset0:69 offset1:77
	ds_read2_b32 v[26:27], v117 offset0:134 offset1:142
	ds_read2_b32 v[28:29], v117 offset0:199 offset1:207
	v_add_u32_e32 v32, s12, v75
	s_ashr_i32 s15, s14, 31
	v_ashrrev_i32_e32 v33, 31, v32
	v_lshl_add_u64 v[30:31], s[14:15], 1, v[6:7]
	v_lshlrev_b64 v[32:33], 12, v[32:33]
	s_waitcnt lgkmcnt(6)
	v_cvt_pk_bf16_f32 v10, v16, v14
	s_waitcnt lgkmcnt(4)
	v_cvt_pk_bf16_f32 v11, v18, v20
	s_waitcnt lgkmcnt(2)
	v_cvt_pk_bf16_f32 v12, v22, v24
	s_waitcnt lgkmcnt(0)
	v_cvt_pk_bf16_f32 v13, v26, v28
	v_lshl_add_u64 v[32:33], v[30:31], 0, v[32:33]
	v_add_u32_e32 v14, s12, v80
	global_store_dwordx4 v[32:33], v[10:13], off
	s_nop 1
	v_cvt_pk_bf16_f32 v10, v17, v15
	v_ashrrev_i32_e32 v15, 31, v14
	v_cvt_pk_bf16_f32 v11, v19, v21
	v_cvt_pk_bf16_f32 v12, v23, v25
	v_cvt_pk_bf16_f32 v13, v27, v29
	v_lshlrev_b64 v[14:15], 12, v[14:15]
	ds_read2_b32 v[16:17], v79 offset0:81 offset1:89
	ds_read2_b32 v[18:19], v79 offset0:16 offset1:24
	ds_read2_b32 v[20:21], v79 offset0:146 offset1:154
	ds_read2_b32 v[22:23], v79 offset0:211 offset1:219
	ds_read2_b32 v[24:25], v117 offset0:20 offset1:28
	ds_read2_b32 v[26:27], v117 offset0:85 offset1:93
	ds_read2_b32 v[28:29], v117 offset0:150 offset1:158
	ds_read2_b32 v[32:33], v117 offset0:215 offset1:223
	v_lshl_add_u64 v[14:15], v[30:31], 0, v[14:15]
	global_store_dwordx4 v[14:15], v[10:13], off
	v_add_u32_e32 v14, s12, v81
	v_ashrrev_i32_e32 v15, 31, v14
	v_lshlrev_b64 v[14:15], 12, v[14:15]
	s_waitcnt lgkmcnt(6)
	v_cvt_pk_bf16_f32 v10, v18, v16
	s_waitcnt lgkmcnt(4)
	v_cvt_pk_bf16_f32 v11, v20, v22
	s_waitcnt lgkmcnt(2)
	v_cvt_pk_bf16_f32 v12, v24, v26
	s_waitcnt lgkmcnt(0)
	v_cvt_pk_bf16_f32 v13, v28, v32
	v_lshl_add_u64 v[14:15], v[30:31], 0, v[14:15]
	global_store_dwordx4 v[14:15], v[10:13], off
	v_add_u32_e32 v14, s12, v82
	v_ashrrev_i32_e32 v15, 31, v14
	v_cvt_pk_bf16_f32 v10, v19, v17
	v_cvt_pk_bf16_f32 v11, v21, v23
	v_cvt_pk_bf16_f32 v12, v25, v27
	v_cvt_pk_bf16_f32 v13, v29, v33
	v_lshlrev_b64 v[14:15], 12, v[14:15]
	ds_read2_b32 v[16:17], v79 offset0:32 offset1:40
	ds_read2_b32 v[18:19], v79 offset0:97 offset1:105
	ds_read2_b32 v[20:21], v79 offset0:162 offset1:170
	ds_read2_b32 v[22:23], v79 offset0:227 offset1:235
	ds_read2_b32 v[24:25], v117 offset0:36 offset1:44
	ds_read2_b32 v[26:27], v117 offset0:101 offset1:109
	ds_read2_b32 v[28:29], v117 offset0:166 offset1:174
	ds_read2_b32 v[32:33], v117 offset0:231 offset1:239
	v_lshl_add_u64 v[14:15], v[30:31], 0, v[14:15]
	global_store_dwordx4 v[14:15], v[10:13], off
	v_add_u32_e32 v14, s12, v83
	v_ashrrev_i32_e32 v15, 31, v14
	v_lshlrev_b64 v[14:15], 12, v[14:15]
	s_waitcnt lgkmcnt(6)
	v_cvt_pk_bf16_f32 v10, v16, v18
	s_waitcnt lgkmcnt(4)
	v_cvt_pk_bf16_f32 v11, v20, v22
	s_waitcnt lgkmcnt(2)
	v_cvt_pk_bf16_f32 v12, v24, v26
	s_waitcnt lgkmcnt(0)
	v_cvt_pk_bf16_f32 v13, v28, v32
	v_lshl_add_u64 v[14:15], v[30:31], 0, v[14:15]
	global_store_dwordx4 v[14:15], v[10:13], off
	v_add_u32_e32 v14, s12, v84
	v_ashrrev_i32_e32 v15, 31, v14
	v_cvt_pk_bf16_f32 v10, v17, v19
	v_cvt_pk_bf16_f32 v11, v21, v23
	v_cvt_pk_bf16_f32 v12, v25, v27
	v_cvt_pk_bf16_f32 v13, v29, v33
	v_lshlrev_b64 v[14:15], 12, v[14:15]
	ds_read2_b32 v[16:17], v79 offset0:48 offset1:56
	ds_read2_b32 v[18:19], v79 offset0:113 offset1:121
	ds_read2_b32 v[20:21], v79 offset0:178 offset1:186
	ds_read2_b32 v[22:23], v79 offset0:243 offset1:251
	ds_read2_b32 v[24:25], v117 offset0:52 offset1:60
	ds_read2_b32 v[26:27], v117 offset0:117 offset1:125
	ds_read2_b32 v[28:29], v117 offset0:182 offset1:190
	ds_read2_b32 v[32:33], v117 offset0:247 offset1:255
	v_lshl_add_u64 v[14:15], v[30:31], 0, v[14:15]
	global_store_dwordx4 v[14:15], v[10:13], off
	v_add_u32_e32 v14, s12, v85
	v_ashrrev_i32_e32 v15, 31, v14
	v_lshlrev_b64 v[14:15], 12, v[14:15]
	s_waitcnt lgkmcnt(6)
	v_cvt_pk_bf16_f32 v10, v16, v18
	s_waitcnt lgkmcnt(4)
	v_cvt_pk_bf16_f32 v11, v20, v22
	s_waitcnt lgkmcnt(2)
	v_cvt_pk_bf16_f32 v12, v24, v26
	s_waitcnt lgkmcnt(0)
	v_cvt_pk_bf16_f32 v13, v28, v32
	v_lshl_add_u64 v[14:15], v[30:31], 0, v[14:15]
	global_store_dwordx4 v[14:15], v[10:13], off
	v_add_u32_e32 v14, s12, v86
	v_ashrrev_i32_e32 v15, 31, v14
	v_lshlrev_b64 v[14:15], 12, v[14:15]
	v_cvt_pk_bf16_f32 v10, v17, v19
	v_cvt_pk_bf16_f32 v11, v21, v23
	v_cvt_pk_bf16_f32 v12, v25, v27
	v_cvt_pk_bf16_f32 v13, v29, v33
	v_lshl_add_u64 v[14:15], v[30:31], 0, v[14:15]
	global_store_dwordx4 v[14:15], v[10:13], off
	s_waitcnt lgkmcnt(0)
	s_branch .LBB0_2204

.LBB0_2219:
	s_add_i32 s11, s0, 0xc00
	s_ashr_i32 s10, s11, 31
	s_lshr_b32 s10, s10, 23
	s_add_i32 s12, s11, s10
	s_ashr_i32 s10, s12, 9
	s_and_b32 s12, s12, 0xfe00
	s_sub_i32 s12, s11, s12
	s_sext_i32_i16 s13, s12
	s_bfe_u32 s13, s13, 0x5001a
	s_add_i32 s13, s12, s13
	s_ashr_i32 s11, s10, 31
	s_sext_i32_i16 s44, s13
	s_and_b32 s13, s13, 0xffe0
	s_lshl_b64 s[10:11], s[10:11], 23
	s_ashr_i32 s46, s44, 5
	s_sub_i32 s12, s12, s13
	s_add_u32 s10, s10, 0x8000000
	s_sext_i32_i16 s13, s12
	s_addc_u32 s12, s11, 0
	s_waitcnt lgkmcnt(0)
	s_add_u32 s47, s6, s10
	s_addc_u32 s11, s7, s12
	s_add_u32 s45, s8, s10
	s_addc_u32 s44, s9, s12
	s_lshl_b32 s12, s46, 6
	s_lshl_b32 s10, s13, 6
	s_lshl_b32 s13, s46, 7
	s_and_b32 s46, s13, 0xffffff00
	s_and_b32 s48, s12, 64
	s_ashr_i32 s13, s12, 31
	s_or_b32 s46, s48, s46
	s_lshl_b64 s[12:13], s[12:13], 2
	v_add_u32_e32 v4, s10, v74
	s_add_u32 s12, s47, s12
	v_ashrrev_i32_e32 v5, 31, v4
	s_addc_u32 s13, s11, s13
	v_lshlrev_b64 v[4:5], 12, v[4:5]
	v_lshl_add_u64 v[56:57], s[12:13], 0, v[0:1]
	v_lshl_add_u64 v[4:5], v[56:57], 0, v[4:5]
	v_add_co_u32_e32 v56, vcc, s1, v4
	s_ashr_i32 s11, s10, 31
	s_nop 0
	v_addc_co_u32_e32 v57, vcc, 0, v5, vcc
	v_add_co_u32_e32 v58, vcc, s4, v4
	v_add_u32_e32 v40, s46, v75
	s_nop 0
	v_addc_co_u32_e32 v59, vcc, 0, v5, vcc
	v_add_co_u32_e32 v60, vcc, s5, v4
	s_lshl_b64 s[10:11], s[10:11], 1
	s_nop 0
	v_addc_co_u32_e32 v61, vcc, 0, v5, vcc
	v_add_co_u32_e32 v62, vcc, s14, v4
	v_add_u32_e32 v42, 8, v40
	s_nop 0
	v_addc_co_u32_e32 v63, vcc, 0, v5, vcc
	v_add_co_u32_e32 v64, vcc, s15, v4
	v_add_u32_e32 v44, 16, v40
	s_nop 0
	v_addc_co_u32_e32 v65, vcc, 0, v5, vcc
	v_add_co_u32_e32 v66, vcc, s16, v4
	v_add_u32_e32 v46, 24, v40
	s_nop 0
	v_addc_co_u32_e32 v67, vcc, 0, v5, vcc
	v_add_co_u32_e32 v68, vcc, s17, v4
	v_add_u32_e32 v48, 32, v40
	s_nop 0
	v_addc_co_u32_e32 v69, vcc, 0, v5, vcc
	v_add_co_u32_e32 v70, vcc, s18, v4
	v_add_u32_e32 v50, 40, v40
	s_nop 0
	v_addc_co_u32_e32 v71, vcc, 0, v5, vcc
	v_add_co_u32_e32 v72, vcc, s19, v4
	v_add_u32_e32 v52, 48, v40
	s_nop 0
	v_addc_co_u32_e32 v73, vcc, 0, v5, vcc
	v_add_co_u32_e32 v76, vcc, s20, v4
	v_add_u32_e32 v54, 56, v40
	s_nop 0
	v_addc_co_u32_e32 v77, vcc, 0, v5, vcc
	v_add_co_u32_e32 v78, vcc, s21, v4
	s_add_u32 s10, s45, s10
	s_nop 0
	v_addc_co_u32_e32 v79, vcc, 0, v5, vcc
	v_add_co_u32_e32 v80, vcc, s22, v4
	v_ashrrev_i32_e32 v41, 31, v40
	s_nop 0
	v_addc_co_u32_e32 v81, vcc, 0, v5, vcc
	v_add_co_u32_e32 v82, vcc, s23, v4
	v_ashrrev_i32_e32 v43, 31, v42
	s_nop 0
	v_addc_co_u32_e32 v83, vcc, 0, v5, vcc
	v_add_co_u32_e32 v84, vcc, s24, v4
	v_ashrrev_i32_e32 v45, 31, v44
	s_nop 0
	v_addc_co_u32_e32 v85, vcc, 0, v5, vcc
	v_add_co_u32_e32 v86, vcc, s25, v4
	v_ashrrev_i32_e32 v47, 31, v46
	s_nop 0
	v_addc_co_u32_e32 v87, vcc, 0, v5, vcc
	v_add_co_u32_e32 v88, vcc, s26, v4
	v_ashrrev_i32_e32 v49, 31, v48
	s_nop 0
	v_addc_co_u32_e32 v89, vcc, 0, v5, vcc
	v_add_co_u32_e32 v90, vcc, s27, v4
	v_ashrrev_i32_e32 v51, 31, v50
	s_nop 0
	v_addc_co_u32_e32 v91, vcc, 0, v5, vcc
	v_add_co_u32_e32 v92, vcc, s28, v4
	v_ashrrev_i32_e32 v53, 31, v52
	s_nop 0
	v_addc_co_u32_e32 v93, vcc, 0, v5, vcc
	v_add_co_u32_e32 v94, vcc, s29, v4
	v_ashrrev_i32_e32 v55, 31, v54
	s_nop 0
	v_addc_co_u32_e32 v95, vcc, 0, v5, vcc
	v_add_co_u32_e32 v96, vcc, s30, v4
	s_addc_u32 s11, s44, s11
	s_nop 0
	v_addc_co_u32_e32 v97, vcc, 0, v5, vcc
	v_add_co_u32_e32 v98, vcc, s31, v4
	v_lshlrev_b64 v[40:41], 12, v[40:41]
	s_nop 0
	v_addc_co_u32_e32 v99, vcc, 0, v5, vcc
	v_add_co_u32_e32 v100, vcc, s34, v4
	v_lshlrev_b64 v[42:43], 12, v[42:43]
	s_nop 0
	v_addc_co_u32_e32 v101, vcc, 0, v5, vcc
	v_add_co_u32_e32 v102, vcc, s35, v4
	v_lshlrev_b64 v[44:45], 12, v[44:45]
	s_nop 0
	v_addc_co_u32_e32 v103, vcc, 0, v5, vcc
	v_add_co_u32_e32 v104, vcc, s36, v4
	v_lshlrev_b64 v[46:47], 12, v[46:47]
	s_nop 0
	v_addc_co_u32_e32 v105, vcc, 0, v5, vcc
	v_add_co_u32_e32 v106, vcc, s37, v4
	v_lshlrev_b64 v[48:49], 12, v[48:49]
	s_nop 0
	v_addc_co_u32_e32 v107, vcc, 0, v5, vcc
	v_add_co_u32_e32 v108, vcc, s38, v4
	v_lshlrev_b64 v[50:51], 12, v[50:51]
	s_nop 0
	v_addc_co_u32_e32 v109, vcc, 0, v5, vcc
	v_add_co_u32_e32 v110, vcc, s39, v4
	v_lshlrev_b64 v[52:53], 12, v[52:53]
	s_nop 0
	v_addc_co_u32_e32 v111, vcc, 0, v5, vcc
	v_add_co_u32_e32 v112, vcc, s40, v4
	v_lshlrev_b64 v[54:55], 12, v[54:55]
	s_nop 0
	v_addc_co_u32_e32 v113, vcc, 0, v5, vcc
	v_add_co_u32_e32 v114, vcc, s41, v4
	v_lshl_add_u64 v[120:121], s[10:11], 0, v[2:3]
	s_nop 0
	v_addc_co_u32_e32 v115, vcc, 0, v5, vcc
	v_add_co_u32_e32 v116, vcc, s42, v4
	v_lshl_add_u64 v[122:123], v[120:121], 0, v[40:41]
	s_nop 0
	v_addc_co_u32_e32 v117, vcc, 0, v5, vcc
	v_add_co_u32_e32 v118, vcc, s43, v4
	v_lshl_add_u64 v[124:125], v[120:121], 0, v[42:43]
	s_nop 0
	v_addc_co_u32_e32 v119, vcc, 0, v5, vcc
	global_load_dwordx2 v[4:5], v[4:5], off nt
	s_nop 0
	global_load_dwordx2 v[56:57], v[56:57], off nt
	s_nop 0
	global_load_dwordx2 v[58:59], v[58:59], off nt
	s_nop 0
	global_load_dwordx2 v[60:61], v[60:61], off nt
	s_nop 0
	global_load_dwordx2 v[62:63], v[62:63], off nt
	s_nop 0
	global_load_dwordx2 v[64:65], v[64:65], off nt
	s_nop 0
	global_load_dwordx2 v[66:67], v[66:67], off nt
	s_nop 0
	global_load_dwordx2 v[68:69], v[68:69], off nt
	s_nop 0
	global_load_dwordx2 v[70:71], v[70:71], off nt
	s_nop 0
	global_load_dwordx2 v[72:73], v[72:73], off nt
	s_nop 0
	global_load_dwordx2 v[76:77], v[76:77], off nt
	s_nop 0
	global_load_dwordx2 v[78:79], v[78:79], off nt
	s_nop 0
	global_load_dwordx2 v[80:81], v[80:81], off nt
	s_nop 0
	global_load_dwordx2 v[82:83], v[82:83], off nt
	s_nop 0
	global_load_dwordx2 v[84:85], v[84:85], off nt
	s_nop 0
	global_load_dwordx2 v[86:87], v[86:87], off nt
	s_nop 0
	global_load_dwordx2 v[88:89], v[88:89], off nt
	s_nop 0
	global_load_dwordx2 v[90:91], v[90:91], off nt
	s_nop 0
	global_load_dwordx2 v[92:93], v[92:93], off nt
	s_nop 0
	global_load_dwordx2 v[94:95], v[94:95], off nt
	s_nop 0
	global_load_dwordx2 v[96:97], v[96:97], off nt
	s_nop 0
	global_load_dwordx2 v[98:99], v[98:99], off nt
	s_nop 0
	global_load_dwordx2 v[100:101], v[100:101], off nt
	s_nop 0
	global_load_dwordx2 v[102:103], v[102:103], off nt
	s_nop 0
	global_load_dwordx2 v[104:105], v[104:105], off nt
	s_nop 0
	global_load_dwordx2 v[106:107], v[106:107], off nt
	s_nop 0
	global_load_dwordx2 v[108:109], v[108:109], off nt
	s_nop 0
	global_load_dwordx2 v[110:111], v[110:111], off nt
	s_nop 0
	global_load_dwordx2 v[112:113], v[112:113], off nt
	s_nop 0
	global_load_dwordx2 v[114:115], v[114:115], off nt
	s_nop 0
	global_load_dwordx2 v[116:117], v[116:117], off nt
	s_nop 0
	global_load_dwordx2 v[118:119], v[118:119], off nt
	s_waitcnt vmcnt(0)
	ds_write2_b32 v7, v4, v5 offset1:1
	ds_write2_b32 v7, v56, v57 offset0:130 offset1:131
	ds_write2_b32 v8, v58, v59 offset1:1
	ds_write2_b32 v9, v60, v61 offset1:1
	ds_write2_b32 v10, v62, v63 offset1:1
	ds_write2_b32 v11, v64, v65 offset1:1
	ds_write2_b32 v12, v66, v67 offset1:1
	ds_write2_b32 v13, v68, v69 offset1:1
	ds_write2_b32 v14, v70, v71 offset1:1
	ds_write2_b32 v15, v72, v73 offset1:1
	ds_write2_b32 v16, v76, v77 offset1:1
	ds_write2_b32 v17, v78, v79 offset1:1
	ds_write2_b32 v18, v80, v81 offset1:1
	ds_write2_b32 v19, v82, v83 offset1:1
	ds_write2_b32 v20, v84, v85 offset1:1
	ds_write2_b32 v21, v86, v87 offset1:1
	ds_write2_b32 v22, v88, v89 offset1:1
	ds_write2_b32 v23, v90, v91 offset1:1
	ds_write2_b32 v24, v92, v93 offset1:1
	ds_write2_b32 v25, v94, v95 offset1:1
	ds_write2_b32 v26, v96, v97 offset1:1
	ds_write2_b32 v27, v98, v99 offset1:1
	ds_write2_b32 v28, v100, v101 offset1:1
	ds_write2_b32 v29, v102, v103 offset1:1
	ds_write2_b32 v30, v104, v105 offset1:1
	ds_write2_b32 v31, v106, v107 offset1:1
	ds_write2_b32 v32, v108, v109 offset1:1
	ds_write2_b32 v33, v110, v111 offset1:1
	ds_write2_b32 v34, v112, v113 offset1:1
	ds_write2_b32 v35, v114, v115 offset1:1
	ds_write2_b32 v36, v116, v117 offset1:1
	ds_write2_b32 v37, v118, v119 offset1:1
	s_waitcnt lgkmcnt(0)
	v_lshl_add_u64 v[126:127], v[120:121], 0, v[44:45]
	v_lshl_add_u64 v[128:129], v[120:121], 0, v[46:47]
	v_lshl_add_u64 v[130:131], v[120:121], 0, v[48:49]
	v_lshl_add_u64 v[132:133], v[120:121], 0, v[50:51]
	v_lshl_add_u64 v[134:135], v[120:121], 0, v[52:53]
	v_lshl_add_u64 v[120:121], v[120:121], 0, v[54:55]
	ds_read2_b32 v[4:5], v6 offset0:65 offset1:73
	ds_read2_b32 v[44:45], v6 offset1:8
	ds_read2_b32 v[46:47], v6 offset0:130 offset1:138
	ds_read2_b32 v[48:49], v6 offset0:195 offset1:203
	ds_read2_b32 v[50:51], v38 offset0:4 offset1:12
	ds_read2_b32 v[52:53], v38 offset0:69 offset1:77
	ds_read2_b32 v[54:55], v38 offset0:134 offset1:142
	ds_read2_b32 v[56:57], v38 offset0:199 offset1:207
	ds_read2_b32 v[58:59], v6 offset0:81 offset1:89
	ds_read2_b32 v[60:61], v6 offset0:16 offset1:24
	ds_read2_b32 v[62:63], v6 offset0:146 offset1:154
	ds_read2_b32 v[64:65], v6 offset0:211 offset1:219
	ds_read2_b32 v[66:67], v38 offset0:20 offset1:28
	ds_read2_b32 v[68:69], v38 offset0:85 offset1:93
	ds_read2_b32 v[70:71], v38 offset0:150 offset1:158
	ds_read2_b32 v[72:73], v38 offset0:215 offset1:223
	ds_read2_b32 v[76:77], v6 offset0:32 offset1:40
	ds_read2_b32 v[78:79], v6 offset0:97 offset1:105
	ds_read2_b32 v[80:81], v6 offset0:162 offset1:170
	ds_read2_b32 v[82:83], v6 offset0:227 offset1:235
	ds_read2_b32 v[84:85], v38 offset0:36 offset1:44
	ds_read2_b32 v[86:87], v38 offset0:101 offset1:109
	ds_read2_b32 v[88:89], v38 offset0:166 offset1:174
	ds_read2_b32 v[90:91], v38 offset0:231 offset1:239
	ds_read2_b32 v[92:93], v6 offset0:48 offset1:56
	ds_read2_b32 v[94:95], v6 offset0:113 offset1:121
	ds_read2_b32 v[96:97], v6 offset0:178 offset1:186
	ds_read2_b32 v[98:99], v6 offset0:243 offset1:251
	ds_read2_b32 v[100:101], v38 offset0:52 offset1:60
	ds_read2_b32 v[102:103], v38 offset0:117 offset1:125
	ds_read2_b32 v[104:105], v38 offset0:182 offset1:190
	ds_read2_b32 v[106:107], v38 offset0:247 offset1:255
	s_waitcnt lgkmcnt(14)
	v_cvt_pk_bf16_f32 v40, v44, v4
	v_cvt_pk_bf16_f32 v41, v46, v48
	v_cvt_pk_bf16_f32 v42, v50, v52
	v_cvt_pk_bf16_f32 v43, v54, v56
	v_cvt_pk_bf16_f32 v44, v45, v5
	v_cvt_pk_bf16_f32 v45, v47, v49
	v_cvt_pk_bf16_f32 v46, v51, v53
	v_cvt_pk_bf16_f32 v47, v55, v57
	v_cvt_pk_bf16_f32 v48, v60, v58
	v_cvt_pk_bf16_f32 v49, v62, v64
	v_cvt_pk_bf16_f32 v50, v66, v68
	v_cvt_pk_bf16_f32 v51, v70, v72
	v_cvt_pk_bf16_f32 v52, v61, v59
	v_cvt_pk_bf16_f32 v53, v63, v65
	v_cvt_pk_bf16_f32 v54, v67, v69
	v_cvt_pk_bf16_f32 v55, v71, v73
	v_cvt_pk_bf16_f32 v56, v76, v78
	s_waitcnt lgkmcnt(12)
	v_cvt_pk_bf16_f32 v57, v80, v82
	s_waitcnt lgkmcnt(10)
	v_cvt_pk_bf16_f32 v58, v84, v86
	s_waitcnt lgkmcnt(8)
	v_cvt_pk_bf16_f32 v59, v88, v90
	v_cvt_pk_bf16_f32 v60, v77, v79
	v_cvt_pk_bf16_f32 v61, v81, v83
	v_cvt_pk_bf16_f32 v62, v85, v87
	v_cvt_pk_bf16_f32 v63, v89, v91
	s_waitcnt lgkmcnt(6)
	v_cvt_pk_bf16_f32 v64, v92, v94
	s_waitcnt lgkmcnt(4)
	v_cvt_pk_bf16_f32 v65, v96, v98
	s_waitcnt lgkmcnt(2)
	v_cvt_pk_bf16_f32 v66, v100, v102
	s_waitcnt lgkmcnt(0)
	v_cvt_pk_bf16_f32 v67, v104, v106
	v_cvt_pk_bf16_f32 v68, v93, v95
	v_cvt_pk_bf16_f32 v69, v97, v99
	v_cvt_pk_bf16_f32 v70, v101, v103
	v_cvt_pk_bf16_f32 v71, v105, v107
	global_store_dwordx4 v[122:123], v[40:43], off nt
	global_store_dwordx4 v[124:125], v[44:47], off nt
	global_store_dwordx4 v[126:127], v[48:51], off nt
	global_store_dwordx4 v[128:129], v[52:55], off nt
	global_store_dwordx4 v[130:131], v[56:59], off nt
	global_store_dwordx4 v[132:133], v[60:63], off nt
	global_store_dwordx4 v[134:135], v[64:67], off nt
	global_store_dwordx4 v[120:121], v[68:71], off nt
	s_waitcnt lgkmcnt(0)
	s_addk_i32 s0, 0x400
	s_cmpk_gt_i32 s0, 0x7ff
	s_cbranch_scc0 .LBB0_2219

.LBB0_2286:
	s_ashr_i32 s27, s26, 31
	s_lshl_b64 s[26:27], s[26:27], 12
	s_add_u32 s26, s40, s26
	s_addc_u32 s27, s41, s27
	v_lshl_or_b32 v130, s0, 9, v154
	v_mad_u64_u32 v[146:147], s[28:29], v128, s48, v[130:131]
	global_load_dwordx4 v[140:143], v146, s[26:27]
	s_add_u32 s28, s26, 0x1000
	s_addc_u32 s29, s27, 0
	v_or_b32_e32 v129, 0x100, v146
	global_load_dwordx4 v[160:163], v129, s[28:29]
	global_load_dwordx4 v[164:167], v146, s[28:29]
	global_load_dwordx4 v[168:171], v146, s[26:27] offset:256
	v_add_u32_e32 v129, 0x5e000, v146
	global_load_dwordx4 v[172:175], v129, s[26:27]
	global_load_dwordx4 v[176:179], v129, s[28:29]
	v_add_u32_e32 v246, 0x5e100, v146
	global_load_dwordx4 v[180:183], v246, s[28:29]
	global_load_dwordx4 v[184:187], v129, s[26:27] offset:256
	v_add_u32_e32 v245, 0xbc000, v146
	global_load_dwordx4 v[188:191], v245, s[28:29]
	global_load_dwordx4 v[192:195], v245, s[26:27]
	v_add_u32_e32 v129, 0xbc100, v146
	global_load_dwordx4 v[196:199], v129, s[28:29]
	global_load_dwordx4 v[200:203], v245, s[26:27] offset:256
	s_waitcnt vmcnt(11)
	v_lshlrev_b32_e32 v138, 16, v140
	s_waitcnt vmcnt(10)
	v_lshlrev_b32_e32 v136, 16, v160
	s_waitcnt vmcnt(9)
	v_lshlrev_b32_e32 v129, 16, v165
	v_and_b32_e32 v246, 0xffff0000, v165
	v_lshlrev_b32_e32 v245, 16, v166
	v_and_b32_e32 v244, 0xffff0000, v166
	v_lshlrev_b32_e32 v243, 16, v167
	v_and_b32_e32 v242, 0xffff0000, v167
	v_max_f32_e32 v241, v129, v129
	v_max_f32_e32 v240, v246, v246
	v_and_b32_e32 v239, 0xffff0000, v160
	v_max_f32_e32 v129, v244, v244
	v_max_f32_e32 v246, v242, v242
	v_max_f32_e32 v238, 0x1e3ce508, v241
	v_max_f32_e32 v244, 0x1e3ce508, v240
	v_max_f32_e32 v237, v243, v243
	v_max_f32_e32 v236, v136, v136
	v_max_f32_e32 v242, v239, v239
	v_max_f32_e32 v243, 0x1e3ce508, v129
	v_max_f32_e32 v136, 0x1e3ce508, v246
	v_rcp_f32_e32 v240, v238
	v_rcp_f32_e32 v241, v244
	v_lshlrev_b32_e32 v129, 16, v164
	v_and_b32_e32 v246, 0xffff0000, v164
	v_lshlrev_b32_e32 v244, 16, v162
	v_and_b32_e32 v239, 0xffff0000, v162
	v_max_f32_e32 v238, 0x1e3ce508, v237
	v_max_f32_e32 v235, 0x1e3ce508, v236
	v_max_f32_e32 v234, 0x1e3ce508, v242
	v_lshlrev_b32_e32 v237, 16, v163
	v_max_f32_e32 v236, v246, v246
	v_max_f32_e32 v242, v244, v244
	v_max_f32_e32 v233, v239, v239
	v_rcp_f32_e32 v230, v238
	v_rcp_f32_e32 v228, v235
	v_rcp_f32_e32 v229, v234
	v_and_b32_e32 v139, 0xffff0000, v140
	v_lshlrev_b32_e32 v238, 16, v141
	v_and_b32_e32 v239, 0xffff0000, v141
	v_lshlrev_b32_e32 v246, 16, v161
	v_and_b32_e32 v244, 0xffff0000, v161
	v_max_f32_e32 v235, v129, v129
	v_max_f32_e32 v234, v237, v237
	v_max_f32_e32 v232, 0x1e3ce508, v236
	v_max_f32_e32 v129, 0x1e3ce508, v242
	v_max_f32_e32 v237, 0x1e3ce508, v233
	v_max_f32_e32 v236, v246, v246
	v_max_f32_e32 v242, v244, v244
	v_max_f32_e32 v233, 0x1e3ce508, v235
	v_max_f32_e32 v246, 0x1e3ce508, v234
	v_rcp_f32_e32 v227, v232
	v_rcp_f32_e32 v224, v129
	v_rcp_f32_e32 v225, v237
	v_pk_mul_f32 v[234:235], v[240:241], v[238:239]
	v_max_f32_e32 v244, 0x1e3ce508, v236
	v_max_f32_e32 v232, 0x1e3ce508, v242
	v_rcp_f32_e32 v226, v233
	v_pk_mul_f32 v[110:111], v[110:111], v[234:235]
	v_and_b32_e32 v129, 0xffff0000, v163
	s_waitcnt vmcnt(8)
	v_lshlrev_b32_e32 v240, 16, v168
	v_and_b32_e32 v241, 0xffff0000, v168
	v_max_f32_e32 v242, v245, v245
	v_rcp_f32_e32 v234, v244
	v_rcp_f32_e32 v235, v232
	v_max_f32_e32 v245, v129, v129
	v_pk_mul_f32 v[238:239], v[228:229], v[240:241]
	v_max_f32_e32 v244, 0x1e3ce508, v242
	v_max_f32_e32 v129, 0x1e3ce508, v245
	v_pk_mul_f32 v[76:77], v[76:77], v[238:239]
	v_lshlrev_b32_e32 v232, 16, v170
	v_and_b32_e32 v233, 0xffff0000, v170
	v_rcp_f32_e32 v228, v244
	v_rcp_f32_e32 v231, v136
	v_rcp_f32_e32 v240, v246
	v_rcp_f32_e32 v241, v129
	v_pk_mul_f32 v[244:245], v[224:225], v[232:233]
	s_waitcnt vmcnt(6)
	v_lshlrev_b32_e32 v246, 16, v176
	v_pk_mul_f32 v[72:73], v[72:73], v[244:245]
	v_lshlrev_b32_e32 v232, 16, v169
	v_and_b32_e32 v233, 0xffff0000, v169
	v_max_f32_e32 v242, v246, v246
	v_pk_mul_f32 v[224:225], v[226:227], v[138:139]
	v_pk_mul_f32 v[244:245], v[234:235], v[232:233]
	v_max_f32_e32 v246, 0x1e3ce508, v242
	v_lshlrev_b32_e32 v226, 16, v142
	v_and_b32_e32 v227, 0xffff0000, v142
	v_lshlrev_b32_e32 v138, 16, v143
	v_and_b32_e32 v139, 0xffff0000, v143
	v_pk_mul_f32 v[108:109], v[108:109], v[224:225]
	v_pk_mul_f32 v[78:79], v[78:79], v[244:245]
	v_lshlrev_b32_e32 v238, 16, v171
	v_and_b32_e32 v239, 0xffff0000, v171
	v_rcp_f32_e32 v244, v246
	v_and_b32_e32 v242, 0xffff0000, v176
	v_pk_mul_f32 v[236:237], v[230:231], v[138:139]
	v_pk_mul_f32 v[224:225], v[240:241], v[238:239]
	v_max_f32_e32 v246, v242, v242
	v_rcp_f32_e32 v229, v243
	v_pk_mul_f32 v[106:107], v[106:107], v[236:237]
	v_pk_mul_f32 v[74:75], v[74:75], v[224:225]
	v_max_f32_e32 v129, 0x1e3ce508, v246
	v_rcp_f32_e32 v245, v129
	v_lshlrev_b32_e32 v231, 16, v177
	v_max_f32_e32 v246, v231, v231
	v_max_f32_e32 v129, 0x1e3ce508, v246
	v_pk_mul_f32 v[224:225], v[228:229], v[226:227]
	v_rcp_f32_e32 v138, v129
	v_and_b32_e32 v246, 0xffff0000, v177
	v_max_f32_e32 v136, v246, v246
	v_max_f32_e32 v129, 0x1e3ce508, v136
	v_rcp_f32_e32 v139, v129
	v_lshlrev_b32_e32 v246, 16, v178
	v_max_f32_e32 v136, v246, v246
	v_max_f32_e32 v129, 0x1e3ce508, v136
	v_rcp_f32_e32 v226, v129
	v_pk_mul_f32 v[104:105], v[104:105], v[224:225]
	v_and_b32_e32 v246, 0xffff0000, v178
	v_max_f32_e32 v136, v246, v246
	v_max_f32_e32 v129, 0x1e3ce508, v136
	v_rcp_f32_e32 v227, v129
	v_lshlrev_b32_e32 v246, 16, v179
	v_max_f32_e32 v136, v246, v246
	v_max_f32_e32 v129, 0x1e3ce508, v136
	v_lshlrev_b32_e32 v224, 16, v172
	v_and_b32_e32 v225, 0xffff0000, v172
	v_rcp_f32_e32 v242, v129
	v_and_b32_e32 v246, 0xffff0000, v179
	v_pk_mul_f32 v[240:241], v[244:245], v[224:225]
	v_max_f32_e32 v136, v246, v246
	v_pk_mul_f32 v[100:101], v[100:101], v[240:241]
	v_lshlrev_b32_e32 v224, 16, v174
	v_and_b32_e32 v225, 0xffff0000, v174
	v_max_f32_e32 v129, 0x1e3ce508, v136
	v_pk_mul_f32 v[240:241], v[226:227], v[224:225]
	v_rcp_f32_e32 v243, v129
	v_pk_mul_f32 v[96:97], v[96:97], v[240:241]
	v_lshlrev_b32_e32 v244, 16, v173
	v_and_b32_e32 v245, 0xffff0000, v173
	v_pk_mul_f32 v[240:241], v[138:139], v[244:245]
	s_waitcnt vmcnt(5)
	v_lshlrev_b32_e32 v129, 16, v180
	v_pk_mul_f32 v[102:103], v[102:103], v[240:241]
	v_lshlrev_b32_e32 v244, 16, v175
	v_and_b32_e32 v245, 0xffff0000, v175
	v_max_f32_e32 v246, v129, v129
	v_pk_mul_f32 v[240:241], v[242:243], v[244:245]
	v_max_f32_e32 v139, 0x1e3ce508, v246
	v_pk_mul_f32 v[98:99], v[98:99], v[240:241]
	v_rcp_f32_e32 v244, v139
	v_lshlrev_b32_e32 v246, 16, v182
	v_max_f32_e32 v129, v246, v246
	v_max_f32_e32 v139, 0x1e3ce508, v129
	v_rcp_f32_e32 v242, v139
	v_and_b32_e32 v246, 0xffff0000, v180
	v_max_f32_e32 v129, v246, v246
	v_max_f32_e32 v241, 0x1e3ce508, v129
	v_and_b32_e32 v240, 0xffff0000, v182
	v_rcp_f32_e32 v245, v241
	v_lshlrev_b32_e32 v246, 16, v181
	v_and_b32_e32 v129, 0xffff0000, v181
	v_max_f32_e32 v241, v240, v240
	v_max_f32_e32 v139, v246, v246
	v_max_f32_e32 v138, v129, v129
	v_max_f32_e32 v240, 0x1e3ce508, v241
	v_max_f32_e32 v246, 0x1e3ce508, v139
	v_max_f32_e32 v129, 0x1e3ce508, v138
	v_rcp_f32_e32 v243, v240
	v_lshlrev_b32_e32 v241, 16, v183
	v_and_b32_e32 v139, 0xffff0000, v183
	v_rcp_f32_e32 v238, v246
	v_rcp_f32_e32 v239, v129
	v_max_f32_e32 v240, v241, v241
	v_max_f32_e32 v246, v139, v139
	v_max_f32_e32 v129, 0x1e3ce508, v240
	v_max_f32_e32 v241, 0x1e3ce508, v246
	v_rcp_f32_e32 v236, v129
	v_rcp_f32_e32 v237, v241
	s_waitcnt vmcnt(4)
	v_lshlrev_b32_e32 v138, 16, v184
	v_and_b32_e32 v139, 0xffff0000, v184
	v_lshlrev_b32_e32 v240, 16, v185
	v_and_b32_e32 v241, 0xffff0000, v185
	v_pk_mul_f32 v[234:235], v[238:239], v[240:241]
	v_pk_mul_f32 v[232:233], v[244:245], v[138:139]
	v_pk_mul_f32 v[70:71], v[70:71], v[234:235]
	v_lshlrev_b32_e32 v240, 16, v187
	v_and_b32_e32 v241, 0xffff0000, v187
	v_pk_mul_f32 v[238:239], v[236:237], v[240:241]
	v_pk_mul_f32 v[68:69], v[68:69], v[232:233]
	v_pk_mul_f32 v[66:67], v[66:67], v[238:239]
	v_lshlrev_b32_e32 v240, 16, v186
	v_and_b32_e32 v241, 0xffff0000, v186
	v_pk_mul_f32 v[244:245], v[242:243], v[240:241]
	s_waitcnt vmcnt(3)
	v_lshlrev_b32_e32 v246, 16, v188
	v_max_f32_e32 v129, v246, v246
	v_max_f32_e32 v139, 0x1e3ce508, v129
	v_pk_mul_f32 v[64:65], v[64:65], v[244:245]
	v_rcp_f32_e32 v242, v139
	v_and_b32_e32 v129, 0xffff0000, v188
	v_max_f32_e32 v241, v129, v129
	v_max_f32_e32 v240, 0x1e3ce508, v241
	v_rcp_f32_e32 v243, v240
	v_lshlrev_b32_e32 v129, 16, v189
	v_max_f32_e32 v241, v129, v129
	v_max_f32_e32 v240, 0x1e3ce508, v241
	v_rcp_f32_e32 v244, v240
	v_and_b32_e32 v246, 0xffff0000, v189
	v_max_f32_e32 v129, v246, v246
	v_max_f32_e32 v241, 0x1e3ce508, v129
	v_rcp_f32_e32 v245, v241
	v_lshlrev_b32_e32 v246, 16, v190
	v_max_f32_e32 v129, v246, v246
	v_max_f32_e32 v241, 0x1e3ce508, v129
	v_rcp_f32_e32 v138, v241
	v_add_u32_e32 v246, 0x11a000, v146
	global_load_dwordx4 v[140:143], v246, s[28:29]
	v_and_b32_e32 v136, 0xffff0000, v190
	v_max_f32_e32 v129, v136, v136
	v_max_f32_e32 v241, 0x1e3ce508, v129
	v_rcp_f32_e32 v139, v241
	v_lshlrev_b32_e32 v136, 16, v191
	v_max_f32_e32 v129, v136, v136
	v_max_f32_e32 v241, 0x1e3ce508, v129
	v_rcp_f32_e32 v238, v241
	v_and_b32_e32 v136, 0xffff0000, v191
	s_waitcnt vmcnt(3)
	v_lshlrev_b32_e32 v236, 16, v192
	v_and_b32_e32 v237, 0xffff0000, v192
	v_max_f32_e32 v129, v136, v136
	v_pk_mul_f32 v[240:241], v[242:243], v[236:237]
	v_max_f32_e32 v235, 0x1e3ce508, v129
	v_pk_mul_f32 v[92:93], v[92:93], v[240:241]
	v_lshlrev_b32_e32 v236, 16, v194
	v_and_b32_e32 v237, 0xffff0000, v194
	v_rcp_f32_e32 v239, v235
	v_pk_mul_f32 v[242:243], v[138:139], v[236:237]
	s_waitcnt vmcnt(2)
	v_lshlrev_b32_e32 v129, 16, v196
	v_pk_mul_f32 v[88:89], v[88:89], v[242:243]
	v_lshlrev_b32_e32 v236, 16, v193
	v_and_b32_e32 v237, 0xffff0000, v193
	v_pk_mul_f32 v[138:139], v[244:245], v[236:237]
	v_max_f32_e32 v136, v129, v129
	v_pk_mul_f32 v[94:95], v[94:95], v[138:139]
	v_lshlrev_b32_e32 v244, 16, v195
	v_and_b32_e32 v245, 0xffff0000, v195
	v_pk_mul_f32 v[236:237], v[238:239], v[244:245]
	global_load_dwordx4 v[160:163], v246, s[26:27]
	v_max_f32_e32 v129, 0x1e3ce508, v136
	v_pk_mul_f32 v[90:91], v[90:91], v[236:237]
	v_rcp_f32_e32 v244, v129
	v_and_b32_e32 v139, 0xffff0000, v196
	v_add_u32_e32 v138, 0x11a100, v146
	v_max_f32_e32 v136, v139, v139
	global_load_dwordx4 v[164:167], v138, s[28:29]
	v_max_f32_e32 v129, 0x1e3ce508, v136
	v_rcp_f32_e32 v245, v129
	v_lshlrev_b32_e32 v139, 16, v197
	v_max_f32_e32 v138, v139, v139
	v_max_f32_e32 v129, 0x1e3ce508, v138
	v_rcp_f32_e32 v242, v129
	v_and_b32_e32 v241, 0xffff0000, v197
	v_max_f32_e32 v240, v241, v241
	v_max_f32_e32 v129, 0x1e3ce508, v240
	v_rcp_f32_e32 v243, v129
	v_lshlrev_b32_e32 v241, 16, v198
	v_max_f32_e32 v240, v241, v241
	v_max_f32_e32 v129, 0x1e3ce508, v240
	v_rcp_f32_e32 v138, v129
	v_and_b32_e32 v136, 0xffff0000, v198
	v_max_f32_e32 v241, v136, v136
	v_max_f32_e32 v240, 0x1e3ce508, v241
	v_rcp_f32_e32 v139, v240
	v_lshlrev_b32_e32 v136, 16, v199
	v_max_f32_e32 v129, v136, v136
	v_max_f32_e32 v241, 0x1e3ce508, v129
	v_rcp_f32_e32 v238, v241
	v_and_b32_e32 v136, 0xffff0000, v199
	v_max_f32_e32 v129, v136, v136
	v_max_f32_e32 v241, 0x1e3ce508, v129
	v_rcp_f32_e32 v239, v241
	s_waitcnt vmcnt(3)
	v_lshlrev_b32_e32 v236, 16, v200
	v_and_b32_e32 v237, 0xffff0000, v200
	v_lshlrev_b32_e32 v240, 16, v201
	v_and_b32_e32 v241, 0xffff0000, v201
	v_pk_mul_f32 v[234:235], v[242:243], v[240:241]
	v_pk_mul_f32 v[232:233], v[244:245], v[236:237]
	v_pk_mul_f32 v[62:63], v[62:63], v[234:235]
	v_lshlrev_b32_e32 v242, 16, v203
	v_and_b32_e32 v243, 0xffff0000, v203
	v_pk_mul_f32 v[244:245], v[238:239], v[242:243]
	v_pk_mul_f32 v[60:61], v[60:61], v[232:233]
	v_lshlrev_b32_e32 v240, 16, v202
	v_and_b32_e32 v241, 0xffff0000, v202
	v_pk_mul_f32 v[58:59], v[58:59], v[244:245]
	global_load_dwordx4 v[168:171], v246, s[26:27] offset:256
	v_pk_mul_f32 v[242:243], v[138:139], v[240:241]
	s_waitcnt vmcnt(3)
	v_lshlrev_b32_e32 v129, 16, v140
	v_max_f32_e32 v246, v129, v129
	v_max_f32_e32 v245, 0x1e3ce508, v246
	v_pk_mul_f32 v[56:57], v[56:57], v[242:243]
	v_rcp_f32_e32 v138, v245
	v_and_b32_e32 v136, 0xffff0000, v140
	v_max_f32_e32 v129, v136, v136
	v_max_f32_e32 v246, 0x1e3ce508, v129
	v_rcp_f32_e32 v139, v246
	v_lshlrev_b32_e32 v136, 16, v141
	v_max_f32_e32 v129, v136, v136
	v_max_f32_e32 v246, 0x1e3ce508, v129
	v_rcp_f32_e32 v244, v246
	v_and_b32_e32 v136, 0xffff0000, v141
	v_max_f32_e32 v129, v136, v136
	v_max_f32_e32 v246, 0x1e3ce508, v129
	v_rcp_f32_e32 v245, v246
	v_lshlrev_b32_e32 v136, 16, v142
	v_max_f32_e32 v129, v136, v136
	v_max_f32_e32 v246, 0x1e3ce508, v129
	v_rcp_f32_e32 v242, v246
	v_and_b32_e32 v136, 0xffff0000, v142
	v_max_f32_e32 v129, v136, v136
	v_max_f32_e32 v246, 0x1e3ce508, v129
	v_rcp_f32_e32 v243, v246
	v_lshlrev_b32_e32 v136, 16, v143
	v_max_f32_e32 v129, v136, v136
	v_max_f32_e32 v246, 0x1e3ce508, v129
	v_rcp_f32_e32 v240, v246
	v_and_b32_e32 v136, 0xffff0000, v143
	s_waitcnt vmcnt(2)
	v_lshlrev_b32_e32 v238, 16, v160
	v_and_b32_e32 v239, 0xffff0000, v160
	v_max_f32_e32 v246, v136, v136
	v_pk_mul_f32 v[236:237], v[138:139], v[238:239]
	v_max_f32_e32 v129, 0x1e3ce508, v246
	v_pk_mul_f32 v[84:85], v[84:85], v[236:237]
	v_lshlrev_b32_e32 v138, 16, v162
	v_and_b32_e32 v139, 0xffff0000, v162
	v_rcp_f32_e32 v241, v129
	v_pk_mul_f32 v[238:239], v[242:243], v[138:139]
	s_waitcnt vmcnt(1)
	v_lshlrev_b32_e32 v246, 16, v164
	v_pk_mul_f32 v[80:81], v[80:81], v[238:239]
	v_lshlrev_b32_e32 v242, 16, v161
	v_and_b32_e32 v243, 0xffff0000, v161
	v_pk_mul_f32 v[138:139], v[244:245], v[242:243]
	v_max_f32_e32 v136, v246, v246
	v_pk_mul_f32 v[86:87], v[86:87], v[138:139]
	v_lshlrev_b32_e32 v242, 16, v163
	v_and_b32_e32 v243, 0xffff0000, v163
	v_pk_mul_f32 v[138:139], v[240:241], v[242:243]
	v_max_f32_e32 v129, 0x1e3ce508, v136
	v_pk_mul_f32 v[82:83], v[82:83], v[138:139]
	v_rcp_f32_e32 v244, v129
	v_and_b32_e32 v246, 0xffff0000, v164
	v_max_f32_e32 v139, v246, v246
	v_max_f32_e32 v129, 0x1e3ce508, v139
	v_rcp_f32_e32 v245, v129
	v_lshlrev_b32_e32 v246, 16, v165
	v_max_f32_e32 v139, v246, v246
	v_max_f32_e32 v129, 0x1e3ce508, v139
	v_rcp_f32_e32 v242, v129
	v_and_b32_e32 v246, 0xffff0000, v165
	v_max_f32_e32 v241, v246, v246
	v_max_f32_e32 v240, 0x1e3ce508, v241
	v_rcp_f32_e32 v243, v240
	v_lshlrev_b32_e32 v246, 16, v166
	v_max_f32_e32 v129, v246, v246
	v_max_f32_e32 v241, 0x1e3ce508, v129
	v_rcp_f32_e32 v138, v241
	v_and_b32_e32 v246, 0xffff0000, v166
	v_max_f32_e32 v136, v246, v246
	v_max_f32_e32 v129, 0x1e3ce508, v136
	v_rcp_f32_e32 v139, v129
	v_lshlrev_b32_e32 v246, 16, v167
	v_max_f32_e32 v136, v246, v246
	v_max_f32_e32 v129, 0x1e3ce508, v136
	v_rcp_f32_e32 v240, v129
	v_and_b32_e32 v246, 0xffff0000, v167
	v_max_f32_e32 v136, v246, v246
	v_max_f32_e32 v129, 0x1e3ce508, v136
	v_rcp_f32_e32 v241, v129
	s_waitcnt vmcnt(0)
	v_lshlrev_b32_e32 v238, 16, v168
	v_and_b32_e32 v239, 0xffff0000, v168
	v_lshlrev_b32_e32 v236, 16, v169
	v_and_b32_e32 v237, 0xffff0000, v169
	v_pk_mul_f32 v[234:235], v[244:245], v[238:239]
	v_pk_mul_f32 v[232:233], v[242:243], v[236:237]
	v_pk_mul_f32 v[52:53], v[52:53], v[234:235]
	v_lshlrev_b32_e32 v244, 16, v170
	v_and_b32_e32 v245, 0xffff0000, v170
	v_pk_mul_f32 v[54:55], v[54:55], v[232:233]
	v_lshlrev_b32_e32 v242, 16, v171
	v_and_b32_e32 v243, 0xffff0000, v171
	v_pk_mul_f32 v[238:239], v[138:139], v[244:245]
	v_pk_mul_f32 v[236:237], v[240:241], v[242:243]
	v_pk_mul_f32 v[48:49], v[48:49], v[238:239]
	v_pk_mul_f32 v[50:51], v[50:51], v[236:237]
	v_add_u32_e32 v129, 0x2f0000, v146
	v_add_u32_e32 v246, 0x2f0100, v146
	global_load_dwordx4 v[140:143], v129, s[28:29]
	global_load_dwordx4 v[160:163], v129, s[26:27]
	global_load_dwordx4 v[164:167], v246, s[28:29]
	v_add_u32_e32 v245, 0x34e100, v146
	v_add_u32_e32 v244, 0x34e000, v146
	global_load_dwordx4 v[168:171], v129, s[26:27] offset:256
	global_load_dwordx4 v[172:175], v244, s[26:27]
	global_load_dwordx4 v[176:179], v244, s[28:29]
	global_load_dwordx4 v[180:183], v245, s[28:29]
	s_waitcnt vmcnt(6)
	v_lshlrev_b32_e32 v129, 16, v140
	v_and_b32_e32 v246, 0xffff0000, v140
	v_lshlrev_b32_e32 v245, 16, v141
	v_and_b32_e32 v139, 0xffff0000, v141
	v_lshlrev_b32_e32 v138, 16, v142
	v_and_b32_e32 v136, 0xffff0000, v142
	v_lshlrev_b32_e32 v243, 16, v143
	v_and_b32_e32 v242, 0xffff0000, v143
	s_waitcnt vmcnt(5)
	v_lshlrev_b32_e32 v240, 16, v160
	v_and_b32_e32 v241, 0xffff0000, v160
	v_lshlrev_b32_e32 v238, 16, v162
	v_and_b32_e32 v239, 0xffff0000, v162
	v_lshlrev_b32_e32 v236, 16, v161
	v_and_b32_e32 v237, 0xffff0000, v161
	v_lshlrev_b32_e32 v234, 16, v163
	v_and_b32_e32 v235, 0xffff0000, v163
	s_waitcnt vmcnt(4)
	v_lshlrev_b32_e32 v233, 16, v164
	v_and_b32_e32 v232, 0xffff0000, v164
	v_max_f32_e32 v231, v129, v129
	v_max_f32_e32 v230, v246, v246
	v_max_f32_e32 v229, v233, v233
	v_max_f32_e32 v228, v232, v232
	v_max_f32_e32 v246, 0x1e3ce508, v231
	v_max_f32_e32 v129, 0x1e3ce508, v230
	v_lshlrev_b32_e32 v233, 16, v165
	v_and_b32_e32 v232, 0xffff0000, v165
	v_lshlrev_b32_e32 v231, 16, v166
	v_and_b32_e32 v230, 0xffff0000, v166
	v_max_f32_e32 v227, v139, v139
	v_max_f32_e32 v226, v138, v138
	v_max_f32_e32 v225, 0x1e3ce508, v229
	v_max_f32_e32 v224, 0x1e3ce508, v228
	v_rcp_f32_e32 v138, v246
	v_rcp_f32_e32 v139, v129
	v_max_f32_e32 v229, v232, v232
	v_max_f32_e32 v246, v230, v230
	v_max_f32_e32 v129, 0x1e3ce508, v227
	v_max_f32_e32 v232, 0x1e3ce508, v226
	v_max_f32_e32 v230, v245, v245
	v_max_f32_e32 v228, v242, v242
	v_max_f32_e32 v227, v231, v231
	v_max_f32_e32 v245, 0x1e3ce508, v229
	v_max_f32_e32 v242, 0x1e3ce508, v246
	v_rcp_f32_e32 v223, v129
	v_rcp_f32_e32 v220, v232
	v_rcp_f32_e32 v218, v225
	v_rcp_f32_e32 v219, v224
	v_max_f32_e32 v246, v233, v233
	v_max_f32_e32 v129, 0x1e3ce508, v230
	v_max_f32_e32 v232, 0x1e3ce508, v228
	v_max_f32_e32 v233, 0x1e3ce508, v227
	v_lshlrev_b32_e32 v217, 16, v167
	v_and_b32_e32 v216, 0xffff0000, v167
	v_max_f32_e32 v231, v136, v136
	v_max_f32_e32 v230, v243, v243
	v_max_f32_e32 v229, 0x1e3ce508, v246
	v_rcp_f32_e32 v222, v129
	v_rcp_f32_e32 v227, v232
	v_rcp_f32_e32 v224, v233
	v_rcp_f32_e32 v225, v242
	v_pk_mul_f32 v[214:215], v[138:139], v[240:241]
	v_max_f32_e32 v246, v216, v216
	v_max_f32_e32 v228, 0x1e3ce508, v231
	v_max_f32_e32 v129, 0x1e3ce508, v230
	v_pk_mul_f32 v[44:45], v[44:45], v[214:215]
	s_waitcnt vmcnt(3)
	v_lshlrev_b32_e32 v232, 16, v168
	v_and_b32_e32 v233, 0xffff0000, v168
	v_max_f32_e32 v216, v217, v217
	v_max_f32_e32 v231, 0x1e3ce508, v246
	v_rcp_f32_e32 v221, v228
	v_rcp_f32_e32 v226, v129
	v_rcp_f32_e32 v138, v229
	v_rcp_f32_e32 v139, v245
	v_pk_mul_f32 v[242:243], v[218:219], v[232:233]
	v_max_f32_e32 v136, 0x1e3ce508, v216
	v_pk_mul_f32 v[12:13], v[12:13], v[242:243]
	v_lshlrev_b32_e32 v232, 16, v170
	v_and_b32_e32 v233, 0xffff0000, v170
	v_rcp_f32_e32 v228, v136
	v_rcp_f32_e32 v229, v231
	v_pk_mul_f32 v[242:243], v[224:225], v[232:233]
	s_waitcnt vmcnt(1)
	v_lshlrev_b32_e32 v136, 16, v176
	v_pk_mul_f32 v[8:9], v[8:9], v[242:243]
	v_lshlrev_b32_e32 v232, 16, v169
	v_and_b32_e32 v233, 0xffff0000, v169
	v_max_f32_e32 v129, v136, v136
	v_pk_mul_f32 v[230:231], v[222:223], v[236:237]
	v_pk_mul_f32 v[224:225], v[138:139], v[232:233]
	v_max_f32_e32 v246, 0x1e3ce508, v129
	v_pk_mul_f32 v[46:47], v[46:47], v[230:231]
	v_pk_mul_f32 v[14:15], v[14:15], v[224:225]
	v_lshlrev_b32_e32 v236, 16, v171
	v_and_b32_e32 v237, 0xffff0000, v171
	v_rcp_f32_e32 v232, v246
	v_and_b32_e32 v129, 0xffff0000, v176
	v_pk_mul_f32 v[230:231], v[220:221], v[238:239]
	v_pk_mul_f32 v[224:225], v[228:229], v[236:237]
	v_max_f32_e32 v246, v129, v129
	v_pk_mul_f32 v[40:41], v[40:41], v[230:231]
	v_pk_mul_f32 v[10:11], v[10:11], v[224:225]
	global_load_dwordx4 v[140:143], v244, s[26:27] offset:256
	v_max_f32_e32 v129, 0x1e3ce508, v246
	v_rcp_f32_e32 v233, v129
	v_lshlrev_b32_e32 v225, 16, v177
	v_max_f32_e32 v224, v225, v225
	v_max_f32_e32 v129, 0x1e3ce508, v224
	v_rcp_f32_e32 v244, v129
	v_and_b32_e32 v246, 0xffff0000, v177
	v_max_f32_e32 v225, v246, v246
	v_max_f32_e32 v224, 0x1e3ce508, v225
	v_rcp_f32_e32 v245, v224
	v_lshlrev_b32_e32 v246, 16, v178
	v_max_f32_e32 v129, v246, v246
	v_max_f32_e32 v225, 0x1e3ce508, v129
	v_pk_mul_f32 v[138:139], v[226:227], v[234:235]
	v_rcp_f32_e32 v242, v225
	v_add_u32_e32 v246, 0x3ac000, v146
	v_pk_mul_f32 v[42:43], v[42:43], v[138:139]
	global_load_dwordx4 v[160:163], v246, s[28:29]
	v_and_b32_e32 v129, 0xffff0000, v178
	v_max_f32_e32 v241, v129, v129
	v_max_f32_e32 v240, 0x1e3ce508, v241
	v_rcp_f32_e32 v243, v240
	v_lshlrev_b32_e32 v234, 16, v172
	v_and_b32_e32 v235, 0xffff0000, v172
	v_pk_mul_f32 v[240:241], v[232:233], v[234:235]
	v_lshlrev_b32_e32 v129, 16, v179
	v_pk_mul_f32 v[36:37], v[36:37], v[240:241]
	v_lshlrev_b32_e32 v138, 16, v174
	v_and_b32_e32 v139, 0xffff0000, v174
	v_pk_mul_f32 v[240:241], v[242:243], v[138:139]
	v_max_f32_e32 v136, v129, v129
	v_pk_mul_f32 v[32:33], v[32:33], v[240:241]
	v_lshlrev_b32_e32 v138, 16, v173
	v_and_b32_e32 v139, 0xffff0000, v173
	v_pk_mul_f32 v[242:243], v[244:245], v[138:139]
	global_load_dwordx4 v[164:167], v246, s[26:27]
	v_max_f32_e32 v129, 0x1e3ce508, v136
	v_rcp_f32_e32 v244, v129
	v_and_b32_e32 v241, 0xffff0000, v179
	v_max_f32_e32 v240, v241, v241
	v_max_f32_e32 v129, 0x1e3ce508, v240
	v_rcp_f32_e32 v245, v129
	s_waitcnt vmcnt(3)
	v_lshlrev_b32_e32 v241, 16, v180
	v_pk_mul_f32 v[38:39], v[38:39], v[242:243]
	v_lshlrev_b32_e32 v138, 16, v175
	v_and_b32_e32 v139, 0xffff0000, v175
	v_max_f32_e32 v136, v241, v241
	v_pk_mul_f32 v[242:243], v[244:245], v[138:139]
	v_max_f32_e32 v129, 0x1e3ce508, v136
	v_pk_mul_f32 v[34:35], v[34:35], v[242:243]
	v_rcp_f32_e32 v244, v129
	v_lshlrev_b32_e32 v139, 16, v182
	v_max_f32_e32 v138, v139, v139
	v_max_f32_e32 v129, 0x1e3ce508, v138
	v_rcp_f32_e32 v242, v129
	v_add_u32_e32 v241, 0x3ac100, v146
	global_load_dwordx4 v[168:171], v241, s[28:29]
	v_and_b32_e32 v129, 0xffff0000, v180
	v_max_f32_e32 v240, v129, v129
	v_max_f32_e32 v241, 0x1e3ce508, v240
	v_and_b32_e32 v139, 0xffff0000, v182
	v_rcp_f32_e32 v245, v241
	v_lshlrev_b32_e32 v129, 16, v181
	v_and_b32_e32 v240, 0xffff0000, v181
	v_max_f32_e32 v241, v139, v139
	v_max_f32_e32 v138, v129, v129
	v_max_f32_e32 v136, v240, v240
	v_max_f32_e32 v139, 0x1e3ce508, v241
	v_max_f32_e32 v129, 0x1e3ce508, v138
	v_max_f32_e32 v240, 0x1e3ce508, v136
	v_rcp_f32_e32 v243, v139
	v_lshlrev_b32_e32 v241, 16, v183
	v_and_b32_e32 v138, 0xffff0000, v183
	v_rcp_f32_e32 v238, v129
	v_rcp_f32_e32 v239, v240
	v_max_f32_e32 v237, v241, v241
	v_max_f32_e32 v236, v138, v138
	v_max_f32_e32 v129, 0x1e3ce508, v237
	v_max_f32_e32 v241, 0x1e3ce508, v236
	v_rcp_f32_e32 v138, v129
	v_rcp_f32_e32 v139, v241
	s_waitcnt vmcnt(3)
	v_lshlrev_b32_e32 v236, 16, v140
	v_and_b32_e32 v237, 0xffff0000, v140
	v_lshlrev_b32_e32 v240, 16, v141
	v_and_b32_e32 v241, 0xffff0000, v141
	v_pk_mul_f32 v[234:235], v[238:239], v[240:241]
	v_pk_mul_f32 v[232:233], v[244:245], v[236:237]
	v_pk_mul_f32 v[6:7], v[6:7], v[234:235]
	v_lshlrev_b32_e32 v240, 16, v143
	v_and_b32_e32 v241, 0xffff0000, v143
	v_pk_mul_f32 v[244:245], v[138:139], v[240:241]
	v_pk_mul_f32 v[4:5], v[4:5], v[232:233]
	v_pk_mul_f32 v[2:3], v[2:3], v[244:245]
	v_lshlrev_b32_e32 v240, 16, v142
	v_and_b32_e32 v241, 0xffff0000, v142
	v_pk_mul_f32 v[244:245], v[242:243], v[240:241]
	s_waitcnt vmcnt(2)
	v_lshlrev_b32_e32 v129, 16, v160
	v_max_f32_e32 v139, v129, v129
	v_max_f32_e32 v138, 0x1e3ce508, v139
	v_pk_mul_f32 v[0:1], v[0:1], v[244:245]
	v_rcp_f32_e32 v242, v138
	v_and_b32_e32 v129, 0xffff0000, v160
	v_max_f32_e32 v245, v129, v129
	global_load_dwordx4 v[140:143], v246, s[26:27] offset:256
	v_max_f32_e32 v244, 0x1e3ce508, v245
	v_rcp_f32_e32 v243, v244
	v_lshlrev_b32_e32 v129, 16, v161
	v_max_f32_e32 v241, v129, v129
	v_max_f32_e32 v240, 0x1e3ce508, v241
	v_rcp_f32_e32 v244, v240
	v_and_b32_e32 v246, 0xffff0000, v161
	v_max_f32_e32 v129, v246, v246
	v_max_f32_e32 v241, 0x1e3ce508, v129
	v_rcp_f32_e32 v245, v241
	v_lshlrev_b32_e32 v246, 16, v162
	v_max_f32_e32 v129, v246, v246
	v_max_f32_e32 v241, 0x1e3ce508, v129
	v_rcp_f32_e32 v138, v241
	v_add_u32_e32 v246, 0x40a000, v146
	global_load_dwordx4 v[172:175], v246, s[28:29]
	v_and_b32_e32 v136, 0xffff0000, v162
	v_max_f32_e32 v129, v136, v136
	v_max_f32_e32 v241, 0x1e3ce508, v129
	v_rcp_f32_e32 v139, v241
	v_lshlrev_b32_e32 v136, 16, v163
	v_max_f32_e32 v129, v136, v136
	v_max_f32_e32 v241, 0x1e3ce508, v129
	v_rcp_f32_e32 v238, v241
	v_and_b32_e32 v136, 0xffff0000, v163
	s_waitcnt vmcnt(3)
	v_lshlrev_b32_e32 v236, 16, v164
	v_and_b32_e32 v237, 0xffff0000, v164
	v_max_f32_e32 v129, v136, v136
	v_pk_mul_f32 v[240:241], v[242:243], v[236:237]
	v_max_f32_e32 v235, 0x1e3ce508, v129
	v_pk_mul_f32 v[28:29], v[28:29], v[240:241]
	v_lshlrev_b32_e32 v236, 16, v166
	v_and_b32_e32 v237, 0xffff0000, v166
	v_rcp_f32_e32 v239, v235
	v_pk_mul_f32 v[242:243], v[138:139], v[236:237]
	v_add_u32_e32 v129, 0x40a100, v146
	v_pk_mul_f32 v[24:25], v[24:25], v[242:243]
	v_lshlrev_b32_e32 v236, 16, v165
	v_and_b32_e32 v237, 0xffff0000, v165
	v_pk_mul_f32 v[146:147], v[244:245], v[236:237]
	s_waitcnt vmcnt(2)
	v_lshlrev_b32_e32 v139, 16, v168
	v_pk_mul_f32 v[30:31], v[30:31], v[146:147]
	v_lshlrev_b32_e32 v244, 16, v167
	v_and_b32_e32 v245, 0xffff0000, v167
	v_pk_mul_f32 v[236:237], v[238:239], v[244:245]
	global_load_dwordx4 v[160:163], v246, s[26:27]
	global_load_dwordx4 v[164:167], v129, s[28:29]
	v_max_f32_e32 v245, v139, v139
	v_max_f32_e32 v244, 0x1e3ce508, v245
	v_pk_mul_f32 v[26:27], v[26:27], v[236:237]
	v_rcp_f32_e32 v146, v244
	v_and_b32_e32 v129, 0xffff0000, v168
	v_max_f32_e32 v245, v129, v129
	v_max_f32_e32 v244, 0x1e3ce508, v245
	v_rcp_f32_e32 v147, v244
	v_lshlrev_b32_e32 v129, 16, v169
	v_max_f32_e32 v245, v129, v129
	v_max_f32_e32 v244, 0x1e3ce508, v245
	v_rcp_f32_e32 v138, v244
	v_and_b32_e32 v136, 0xffff0000, v169
	v_max_f32_e32 v129, v136, v136
	v_max_f32_e32 v245, 0x1e3ce508, v129
	v_rcp_f32_e32 v139, v245
	v_lshlrev_b32_e32 v136, 16, v170
	v_max_f32_e32 v129, v136, v136
	v_max_f32_e32 v245, 0x1e3ce508, v129
	v_and_b32_e32 v244, 0xffff0000, v170
	v_lshlrev_b32_e32 v136, 16, v171
	v_and_b32_e32 v129, 0xffff0000, v171
	v_max_f32_e32 v243, v136, v136
	v_max_f32_e32 v242, v129, v129
	v_max_f32_e32 v241, 0x1e3ce508, v243
	v_max_f32_e32 v136, 0x1e3ce508, v242
	v_rcp_f32_e32 v238, v241
	v_rcp_f32_e32 v239, v136
	v_max_f32_e32 v129, v244, v244
	v_max_f32_e32 v237, 0x1e3ce508, v129
	v_rcp_f32_e32 v242, v245
	v_rcp_f32_e32 v243, v237
	s_waitcnt vmcnt(3)
	v_lshlrev_b32_e32 v240, 16, v140
	v_and_b32_e32 v241, 0xffff0000, v140
	v_lshlrev_b32_e32 v244, 16, v141
	v_and_b32_e32 v245, 0xffff0000, v141
	v_pk_mul_f32 v[236:237], v[138:139], v[244:245]
	v_pk_mul_f32 v[234:235], v[146:147], v[240:241]
	v_pk_mul_f32 v[114:115], v[114:115], v[236:237]
	v_lshlrev_b32_e32 v244, 16, v143
	v_and_b32_e32 v245, 0xffff0000, v143
	v_pk_mul_f32 v[240:241], v[238:239], v[244:245]
	v_pk_mul_f32 v[112:113], v[112:113], v[234:235]
	v_lshlrev_b32_e32 v146, 16, v142
	v_and_b32_e32 v147, 0xffff0000, v142
	v_pk_mul_f32 v[118:119], v[118:119], v[240:241]
	global_load_dwordx4 v[168:171], v246, s[26:27] offset:256
	v_pk_mul_f32 v[244:245], v[242:243], v[146:147]
	s_waitcnt vmcnt(2)
	v_lshlrev_b32_e32 v138, 16, v160
	v_pk_mul_f32 v[116:117], v[116:117], v[244:245]
	v_lshlrev_b32_e32 v136, 16, v172
	v_max_f32_e32 v129, v136, v136
	v_max_f32_e32 v147, 0x1e3ce508, v129
	v_rcp_f32_e32 v244, v147
	v_and_b32_e32 v246, 0xffff0000, v172
	v_max_f32_e32 v136, v246, v246
	v_max_f32_e32 v129, 0x1e3ce508, v136
	v_rcp_f32_e32 v245, v129
	v_lshlrev_b32_e32 v246, 16, v173
	v_max_f32_e32 v136, v246, v246
	v_max_f32_e32 v129, 0x1e3ce508, v136
	v_rcp_f32_e32 v146, v129
	v_and_b32_e32 v246, 0xffff0000, v173
	v_max_f32_e32 v136, v246, v246
	v_max_f32_e32 v129, 0x1e3ce508, v136
	v_rcp_f32_e32 v147, v129
	v_lshlrev_b32_e32 v246, 16, v174
	v_max_f32_e32 v136, v246, v246
	v_max_f32_e32 v129, 0x1e3ce508, v136
	v_rcp_f32_e32 v242, v129
	v_and_b32_e32 v246, 0xffff0000, v174
	v_max_f32_e32 v136, v246, v246
	v_max_f32_e32 v129, 0x1e3ce508, v136
	v_rcp_f32_e32 v243, v129
	v_lshlrev_b32_e32 v246, 16, v175
	v_max_f32_e32 v136, v246, v246
	v_max_f32_e32 v129, 0x1e3ce508, v136
	v_rcp_f32_e32 v240, v129
	v_and_b32_e32 v246, 0xffff0000, v175
	v_and_b32_e32 v139, 0xffff0000, v160
	v_max_f32_e32 v136, v246, v246
	v_pk_mul_f32 v[238:239], v[244:245], v[138:139]
	v_max_f32_e32 v129, 0x1e3ce508, v136
	v_pk_mul_f32 v[20:21], v[20:21], v[238:239]
	v_lshlrev_b32_e32 v244, 16, v162
	v_and_b32_e32 v245, 0xffff0000, v162
	v_rcp_f32_e32 v241, v129
	v_pk_mul_f32 v[138:139], v[242:243], v[244:245]
	s_waitcnt vmcnt(1)
	v_lshlrev_b32_e32 v136, 16, v164
	v_pk_mul_f32 v[16:17], v[16:17], v[138:139]
	v_lshlrev_b32_e32 v242, 16, v161
	v_and_b32_e32 v243, 0xffff0000, v161
	v_pk_mul_f32 v[138:139], v[146:147], v[242:243]
	v_max_f32_e32 v129, v136, v136
	v_pk_mul_f32 v[22:23], v[22:23], v[138:139]
	v_lshlrev_b32_e32 v242, 16, v163
	v_and_b32_e32 v243, 0xffff0000, v163
	v_pk_mul_f32 v[146:147], v[240:241], v[242:243]
	v_max_f32_e32 v246, 0x1e3ce508, v129
	v_pk_mul_f32 v[18:19], v[18:19], v[146:147]
	v_rcp_f32_e32 v244, v246
	v_and_b32_e32 v129, 0xffff0000, v164
	v_max_f32_e32 v147, v129, v129
	v_max_f32_e32 v246, 0x1e3ce508, v147
	v_rcp_f32_e32 v245, v246
	v_lshlrev_b32_e32 v129, 16, v165
	v_max_f32_e32 v147, v129, v129
	v_max_f32_e32 v246, 0x1e3ce508, v147
	v_rcp_f32_e32 v138, v246
	v_and_b32_e32 v136, 0xffff0000, v165
	v_max_f32_e32 v129, v136, v136
	v_max_f32_e32 v246, 0x1e3ce508, v129
	v_rcp_f32_e32 v139, v246
	v_lshlrev_b32_e32 v136, 16, v166
	v_max_f32_e32 v129, v136, v136
	v_max_f32_e32 v246, 0x1e3ce508, v129
	v_rcp_f32_e32 v146, v246
	v_and_b32_e32 v136, 0xffff0000, v166
	v_max_f32_e32 v129, v136, v136
	v_max_f32_e32 v246, 0x1e3ce508, v129
	v_rcp_f32_e32 v147, v246
	v_lshlrev_b32_e32 v136, 16, v167
	v_max_f32_e32 v129, v136, v136
	v_max_f32_e32 v246, 0x1e3ce508, v129
	v_rcp_f32_e32 v242, v246
	v_and_b32_e32 v136, 0xffff0000, v167
	v_max_f32_e32 v129, v136, v136
	v_max_f32_e32 v246, 0x1e3ce508, v129
	v_rcp_f32_e32 v243, v246
	s_waitcnt vmcnt(0)
	v_lshlrev_b32_e32 v240, 16, v168
	v_and_b32_e32 v241, 0xffff0000, v168
	v_lshlrev_b32_e32 v238, 16, v169
	v_and_b32_e32 v239, 0xffff0000, v169
	v_pk_mul_f32 v[236:237], v[244:245], v[240:241]
	v_pk_mul_f32 v[234:235], v[138:139], v[238:239]
	v_pk_mul_f32 v[120:121], v[120:121], v[236:237]
	v_lshlrev_b32_e32 v240, 16, v170
	v_and_b32_e32 v241, 0xffff0000, v170
	v_pk_mul_f32 v[122:123], v[122:123], v[234:235]
	v_lshlrev_b32_e32 v244, 16, v171
	v_and_b32_e32 v245, 0xffff0000, v171
	v_pk_mul_f32 v[138:139], v[146:147], v[240:241]
	v_pk_mul_f32 v[238:239], v[242:243], v[244:245]
	v_pk_mul_f32 v[124:125], v[124:125], v[138:139]
	v_pk_mul_f32 v[126:127], v[126:127], v[238:239]
	s_cmp_eq_u32 s55, 2
	s_mov_b64 s[26:27], -1
	s_cbranch_scc1 .LBB0_2273
